# conv: hand-written scalar-addressed fast path, two 2-row batches of tap loads in flight (grid 256; other grids use the original loop)
# speedup vs baseline: 1.0024x; 1.0024x over previous
.LBB0_334:
	s_cmp_lt_i32 s88, 5
	s_cselect_b64 s[14:15], -1, 0
	s_and_b64 s[2:3], s[14:15], s[2:3]
	s_andn2_b64 vcc, exec, s[2:3]
	s_cbranch_vccnz .LBB0_357
	v_mbcnt_lo_u32_b32 v0, -1, 0
	v_mbcnt_hi_u32_b32 v0, -1, v0
	v_readlane_b32 s2, v254, 0
	s_mov_b64 s[16:17], s[86:87]
	v_lshl_or_b32 v80, s96, 6, v0
	s_waitcnt lgkmcnt(0)
	s_mov_b32 s18, s2
	s_load_dword s21, s[0:1], 0x108
	v_lshl_add_u32 v0, s18, 9, v80
	v_ashrrev_i32_e32 v74, 7, v0
	s_mov_b32 s19, 0x8800
	v_lshlrev_b32_e32 v78, 3, v80
	v_cmp_gt_i32_e32 vcc, s19, v74
	s_load_dwordx2 s[2:3], s[0:1], 0x60
	s_waitcnt lgkmcnt(0)
	s_load_dwordx2 s[8:9], s[0:1], 0x68
	s_waitcnt lgkmcnt(0)
	s_and_saveexec_b64 s[4:5], vcc
	s_cbranch_execz .LBB0_340
	v_and_b32_e32 v56, 0x3f8, v78
	v_mov_b32_e32 v73, 0
	v_lshlrev_b32_e32 v72, 2, v56
	v_lshl_add_u64 v[24:25], s[2:3], 0, v[72:73]
	v_add_co_u32_e32 v18, vcc, 0x3000, v24
	s_mov_b32 s22, 0x8000
	s_nop 0
	v_addc_co_u32_e32 v19, vcc, 0, v25, vcc
	v_add_co_u32_e32 v28, vcc, 0x2000, v24
	v_mov_b32_e32 v82, 0xff
	s_nop 0
	v_addc_co_u32_e32 v29, vcc, 0, v25, vcc
	v_add_co_u32_e32 v60, vcc, 0x1000, v24
	v_mov_b32_e32 v83, 0xfff
	s_nop 0
	v_addc_co_u32_e32 v61, vcc, 0, v25, vcc
	v_cmp_gt_i32_e32 vcc, s22, v74
	v_mov_b32_e32 v79, 0x100
	v_mov_b32_e32 v81, 0x1000
	v_cndmask_b32_e32 v32, v82, v83, vcc
	v_and_b32_e32 v37, v32, v74
	s_add_u32 s6, s16, 0x17900000
	global_load_dwordx4 v[0:3], v72, s[8:9]
	global_load_dwordx4 v[4:7], v72, s[8:9] offset:16
	s_mov_b64 s[8:9], 0x3000
	v_cndmask_b32_e32 v36, v79, v81, vcc
	v_add_u32_e32 v32, -2, v37
	s_addc_u32 s7, s17, 0
	v_lshl_add_u64 v[16:17], v[24:25], 0, s[8:9]
	s_mov_b64 s[8:9], 0x2000
	v_add_u32_e32 v33, -2, v74
	v_cmp_lt_u32_e32 vcc, v32, v36
	v_lshl_add_u64 v[26:27], v[24:25], 0, s[8:9]
	s_mov_b64 s[8:9], 0x1000
	v_cndmask_b32_e32 v34, v74, v33, vcc
	s_movk_i32 s23, 0x5a00
	v_mov_b64_e32 v[32:33], s[6:7]
	global_load_dwordx4 v[8:11], v[18:19], off
	global_load_dwordx4 v[12:15], v[16:17], off offset:16
	s_nop 0
	global_load_dwordx4 v[16:19], v[28:29], off
	global_load_dwordx4 v[20:23], v[26:27], off offset:16
	v_lshl_add_u64 v[58:59], v[24:25], 0, s[8:9]
	global_load_dwordx4 v[24:27], v72, s[2:3]
	global_load_dwordx4 v[28:31], v72, s[2:3] offset:16
	v_mad_i64_i32 v[34:35], s[2:3], v34, s23, v[32:33]
	v_lshlrev_b32_e32 v72, 1, v56
	s_movk_i32 s20, 0x1000
	v_lshl_add_u64 v[34:35], v[34:35], 0, v[72:73]
	v_add_co_u32_e32 v62, vcc, s20, v34
	v_add_u32_e32 v34, -1, v37
	s_nop 0
	v_addc_co_u32_e32 v63, vcc, 0, v35, vcc
	v_cmp_lt_u32_e32 vcc, v34, v36
	v_ashrrev_i32_e32 v75, 31, v74
	v_and_b32_e32 v57, 0x7f, v80
	v_subbrev_co_u32_e32 v34, vcc, 0, v74, vcc
	v_mad_i64_i32 v[34:35], s[2:3], v34, s23, v[32:33]
	v_lshl_add_u64 v[34:35], v[34:35], 0, v[72:73]
	v_add_co_u32_e32 v64, vcc, s20, v34
	s_waitcnt lgkmcnt(0)
	s_lshl_b32 s8, s21, 2
	v_addc_co_u32_e32 v65, vcc, 0, v35, vcc
	v_mad_i64_i32 v[34:35], s[2:3], v74, s23, v[32:33]
	v_lshl_add_u64 v[34:35], v[34:35], 0, v[72:73]
	v_add_co_u32_e32 v66, vcc, s20, v34
	v_add_u32_e32 v34, 1, v37
	s_nop 0
	v_addc_co_u32_e32 v67, vcc, 0, v35, vcc
	v_cmp_lt_u32_e32 vcc, v34, v36
	s_ashr_i32 s9, s8, 31
	s_lshl_b64 s[10:11], s[8:9], 11
	v_addc_co_u32_e32 v34, vcc, 0, v74, vcc
	v_mad_i64_i32 v[32:33], s[2:3], v34, s23, v[32:33]
	v_lshl_add_u64 v[32:33], v[32:33], 0, v[72:73]
	v_add_co_u32_e32 v68, vcc, s20, v32
	s_mov_b64 s[2:3], 0x6a600000
	s_nop 0
	v_addc_co_u32_e32 v69, vcc, 0, v33, vcc
	global_load_dwordx4 v[44:47], v[66:67], off offset:2048
	global_load_dwordx4 v[40:43], v[68:69], off offset:2048
	global_load_dwordx4 v[52:55], v[62:63], off offset:2048
	global_load_dwordx4 v[48:51], v[64:65], off offset:2048
	global_load_dwordx4 v[32:35], v[60:61], off
	global_load_dwordx4 v[36:39], v[58:59], off offset:16
	v_lshlrev_b64 v[58:59], 11, v[74:75]
	v_lshl_or_b32 v58, v57, 4, v58
	v_lshl_add_u64 v[58:59], s[16:17], 0, v[58:59]
	v_lshl_add_u64 v[76:77], v[58:59], 0, s[2:3]
	v_lshlrev_b32_e32 v72, 1, v56
	s_mov_b64 s[12:13], 0
	s_mov_b32 s9, 0x87ff
	s_waitcnt vmcnt(0)
	v_mov_b64_e32 v[66:67], v[46:47]
	v_mov_b64_e32 v[70:71], v[42:43]
	v_mov_b64_e32 v[58:59], v[54:55]
	v_mov_b64_e32 v[62:63], v[50:51]
	v_mov_b64_e32 v[68:69], v[40:41]
	v_mov_b64_e32 v[64:65], v[44:45]
	v_mov_b64_e32 v[60:61], v[48:49]
	v_mov_b64_e32 v[56:57], v[52:53]
	s_cmp_eq_u32 s21, 0x100
	s_cbranch_scc1 .Lconv_fast_L0
	s_branch .LBB0_338
.Lconv_fast_L0:
	v_mbcnt_lo_u32_b32 v126, -1, 0
	v_mbcnt_hi_u32_b32 v126, -1, v126
	s_and_b32 s40, s96, 1
	s_lshl_b32 s40, s40, 6
	v_or_b32_e32 v126, s40, v126
	v_lshlrev_b32_e32 v127, 5, v126
	v_lshlrev_b32_e32 v126, 4, v126
	v_readlane_b32 s41, v254, 0
	s_lshr_b32 s42, s96, 1
	s_lshl_b32 s41, s41, 2
	s_add_i32 s41, s41, s42
	s_load_dwordx2 s[44:45], s[0:1], 0x60
	s_load_dwordx2 s[46:47], s[0:1], 0x68
	s_waitcnt lgkmcnt(0)
	s_add_u32 s48, s44, 0x0
	s_addc_u32 s49, s45, 0
	global_load_dwordx4 v[128:131], v127, s[48:49]
	global_load_dwordx4 v[132:135], v127, s[48:49] offset:16
	s_add_u32 s48, s44, 0x1000
	s_addc_u32 s49, s45, 0
	global_load_dwordx4 v[136:139], v127, s[48:49]
	global_load_dwordx4 v[140:143], v127, s[48:49] offset:16
	s_add_u32 s48, s44, 0x2000
	s_addc_u32 s49, s45, 0
	global_load_dwordx4 v[144:147], v127, s[48:49]
	global_load_dwordx4 v[148:151], v127, s[48:49] offset:16
	s_add_u32 s48, s44, 0x3000
	s_addc_u32 s49, s45, 0
	global_load_dwordx4 v[152:155], v127, s[48:49]
	global_load_dwordx4 v[156:159], v127, s[48:49] offset:16
	s_add_u32 s48, s46, 0x0
	s_addc_u32 s49, s47, 0
	global_load_dwordx4 v[160:163], v127, s[48:49]
	global_load_dwordx4 v[164:167], v127, s[48:49] offset:16
	s_add_u32 s50, s86, 0x17901800
	s_addc_u32 s51, s87, 0
	s_add_u32 s52, s86, 0x6a600000
	s_addc_u32 s53, s87, 0
	s_movk_i32 s70, 0xfff
	s_movk_i32 s71, 0xff
	s_waitcnt vmcnt(0)
	s_add_i32 s54, s41, 0x0
	s_cmp_lt_u32 s54, 0x8000
	s_cselect_b32 s55, s70, s71
	s_and_b32 s56, s54, s55
	s_add_i32 s57, s55, 1
	s_add_i32 s58, s56, -2
	s_cmp_lt_u32 s58, s57
	s_cselect_b32 s58, -2, 0
	s_add_i32 s58, s54, s58
	s_mul_i32 s58, s58, 0x5a00
	s_add_u32 s60, s50, s58
	s_addc_u32 s61, s51, 0
	global_load_dwordx4 v[168:171], v126, s[60:61]
	s_add_i32 s58, s56, -1
	s_cmp_lt_u32 s58, s57
	s_cselect_b32 s58, -1, 0
	s_add_i32 s58, s54, s58
	s_mul_i32 s58, s58, 0x5a00
	s_add_u32 s60, s50, s58
	s_addc_u32 s61, s51, 0
	global_load_dwordx4 v[172:175], v126, s[60:61]
	s_mul_i32 s58, s54, 0x5a00
	s_add_u32 s60, s50, s58
	s_addc_u32 s61, s51, 0
	global_load_dwordx4 v[176:179], v126, s[60:61]
	s_add_i32 s58, s56, 1
	s_cmp_lt_u32 s58, s57
	s_cselect_b32 s58, 1, 0
	s_add_i32 s58, s54, s58
	s_mul_i32 s58, s58, 0x5a00
	s_add_u32 s60, s50, s58
	s_addc_u32 s61, s51, 0
	global_load_dwordx4 v[180:183], v126, s[60:61]
	s_add_i32 s54, s41, 0x400
	s_cmp_lt_u32 s54, 0x8000
	s_cselect_b32 s55, s70, s71
	s_and_b32 s56, s54, s55
	s_add_i32 s57, s55, 1
	s_add_i32 s58, s56, -2
	s_cmp_lt_u32 s58, s57
	s_cselect_b32 s58, -2, 0
	s_add_i32 s58, s54, s58
	s_mul_i32 s58, s58, 0x5a00
	s_add_u32 s60, s50, s58
	s_addc_u32 s61, s51, 0
	global_load_dwordx4 v[184:187], v126, s[60:61]
	s_add_i32 s58, s56, -1
	s_cmp_lt_u32 s58, s57
	s_cselect_b32 s58, -1, 0
	s_add_i32 s58, s54, s58
	s_mul_i32 s58, s58, 0x5a00
	s_add_u32 s60, s50, s58
	s_addc_u32 s61, s51, 0
	global_load_dwordx4 v[188:191], v126, s[60:61]
	s_mul_i32 s58, s54, 0x5a00
	s_add_u32 s60, s50, s58
	s_addc_u32 s61, s51, 0
	global_load_dwordx4 v[192:195], v126, s[60:61]
	s_add_i32 s58, s56, 1
	s_cmp_lt_u32 s58, s57
	s_cselect_b32 s58, 1, 0
	s_add_i32 s58, s54, s58
	s_mul_i32 s58, s58, 0x5a00
	s_add_u32 s60, s50, s58
	s_addc_u32 s61, s51, 0
	global_load_dwordx4 v[196:199], v126, s[60:61]
	s_add_i32 s54, s41, 0x800
	s_cmp_lt_u32 s54, 0x8000
	s_cselect_b32 s55, s70, s71
	s_and_b32 s56, s54, s55
	s_add_i32 s57, s55, 1
	s_add_i32 s58, s56, -2
	s_cmp_lt_u32 s58, s57
	s_cselect_b32 s58, -2, 0
	s_add_i32 s58, s54, s58
	s_mul_i32 s58, s58, 0x5a00
	s_add_u32 s60, s50, s58
	s_addc_u32 s61, s51, 0
	global_load_dwordx4 v[200:203], v126, s[60:61]
	s_add_i32 s58, s56, -1
	s_cmp_lt_u32 s58, s57
	s_cselect_b32 s58, -1, 0
	s_add_i32 s58, s54, s58
	s_mul_i32 s58, s58, 0x5a00
	s_add_u32 s60, s50, s58
	s_addc_u32 s61, s51, 0
	global_load_dwordx4 v[204:207], v126, s[60:61]
	s_mul_i32 s58, s54, 0x5a00
	s_add_u32 s60, s50, s58
	s_addc_u32 s61, s51, 0
	global_load_dwordx4 v[208:211], v126, s[60:61]
	s_add_i32 s58, s56, 1
	s_cmp_lt_u32 s58, s57
	s_cselect_b32 s58, 1, 0
	s_add_i32 s58, s54, s58
	s_mul_i32 s58, s58, 0x5a00
	s_add_u32 s60, s50, s58
	s_addc_u32 s61, s51, 0
	global_load_dwordx4 v[212:215], v126, s[60:61]
	s_add_i32 s54, s41, 0xc00
	s_cmp_lt_u32 s54, 0x8000
	s_cselect_b32 s55, s70, s71
	s_and_b32 s56, s54, s55
	s_add_i32 s57, s55, 1
	s_add_i32 s58, s56, -2
	s_cmp_lt_u32 s58, s57
	s_cselect_b32 s58, -2, 0
	s_add_i32 s58, s54, s58
	s_mul_i32 s58, s58, 0x5a00
	s_add_u32 s60, s50, s58
	s_addc_u32 s61, s51, 0
	global_load_dwordx4 v[216:219], v126, s[60:61]
	s_add_i32 s58, s56, -1
	s_cmp_lt_u32 s58, s57
	s_cselect_b32 s58, -1, 0
	s_add_i32 s58, s54, s58
	s_mul_i32 s58, s58, 0x5a00
	s_add_u32 s60, s50, s58
	s_addc_u32 s61, s51, 0
	global_load_dwordx4 v[220:223], v126, s[60:61]
	s_mul_i32 s58, s54, 0x5a00
	s_add_u32 s60, s50, s58
	s_addc_u32 s61, s51, 0
	global_load_dwordx4 v[224:227], v126, s[60:61]
	s_add_i32 s58, s56, 1
	s_cmp_lt_u32 s58, s57
	s_cselect_b32 s58, 1, 0
	s_add_i32 s58, s54, s58
	s_mul_i32 s58, s58, 0x5a00
	s_add_u32 s60, s50, s58
	s_addc_u32 s61, s51, 0
	global_load_dwordx4 v[228:231], v126, s[60:61]
	s_add_i32 s54, s41, 0x1000
	s_cmp_lt_u32 s54, 0x8000
	s_cselect_b32 s55, s70, s71
	s_and_b32 s56, s54, s55
	s_add_i32 s57, s55, 1
	s_add_i32 s58, s56, -2
	s_cmp_lt_u32 s58, s57
	s_cselect_b32 s58, -2, 0
	s_add_i32 s58, s54, s58
	s_mul_i32 s58, s58, 0x5a00
	s_add_u32 s60, s50, s58
	s_addc_u32 s61, s51, 0
	global_load_dwordx4 v[40:43], v126, s[60:61]
	s_add_i32 s58, s56, -1
	s_cmp_lt_u32 s58, s57
	s_cselect_b32 s58, -1, 0
	s_add_i32 s58, s54, s58
	s_mul_i32 s58, s58, 0x5a00
	s_add_u32 s60, s50, s58
	s_addc_u32 s61, s51, 0
	global_load_dwordx4 v[44:47], v126, s[60:61]
	s_mul_i32 s58, s54, 0x5a00
	s_add_u32 s60, s50, s58
	s_addc_u32 s61, s51, 0
	global_load_dwordx4 v[48:51], v126, s[60:61]
	s_add_i32 s58, s56, 1
	s_cmp_lt_u32 s58, s57
	s_cselect_b32 s58, 1, 0
	s_add_i32 s58, s54, s58
	s_mul_i32 s58, s58, 0x5a00
	s_add_u32 s60, s50, s58
	s_addc_u32 s61, s51, 0
	global_load_dwordx4 v[52:55], v126, s[60:61]
	s_add_i32 s54, s41, 0x1400
	s_cmp_lt_u32 s54, 0x8000
	s_cselect_b32 s55, s70, s71
	s_and_b32 s56, s54, s55
	s_add_i32 s57, s55, 1
	s_add_i32 s58, s56, -2
	s_cmp_lt_u32 s58, s57
	s_cselect_b32 s58, -2, 0
	s_add_i32 s58, s54, s58
	s_mul_i32 s58, s58, 0x5a00
	s_add_u32 s60, s50, s58
	s_addc_u32 s61, s51, 0
	global_load_dwordx4 v[56:59], v126, s[60:61]
	s_add_i32 s58, s56, -1
	s_cmp_lt_u32 s58, s57
	s_cselect_b32 s58, -1, 0
	s_add_i32 s58, s54, s58
	s_mul_i32 s58, s58, 0x5a00
	s_add_u32 s60, s50, s58
	s_addc_u32 s61, s51, 0
	global_load_dwordx4 v[60:63], v126, s[60:61]
	s_mul_i32 s58, s54, 0x5a00
	s_add_u32 s60, s50, s58
	s_addc_u32 s61, s51, 0
	global_load_dwordx4 v[64:67], v126, s[60:61]
	s_add_i32 s58, s56, 1
	s_cmp_lt_u32 s58, s57
	s_cselect_b32 s58, 1, 0
	s_add_i32 s58, s54, s58
	s_mul_i32 s58, s58, 0x5a00
	s_add_u32 s60, s50, s58
	s_addc_u32 s61, s51, 0
	global_load_dwordx4 v[68:71], v126, s[60:61]
	s_waitcnt vmcnt(16)
	s_add_i32 s54, s41, 0x0
	s_cmp_lt_u32 s54, 0x8000
	s_cselect_b32 s55, s70, s71
	s_and_b32 s56, s54, s55
	s_add_i32 s57, s55, 1
	s_add_i32 s58, s56, -2
	s_cmp_lt_u32 s58, s57
	s_cselect_b32 s62, 1.0, 0
	s_add_i32 s58, s56, -1
	s_cmp_lt_u32 s58, s57
	s_cselect_b32 s64, 1.0, 0
	s_mov_b32 s66, 1.0
	s_add_i32 s58, s56, 1
	s_cmp_lt_u32 s58, s57
	s_cselect_b32 s68, 1.0, 0
	v_pk_mul_f32 v[240:241], v[128:129], s[62:63] op_sel_hi:[1,0]
	v_lshlrev_b32_e32 v242, 16, v168
	v_and_b32_e32 v243, 0xffff0000, v168
	v_pk_fma_f32 v[232:233], v[240:241], v[242:243], v[160:161]
	v_pk_mul_f32 v[240:241], v[130:131], s[62:63] op_sel_hi:[1,0]
	v_lshlrev_b32_e32 v242, 16, v169
	v_and_b32_e32 v243, 0xffff0000, v169
	v_pk_fma_f32 v[234:235], v[240:241], v[242:243], v[162:163]
	v_pk_mul_f32 v[240:241], v[132:133], s[62:63] op_sel_hi:[1,0]
	v_lshlrev_b32_e32 v242, 16, v170
	v_and_b32_e32 v243, 0xffff0000, v170
	v_pk_fma_f32 v[236:237], v[240:241], v[242:243], v[164:165]
	v_pk_mul_f32 v[240:241], v[134:135], s[62:63] op_sel_hi:[1,0]
	v_lshlrev_b32_e32 v242, 16, v171
	v_and_b32_e32 v243, 0xffff0000, v171
	v_pk_fma_f32 v[238:239], v[240:241], v[242:243], v[166:167]
	v_pk_mul_f32 v[240:241], v[136:137], s[64:65] op_sel_hi:[1,0]
	v_lshlrev_b32_e32 v242, 16, v172
	v_and_b32_e32 v243, 0xffff0000, v172
	v_pk_fma_f32 v[232:233], v[240:241], v[242:243], v[232:233]
	v_pk_mul_f32 v[240:241], v[138:139], s[64:65] op_sel_hi:[1,0]
	v_lshlrev_b32_e32 v242, 16, v173
	v_and_b32_e32 v243, 0xffff0000, v173
	v_pk_fma_f32 v[234:235], v[240:241], v[242:243], v[234:235]
	v_pk_mul_f32 v[240:241], v[140:141], s[64:65] op_sel_hi:[1,0]
	v_lshlrev_b32_e32 v242, 16, v174
	v_and_b32_e32 v243, 0xffff0000, v174
	v_pk_fma_f32 v[236:237], v[240:241], v[242:243], v[236:237]
	v_pk_mul_f32 v[240:241], v[142:143], s[64:65] op_sel_hi:[1,0]
	v_lshlrev_b32_e32 v242, 16, v175
	v_and_b32_e32 v243, 0xffff0000, v175
	v_pk_fma_f32 v[238:239], v[240:241], v[242:243], v[238:239]
	v_pk_mul_f32 v[240:241], v[144:145], s[66:67] op_sel_hi:[1,0]
	v_lshlrev_b32_e32 v242, 16, v176
	v_and_b32_e32 v243, 0xffff0000, v176
	v_pk_fma_f32 v[232:233], v[240:241], v[242:243], v[232:233]
	v_pk_mul_f32 v[240:241], v[146:147], s[66:67] op_sel_hi:[1,0]
	v_lshlrev_b32_e32 v242, 16, v177
	v_and_b32_e32 v243, 0xffff0000, v177
	v_pk_fma_f32 v[234:235], v[240:241], v[242:243], v[234:235]
	v_pk_mul_f32 v[240:241], v[148:149], s[66:67] op_sel_hi:[1,0]
	v_lshlrev_b32_e32 v242, 16, v178
	v_and_b32_e32 v243, 0xffff0000, v178
	v_pk_fma_f32 v[236:237], v[240:241], v[242:243], v[236:237]
	v_pk_mul_f32 v[240:241], v[150:151], s[66:67] op_sel_hi:[1,0]
	v_lshlrev_b32_e32 v242, 16, v179
	v_and_b32_e32 v243, 0xffff0000, v179
	v_pk_fma_f32 v[238:239], v[240:241], v[242:243], v[238:239]
	v_pk_mul_f32 v[240:241], v[152:153], s[68:69] op_sel_hi:[1,0]
	v_lshlrev_b32_e32 v242, 16, v180
	v_and_b32_e32 v243, 0xffff0000, v180
	v_pk_fma_f32 v[232:233], v[240:241], v[242:243], v[232:233]
	v_pk_mul_f32 v[240:241], v[154:155], s[68:69] op_sel_hi:[1,0]
	v_lshlrev_b32_e32 v242, 16, v181
	v_and_b32_e32 v243, 0xffff0000, v181
	v_pk_fma_f32 v[234:235], v[240:241], v[242:243], v[234:235]
	v_pk_mul_f32 v[240:241], v[156:157], s[68:69] op_sel_hi:[1,0]
	v_lshlrev_b32_e32 v242, 16, v182
	v_and_b32_e32 v243, 0xffff0000, v182
	v_pk_fma_f32 v[236:237], v[240:241], v[242:243], v[236:237]
	v_pk_mul_f32 v[240:241], v[158:159], s[68:69] op_sel_hi:[1,0]
	v_lshlrev_b32_e32 v242, 16, v183
	v_and_b32_e32 v243, 0xffff0000, v183
	v_pk_fma_f32 v[238:239], v[240:241], v[242:243], v[238:239]
	v_cvt_pk_bf16_f32 v248, v232, v233
	v_cvt_pk_bf16_f32 v249, v234, v235
	v_cvt_pk_bf16_f32 v250, v236, v237
	v_cvt_pk_bf16_f32 v251, v238, v239
	s_lshl_b32 s58, s54, 11
	s_add_u32 s60, s52, s58
	s_addc_u32 s61, s53, 0
	global_store_dwordx4 v126, v[248:251], s[60:61]
	s_add_i32 s54, s41, 0x400
	s_cmp_lt_u32 s54, 0x8000
	s_cselect_b32 s55, s70, s71
	s_and_b32 s56, s54, s55
	s_add_i32 s57, s55, 1
	s_add_i32 s58, s56, -2
	s_cmp_lt_u32 s58, s57
	s_cselect_b32 s62, 1.0, 0
	s_add_i32 s58, s56, -1
	s_cmp_lt_u32 s58, s57
	s_cselect_b32 s64, 1.0, 0
	s_mov_b32 s66, 1.0
	s_add_i32 s58, s56, 1
	s_cmp_lt_u32 s58, s57
	s_cselect_b32 s68, 1.0, 0
	v_pk_mul_f32 v[240:241], v[128:129], s[62:63] op_sel_hi:[1,0]
	v_lshlrev_b32_e32 v242, 16, v184
	v_and_b32_e32 v243, 0xffff0000, v184
	v_pk_fma_f32 v[232:233], v[240:241], v[242:243], v[160:161]
	v_pk_mul_f32 v[240:241], v[130:131], s[62:63] op_sel_hi:[1,0]
	v_lshlrev_b32_e32 v242, 16, v185
	v_and_b32_e32 v243, 0xffff0000, v185
	v_pk_fma_f32 v[234:235], v[240:241], v[242:243], v[162:163]
	v_pk_mul_f32 v[240:241], v[132:133], s[62:63] op_sel_hi:[1,0]
	v_lshlrev_b32_e32 v242, 16, v186
	v_and_b32_e32 v243, 0xffff0000, v186
	v_pk_fma_f32 v[236:237], v[240:241], v[242:243], v[164:165]
	v_pk_mul_f32 v[240:241], v[134:135], s[62:63] op_sel_hi:[1,0]
	v_lshlrev_b32_e32 v242, 16, v187
	v_and_b32_e32 v243, 0xffff0000, v187
	v_pk_fma_f32 v[238:239], v[240:241], v[242:243], v[166:167]
	v_pk_mul_f32 v[240:241], v[136:137], s[64:65] op_sel_hi:[1,0]
	v_lshlrev_b32_e32 v242, 16, v188
	v_and_b32_e32 v243, 0xffff0000, v188
	v_pk_fma_f32 v[232:233], v[240:241], v[242:243], v[232:233]
	v_pk_mul_f32 v[240:241], v[138:139], s[64:65] op_sel_hi:[1,0]
	v_lshlrev_b32_e32 v242, 16, v189
	v_and_b32_e32 v243, 0xffff0000, v189
	v_pk_fma_f32 v[234:235], v[240:241], v[242:243], v[234:235]
	v_pk_mul_f32 v[240:241], v[140:141], s[64:65] op_sel_hi:[1,0]
	v_lshlrev_b32_e32 v242, 16, v190
	v_and_b32_e32 v243, 0xffff0000, v190
	v_pk_fma_f32 v[236:237], v[240:241], v[242:243], v[236:237]
	v_pk_mul_f32 v[240:241], v[142:143], s[64:65] op_sel_hi:[1,0]
	v_lshlrev_b32_e32 v242, 16, v191
	v_and_b32_e32 v243, 0xffff0000, v191
	v_pk_fma_f32 v[238:239], v[240:241], v[242:243], v[238:239]
	v_pk_mul_f32 v[240:241], v[144:145], s[66:67] op_sel_hi:[1,0]
	v_lshlrev_b32_e32 v242, 16, v192
	v_and_b32_e32 v243, 0xffff0000, v192
	v_pk_fma_f32 v[232:233], v[240:241], v[242:243], v[232:233]
	v_pk_mul_f32 v[240:241], v[146:147], s[66:67] op_sel_hi:[1,0]
	v_lshlrev_b32_e32 v242, 16, v193
	v_and_b32_e32 v243, 0xffff0000, v193
	v_pk_fma_f32 v[234:235], v[240:241], v[242:243], v[234:235]
	v_pk_mul_f32 v[240:241], v[148:149], s[66:67] op_sel_hi:[1,0]
	v_lshlrev_b32_e32 v242, 16, v194
	v_and_b32_e32 v243, 0xffff0000, v194
	v_pk_fma_f32 v[236:237], v[240:241], v[242:243], v[236:237]
	v_pk_mul_f32 v[240:241], v[150:151], s[66:67] op_sel_hi:[1,0]
	v_lshlrev_b32_e32 v242, 16, v195
	v_and_b32_e32 v243, 0xffff0000, v195
	v_pk_fma_f32 v[238:239], v[240:241], v[242:243], v[238:239]
	v_pk_mul_f32 v[240:241], v[152:153], s[68:69] op_sel_hi:[1,0]
	v_lshlrev_b32_e32 v242, 16, v196
	v_and_b32_e32 v243, 0xffff0000, v196
	v_pk_fma_f32 v[232:233], v[240:241], v[242:243], v[232:233]
	v_pk_mul_f32 v[240:241], v[154:155], s[68:69] op_sel_hi:[1,0]
	v_lshlrev_b32_e32 v242, 16, v197
	v_and_b32_e32 v243, 0xffff0000, v197
	v_pk_fma_f32 v[234:235], v[240:241], v[242:243], v[234:235]
	v_pk_mul_f32 v[240:241], v[156:157], s[68:69] op_sel_hi:[1,0]
	v_lshlrev_b32_e32 v242, 16, v198
	v_and_b32_e32 v243, 0xffff0000, v198
	v_pk_fma_f32 v[236:237], v[240:241], v[242:243], v[236:237]
	v_pk_mul_f32 v[240:241], v[158:159], s[68:69] op_sel_hi:[1,0]
	v_lshlrev_b32_e32 v242, 16, v199
	v_and_b32_e32 v243, 0xffff0000, v199
	v_pk_fma_f32 v[238:239], v[240:241], v[242:243], v[238:239]
	v_cvt_pk_bf16_f32 v248, v232, v233
	v_cvt_pk_bf16_f32 v249, v234, v235
	v_cvt_pk_bf16_f32 v250, v236, v237
	v_cvt_pk_bf16_f32 v251, v238, v239
	s_lshl_b32 s58, s54, 11
	s_add_u32 s60, s52, s58
	s_addc_u32 s61, s53, 0
	global_store_dwordx4 v126, v[248:251], s[60:61]
	s_add_i32 s54, s41, 0x1800
	s_cmp_lt_u32 s54, 0x8000
	s_cselect_b32 s55, s70, s71
	s_and_b32 s56, s54, s55
	s_add_i32 s57, s55, 1
	s_add_i32 s58, s56, -2
	s_cmp_lt_u32 s58, s57
	s_cselect_b32 s58, -2, 0
	s_add_i32 s58, s54, s58
	s_mul_i32 s58, s58, 0x5a00
	s_add_u32 s60, s50, s58
	s_addc_u32 s61, s51, 0
	global_load_dwordx4 v[168:171], v126, s[60:61]
	s_add_i32 s58, s56, -1
	s_cmp_lt_u32 s58, s57
	s_cselect_b32 s58, -1, 0
	s_add_i32 s58, s54, s58
	s_mul_i32 s58, s58, 0x5a00
	s_add_u32 s60, s50, s58
	s_addc_u32 s61, s51, 0
	global_load_dwordx4 v[172:175], v126, s[60:61]
	s_mul_i32 s58, s54, 0x5a00
	s_add_u32 s60, s50, s58
	s_addc_u32 s61, s51, 0
	global_load_dwordx4 v[176:179], v126, s[60:61]
	s_add_i32 s58, s56, 1
	s_cmp_lt_u32 s58, s57
	s_cselect_b32 s58, 1, 0
	s_add_i32 s58, s54, s58
	s_mul_i32 s58, s58, 0x5a00
	s_add_u32 s60, s50, s58
	s_addc_u32 s61, s51, 0
	global_load_dwordx4 v[180:183], v126, s[60:61]
	s_add_i32 s54, s41, 0x1c00
	s_cmp_lt_u32 s54, 0x8000
	s_cselect_b32 s55, s70, s71
	s_and_b32 s56, s54, s55
	s_add_i32 s57, s55, 1
	s_add_i32 s58, s56, -2
	s_cmp_lt_u32 s58, s57
	s_cselect_b32 s58, -2, 0
	s_add_i32 s58, s54, s58
	s_mul_i32 s58, s58, 0x5a00
	s_add_u32 s60, s50, s58
	s_addc_u32 s61, s51, 0
	global_load_dwordx4 v[184:187], v126, s[60:61]
	s_add_i32 s58, s56, -1
	s_cmp_lt_u32 s58, s57
	s_cselect_b32 s58, -1, 0
	s_add_i32 s58, s54, s58
	s_mul_i32 s58, s58, 0x5a00
	s_add_u32 s60, s50, s58
	s_addc_u32 s61, s51, 0
	global_load_dwordx4 v[188:191], v126, s[60:61]
	s_mul_i32 s58, s54, 0x5a00
	s_add_u32 s60, s50, s58
	s_addc_u32 s61, s51, 0
	global_load_dwordx4 v[192:195], v126, s[60:61]
	s_add_i32 s58, s56, 1
	s_cmp_lt_u32 s58, s57
	s_cselect_b32 s58, 1, 0
	s_add_i32 s58, s54, s58
	s_mul_i32 s58, s58, 0x5a00
	s_add_u32 s60, s50, s58
	s_addc_u32 s61, s51, 0
	global_load_dwordx4 v[196:199], v126, s[60:61]
	s_waitcnt vmcnt(18)
	s_add_i32 s54, s41, 0x800
	s_cmp_lt_u32 s54, 0x8000
	s_cselect_b32 s55, s70, s71
	s_and_b32 s56, s54, s55
	s_add_i32 s57, s55, 1
	s_add_i32 s58, s56, -2
	s_cmp_lt_u32 s58, s57
	s_cselect_b32 s62, 1.0, 0
	s_add_i32 s58, s56, -1
	s_cmp_lt_u32 s58, s57
	s_cselect_b32 s64, 1.0, 0
	s_mov_b32 s66, 1.0
	s_add_i32 s58, s56, 1
	s_cmp_lt_u32 s58, s57
	s_cselect_b32 s68, 1.0, 0
	v_pk_mul_f32 v[240:241], v[128:129], s[62:63] op_sel_hi:[1,0]
	v_lshlrev_b32_e32 v242, 16, v200
	v_and_b32_e32 v243, 0xffff0000, v200
	v_pk_fma_f32 v[232:233], v[240:241], v[242:243], v[160:161]
	v_pk_mul_f32 v[240:241], v[130:131], s[62:63] op_sel_hi:[1,0]
	v_lshlrev_b32_e32 v242, 16, v201
	v_and_b32_e32 v243, 0xffff0000, v201
	v_pk_fma_f32 v[234:235], v[240:241], v[242:243], v[162:163]
	v_pk_mul_f32 v[240:241], v[132:133], s[62:63] op_sel_hi:[1,0]
	v_lshlrev_b32_e32 v242, 16, v202
	v_and_b32_e32 v243, 0xffff0000, v202
	v_pk_fma_f32 v[236:237], v[240:241], v[242:243], v[164:165]
	v_pk_mul_f32 v[240:241], v[134:135], s[62:63] op_sel_hi:[1,0]
	v_lshlrev_b32_e32 v242, 16, v203
	v_and_b32_e32 v243, 0xffff0000, v203
	v_pk_fma_f32 v[238:239], v[240:241], v[242:243], v[166:167]
	v_pk_mul_f32 v[240:241], v[136:137], s[64:65] op_sel_hi:[1,0]
	v_lshlrev_b32_e32 v242, 16, v204
	v_and_b32_e32 v243, 0xffff0000, v204
	v_pk_fma_f32 v[232:233], v[240:241], v[242:243], v[232:233]
	v_pk_mul_f32 v[240:241], v[138:139], s[64:65] op_sel_hi:[1,0]
	v_lshlrev_b32_e32 v242, 16, v205
	v_and_b32_e32 v243, 0xffff0000, v205
	v_pk_fma_f32 v[234:235], v[240:241], v[242:243], v[234:235]
	v_pk_mul_f32 v[240:241], v[140:141], s[64:65] op_sel_hi:[1,0]
	v_lshlrev_b32_e32 v242, 16, v206
	v_and_b32_e32 v243, 0xffff0000, v206
	v_pk_fma_f32 v[236:237], v[240:241], v[242:243], v[236:237]
	v_pk_mul_f32 v[240:241], v[142:143], s[64:65] op_sel_hi:[1,0]
	v_lshlrev_b32_e32 v242, 16, v207
	v_and_b32_e32 v243, 0xffff0000, v207
	v_pk_fma_f32 v[238:239], v[240:241], v[242:243], v[238:239]
	v_pk_mul_f32 v[240:241], v[144:145], s[66:67] op_sel_hi:[1,0]
	v_lshlrev_b32_e32 v242, 16, v208
	v_and_b32_e32 v243, 0xffff0000, v208
	v_pk_fma_f32 v[232:233], v[240:241], v[242:243], v[232:233]
	v_pk_mul_f32 v[240:241], v[146:147], s[66:67] op_sel_hi:[1,0]
	v_lshlrev_b32_e32 v242, 16, v209
	v_and_b32_e32 v243, 0xffff0000, v209
	v_pk_fma_f32 v[234:235], v[240:241], v[242:243], v[234:235]
	v_pk_mul_f32 v[240:241], v[148:149], s[66:67] op_sel_hi:[1,0]
	v_lshlrev_b32_e32 v242, 16, v210
	v_and_b32_e32 v243, 0xffff0000, v210
	v_pk_fma_f32 v[236:237], v[240:241], v[242:243], v[236:237]
	v_pk_mul_f32 v[240:241], v[150:151], s[66:67] op_sel_hi:[1,0]
	v_lshlrev_b32_e32 v242, 16, v211
	v_and_b32_e32 v243, 0xffff0000, v211
	v_pk_fma_f32 v[238:239], v[240:241], v[242:243], v[238:239]
	v_pk_mul_f32 v[240:241], v[152:153], s[68:69] op_sel_hi:[1,0]
	v_lshlrev_b32_e32 v242, 16, v212
	v_and_b32_e32 v243, 0xffff0000, v212
	v_pk_fma_f32 v[232:233], v[240:241], v[242:243], v[232:233]
	v_pk_mul_f32 v[240:241], v[154:155], s[68:69] op_sel_hi:[1,0]
	v_lshlrev_b32_e32 v242, 16, v213
	v_and_b32_e32 v243, 0xffff0000, v213
	v_pk_fma_f32 v[234:235], v[240:241], v[242:243], v[234:235]
	v_pk_mul_f32 v[240:241], v[156:157], s[68:69] op_sel_hi:[1,0]
	v_lshlrev_b32_e32 v242, 16, v214
	v_and_b32_e32 v243, 0xffff0000, v214
	v_pk_fma_f32 v[236:237], v[240:241], v[242:243], v[236:237]
	v_pk_mul_f32 v[240:241], v[158:159], s[68:69] op_sel_hi:[1,0]
	v_lshlrev_b32_e32 v242, 16, v215
	v_and_b32_e32 v243, 0xffff0000, v215
	v_pk_fma_f32 v[238:239], v[240:241], v[242:243], v[238:239]
	v_cvt_pk_bf16_f32 v248, v232, v233
	v_cvt_pk_bf16_f32 v249, v234, v235
	v_cvt_pk_bf16_f32 v250, v236, v237
	v_cvt_pk_bf16_f32 v251, v238, v239
	s_lshl_b32 s58, s54, 11
	s_add_u32 s60, s52, s58
	s_addc_u32 s61, s53, 0
	global_store_dwordx4 v126, v[248:251], s[60:61]
	s_add_i32 s54, s41, 0xc00
	s_cmp_lt_u32 s54, 0x8000
	s_cselect_b32 s55, s70, s71
	s_and_b32 s56, s54, s55
	s_add_i32 s57, s55, 1
	s_add_i32 s58, s56, -2
	s_cmp_lt_u32 s58, s57
	s_cselect_b32 s62, 1.0, 0
	s_add_i32 s58, s56, -1
	s_cmp_lt_u32 s58, s57
	s_cselect_b32 s64, 1.0, 0
	s_mov_b32 s66, 1.0
	s_add_i32 s58, s56, 1
	s_cmp_lt_u32 s58, s57
	s_cselect_b32 s68, 1.0, 0
	v_pk_mul_f32 v[240:241], v[128:129], s[62:63] op_sel_hi:[1,0]
	v_lshlrev_b32_e32 v242, 16, v216
	v_and_b32_e32 v243, 0xffff0000, v216
	v_pk_fma_f32 v[232:233], v[240:241], v[242:243], v[160:161]
	v_pk_mul_f32 v[240:241], v[130:131], s[62:63] op_sel_hi:[1,0]
	v_lshlrev_b32_e32 v242, 16, v217
	v_and_b32_e32 v243, 0xffff0000, v217
	v_pk_fma_f32 v[234:235], v[240:241], v[242:243], v[162:163]
	v_pk_mul_f32 v[240:241], v[132:133], s[62:63] op_sel_hi:[1,0]
	v_lshlrev_b32_e32 v242, 16, v218
	v_and_b32_e32 v243, 0xffff0000, v218
	v_pk_fma_f32 v[236:237], v[240:241], v[242:243], v[164:165]
	v_pk_mul_f32 v[240:241], v[134:135], s[62:63] op_sel_hi:[1,0]
	v_lshlrev_b32_e32 v242, 16, v219
	v_and_b32_e32 v243, 0xffff0000, v219
	v_pk_fma_f32 v[238:239], v[240:241], v[242:243], v[166:167]
	v_pk_mul_f32 v[240:241], v[136:137], s[64:65] op_sel_hi:[1,0]
	v_lshlrev_b32_e32 v242, 16, v220
	v_and_b32_e32 v243, 0xffff0000, v220
	v_pk_fma_f32 v[232:233], v[240:241], v[242:243], v[232:233]
	v_pk_mul_f32 v[240:241], v[138:139], s[64:65] op_sel_hi:[1,0]
	v_lshlrev_b32_e32 v242, 16, v221
	v_and_b32_e32 v243, 0xffff0000, v221
	v_pk_fma_f32 v[234:235], v[240:241], v[242:243], v[234:235]
	v_pk_mul_f32 v[240:241], v[140:141], s[64:65] op_sel_hi:[1,0]
	v_lshlrev_b32_e32 v242, 16, v222
	v_and_b32_e32 v243, 0xffff0000, v222
	v_pk_fma_f32 v[236:237], v[240:241], v[242:243], v[236:237]
	v_pk_mul_f32 v[240:241], v[142:143], s[64:65] op_sel_hi:[1,0]
	v_lshlrev_b32_e32 v242, 16, v223
	v_and_b32_e32 v243, 0xffff0000, v223
	v_pk_fma_f32 v[238:239], v[240:241], v[242:243], v[238:239]
	v_pk_mul_f32 v[240:241], v[144:145], s[66:67] op_sel_hi:[1,0]
	v_lshlrev_b32_e32 v242, 16, v224
	v_and_b32_e32 v243, 0xffff0000, v224
	v_pk_fma_f32 v[232:233], v[240:241], v[242:243], v[232:233]
	v_pk_mul_f32 v[240:241], v[146:147], s[66:67] op_sel_hi:[1,0]
	v_lshlrev_b32_e32 v242, 16, v225
	v_and_b32_e32 v243, 0xffff0000, v225
	v_pk_fma_f32 v[234:235], v[240:241], v[242:243], v[234:235]
	v_pk_mul_f32 v[240:241], v[148:149], s[66:67] op_sel_hi:[1,0]
	v_lshlrev_b32_e32 v242, 16, v226
	v_and_b32_e32 v243, 0xffff0000, v226
	v_pk_fma_f32 v[236:237], v[240:241], v[242:243], v[236:237]
	v_pk_mul_f32 v[240:241], v[150:151], s[66:67] op_sel_hi:[1,0]
	v_lshlrev_b32_e32 v242, 16, v227
	v_and_b32_e32 v243, 0xffff0000, v227
	v_pk_fma_f32 v[238:239], v[240:241], v[242:243], v[238:239]
	v_pk_mul_f32 v[240:241], v[152:153], s[68:69] op_sel_hi:[1,0]
	v_lshlrev_b32_e32 v242, 16, v228
	v_and_b32_e32 v243, 0xffff0000, v228
	v_pk_fma_f32 v[232:233], v[240:241], v[242:243], v[232:233]
	v_pk_mul_f32 v[240:241], v[154:155], s[68:69] op_sel_hi:[1,0]
	v_lshlrev_b32_e32 v242, 16, v229
	v_and_b32_e32 v243, 0xffff0000, v229
	v_pk_fma_f32 v[234:235], v[240:241], v[242:243], v[234:235]
	v_pk_mul_f32 v[240:241], v[156:157], s[68:69] op_sel_hi:[1,0]
	v_lshlrev_b32_e32 v242, 16, v230
	v_and_b32_e32 v243, 0xffff0000, v230
	v_pk_fma_f32 v[236:237], v[240:241], v[242:243], v[236:237]
	v_pk_mul_f32 v[240:241], v[158:159], s[68:69] op_sel_hi:[1,0]
	v_lshlrev_b32_e32 v242, 16, v231
	v_and_b32_e32 v243, 0xffff0000, v231
	v_pk_fma_f32 v[238:239], v[240:241], v[242:243], v[238:239]
	v_cvt_pk_bf16_f32 v248, v232, v233
	v_cvt_pk_bf16_f32 v249, v234, v235
	v_cvt_pk_bf16_f32 v250, v236, v237
	v_cvt_pk_bf16_f32 v251, v238, v239
	s_lshl_b32 s58, s54, 11
	s_add_u32 s60, s52, s58
	s_addc_u32 s61, s53, 0
	global_store_dwordx4 v126, v[248:251], s[60:61]
	s_add_i32 s54, s41, 0x2000
	s_cmp_lt_u32 s54, 0x8000
	s_cselect_b32 s55, s70, s71
	s_and_b32 s56, s54, s55
	s_add_i32 s57, s55, 1
	s_add_i32 s58, s56, -2
	s_cmp_lt_u32 s58, s57
	s_cselect_b32 s58, -2, 0
	s_add_i32 s58, s54, s58
	s_mul_i32 s58, s58, 0x5a00
	s_add_u32 s60, s50, s58
	s_addc_u32 s61, s51, 0
	global_load_dwordx4 v[200:203], v126, s[60:61]
	s_add_i32 s58, s56, -1
	s_cmp_lt_u32 s58, s57
	s_cselect_b32 s58, -1, 0
	s_add_i32 s58, s54, s58
	s_mul_i32 s58, s58, 0x5a00
	s_add_u32 s60, s50, s58
	s_addc_u32 s61, s51, 0
	global_load_dwordx4 v[204:207], v126, s[60:61]
	s_mul_i32 s58, s54, 0x5a00
	s_add_u32 s60, s50, s58
	s_addc_u32 s61, s51, 0
	global_load_dwordx4 v[208:211], v126, s[60:61]
	s_add_i32 s58, s56, 1
	s_cmp_lt_u32 s58, s57
	s_cselect_b32 s58, 1, 0
	s_add_i32 s58, s54, s58
	s_mul_i32 s58, s58, 0x5a00
	s_add_u32 s60, s50, s58
	s_addc_u32 s61, s51, 0
	global_load_dwordx4 v[212:215], v126, s[60:61]
	s_add_i32 s54, s41, 0x2400
	s_cmp_lt_u32 s54, 0x8000
	s_cselect_b32 s55, s70, s71
	s_and_b32 s56, s54, s55
	s_add_i32 s57, s55, 1
	s_add_i32 s58, s56, -2
	s_cmp_lt_u32 s58, s57
	s_cselect_b32 s58, -2, 0
	s_add_i32 s58, s54, s58
	s_mul_i32 s58, s58, 0x5a00
	s_add_u32 s60, s50, s58
	s_addc_u32 s61, s51, 0
	global_load_dwordx4 v[216:219], v126, s[60:61]
	s_add_i32 s58, s56, -1
	s_cmp_lt_u32 s58, s57
	s_cselect_b32 s58, -1, 0
	s_add_i32 s58, s54, s58
	s_mul_i32 s58, s58, 0x5a00
	s_add_u32 s60, s50, s58
	s_addc_u32 s61, s51, 0
	global_load_dwordx4 v[220:223], v126, s[60:61]
	s_mul_i32 s58, s54, 0x5a00
	s_add_u32 s60, s50, s58
	s_addc_u32 s61, s51, 0
	global_load_dwordx4 v[224:227], v126, s[60:61]
	s_add_i32 s58, s56, 1
	s_cmp_lt_u32 s58, s57
	s_cselect_b32 s58, 1, 0
	s_add_i32 s58, s54, s58
	s_mul_i32 s58, s58, 0x5a00
	s_add_u32 s60, s50, s58
	s_addc_u32 s61, s51, 0
	global_load_dwordx4 v[228:231], v126, s[60:61]
	s_waitcnt vmcnt(20)
	s_add_i32 s54, s41, 0x1000
	s_cmp_lt_u32 s54, 0x8000
	s_cselect_b32 s55, s70, s71
	s_and_b32 s56, s54, s55
	s_add_i32 s57, s55, 1
	s_add_i32 s58, s56, -2
	s_cmp_lt_u32 s58, s57
	s_cselect_b32 s62, 1.0, 0
	s_add_i32 s58, s56, -1
	s_cmp_lt_u32 s58, s57
	s_cselect_b32 s64, 1.0, 0
	s_mov_b32 s66, 1.0
	s_add_i32 s58, s56, 1
	s_cmp_lt_u32 s58, s57
	s_cselect_b32 s68, 1.0, 0
	v_pk_mul_f32 v[240:241], v[128:129], s[62:63] op_sel_hi:[1,0]
	v_lshlrev_b32_e32 v242, 16, v40
	v_and_b32_e32 v243, 0xffff0000, v40
	v_pk_fma_f32 v[232:233], v[240:241], v[242:243], v[160:161]
	v_pk_mul_f32 v[240:241], v[130:131], s[62:63] op_sel_hi:[1,0]
	v_lshlrev_b32_e32 v242, 16, v41
	v_and_b32_e32 v243, 0xffff0000, v41
	v_pk_fma_f32 v[234:235], v[240:241], v[242:243], v[162:163]
	v_pk_mul_f32 v[240:241], v[132:133], s[62:63] op_sel_hi:[1,0]
	v_lshlrev_b32_e32 v242, 16, v42
	v_and_b32_e32 v243, 0xffff0000, v42
	v_pk_fma_f32 v[236:237], v[240:241], v[242:243], v[164:165]
	v_pk_mul_f32 v[240:241], v[134:135], s[62:63] op_sel_hi:[1,0]
	v_lshlrev_b32_e32 v242, 16, v43
	v_and_b32_e32 v243, 0xffff0000, v43
	v_pk_fma_f32 v[238:239], v[240:241], v[242:243], v[166:167]
	v_pk_mul_f32 v[240:241], v[136:137], s[64:65] op_sel_hi:[1,0]
	v_lshlrev_b32_e32 v242, 16, v44
	v_and_b32_e32 v243, 0xffff0000, v44
	v_pk_fma_f32 v[232:233], v[240:241], v[242:243], v[232:233]
	v_pk_mul_f32 v[240:241], v[138:139], s[64:65] op_sel_hi:[1,0]
	v_lshlrev_b32_e32 v242, 16, v45
	v_and_b32_e32 v243, 0xffff0000, v45
	v_pk_fma_f32 v[234:235], v[240:241], v[242:243], v[234:235]
	v_pk_mul_f32 v[240:241], v[140:141], s[64:65] op_sel_hi:[1,0]
	v_lshlrev_b32_e32 v242, 16, v46
	v_and_b32_e32 v243, 0xffff0000, v46
	v_pk_fma_f32 v[236:237], v[240:241], v[242:243], v[236:237]
	v_pk_mul_f32 v[240:241], v[142:143], s[64:65] op_sel_hi:[1,0]
	v_lshlrev_b32_e32 v242, 16, v47
	v_and_b32_e32 v243, 0xffff0000, v47
	v_pk_fma_f32 v[238:239], v[240:241], v[242:243], v[238:239]
	v_pk_mul_f32 v[240:241], v[144:145], s[66:67] op_sel_hi:[1,0]
	v_lshlrev_b32_e32 v242, 16, v48
	v_and_b32_e32 v243, 0xffff0000, v48
	v_pk_fma_f32 v[232:233], v[240:241], v[242:243], v[232:233]
	v_pk_mul_f32 v[240:241], v[146:147], s[66:67] op_sel_hi:[1,0]
	v_lshlrev_b32_e32 v242, 16, v49
	v_and_b32_e32 v243, 0xffff0000, v49
	v_pk_fma_f32 v[234:235], v[240:241], v[242:243], v[234:235]
	v_pk_mul_f32 v[240:241], v[148:149], s[66:67] op_sel_hi:[1,0]
	v_lshlrev_b32_e32 v242, 16, v50
	v_and_b32_e32 v243, 0xffff0000, v50
	v_pk_fma_f32 v[236:237], v[240:241], v[242:243], v[236:237]
	v_pk_mul_f32 v[240:241], v[150:151], s[66:67] op_sel_hi:[1,0]
	v_lshlrev_b32_e32 v242, 16, v51
	v_and_b32_e32 v243, 0xffff0000, v51
	v_pk_fma_f32 v[238:239], v[240:241], v[242:243], v[238:239]
	v_pk_mul_f32 v[240:241], v[152:153], s[68:69] op_sel_hi:[1,0]
	v_lshlrev_b32_e32 v242, 16, v52
	v_and_b32_e32 v243, 0xffff0000, v52
	v_pk_fma_f32 v[232:233], v[240:241], v[242:243], v[232:233]
	v_pk_mul_f32 v[240:241], v[154:155], s[68:69] op_sel_hi:[1,0]
	v_lshlrev_b32_e32 v242, 16, v53
	v_and_b32_e32 v243, 0xffff0000, v53
	v_pk_fma_f32 v[234:235], v[240:241], v[242:243], v[234:235]
	v_pk_mul_f32 v[240:241], v[156:157], s[68:69] op_sel_hi:[1,0]
	v_lshlrev_b32_e32 v242, 16, v54
	v_and_b32_e32 v243, 0xffff0000, v54
	v_pk_fma_f32 v[236:237], v[240:241], v[242:243], v[236:237]
	v_pk_mul_f32 v[240:241], v[158:159], s[68:69] op_sel_hi:[1,0]
	v_lshlrev_b32_e32 v242, 16, v55
	v_and_b32_e32 v243, 0xffff0000, v55
	v_pk_fma_f32 v[238:239], v[240:241], v[242:243], v[238:239]
	v_cvt_pk_bf16_f32 v248, v232, v233
	v_cvt_pk_bf16_f32 v249, v234, v235
	v_cvt_pk_bf16_f32 v250, v236, v237
	v_cvt_pk_bf16_f32 v251, v238, v239
	s_lshl_b32 s58, s54, 11
	s_add_u32 s60, s52, s58
	s_addc_u32 s61, s53, 0
	global_store_dwordx4 v126, v[248:251], s[60:61]
	s_add_i32 s54, s41, 0x1400
	s_cmp_lt_u32 s54, 0x8000
	s_cselect_b32 s55, s70, s71
	s_and_b32 s56, s54, s55
	s_add_i32 s57, s55, 1
	s_add_i32 s58, s56, -2
	s_cmp_lt_u32 s58, s57
	s_cselect_b32 s62, 1.0, 0
	s_add_i32 s58, s56, -1
	s_cmp_lt_u32 s58, s57
	s_cselect_b32 s64, 1.0, 0
	s_mov_b32 s66, 1.0
	s_add_i32 s58, s56, 1
	s_cmp_lt_u32 s58, s57
	s_cselect_b32 s68, 1.0, 0
	v_pk_mul_f32 v[240:241], v[128:129], s[62:63] op_sel_hi:[1,0]
	v_lshlrev_b32_e32 v242, 16, v56
	v_and_b32_e32 v243, 0xffff0000, v56
	v_pk_fma_f32 v[232:233], v[240:241], v[242:243], v[160:161]
	v_pk_mul_f32 v[240:241], v[130:131], s[62:63] op_sel_hi:[1,0]
	v_lshlrev_b32_e32 v242, 16, v57
	v_and_b32_e32 v243, 0xffff0000, v57
	v_pk_fma_f32 v[234:235], v[240:241], v[242:243], v[162:163]
	v_pk_mul_f32 v[240:241], v[132:133], s[62:63] op_sel_hi:[1,0]
	v_lshlrev_b32_e32 v242, 16, v58
	v_and_b32_e32 v243, 0xffff0000, v58
	v_pk_fma_f32 v[236:237], v[240:241], v[242:243], v[164:165]
	v_pk_mul_f32 v[240:241], v[134:135], s[62:63] op_sel_hi:[1,0]
	v_lshlrev_b32_e32 v242, 16, v59
	v_and_b32_e32 v243, 0xffff0000, v59
	v_pk_fma_f32 v[238:239], v[240:241], v[242:243], v[166:167]
	v_pk_mul_f32 v[240:241], v[136:137], s[64:65] op_sel_hi:[1,0]
	v_lshlrev_b32_e32 v242, 16, v60
	v_and_b32_e32 v243, 0xffff0000, v60
	v_pk_fma_f32 v[232:233], v[240:241], v[242:243], v[232:233]
	v_pk_mul_f32 v[240:241], v[138:139], s[64:65] op_sel_hi:[1,0]
	v_lshlrev_b32_e32 v242, 16, v61
	v_and_b32_e32 v243, 0xffff0000, v61
	v_pk_fma_f32 v[234:235], v[240:241], v[242:243], v[234:235]
	v_pk_mul_f32 v[240:241], v[140:141], s[64:65] op_sel_hi:[1,0]
	v_lshlrev_b32_e32 v242, 16, v62
	v_and_b32_e32 v243, 0xffff0000, v62
	v_pk_fma_f32 v[236:237], v[240:241], v[242:243], v[236:237]
	v_pk_mul_f32 v[240:241], v[142:143], s[64:65] op_sel_hi:[1,0]
	v_lshlrev_b32_e32 v242, 16, v63
	v_and_b32_e32 v243, 0xffff0000, v63
	v_pk_fma_f32 v[238:239], v[240:241], v[242:243], v[238:239]
	v_pk_mul_f32 v[240:241], v[144:145], s[66:67] op_sel_hi:[1,0]
	v_lshlrev_b32_e32 v242, 16, v64
	v_and_b32_e32 v243, 0xffff0000, v64
	v_pk_fma_f32 v[232:233], v[240:241], v[242:243], v[232:233]
	v_pk_mul_f32 v[240:241], v[146:147], s[66:67] op_sel_hi:[1,0]
	v_lshlrev_b32_e32 v242, 16, v65
	v_and_b32_e32 v243, 0xffff0000, v65
	v_pk_fma_f32 v[234:235], v[240:241], v[242:243], v[234:235]
	v_pk_mul_f32 v[240:241], v[148:149], s[66:67] op_sel_hi:[1,0]
	v_lshlrev_b32_e32 v242, 16, v66
	v_and_b32_e32 v243, 0xffff0000, v66
	v_pk_fma_f32 v[236:237], v[240:241], v[242:243], v[236:237]
	v_pk_mul_f32 v[240:241], v[150:151], s[66:67] op_sel_hi:[1,0]
	v_lshlrev_b32_e32 v242, 16, v67
	v_and_b32_e32 v243, 0xffff0000, v67
	v_pk_fma_f32 v[238:239], v[240:241], v[242:243], v[238:239]
	v_pk_mul_f32 v[240:241], v[152:153], s[68:69] op_sel_hi:[1,0]
	v_lshlrev_b32_e32 v242, 16, v68
	v_and_b32_e32 v243, 0xffff0000, v68
	v_pk_fma_f32 v[232:233], v[240:241], v[242:243], v[232:233]
	v_pk_mul_f32 v[240:241], v[154:155], s[68:69] op_sel_hi:[1,0]
	v_lshlrev_b32_e32 v242, 16, v69
	v_and_b32_e32 v243, 0xffff0000, v69
	v_pk_fma_f32 v[234:235], v[240:241], v[242:243], v[234:235]
	v_pk_mul_f32 v[240:241], v[156:157], s[68:69] op_sel_hi:[1,0]
	v_lshlrev_b32_e32 v242, 16, v70
	v_and_b32_e32 v243, 0xffff0000, v70
	v_pk_fma_f32 v[236:237], v[240:241], v[242:243], v[236:237]
	v_pk_mul_f32 v[240:241], v[158:159], s[68:69] op_sel_hi:[1,0]
	v_lshlrev_b32_e32 v242, 16, v71
	v_and_b32_e32 v243, 0xffff0000, v71
	v_pk_fma_f32 v[238:239], v[240:241], v[242:243], v[238:239]
	v_cvt_pk_bf16_f32 v248, v232, v233
	v_cvt_pk_bf16_f32 v249, v234, v235
	v_cvt_pk_bf16_f32 v250, v236, v237
	v_cvt_pk_bf16_f32 v251, v238, v239
	s_lshl_b32 s58, s54, 11
	s_add_u32 s60, s52, s58
	s_addc_u32 s61, s53, 0
	global_store_dwordx4 v126, v[248:251], s[60:61]
	s_add_i32 s54, s41, 0x2800
	s_cmp_lt_u32 s54, 0x8000
	s_cselect_b32 s55, s70, s71
	s_and_b32 s56, s54, s55
	s_add_i32 s57, s55, 1
	s_add_i32 s58, s56, -2
	s_cmp_lt_u32 s58, s57
	s_cselect_b32 s58, -2, 0
	s_add_i32 s58, s54, s58
	s_mul_i32 s58, s58, 0x5a00
	s_add_u32 s60, s50, s58
	s_addc_u32 s61, s51, 0
	global_load_dwordx4 v[40:43], v126, s[60:61]
	s_add_i32 s58, s56, -1
	s_cmp_lt_u32 s58, s57
	s_cselect_b32 s58, -1, 0
	s_add_i32 s58, s54, s58
	s_mul_i32 s58, s58, 0x5a00
	s_add_u32 s60, s50, s58
	s_addc_u32 s61, s51, 0
	global_load_dwordx4 v[44:47], v126, s[60:61]
	s_mul_i32 s58, s54, 0x5a00
	s_add_u32 s60, s50, s58
	s_addc_u32 s61, s51, 0
	global_load_dwordx4 v[48:51], v126, s[60:61]
	s_add_i32 s58, s56, 1
	s_cmp_lt_u32 s58, s57
	s_cselect_b32 s58, 1, 0
	s_add_i32 s58, s54, s58
	s_mul_i32 s58, s58, 0x5a00
	s_add_u32 s60, s50, s58
	s_addc_u32 s61, s51, 0
	global_load_dwordx4 v[52:55], v126, s[60:61]
	s_add_i32 s54, s41, 0x2c00
	s_cmp_lt_u32 s54, 0x8000
	s_cselect_b32 s55, s70, s71
	s_and_b32 s56, s54, s55
	s_add_i32 s57, s55, 1
	s_add_i32 s58, s56, -2
	s_cmp_lt_u32 s58, s57
	s_cselect_b32 s58, -2, 0
	s_add_i32 s58, s54, s58
	s_mul_i32 s58, s58, 0x5a00
	s_add_u32 s60, s50, s58
	s_addc_u32 s61, s51, 0
	global_load_dwordx4 v[56:59], v126, s[60:61]
	s_add_i32 s58, s56, -1
	s_cmp_lt_u32 s58, s57
	s_cselect_b32 s58, -1, 0
	s_add_i32 s58, s54, s58
	s_mul_i32 s58, s58, 0x5a00
	s_add_u32 s60, s50, s58
	s_addc_u32 s61, s51, 0
	global_load_dwordx4 v[60:63], v126, s[60:61]
	s_mul_i32 s58, s54, 0x5a00
	s_add_u32 s60, s50, s58
	s_addc_u32 s61, s51, 0
	global_load_dwordx4 v[64:67], v126, s[60:61]
	s_add_i32 s58, s56, 1
	s_cmp_lt_u32 s58, s57
	s_cselect_b32 s58, 1, 0
	s_add_i32 s58, s54, s58
	s_mul_i32 s58, s58, 0x5a00
	s_add_u32 s60, s50, s58
	s_addc_u32 s61, s51, 0
	global_load_dwordx4 v[68:71], v126, s[60:61]
	s_waitcnt vmcnt(20)
	s_add_i32 s54, s41, 0x1800
	s_cmp_lt_u32 s54, 0x8000
	s_cselect_b32 s55, s70, s71
	s_and_b32 s56, s54, s55
	s_add_i32 s57, s55, 1
	s_add_i32 s58, s56, -2
	s_cmp_lt_u32 s58, s57
	s_cselect_b32 s62, 1.0, 0
	s_add_i32 s58, s56, -1
	s_cmp_lt_u32 s58, s57
	s_cselect_b32 s64, 1.0, 0
	s_mov_b32 s66, 1.0
	s_add_i32 s58, s56, 1
	s_cmp_lt_u32 s58, s57
	s_cselect_b32 s68, 1.0, 0
	v_pk_mul_f32 v[240:241], v[128:129], s[62:63] op_sel_hi:[1,0]
	v_lshlrev_b32_e32 v242, 16, v168
	v_and_b32_e32 v243, 0xffff0000, v168
	v_pk_fma_f32 v[232:233], v[240:241], v[242:243], v[160:161]
	v_pk_mul_f32 v[240:241], v[130:131], s[62:63] op_sel_hi:[1,0]
	v_lshlrev_b32_e32 v242, 16, v169
	v_and_b32_e32 v243, 0xffff0000, v169
	v_pk_fma_f32 v[234:235], v[240:241], v[242:243], v[162:163]
	v_pk_mul_f32 v[240:241], v[132:133], s[62:63] op_sel_hi:[1,0]
	v_lshlrev_b32_e32 v242, 16, v170
	v_and_b32_e32 v243, 0xffff0000, v170
	v_pk_fma_f32 v[236:237], v[240:241], v[242:243], v[164:165]
	v_pk_mul_f32 v[240:241], v[134:135], s[62:63] op_sel_hi:[1,0]
	v_lshlrev_b32_e32 v242, 16, v171
	v_and_b32_e32 v243, 0xffff0000, v171
	v_pk_fma_f32 v[238:239], v[240:241], v[242:243], v[166:167]
	v_pk_mul_f32 v[240:241], v[136:137], s[64:65] op_sel_hi:[1,0]
	v_lshlrev_b32_e32 v242, 16, v172
	v_and_b32_e32 v243, 0xffff0000, v172
	v_pk_fma_f32 v[232:233], v[240:241], v[242:243], v[232:233]
	v_pk_mul_f32 v[240:241], v[138:139], s[64:65] op_sel_hi:[1,0]
	v_lshlrev_b32_e32 v242, 16, v173
	v_and_b32_e32 v243, 0xffff0000, v173
	v_pk_fma_f32 v[234:235], v[240:241], v[242:243], v[234:235]
	v_pk_mul_f32 v[240:241], v[140:141], s[64:65] op_sel_hi:[1,0]
	v_lshlrev_b32_e32 v242, 16, v174
	v_and_b32_e32 v243, 0xffff0000, v174
	v_pk_fma_f32 v[236:237], v[240:241], v[242:243], v[236:237]
	v_pk_mul_f32 v[240:241], v[142:143], s[64:65] op_sel_hi:[1,0]
	v_lshlrev_b32_e32 v242, 16, v175
	v_and_b32_e32 v243, 0xffff0000, v175
	v_pk_fma_f32 v[238:239], v[240:241], v[242:243], v[238:239]
	v_pk_mul_f32 v[240:241], v[144:145], s[66:67] op_sel_hi:[1,0]
	v_lshlrev_b32_e32 v242, 16, v176
	v_and_b32_e32 v243, 0xffff0000, v176
	v_pk_fma_f32 v[232:233], v[240:241], v[242:243], v[232:233]
	v_pk_mul_f32 v[240:241], v[146:147], s[66:67] op_sel_hi:[1,0]
	v_lshlrev_b32_e32 v242, 16, v177
	v_and_b32_e32 v243, 0xffff0000, v177
	v_pk_fma_f32 v[234:235], v[240:241], v[242:243], v[234:235]
	v_pk_mul_f32 v[240:241], v[148:149], s[66:67] op_sel_hi:[1,0]
	v_lshlrev_b32_e32 v242, 16, v178
	v_and_b32_e32 v243, 0xffff0000, v178
	v_pk_fma_f32 v[236:237], v[240:241], v[242:243], v[236:237]
	v_pk_mul_f32 v[240:241], v[150:151], s[66:67] op_sel_hi:[1,0]
	v_lshlrev_b32_e32 v242, 16, v179
	v_and_b32_e32 v243, 0xffff0000, v179
	v_pk_fma_f32 v[238:239], v[240:241], v[242:243], v[238:239]
	v_pk_mul_f32 v[240:241], v[152:153], s[68:69] op_sel_hi:[1,0]
	v_lshlrev_b32_e32 v242, 16, v180
	v_and_b32_e32 v243, 0xffff0000, v180
	v_pk_fma_f32 v[232:233], v[240:241], v[242:243], v[232:233]
	v_pk_mul_f32 v[240:241], v[154:155], s[68:69] op_sel_hi:[1,0]
	v_lshlrev_b32_e32 v242, 16, v181
	v_and_b32_e32 v243, 0xffff0000, v181
	v_pk_fma_f32 v[234:235], v[240:241], v[242:243], v[234:235]
	v_pk_mul_f32 v[240:241], v[156:157], s[68:69] op_sel_hi:[1,0]
	v_lshlrev_b32_e32 v242, 16, v182
	v_and_b32_e32 v243, 0xffff0000, v182
	v_pk_fma_f32 v[236:237], v[240:241], v[242:243], v[236:237]
	v_pk_mul_f32 v[240:241], v[158:159], s[68:69] op_sel_hi:[1,0]
	v_lshlrev_b32_e32 v242, 16, v183
	v_and_b32_e32 v243, 0xffff0000, v183
	v_pk_fma_f32 v[238:239], v[240:241], v[242:243], v[238:239]
	v_cvt_pk_bf16_f32 v248, v232, v233
	v_cvt_pk_bf16_f32 v249, v234, v235
	v_cvt_pk_bf16_f32 v250, v236, v237
	v_cvt_pk_bf16_f32 v251, v238, v239
	s_lshl_b32 s58, s54, 11
	s_add_u32 s60, s52, s58
	s_addc_u32 s61, s53, 0
	global_store_dwordx4 v126, v[248:251], s[60:61]
	s_add_i32 s54, s41, 0x1c00
	s_cmp_lt_u32 s54, 0x8000
	s_cselect_b32 s55, s70, s71
	s_and_b32 s56, s54, s55
	s_add_i32 s57, s55, 1
	s_add_i32 s58, s56, -2
	s_cmp_lt_u32 s58, s57
	s_cselect_b32 s62, 1.0, 0
	s_add_i32 s58, s56, -1
	s_cmp_lt_u32 s58, s57
	s_cselect_b32 s64, 1.0, 0
	s_mov_b32 s66, 1.0
	s_add_i32 s58, s56, 1
	s_cmp_lt_u32 s58, s57
	s_cselect_b32 s68, 1.0, 0
	v_pk_mul_f32 v[240:241], v[128:129], s[62:63] op_sel_hi:[1,0]
	v_lshlrev_b32_e32 v242, 16, v184
	v_and_b32_e32 v243, 0xffff0000, v184
	v_pk_fma_f32 v[232:233], v[240:241], v[242:243], v[160:161]
	v_pk_mul_f32 v[240:241], v[130:131], s[62:63] op_sel_hi:[1,0]
	v_lshlrev_b32_e32 v242, 16, v185
	v_and_b32_e32 v243, 0xffff0000, v185
	v_pk_fma_f32 v[234:235], v[240:241], v[242:243], v[162:163]
	v_pk_mul_f32 v[240:241], v[132:133], s[62:63] op_sel_hi:[1,0]
	v_lshlrev_b32_e32 v242, 16, v186
	v_and_b32_e32 v243, 0xffff0000, v186
	v_pk_fma_f32 v[236:237], v[240:241], v[242:243], v[164:165]
	v_pk_mul_f32 v[240:241], v[134:135], s[62:63] op_sel_hi:[1,0]
	v_lshlrev_b32_e32 v242, 16, v187
	v_and_b32_e32 v243, 0xffff0000, v187
	v_pk_fma_f32 v[238:239], v[240:241], v[242:243], v[166:167]
	v_pk_mul_f32 v[240:241], v[136:137], s[64:65] op_sel_hi:[1,0]
	v_lshlrev_b32_e32 v242, 16, v188
	v_and_b32_e32 v243, 0xffff0000, v188
	v_pk_fma_f32 v[232:233], v[240:241], v[242:243], v[232:233]
	v_pk_mul_f32 v[240:241], v[138:139], s[64:65] op_sel_hi:[1,0]
	v_lshlrev_b32_e32 v242, 16, v189
	v_and_b32_e32 v243, 0xffff0000, v189
	v_pk_fma_f32 v[234:235], v[240:241], v[242:243], v[234:235]
	v_pk_mul_f32 v[240:241], v[140:141], s[64:65] op_sel_hi:[1,0]
	v_lshlrev_b32_e32 v242, 16, v190
	v_and_b32_e32 v243, 0xffff0000, v190
	v_pk_fma_f32 v[236:237], v[240:241], v[242:243], v[236:237]
	v_pk_mul_f32 v[240:241], v[142:143], s[64:65] op_sel_hi:[1,0]
	v_lshlrev_b32_e32 v242, 16, v191
	v_and_b32_e32 v243, 0xffff0000, v191
	v_pk_fma_f32 v[238:239], v[240:241], v[242:243], v[238:239]
	v_pk_mul_f32 v[240:241], v[144:145], s[66:67] op_sel_hi:[1,0]
	v_lshlrev_b32_e32 v242, 16, v192
	v_and_b32_e32 v243, 0xffff0000, v192
	v_pk_fma_f32 v[232:233], v[240:241], v[242:243], v[232:233]
	v_pk_mul_f32 v[240:241], v[146:147], s[66:67] op_sel_hi:[1,0]
	v_lshlrev_b32_e32 v242, 16, v193
	v_and_b32_e32 v243, 0xffff0000, v193
	v_pk_fma_f32 v[234:235], v[240:241], v[242:243], v[234:235]
	v_pk_mul_f32 v[240:241], v[148:149], s[66:67] op_sel_hi:[1,0]
	v_lshlrev_b32_e32 v242, 16, v194
	v_and_b32_e32 v243, 0xffff0000, v194
	v_pk_fma_f32 v[236:237], v[240:241], v[242:243], v[236:237]
	v_pk_mul_f32 v[240:241], v[150:151], s[66:67] op_sel_hi:[1,0]
	v_lshlrev_b32_e32 v242, 16, v195
	v_and_b32_e32 v243, 0xffff0000, v195
	v_pk_fma_f32 v[238:239], v[240:241], v[242:243], v[238:239]
	v_pk_mul_f32 v[240:241], v[152:153], s[68:69] op_sel_hi:[1,0]
	v_lshlrev_b32_e32 v242, 16, v196
	v_and_b32_e32 v243, 0xffff0000, v196
	v_pk_fma_f32 v[232:233], v[240:241], v[242:243], v[232:233]
	v_pk_mul_f32 v[240:241], v[154:155], s[68:69] op_sel_hi:[1,0]
	v_lshlrev_b32_e32 v242, 16, v197
	v_and_b32_e32 v243, 0xffff0000, v197
	v_pk_fma_f32 v[234:235], v[240:241], v[242:243], v[234:235]
	v_pk_mul_f32 v[240:241], v[156:157], s[68:69] op_sel_hi:[1,0]
	v_lshlrev_b32_e32 v242, 16, v198
	v_and_b32_e32 v243, 0xffff0000, v198
	v_pk_fma_f32 v[236:237], v[240:241], v[242:243], v[236:237]
	v_pk_mul_f32 v[240:241], v[158:159], s[68:69] op_sel_hi:[1,0]
	v_lshlrev_b32_e32 v242, 16, v199
	v_and_b32_e32 v243, 0xffff0000, v199
	v_pk_fma_f32 v[238:239], v[240:241], v[242:243], v[238:239]
	v_cvt_pk_bf16_f32 v248, v232, v233
	v_cvt_pk_bf16_f32 v249, v234, v235
	v_cvt_pk_bf16_f32 v250, v236, v237
	v_cvt_pk_bf16_f32 v251, v238, v239
	s_lshl_b32 s58, s54, 11
	s_add_u32 s60, s52, s58
	s_addc_u32 s61, s53, 0
	global_store_dwordx4 v126, v[248:251], s[60:61]
	s_add_i32 s54, s41, 0x3000
	s_cmp_lt_u32 s54, 0x8000
	s_cselect_b32 s55, s70, s71
	s_and_b32 s56, s54, s55
	s_add_i32 s57, s55, 1
	s_add_i32 s58, s56, -2
	s_cmp_lt_u32 s58, s57
	s_cselect_b32 s58, -2, 0
	s_add_i32 s58, s54, s58
	s_mul_i32 s58, s58, 0x5a00
	s_add_u32 s60, s50, s58
	s_addc_u32 s61, s51, 0
	global_load_dwordx4 v[168:171], v126, s[60:61]
	s_add_i32 s58, s56, -1
	s_cmp_lt_u32 s58, s57
	s_cselect_b32 s58, -1, 0
	s_add_i32 s58, s54, s58
	s_mul_i32 s58, s58, 0x5a00
	s_add_u32 s60, s50, s58
	s_addc_u32 s61, s51, 0
	global_load_dwordx4 v[172:175], v126, s[60:61]
	s_mul_i32 s58, s54, 0x5a00
	s_add_u32 s60, s50, s58
	s_addc_u32 s61, s51, 0
	global_load_dwordx4 v[176:179], v126, s[60:61]
	s_add_i32 s58, s56, 1
	s_cmp_lt_u32 s58, s57
	s_cselect_b32 s58, 1, 0
	s_add_i32 s58, s54, s58
	s_mul_i32 s58, s58, 0x5a00
	s_add_u32 s60, s50, s58
	s_addc_u32 s61, s51, 0
	global_load_dwordx4 v[180:183], v126, s[60:61]
	s_add_i32 s54, s41, 0x3400
	s_cmp_lt_u32 s54, 0x8000
	s_cselect_b32 s55, s70, s71
	s_and_b32 s56, s54, s55
	s_add_i32 s57, s55, 1
	s_add_i32 s58, s56, -2
	s_cmp_lt_u32 s58, s57
	s_cselect_b32 s58, -2, 0
	s_add_i32 s58, s54, s58
	s_mul_i32 s58, s58, 0x5a00
	s_add_u32 s60, s50, s58
	s_addc_u32 s61, s51, 0
	global_load_dwordx4 v[184:187], v126, s[60:61]
	s_add_i32 s58, s56, -1
	s_cmp_lt_u32 s58, s57
	s_cselect_b32 s58, -1, 0
	s_add_i32 s58, s54, s58
	s_mul_i32 s58, s58, 0x5a00
	s_add_u32 s60, s50, s58
	s_addc_u32 s61, s51, 0
	global_load_dwordx4 v[188:191], v126, s[60:61]
	s_mul_i32 s58, s54, 0x5a00
	s_add_u32 s60, s50, s58
	s_addc_u32 s61, s51, 0
	global_load_dwordx4 v[192:195], v126, s[60:61]
	s_add_i32 s58, s56, 1
	s_cmp_lt_u32 s58, s57
	s_cselect_b32 s58, 1, 0
	s_add_i32 s58, s54, s58
	s_mul_i32 s58, s58, 0x5a00
	s_add_u32 s60, s50, s58
	s_addc_u32 s61, s51, 0
	global_load_dwordx4 v[196:199], v126, s[60:61]
	s_waitcnt vmcnt(20)
	s_add_i32 s54, s41, 0x2000
	s_cmp_lt_u32 s54, 0x8000
	s_cselect_b32 s55, s70, s71
	s_and_b32 s56, s54, s55
	s_add_i32 s57, s55, 1
	s_add_i32 s58, s56, -2
	s_cmp_lt_u32 s58, s57
	s_cselect_b32 s62, 1.0, 0
	s_add_i32 s58, s56, -1
	s_cmp_lt_u32 s58, s57
	s_cselect_b32 s64, 1.0, 0
	s_mov_b32 s66, 1.0
	s_add_i32 s58, s56, 1
	s_cmp_lt_u32 s58, s57
	s_cselect_b32 s68, 1.0, 0
	v_pk_mul_f32 v[240:241], v[128:129], s[62:63] op_sel_hi:[1,0]
	v_lshlrev_b32_e32 v242, 16, v200
	v_and_b32_e32 v243, 0xffff0000, v200
	v_pk_fma_f32 v[232:233], v[240:241], v[242:243], v[160:161]
	v_pk_mul_f32 v[240:241], v[130:131], s[62:63] op_sel_hi:[1,0]
	v_lshlrev_b32_e32 v242, 16, v201
	v_and_b32_e32 v243, 0xffff0000, v201
	v_pk_fma_f32 v[234:235], v[240:241], v[242:243], v[162:163]
	v_pk_mul_f32 v[240:241], v[132:133], s[62:63] op_sel_hi:[1,0]
	v_lshlrev_b32_e32 v242, 16, v202
	v_and_b32_e32 v243, 0xffff0000, v202
	v_pk_fma_f32 v[236:237], v[240:241], v[242:243], v[164:165]
	v_pk_mul_f32 v[240:241], v[134:135], s[62:63] op_sel_hi:[1,0]
	v_lshlrev_b32_e32 v242, 16, v203
	v_and_b32_e32 v243, 0xffff0000, v203
	v_pk_fma_f32 v[238:239], v[240:241], v[242:243], v[166:167]
	v_pk_mul_f32 v[240:241], v[136:137], s[64:65] op_sel_hi:[1,0]
	v_lshlrev_b32_e32 v242, 16, v204
	v_and_b32_e32 v243, 0xffff0000, v204
	v_pk_fma_f32 v[232:233], v[240:241], v[242:243], v[232:233]
	v_pk_mul_f32 v[240:241], v[138:139], s[64:65] op_sel_hi:[1,0]
	v_lshlrev_b32_e32 v242, 16, v205
	v_and_b32_e32 v243, 0xffff0000, v205
	v_pk_fma_f32 v[234:235], v[240:241], v[242:243], v[234:235]
	v_pk_mul_f32 v[240:241], v[140:141], s[64:65] op_sel_hi:[1,0]
	v_lshlrev_b32_e32 v242, 16, v206
	v_and_b32_e32 v243, 0xffff0000, v206
	v_pk_fma_f32 v[236:237], v[240:241], v[242:243], v[236:237]
	v_pk_mul_f32 v[240:241], v[142:143], s[64:65] op_sel_hi:[1,0]
	v_lshlrev_b32_e32 v242, 16, v207
	v_and_b32_e32 v243, 0xffff0000, v207
	v_pk_fma_f32 v[238:239], v[240:241], v[242:243], v[238:239]
	v_pk_mul_f32 v[240:241], v[144:145], s[66:67] op_sel_hi:[1,0]
	v_lshlrev_b32_e32 v242, 16, v208
	v_and_b32_e32 v243, 0xffff0000, v208
	v_pk_fma_f32 v[232:233], v[240:241], v[242:243], v[232:233]
	v_pk_mul_f32 v[240:241], v[146:147], s[66:67] op_sel_hi:[1,0]
	v_lshlrev_b32_e32 v242, 16, v209
	v_and_b32_e32 v243, 0xffff0000, v209
	v_pk_fma_f32 v[234:235], v[240:241], v[242:243], v[234:235]
	v_pk_mul_f32 v[240:241], v[148:149], s[66:67] op_sel_hi:[1,0]
	v_lshlrev_b32_e32 v242, 16, v210
	v_and_b32_e32 v243, 0xffff0000, v210
	v_pk_fma_f32 v[236:237], v[240:241], v[242:243], v[236:237]
	v_pk_mul_f32 v[240:241], v[150:151], s[66:67] op_sel_hi:[1,0]
	v_lshlrev_b32_e32 v242, 16, v211
	v_and_b32_e32 v243, 0xffff0000, v211
	v_pk_fma_f32 v[238:239], v[240:241], v[242:243], v[238:239]
	v_pk_mul_f32 v[240:241], v[152:153], s[68:69] op_sel_hi:[1,0]
	v_lshlrev_b32_e32 v242, 16, v212
	v_and_b32_e32 v243, 0xffff0000, v212
	v_pk_fma_f32 v[232:233], v[240:241], v[242:243], v[232:233]
	v_pk_mul_f32 v[240:241], v[154:155], s[68:69] op_sel_hi:[1,0]
	v_lshlrev_b32_e32 v242, 16, v213
	v_and_b32_e32 v243, 0xffff0000, v213
	v_pk_fma_f32 v[234:235], v[240:241], v[242:243], v[234:235]
	v_pk_mul_f32 v[240:241], v[156:157], s[68:69] op_sel_hi:[1,0]
	v_lshlrev_b32_e32 v242, 16, v214
	v_and_b32_e32 v243, 0xffff0000, v214
	v_pk_fma_f32 v[236:237], v[240:241], v[242:243], v[236:237]
	v_pk_mul_f32 v[240:241], v[158:159], s[68:69] op_sel_hi:[1,0]
	v_lshlrev_b32_e32 v242, 16, v215
	v_and_b32_e32 v243, 0xffff0000, v215
	v_pk_fma_f32 v[238:239], v[240:241], v[242:243], v[238:239]
	v_cvt_pk_bf16_f32 v248, v232, v233
	v_cvt_pk_bf16_f32 v249, v234, v235
	v_cvt_pk_bf16_f32 v250, v236, v237
	v_cvt_pk_bf16_f32 v251, v238, v239
	s_lshl_b32 s58, s54, 11
	s_add_u32 s60, s52, s58
	s_addc_u32 s61, s53, 0
	global_store_dwordx4 v126, v[248:251], s[60:61]
	s_add_i32 s54, s41, 0x2400
	s_cmp_lt_u32 s54, 0x8000
	s_cselect_b32 s55, s70, s71
	s_and_b32 s56, s54, s55
	s_add_i32 s57, s55, 1
	s_add_i32 s58, s56, -2
	s_cmp_lt_u32 s58, s57
	s_cselect_b32 s62, 1.0, 0
	s_add_i32 s58, s56, -1
	s_cmp_lt_u32 s58, s57
	s_cselect_b32 s64, 1.0, 0
	s_mov_b32 s66, 1.0
	s_add_i32 s58, s56, 1
	s_cmp_lt_u32 s58, s57
	s_cselect_b32 s68, 1.0, 0
	v_pk_mul_f32 v[240:241], v[128:129], s[62:63] op_sel_hi:[1,0]
	v_lshlrev_b32_e32 v242, 16, v216
	v_and_b32_e32 v243, 0xffff0000, v216
	v_pk_fma_f32 v[232:233], v[240:241], v[242:243], v[160:161]
	v_pk_mul_f32 v[240:241], v[130:131], s[62:63] op_sel_hi:[1,0]
	v_lshlrev_b32_e32 v242, 16, v217
	v_and_b32_e32 v243, 0xffff0000, v217
	v_pk_fma_f32 v[234:235], v[240:241], v[242:243], v[162:163]
	v_pk_mul_f32 v[240:241], v[132:133], s[62:63] op_sel_hi:[1,0]
	v_lshlrev_b32_e32 v242, 16, v218
	v_and_b32_e32 v243, 0xffff0000, v218
	v_pk_fma_f32 v[236:237], v[240:241], v[242:243], v[164:165]
	v_pk_mul_f32 v[240:241], v[134:135], s[62:63] op_sel_hi:[1,0]
	v_lshlrev_b32_e32 v242, 16, v219
	v_and_b32_e32 v243, 0xffff0000, v219
	v_pk_fma_f32 v[238:239], v[240:241], v[242:243], v[166:167]
	v_pk_mul_f32 v[240:241], v[136:137], s[64:65] op_sel_hi:[1,0]
	v_lshlrev_b32_e32 v242, 16, v220
	v_and_b32_e32 v243, 0xffff0000, v220
	v_pk_fma_f32 v[232:233], v[240:241], v[242:243], v[232:233]
	v_pk_mul_f32 v[240:241], v[138:139], s[64:65] op_sel_hi:[1,0]
	v_lshlrev_b32_e32 v242, 16, v221
	v_and_b32_e32 v243, 0xffff0000, v221
	v_pk_fma_f32 v[234:235], v[240:241], v[242:243], v[234:235]
	v_pk_mul_f32 v[240:241], v[140:141], s[64:65] op_sel_hi:[1,0]
	v_lshlrev_b32_e32 v242, 16, v222
	v_and_b32_e32 v243, 0xffff0000, v222
	v_pk_fma_f32 v[236:237], v[240:241], v[242:243], v[236:237]
	v_pk_mul_f32 v[240:241], v[142:143], s[64:65] op_sel_hi:[1,0]
	v_lshlrev_b32_e32 v242, 16, v223
	v_and_b32_e32 v243, 0xffff0000, v223
	v_pk_fma_f32 v[238:239], v[240:241], v[242:243], v[238:239]
	v_pk_mul_f32 v[240:241], v[144:145], s[66:67] op_sel_hi:[1,0]
	v_lshlrev_b32_e32 v242, 16, v224
	v_and_b32_e32 v243, 0xffff0000, v224
	v_pk_fma_f32 v[232:233], v[240:241], v[242:243], v[232:233]
	v_pk_mul_f32 v[240:241], v[146:147], s[66:67] op_sel_hi:[1,0]
	v_lshlrev_b32_e32 v242, 16, v225
	v_and_b32_e32 v243, 0xffff0000, v225
	v_pk_fma_f32 v[234:235], v[240:241], v[242:243], v[234:235]
	v_pk_mul_f32 v[240:241], v[148:149], s[66:67] op_sel_hi:[1,0]
	v_lshlrev_b32_e32 v242, 16, v226
	v_and_b32_e32 v243, 0xffff0000, v226
	v_pk_fma_f32 v[236:237], v[240:241], v[242:243], v[236:237]
	v_pk_mul_f32 v[240:241], v[150:151], s[66:67] op_sel_hi:[1,0]
	v_lshlrev_b32_e32 v242, 16, v227
	v_and_b32_e32 v243, 0xffff0000, v227
	v_pk_fma_f32 v[238:239], v[240:241], v[242:243], v[238:239]
	v_pk_mul_f32 v[240:241], v[152:153], s[68:69] op_sel_hi:[1,0]
	v_lshlrev_b32_e32 v242, 16, v228
	v_and_b32_e32 v243, 0xffff0000, v228
	v_pk_fma_f32 v[232:233], v[240:241], v[242:243], v[232:233]
	v_pk_mul_f32 v[240:241], v[154:155], s[68:69] op_sel_hi:[1,0]
	v_lshlrev_b32_e32 v242, 16, v229
	v_and_b32_e32 v243, 0xffff0000, v229
	v_pk_fma_f32 v[234:235], v[240:241], v[242:243], v[234:235]
	v_pk_mul_f32 v[240:241], v[156:157], s[68:69] op_sel_hi:[1,0]
	v_lshlrev_b32_e32 v242, 16, v230
	v_and_b32_e32 v243, 0xffff0000, v230
	v_pk_fma_f32 v[236:237], v[240:241], v[242:243], v[236:237]
	v_pk_mul_f32 v[240:241], v[158:159], s[68:69] op_sel_hi:[1,0]
	v_lshlrev_b32_e32 v242, 16, v231
	v_and_b32_e32 v243, 0xffff0000, v231
	v_pk_fma_f32 v[238:239], v[240:241], v[242:243], v[238:239]
	v_cvt_pk_bf16_f32 v248, v232, v233
	v_cvt_pk_bf16_f32 v249, v234, v235
	v_cvt_pk_bf16_f32 v250, v236, v237
	v_cvt_pk_bf16_f32 v251, v238, v239
	s_lshl_b32 s58, s54, 11
	s_add_u32 s60, s52, s58
	s_addc_u32 s61, s53, 0
	global_store_dwordx4 v126, v[248:251], s[60:61]
	s_add_i32 s54, s41, 0x3800
	s_cmp_lt_u32 s54, 0x8000
	s_cselect_b32 s55, s70, s71
	s_and_b32 s56, s54, s55
	s_add_i32 s57, s55, 1
	s_add_i32 s58, s56, -2
	s_cmp_lt_u32 s58, s57
	s_cselect_b32 s58, -2, 0
	s_add_i32 s58, s54, s58
	s_mul_i32 s58, s58, 0x5a00
	s_add_u32 s60, s50, s58
	s_addc_u32 s61, s51, 0
	global_load_dwordx4 v[200:203], v126, s[60:61]
	s_add_i32 s58, s56, -1
	s_cmp_lt_u32 s58, s57
	s_cselect_b32 s58, -1, 0
	s_add_i32 s58, s54, s58
	s_mul_i32 s58, s58, 0x5a00
	s_add_u32 s60, s50, s58
	s_addc_u32 s61, s51, 0
	global_load_dwordx4 v[204:207], v126, s[60:61]
	s_mul_i32 s58, s54, 0x5a00
	s_add_u32 s60, s50, s58
	s_addc_u32 s61, s51, 0
	global_load_dwordx4 v[208:211], v126, s[60:61]
	s_add_i32 s58, s56, 1
	s_cmp_lt_u32 s58, s57
	s_cselect_b32 s58, 1, 0
	s_add_i32 s58, s54, s58
	s_mul_i32 s58, s58, 0x5a00
	s_add_u32 s60, s50, s58
	s_addc_u32 s61, s51, 0
	global_load_dwordx4 v[212:215], v126, s[60:61]
	s_add_i32 s54, s41, 0x3c00
	s_cmp_lt_u32 s54, 0x8000
	s_cselect_b32 s55, s70, s71
	s_and_b32 s56, s54, s55
	s_add_i32 s57, s55, 1
	s_add_i32 s58, s56, -2
	s_cmp_lt_u32 s58, s57
	s_cselect_b32 s58, -2, 0
	s_add_i32 s58, s54, s58
	s_mul_i32 s58, s58, 0x5a00
	s_add_u32 s60, s50, s58
	s_addc_u32 s61, s51, 0
	global_load_dwordx4 v[216:219], v126, s[60:61]
	s_add_i32 s58, s56, -1
	s_cmp_lt_u32 s58, s57
	s_cselect_b32 s58, -1, 0
	s_add_i32 s58, s54, s58
	s_mul_i32 s58, s58, 0x5a00
	s_add_u32 s60, s50, s58
	s_addc_u32 s61, s51, 0
	global_load_dwordx4 v[220:223], v126, s[60:61]
	s_mul_i32 s58, s54, 0x5a00
	s_add_u32 s60, s50, s58
	s_addc_u32 s61, s51, 0
	global_load_dwordx4 v[224:227], v126, s[60:61]
	s_add_i32 s58, s56, 1
	s_cmp_lt_u32 s58, s57
	s_cselect_b32 s58, 1, 0
	s_add_i32 s58, s54, s58
	s_mul_i32 s58, s58, 0x5a00
	s_add_u32 s60, s50, s58
	s_addc_u32 s61, s51, 0
	global_load_dwordx4 v[228:231], v126, s[60:61]
	s_waitcnt vmcnt(20)
	s_add_i32 s54, s41, 0x2800
	s_cmp_lt_u32 s54, 0x8000
	s_cselect_b32 s55, s70, s71
	s_and_b32 s56, s54, s55
	s_add_i32 s57, s55, 1
	s_add_i32 s58, s56, -2
	s_cmp_lt_u32 s58, s57
	s_cselect_b32 s62, 1.0, 0
	s_add_i32 s58, s56, -1
	s_cmp_lt_u32 s58, s57
	s_cselect_b32 s64, 1.0, 0
	s_mov_b32 s66, 1.0
	s_add_i32 s58, s56, 1
	s_cmp_lt_u32 s58, s57
	s_cselect_b32 s68, 1.0, 0
	v_pk_mul_f32 v[240:241], v[128:129], s[62:63] op_sel_hi:[1,0]
	v_lshlrev_b32_e32 v242, 16, v40
	v_and_b32_e32 v243, 0xffff0000, v40
	v_pk_fma_f32 v[232:233], v[240:241], v[242:243], v[160:161]
	v_pk_mul_f32 v[240:241], v[130:131], s[62:63] op_sel_hi:[1,0]
	v_lshlrev_b32_e32 v242, 16, v41
	v_and_b32_e32 v243, 0xffff0000, v41
	v_pk_fma_f32 v[234:235], v[240:241], v[242:243], v[162:163]
	v_pk_mul_f32 v[240:241], v[132:133], s[62:63] op_sel_hi:[1,0]
	v_lshlrev_b32_e32 v242, 16, v42
	v_and_b32_e32 v243, 0xffff0000, v42
	v_pk_fma_f32 v[236:237], v[240:241], v[242:243], v[164:165]
	v_pk_mul_f32 v[240:241], v[134:135], s[62:63] op_sel_hi:[1,0]
	v_lshlrev_b32_e32 v242, 16, v43
	v_and_b32_e32 v243, 0xffff0000, v43
	v_pk_fma_f32 v[238:239], v[240:241], v[242:243], v[166:167]
	v_pk_mul_f32 v[240:241], v[136:137], s[64:65] op_sel_hi:[1,0]
	v_lshlrev_b32_e32 v242, 16, v44
	v_and_b32_e32 v243, 0xffff0000, v44
	v_pk_fma_f32 v[232:233], v[240:241], v[242:243], v[232:233]
	v_pk_mul_f32 v[240:241], v[138:139], s[64:65] op_sel_hi:[1,0]
	v_lshlrev_b32_e32 v242, 16, v45
	v_and_b32_e32 v243, 0xffff0000, v45
	v_pk_fma_f32 v[234:235], v[240:241], v[242:243], v[234:235]
	v_pk_mul_f32 v[240:241], v[140:141], s[64:65] op_sel_hi:[1,0]
	v_lshlrev_b32_e32 v242, 16, v46
	v_and_b32_e32 v243, 0xffff0000, v46
	v_pk_fma_f32 v[236:237], v[240:241], v[242:243], v[236:237]
	v_pk_mul_f32 v[240:241], v[142:143], s[64:65] op_sel_hi:[1,0]
	v_lshlrev_b32_e32 v242, 16, v47
	v_and_b32_e32 v243, 0xffff0000, v47
	v_pk_fma_f32 v[238:239], v[240:241], v[242:243], v[238:239]
	v_pk_mul_f32 v[240:241], v[144:145], s[66:67] op_sel_hi:[1,0]
	v_lshlrev_b32_e32 v242, 16, v48
	v_and_b32_e32 v243, 0xffff0000, v48
	v_pk_fma_f32 v[232:233], v[240:241], v[242:243], v[232:233]
	v_pk_mul_f32 v[240:241], v[146:147], s[66:67] op_sel_hi:[1,0]
	v_lshlrev_b32_e32 v242, 16, v49
	v_and_b32_e32 v243, 0xffff0000, v49
	v_pk_fma_f32 v[234:235], v[240:241], v[242:243], v[234:235]
	v_pk_mul_f32 v[240:241], v[148:149], s[66:67] op_sel_hi:[1,0]
	v_lshlrev_b32_e32 v242, 16, v50
	v_and_b32_e32 v243, 0xffff0000, v50
	v_pk_fma_f32 v[236:237], v[240:241], v[242:243], v[236:237]
	v_pk_mul_f32 v[240:241], v[150:151], s[66:67] op_sel_hi:[1,0]
	v_lshlrev_b32_e32 v242, 16, v51
	v_and_b32_e32 v243, 0xffff0000, v51
	v_pk_fma_f32 v[238:239], v[240:241], v[242:243], v[238:239]
	v_pk_mul_f32 v[240:241], v[152:153], s[68:69] op_sel_hi:[1,0]
	v_lshlrev_b32_e32 v242, 16, v52
	v_and_b32_e32 v243, 0xffff0000, v52
	v_pk_fma_f32 v[232:233], v[240:241], v[242:243], v[232:233]
	v_pk_mul_f32 v[240:241], v[154:155], s[68:69] op_sel_hi:[1,0]
	v_lshlrev_b32_e32 v242, 16, v53
	v_and_b32_e32 v243, 0xffff0000, v53
	v_pk_fma_f32 v[234:235], v[240:241], v[242:243], v[234:235]
	v_pk_mul_f32 v[240:241], v[156:157], s[68:69] op_sel_hi:[1,0]
	v_lshlrev_b32_e32 v242, 16, v54
	v_and_b32_e32 v243, 0xffff0000, v54
	v_pk_fma_f32 v[236:237], v[240:241], v[242:243], v[236:237]
	v_pk_mul_f32 v[240:241], v[158:159], s[68:69] op_sel_hi:[1,0]
	v_lshlrev_b32_e32 v242, 16, v55
	v_and_b32_e32 v243, 0xffff0000, v55
	v_pk_fma_f32 v[238:239], v[240:241], v[242:243], v[238:239]
	v_cvt_pk_bf16_f32 v248, v232, v233
	v_cvt_pk_bf16_f32 v249, v234, v235
	v_cvt_pk_bf16_f32 v250, v236, v237
	v_cvt_pk_bf16_f32 v251, v238, v239
	s_lshl_b32 s58, s54, 11
	s_add_u32 s60, s52, s58
	s_addc_u32 s61, s53, 0
	global_store_dwordx4 v126, v[248:251], s[60:61]
	s_add_i32 s54, s41, 0x2c00
	s_cmp_lt_u32 s54, 0x8000
	s_cselect_b32 s55, s70, s71
	s_and_b32 s56, s54, s55
	s_add_i32 s57, s55, 1
	s_add_i32 s58, s56, -2
	s_cmp_lt_u32 s58, s57
	s_cselect_b32 s62, 1.0, 0
	s_add_i32 s58, s56, -1
	s_cmp_lt_u32 s58, s57
	s_cselect_b32 s64, 1.0, 0
	s_mov_b32 s66, 1.0
	s_add_i32 s58, s56, 1
	s_cmp_lt_u32 s58, s57
	s_cselect_b32 s68, 1.0, 0
	v_pk_mul_f32 v[240:241], v[128:129], s[62:63] op_sel_hi:[1,0]
	v_lshlrev_b32_e32 v242, 16, v56
	v_and_b32_e32 v243, 0xffff0000, v56
	v_pk_fma_f32 v[232:233], v[240:241], v[242:243], v[160:161]
	v_pk_mul_f32 v[240:241], v[130:131], s[62:63] op_sel_hi:[1,0]
	v_lshlrev_b32_e32 v242, 16, v57
	v_and_b32_e32 v243, 0xffff0000, v57
	v_pk_fma_f32 v[234:235], v[240:241], v[242:243], v[162:163]
	v_pk_mul_f32 v[240:241], v[132:133], s[62:63] op_sel_hi:[1,0]
	v_lshlrev_b32_e32 v242, 16, v58
	v_and_b32_e32 v243, 0xffff0000, v58
	v_pk_fma_f32 v[236:237], v[240:241], v[242:243], v[164:165]
	v_pk_mul_f32 v[240:241], v[134:135], s[62:63] op_sel_hi:[1,0]
	v_lshlrev_b32_e32 v242, 16, v59
	v_and_b32_e32 v243, 0xffff0000, v59
	v_pk_fma_f32 v[238:239], v[240:241], v[242:243], v[166:167]
	v_pk_mul_f32 v[240:241], v[136:137], s[64:65] op_sel_hi:[1,0]
	v_lshlrev_b32_e32 v242, 16, v60
	v_and_b32_e32 v243, 0xffff0000, v60
	v_pk_fma_f32 v[232:233], v[240:241], v[242:243], v[232:233]
	v_pk_mul_f32 v[240:241], v[138:139], s[64:65] op_sel_hi:[1,0]
	v_lshlrev_b32_e32 v242, 16, v61
	v_and_b32_e32 v243, 0xffff0000, v61
	v_pk_fma_f32 v[234:235], v[240:241], v[242:243], v[234:235]
	v_pk_mul_f32 v[240:241], v[140:141], s[64:65] op_sel_hi:[1,0]
	v_lshlrev_b32_e32 v242, 16, v62
	v_and_b32_e32 v243, 0xffff0000, v62
	v_pk_fma_f32 v[236:237], v[240:241], v[242:243], v[236:237]
	v_pk_mul_f32 v[240:241], v[142:143], s[64:65] op_sel_hi:[1,0]
	v_lshlrev_b32_e32 v242, 16, v63
	v_and_b32_e32 v243, 0xffff0000, v63
	v_pk_fma_f32 v[238:239], v[240:241], v[242:243], v[238:239]
	v_pk_mul_f32 v[240:241], v[144:145], s[66:67] op_sel_hi:[1,0]
	v_lshlrev_b32_e32 v242, 16, v64
	v_and_b32_e32 v243, 0xffff0000, v64
	v_pk_fma_f32 v[232:233], v[240:241], v[242:243], v[232:233]
	v_pk_mul_f32 v[240:241], v[146:147], s[66:67] op_sel_hi:[1,0]
	v_lshlrev_b32_e32 v242, 16, v65
	v_and_b32_e32 v243, 0xffff0000, v65
	v_pk_fma_f32 v[234:235], v[240:241], v[242:243], v[234:235]
	v_pk_mul_f32 v[240:241], v[148:149], s[66:67] op_sel_hi:[1,0]
	v_lshlrev_b32_e32 v242, 16, v66
	v_and_b32_e32 v243, 0xffff0000, v66
	v_pk_fma_f32 v[236:237], v[240:241], v[242:243], v[236:237]
	v_pk_mul_f32 v[240:241], v[150:151], s[66:67] op_sel_hi:[1,0]
	v_lshlrev_b32_e32 v242, 16, v67
	v_and_b32_e32 v243, 0xffff0000, v67
	v_pk_fma_f32 v[238:239], v[240:241], v[242:243], v[238:239]
	v_pk_mul_f32 v[240:241], v[152:153], s[68:69] op_sel_hi:[1,0]
	v_lshlrev_b32_e32 v242, 16, v68
	v_and_b32_e32 v243, 0xffff0000, v68
	v_pk_fma_f32 v[232:233], v[240:241], v[242:243], v[232:233]
	v_pk_mul_f32 v[240:241], v[154:155], s[68:69] op_sel_hi:[1,0]
	v_lshlrev_b32_e32 v242, 16, v69
	v_and_b32_e32 v243, 0xffff0000, v69
	v_pk_fma_f32 v[234:235], v[240:241], v[242:243], v[234:235]
	v_pk_mul_f32 v[240:241], v[156:157], s[68:69] op_sel_hi:[1,0]
	v_lshlrev_b32_e32 v242, 16, v70
	v_and_b32_e32 v243, 0xffff0000, v70
	v_pk_fma_f32 v[236:237], v[240:241], v[242:243], v[236:237]
	v_pk_mul_f32 v[240:241], v[158:159], s[68:69] op_sel_hi:[1,0]
	v_lshlrev_b32_e32 v242, 16, v71
	v_and_b32_e32 v243, 0xffff0000, v71
	v_pk_fma_f32 v[238:239], v[240:241], v[242:243], v[238:239]
	v_cvt_pk_bf16_f32 v248, v232, v233
	v_cvt_pk_bf16_f32 v249, v234, v235
	v_cvt_pk_bf16_f32 v250, v236, v237
	v_cvt_pk_bf16_f32 v251, v238, v239
	s_lshl_b32 s58, s54, 11
	s_add_u32 s60, s52, s58
	s_addc_u32 s61, s53, 0
	global_store_dwordx4 v126, v[248:251], s[60:61]
	s_add_i32 s54, s41, 0x4000
	s_cmp_lt_u32 s54, 0x8000
	s_cselect_b32 s55, s70, s71
	s_and_b32 s56, s54, s55
	s_add_i32 s57, s55, 1
	s_add_i32 s58, s56, -2
	s_cmp_lt_u32 s58, s57
	s_cselect_b32 s58, -2, 0
	s_add_i32 s58, s54, s58
	s_mul_i32 s58, s58, 0x5a00
	s_add_u32 s60, s50, s58
	s_addc_u32 s61, s51, 0
	global_load_dwordx4 v[40:43], v126, s[60:61]
	s_add_i32 s58, s56, -1
	s_cmp_lt_u32 s58, s57
	s_cselect_b32 s58, -1, 0
	s_add_i32 s58, s54, s58
	s_mul_i32 s58, s58, 0x5a00
	s_add_u32 s60, s50, s58
	s_addc_u32 s61, s51, 0
	global_load_dwordx4 v[44:47], v126, s[60:61]
	s_mul_i32 s58, s54, 0x5a00
	s_add_u32 s60, s50, s58
	s_addc_u32 s61, s51, 0
	global_load_dwordx4 v[48:51], v126, s[60:61]
	s_add_i32 s58, s56, 1
	s_cmp_lt_u32 s58, s57
	s_cselect_b32 s58, 1, 0
	s_add_i32 s58, s54, s58
	s_mul_i32 s58, s58, 0x5a00
	s_add_u32 s60, s50, s58
	s_addc_u32 s61, s51, 0
	global_load_dwordx4 v[52:55], v126, s[60:61]
	s_add_i32 s54, s41, 0x4400
	s_cmp_lt_u32 s54, 0x8000
	s_cselect_b32 s55, s70, s71
	s_and_b32 s56, s54, s55
	s_add_i32 s57, s55, 1
	s_add_i32 s58, s56, -2
	s_cmp_lt_u32 s58, s57
	s_cselect_b32 s58, -2, 0
	s_add_i32 s58, s54, s58
	s_mul_i32 s58, s58, 0x5a00
	s_add_u32 s60, s50, s58
	s_addc_u32 s61, s51, 0
	global_load_dwordx4 v[56:59], v126, s[60:61]
	s_add_i32 s58, s56, -1
	s_cmp_lt_u32 s58, s57
	s_cselect_b32 s58, -1, 0
	s_add_i32 s58, s54, s58
	s_mul_i32 s58, s58, 0x5a00
	s_add_u32 s60, s50, s58
	s_addc_u32 s61, s51, 0
	global_load_dwordx4 v[60:63], v126, s[60:61]
	s_mul_i32 s58, s54, 0x5a00
	s_add_u32 s60, s50, s58
	s_addc_u32 s61, s51, 0
	global_load_dwordx4 v[64:67], v126, s[60:61]
	s_add_i32 s58, s56, 1
	s_cmp_lt_u32 s58, s57
	s_cselect_b32 s58, 1, 0
	s_add_i32 s58, s54, s58
	s_mul_i32 s58, s58, 0x5a00
	s_add_u32 s60, s50, s58
	s_addc_u32 s61, s51, 0
	global_load_dwordx4 v[68:71], v126, s[60:61]
	s_waitcnt vmcnt(20)
	s_add_i32 s54, s41, 0x3000
	s_cmp_lt_u32 s54, 0x8000
	s_cselect_b32 s55, s70, s71
	s_and_b32 s56, s54, s55
	s_add_i32 s57, s55, 1
	s_add_i32 s58, s56, -2
	s_cmp_lt_u32 s58, s57
	s_cselect_b32 s62, 1.0, 0
	s_add_i32 s58, s56, -1
	s_cmp_lt_u32 s58, s57
	s_cselect_b32 s64, 1.0, 0
	s_mov_b32 s66, 1.0
	s_add_i32 s58, s56, 1
	s_cmp_lt_u32 s58, s57
	s_cselect_b32 s68, 1.0, 0
	v_pk_mul_f32 v[240:241], v[128:129], s[62:63] op_sel_hi:[1,0]
	v_lshlrev_b32_e32 v242, 16, v168
	v_and_b32_e32 v243, 0xffff0000, v168
	v_pk_fma_f32 v[232:233], v[240:241], v[242:243], v[160:161]
	v_pk_mul_f32 v[240:241], v[130:131], s[62:63] op_sel_hi:[1,0]
	v_lshlrev_b32_e32 v242, 16, v169
	v_and_b32_e32 v243, 0xffff0000, v169
	v_pk_fma_f32 v[234:235], v[240:241], v[242:243], v[162:163]
	v_pk_mul_f32 v[240:241], v[132:133], s[62:63] op_sel_hi:[1,0]
	v_lshlrev_b32_e32 v242, 16, v170
	v_and_b32_e32 v243, 0xffff0000, v170
	v_pk_fma_f32 v[236:237], v[240:241], v[242:243], v[164:165]
	v_pk_mul_f32 v[240:241], v[134:135], s[62:63] op_sel_hi:[1,0]
	v_lshlrev_b32_e32 v242, 16, v171
	v_and_b32_e32 v243, 0xffff0000, v171
	v_pk_fma_f32 v[238:239], v[240:241], v[242:243], v[166:167]
	v_pk_mul_f32 v[240:241], v[136:137], s[64:65] op_sel_hi:[1,0]
	v_lshlrev_b32_e32 v242, 16, v172
	v_and_b32_e32 v243, 0xffff0000, v172
	v_pk_fma_f32 v[232:233], v[240:241], v[242:243], v[232:233]
	v_pk_mul_f32 v[240:241], v[138:139], s[64:65] op_sel_hi:[1,0]
	v_lshlrev_b32_e32 v242, 16, v173
	v_and_b32_e32 v243, 0xffff0000, v173
	v_pk_fma_f32 v[234:235], v[240:241], v[242:243], v[234:235]
	v_pk_mul_f32 v[240:241], v[140:141], s[64:65] op_sel_hi:[1,0]
	v_lshlrev_b32_e32 v242, 16, v174
	v_and_b32_e32 v243, 0xffff0000, v174
	v_pk_fma_f32 v[236:237], v[240:241], v[242:243], v[236:237]
	v_pk_mul_f32 v[240:241], v[142:143], s[64:65] op_sel_hi:[1,0]
	v_lshlrev_b32_e32 v242, 16, v175
	v_and_b32_e32 v243, 0xffff0000, v175
	v_pk_fma_f32 v[238:239], v[240:241], v[242:243], v[238:239]
	v_pk_mul_f32 v[240:241], v[144:145], s[66:67] op_sel_hi:[1,0]
	v_lshlrev_b32_e32 v242, 16, v176
	v_and_b32_e32 v243, 0xffff0000, v176
	v_pk_fma_f32 v[232:233], v[240:241], v[242:243], v[232:233]
	v_pk_mul_f32 v[240:241], v[146:147], s[66:67] op_sel_hi:[1,0]
	v_lshlrev_b32_e32 v242, 16, v177
	v_and_b32_e32 v243, 0xffff0000, v177
	v_pk_fma_f32 v[234:235], v[240:241], v[242:243], v[234:235]
	v_pk_mul_f32 v[240:241], v[148:149], s[66:67] op_sel_hi:[1,0]
	v_lshlrev_b32_e32 v242, 16, v178
	v_and_b32_e32 v243, 0xffff0000, v178
	v_pk_fma_f32 v[236:237], v[240:241], v[242:243], v[236:237]
	v_pk_mul_f32 v[240:241], v[150:151], s[66:67] op_sel_hi:[1,0]
	v_lshlrev_b32_e32 v242, 16, v179
	v_and_b32_e32 v243, 0xffff0000, v179
	v_pk_fma_f32 v[238:239], v[240:241], v[242:243], v[238:239]
	v_pk_mul_f32 v[240:241], v[152:153], s[68:69] op_sel_hi:[1,0]
	v_lshlrev_b32_e32 v242, 16, v180
	v_and_b32_e32 v243, 0xffff0000, v180
	v_pk_fma_f32 v[232:233], v[240:241], v[242:243], v[232:233]
	v_pk_mul_f32 v[240:241], v[154:155], s[68:69] op_sel_hi:[1,0]
	v_lshlrev_b32_e32 v242, 16, v181
	v_and_b32_e32 v243, 0xffff0000, v181
	v_pk_fma_f32 v[234:235], v[240:241], v[242:243], v[234:235]
	v_pk_mul_f32 v[240:241], v[156:157], s[68:69] op_sel_hi:[1,0]
	v_lshlrev_b32_e32 v242, 16, v182
	v_and_b32_e32 v243, 0xffff0000, v182
	v_pk_fma_f32 v[236:237], v[240:241], v[242:243], v[236:237]
	v_pk_mul_f32 v[240:241], v[158:159], s[68:69] op_sel_hi:[1,0]
	v_lshlrev_b32_e32 v242, 16, v183
	v_and_b32_e32 v243, 0xffff0000, v183
	v_pk_fma_f32 v[238:239], v[240:241], v[242:243], v[238:239]
	v_cvt_pk_bf16_f32 v248, v232, v233
	v_cvt_pk_bf16_f32 v249, v234, v235
	v_cvt_pk_bf16_f32 v250, v236, v237
	v_cvt_pk_bf16_f32 v251, v238, v239
	s_lshl_b32 s58, s54, 11
	s_add_u32 s60, s52, s58
	s_addc_u32 s61, s53, 0
	global_store_dwordx4 v126, v[248:251], s[60:61]
	s_add_i32 s54, s41, 0x3400
	s_cmp_lt_u32 s54, 0x8000
	s_cselect_b32 s55, s70, s71
	s_and_b32 s56, s54, s55
	s_add_i32 s57, s55, 1
	s_add_i32 s58, s56, -2
	s_cmp_lt_u32 s58, s57
	s_cselect_b32 s62, 1.0, 0
	s_add_i32 s58, s56, -1
	s_cmp_lt_u32 s58, s57
	s_cselect_b32 s64, 1.0, 0
	s_mov_b32 s66, 1.0
	s_add_i32 s58, s56, 1
	s_cmp_lt_u32 s58, s57
	s_cselect_b32 s68, 1.0, 0
	v_pk_mul_f32 v[240:241], v[128:129], s[62:63] op_sel_hi:[1,0]
	v_lshlrev_b32_e32 v242, 16, v184
	v_and_b32_e32 v243, 0xffff0000, v184
	v_pk_fma_f32 v[232:233], v[240:241], v[242:243], v[160:161]
	v_pk_mul_f32 v[240:241], v[130:131], s[62:63] op_sel_hi:[1,0]
	v_lshlrev_b32_e32 v242, 16, v185
	v_and_b32_e32 v243, 0xffff0000, v185
	v_pk_fma_f32 v[234:235], v[240:241], v[242:243], v[162:163]
	v_pk_mul_f32 v[240:241], v[132:133], s[62:63] op_sel_hi:[1,0]
	v_lshlrev_b32_e32 v242, 16, v186
	v_and_b32_e32 v243, 0xffff0000, v186
	v_pk_fma_f32 v[236:237], v[240:241], v[242:243], v[164:165]
	v_pk_mul_f32 v[240:241], v[134:135], s[62:63] op_sel_hi:[1,0]
	v_lshlrev_b32_e32 v242, 16, v187
	v_and_b32_e32 v243, 0xffff0000, v187
	v_pk_fma_f32 v[238:239], v[240:241], v[242:243], v[166:167]
	v_pk_mul_f32 v[240:241], v[136:137], s[64:65] op_sel_hi:[1,0]
	v_lshlrev_b32_e32 v242, 16, v188
	v_and_b32_e32 v243, 0xffff0000, v188
	v_pk_fma_f32 v[232:233], v[240:241], v[242:243], v[232:233]
	v_pk_mul_f32 v[240:241], v[138:139], s[64:65] op_sel_hi:[1,0]
	v_lshlrev_b32_e32 v242, 16, v189
	v_and_b32_e32 v243, 0xffff0000, v189
	v_pk_fma_f32 v[234:235], v[240:241], v[242:243], v[234:235]
	v_pk_mul_f32 v[240:241], v[140:141], s[64:65] op_sel_hi:[1,0]
	v_lshlrev_b32_e32 v242, 16, v190
	v_and_b32_e32 v243, 0xffff0000, v190
	v_pk_fma_f32 v[236:237], v[240:241], v[242:243], v[236:237]
	v_pk_mul_f32 v[240:241], v[142:143], s[64:65] op_sel_hi:[1,0]
	v_lshlrev_b32_e32 v242, 16, v191
	v_and_b32_e32 v243, 0xffff0000, v191
	v_pk_fma_f32 v[238:239], v[240:241], v[242:243], v[238:239]
	v_pk_mul_f32 v[240:241], v[144:145], s[66:67] op_sel_hi:[1,0]
	v_lshlrev_b32_e32 v242, 16, v192
	v_and_b32_e32 v243, 0xffff0000, v192
	v_pk_fma_f32 v[232:233], v[240:241], v[242:243], v[232:233]
	v_pk_mul_f32 v[240:241], v[146:147], s[66:67] op_sel_hi:[1,0]
	v_lshlrev_b32_e32 v242, 16, v193
	v_and_b32_e32 v243, 0xffff0000, v193
	v_pk_fma_f32 v[234:235], v[240:241], v[242:243], v[234:235]
	v_pk_mul_f32 v[240:241], v[148:149], s[66:67] op_sel_hi:[1,0]
	v_lshlrev_b32_e32 v242, 16, v194
	v_and_b32_e32 v243, 0xffff0000, v194
	v_pk_fma_f32 v[236:237], v[240:241], v[242:243], v[236:237]
	v_pk_mul_f32 v[240:241], v[150:151], s[66:67] op_sel_hi:[1,0]
	v_lshlrev_b32_e32 v242, 16, v195
	v_and_b32_e32 v243, 0xffff0000, v195
	v_pk_fma_f32 v[238:239], v[240:241], v[242:243], v[238:239]
	v_pk_mul_f32 v[240:241], v[152:153], s[68:69] op_sel_hi:[1,0]
	v_lshlrev_b32_e32 v242, 16, v196
	v_and_b32_e32 v243, 0xffff0000, v196
	v_pk_fma_f32 v[232:233], v[240:241], v[242:243], v[232:233]
	v_pk_mul_f32 v[240:241], v[154:155], s[68:69] op_sel_hi:[1,0]
	v_lshlrev_b32_e32 v242, 16, v197
	v_and_b32_e32 v243, 0xffff0000, v197
	v_pk_fma_f32 v[234:235], v[240:241], v[242:243], v[234:235]
	v_pk_mul_f32 v[240:241], v[156:157], s[68:69] op_sel_hi:[1,0]
	v_lshlrev_b32_e32 v242, 16, v198
	v_and_b32_e32 v243, 0xffff0000, v198
	v_pk_fma_f32 v[236:237], v[240:241], v[242:243], v[236:237]
	v_pk_mul_f32 v[240:241], v[158:159], s[68:69] op_sel_hi:[1,0]
	v_lshlrev_b32_e32 v242, 16, v199
	v_and_b32_e32 v243, 0xffff0000, v199
	v_pk_fma_f32 v[238:239], v[240:241], v[242:243], v[238:239]
	v_cvt_pk_bf16_f32 v248, v232, v233
	v_cvt_pk_bf16_f32 v249, v234, v235
	v_cvt_pk_bf16_f32 v250, v236, v237
	v_cvt_pk_bf16_f32 v251, v238, v239
	s_lshl_b32 s58, s54, 11
	s_add_u32 s60, s52, s58
	s_addc_u32 s61, s53, 0
	global_store_dwordx4 v126, v[248:251], s[60:61]
	s_add_i32 s54, s41, 0x4800
	s_cmp_lt_u32 s54, 0x8000
	s_cselect_b32 s55, s70, s71
	s_and_b32 s56, s54, s55
	s_add_i32 s57, s55, 1
	s_add_i32 s58, s56, -2
	s_cmp_lt_u32 s58, s57
	s_cselect_b32 s58, -2, 0
	s_add_i32 s58, s54, s58
	s_mul_i32 s58, s58, 0x5a00
	s_add_u32 s60, s50, s58
	s_addc_u32 s61, s51, 0
	global_load_dwordx4 v[168:171], v126, s[60:61]
	s_add_i32 s58, s56, -1
	s_cmp_lt_u32 s58, s57
	s_cselect_b32 s58, -1, 0
	s_add_i32 s58, s54, s58
	s_mul_i32 s58, s58, 0x5a00
	s_add_u32 s60, s50, s58
	s_addc_u32 s61, s51, 0
	global_load_dwordx4 v[172:175], v126, s[60:61]
	s_mul_i32 s58, s54, 0x5a00
	s_add_u32 s60, s50, s58
	s_addc_u32 s61, s51, 0
	global_load_dwordx4 v[176:179], v126, s[60:61]
	s_add_i32 s58, s56, 1
	s_cmp_lt_u32 s58, s57
	s_cselect_b32 s58, 1, 0
	s_add_i32 s58, s54, s58
	s_mul_i32 s58, s58, 0x5a00
	s_add_u32 s60, s50, s58
	s_addc_u32 s61, s51, 0
	global_load_dwordx4 v[180:183], v126, s[60:61]
	s_add_i32 s54, s41, 0x4c00
	s_cmp_lt_u32 s54, 0x8000
	s_cselect_b32 s55, s70, s71
	s_and_b32 s56, s54, s55
	s_add_i32 s57, s55, 1
	s_add_i32 s58, s56, -2
	s_cmp_lt_u32 s58, s57
	s_cselect_b32 s58, -2, 0
	s_add_i32 s58, s54, s58
	s_mul_i32 s58, s58, 0x5a00
	s_add_u32 s60, s50, s58
	s_addc_u32 s61, s51, 0
	global_load_dwordx4 v[184:187], v126, s[60:61]
	s_add_i32 s58, s56, -1
	s_cmp_lt_u32 s58, s57
	s_cselect_b32 s58, -1, 0
	s_add_i32 s58, s54, s58
	s_mul_i32 s58, s58, 0x5a00
	s_add_u32 s60, s50, s58
	s_addc_u32 s61, s51, 0
	global_load_dwordx4 v[188:191], v126, s[60:61]
	s_mul_i32 s58, s54, 0x5a00
	s_add_u32 s60, s50, s58
	s_addc_u32 s61, s51, 0
	global_load_dwordx4 v[192:195], v126, s[60:61]
	s_add_i32 s58, s56, 1
	s_cmp_lt_u32 s58, s57
	s_cselect_b32 s58, 1, 0
	s_add_i32 s58, s54, s58
	s_mul_i32 s58, s58, 0x5a00
	s_add_u32 s60, s50, s58
	s_addc_u32 s61, s51, 0
	global_load_dwordx4 v[196:199], v126, s[60:61]
	s_waitcnt vmcnt(20)
	s_add_i32 s54, s41, 0x3800
	s_cmp_lt_u32 s54, 0x8000
	s_cselect_b32 s55, s70, s71
	s_and_b32 s56, s54, s55
	s_add_i32 s57, s55, 1
	s_add_i32 s58, s56, -2
	s_cmp_lt_u32 s58, s57
	s_cselect_b32 s62, 1.0, 0
	s_add_i32 s58, s56, -1
	s_cmp_lt_u32 s58, s57
	s_cselect_b32 s64, 1.0, 0
	s_mov_b32 s66, 1.0
	s_add_i32 s58, s56, 1
	s_cmp_lt_u32 s58, s57
	s_cselect_b32 s68, 1.0, 0
	v_pk_mul_f32 v[240:241], v[128:129], s[62:63] op_sel_hi:[1,0]
	v_lshlrev_b32_e32 v242, 16, v200
	v_and_b32_e32 v243, 0xffff0000, v200
	v_pk_fma_f32 v[232:233], v[240:241], v[242:243], v[160:161]
	v_pk_mul_f32 v[240:241], v[130:131], s[62:63] op_sel_hi:[1,0]
	v_lshlrev_b32_e32 v242, 16, v201
	v_and_b32_e32 v243, 0xffff0000, v201
	v_pk_fma_f32 v[234:235], v[240:241], v[242:243], v[162:163]
	v_pk_mul_f32 v[240:241], v[132:133], s[62:63] op_sel_hi:[1,0]
	v_lshlrev_b32_e32 v242, 16, v202
	v_and_b32_e32 v243, 0xffff0000, v202
	v_pk_fma_f32 v[236:237], v[240:241], v[242:243], v[164:165]
	v_pk_mul_f32 v[240:241], v[134:135], s[62:63] op_sel_hi:[1,0]
	v_lshlrev_b32_e32 v242, 16, v203
	v_and_b32_e32 v243, 0xffff0000, v203
	v_pk_fma_f32 v[238:239], v[240:241], v[242:243], v[166:167]
	v_pk_mul_f32 v[240:241], v[136:137], s[64:65] op_sel_hi:[1,0]
	v_lshlrev_b32_e32 v242, 16, v204
	v_and_b32_e32 v243, 0xffff0000, v204
	v_pk_fma_f32 v[232:233], v[240:241], v[242:243], v[232:233]
	v_pk_mul_f32 v[240:241], v[138:139], s[64:65] op_sel_hi:[1,0]
	v_lshlrev_b32_e32 v242, 16, v205
	v_and_b32_e32 v243, 0xffff0000, v205
	v_pk_fma_f32 v[234:235], v[240:241], v[242:243], v[234:235]
	v_pk_mul_f32 v[240:241], v[140:141], s[64:65] op_sel_hi:[1,0]
	v_lshlrev_b32_e32 v242, 16, v206
	v_and_b32_e32 v243, 0xffff0000, v206
	v_pk_fma_f32 v[236:237], v[240:241], v[242:243], v[236:237]
	v_pk_mul_f32 v[240:241], v[142:143], s[64:65] op_sel_hi:[1,0]
	v_lshlrev_b32_e32 v242, 16, v207
	v_and_b32_e32 v243, 0xffff0000, v207
	v_pk_fma_f32 v[238:239], v[240:241], v[242:243], v[238:239]
	v_pk_mul_f32 v[240:241], v[144:145], s[66:67] op_sel_hi:[1,0]
	v_lshlrev_b32_e32 v242, 16, v208
	v_and_b32_e32 v243, 0xffff0000, v208
	v_pk_fma_f32 v[232:233], v[240:241], v[242:243], v[232:233]
	v_pk_mul_f32 v[240:241], v[146:147], s[66:67] op_sel_hi:[1,0]
	v_lshlrev_b32_e32 v242, 16, v209
	v_and_b32_e32 v243, 0xffff0000, v209
	v_pk_fma_f32 v[234:235], v[240:241], v[242:243], v[234:235]
	v_pk_mul_f32 v[240:241], v[148:149], s[66:67] op_sel_hi:[1,0]
	v_lshlrev_b32_e32 v242, 16, v210
	v_and_b32_e32 v243, 0xffff0000, v210
	v_pk_fma_f32 v[236:237], v[240:241], v[242:243], v[236:237]
	v_pk_mul_f32 v[240:241], v[150:151], s[66:67] op_sel_hi:[1,0]
	v_lshlrev_b32_e32 v242, 16, v211
	v_and_b32_e32 v243, 0xffff0000, v211
	v_pk_fma_f32 v[238:239], v[240:241], v[242:243], v[238:239]
	v_pk_mul_f32 v[240:241], v[152:153], s[68:69] op_sel_hi:[1,0]
	v_lshlrev_b32_e32 v242, 16, v212
	v_and_b32_e32 v243, 0xffff0000, v212
	v_pk_fma_f32 v[232:233], v[240:241], v[242:243], v[232:233]
	v_pk_mul_f32 v[240:241], v[154:155], s[68:69] op_sel_hi:[1,0]
	v_lshlrev_b32_e32 v242, 16, v213
	v_and_b32_e32 v243, 0xffff0000, v213
	v_pk_fma_f32 v[234:235], v[240:241], v[242:243], v[234:235]
	v_pk_mul_f32 v[240:241], v[156:157], s[68:69] op_sel_hi:[1,0]
	v_lshlrev_b32_e32 v242, 16, v214
	v_and_b32_e32 v243, 0xffff0000, v214
	v_pk_fma_f32 v[236:237], v[240:241], v[242:243], v[236:237]
	v_pk_mul_f32 v[240:241], v[158:159], s[68:69] op_sel_hi:[1,0]
	v_lshlrev_b32_e32 v242, 16, v215
	v_and_b32_e32 v243, 0xffff0000, v215
	v_pk_fma_f32 v[238:239], v[240:241], v[242:243], v[238:239]
	v_cvt_pk_bf16_f32 v248, v232, v233
	v_cvt_pk_bf16_f32 v249, v234, v235
	v_cvt_pk_bf16_f32 v250, v236, v237
	v_cvt_pk_bf16_f32 v251, v238, v239
	s_lshl_b32 s58, s54, 11
	s_add_u32 s60, s52, s58
	s_addc_u32 s61, s53, 0
	global_store_dwordx4 v126, v[248:251], s[60:61]
	s_add_i32 s54, s41, 0x3c00
	s_cmp_lt_u32 s54, 0x8000
	s_cselect_b32 s55, s70, s71
	s_and_b32 s56, s54, s55
	s_add_i32 s57, s55, 1
	s_add_i32 s58, s56, -2
	s_cmp_lt_u32 s58, s57
	s_cselect_b32 s62, 1.0, 0
	s_add_i32 s58, s56, -1
	s_cmp_lt_u32 s58, s57
	s_cselect_b32 s64, 1.0, 0
	s_mov_b32 s66, 1.0
	s_add_i32 s58, s56, 1
	s_cmp_lt_u32 s58, s57
	s_cselect_b32 s68, 1.0, 0
	v_pk_mul_f32 v[240:241], v[128:129], s[62:63] op_sel_hi:[1,0]
	v_lshlrev_b32_e32 v242, 16, v216
	v_and_b32_e32 v243, 0xffff0000, v216
	v_pk_fma_f32 v[232:233], v[240:241], v[242:243], v[160:161]
	v_pk_mul_f32 v[240:241], v[130:131], s[62:63] op_sel_hi:[1,0]
	v_lshlrev_b32_e32 v242, 16, v217
	v_and_b32_e32 v243, 0xffff0000, v217
	v_pk_fma_f32 v[234:235], v[240:241], v[242:243], v[162:163]
	v_pk_mul_f32 v[240:241], v[132:133], s[62:63] op_sel_hi:[1,0]
	v_lshlrev_b32_e32 v242, 16, v218
	v_and_b32_e32 v243, 0xffff0000, v218
	v_pk_fma_f32 v[236:237], v[240:241], v[242:243], v[164:165]
	v_pk_mul_f32 v[240:241], v[134:135], s[62:63] op_sel_hi:[1,0]
	v_lshlrev_b32_e32 v242, 16, v219
	v_and_b32_e32 v243, 0xffff0000, v219
	v_pk_fma_f32 v[238:239], v[240:241], v[242:243], v[166:167]
	v_pk_mul_f32 v[240:241], v[136:137], s[64:65] op_sel_hi:[1,0]
	v_lshlrev_b32_e32 v242, 16, v220
	v_and_b32_e32 v243, 0xffff0000, v220
	v_pk_fma_f32 v[232:233], v[240:241], v[242:243], v[232:233]
	v_pk_mul_f32 v[240:241], v[138:139], s[64:65] op_sel_hi:[1,0]
	v_lshlrev_b32_e32 v242, 16, v221
	v_and_b32_e32 v243, 0xffff0000, v221
	v_pk_fma_f32 v[234:235], v[240:241], v[242:243], v[234:235]
	v_pk_mul_f32 v[240:241], v[140:141], s[64:65] op_sel_hi:[1,0]
	v_lshlrev_b32_e32 v242, 16, v222
	v_and_b32_e32 v243, 0xffff0000, v222
	v_pk_fma_f32 v[236:237], v[240:241], v[242:243], v[236:237]
	v_pk_mul_f32 v[240:241], v[142:143], s[64:65] op_sel_hi:[1,0]
	v_lshlrev_b32_e32 v242, 16, v223
	v_and_b32_e32 v243, 0xffff0000, v223
	v_pk_fma_f32 v[238:239], v[240:241], v[242:243], v[238:239]
	v_pk_mul_f32 v[240:241], v[144:145], s[66:67] op_sel_hi:[1,0]
	v_lshlrev_b32_e32 v242, 16, v224
	v_and_b32_e32 v243, 0xffff0000, v224
	v_pk_fma_f32 v[232:233], v[240:241], v[242:243], v[232:233]
	v_pk_mul_f32 v[240:241], v[146:147], s[66:67] op_sel_hi:[1,0]
	v_lshlrev_b32_e32 v242, 16, v225
	v_and_b32_e32 v243, 0xffff0000, v225
	v_pk_fma_f32 v[234:235], v[240:241], v[242:243], v[234:235]
	v_pk_mul_f32 v[240:241], v[148:149], s[66:67] op_sel_hi:[1,0]
	v_lshlrev_b32_e32 v242, 16, v226
	v_and_b32_e32 v243, 0xffff0000, v226
	v_pk_fma_f32 v[236:237], v[240:241], v[242:243], v[236:237]
	v_pk_mul_f32 v[240:241], v[150:151], s[66:67] op_sel_hi:[1,0]
	v_lshlrev_b32_e32 v242, 16, v227
	v_and_b32_e32 v243, 0xffff0000, v227
	v_pk_fma_f32 v[238:239], v[240:241], v[242:243], v[238:239]
	v_pk_mul_f32 v[240:241], v[152:153], s[68:69] op_sel_hi:[1,0]
	v_lshlrev_b32_e32 v242, 16, v228
	v_and_b32_e32 v243, 0xffff0000, v228
	v_pk_fma_f32 v[232:233], v[240:241], v[242:243], v[232:233]
	v_pk_mul_f32 v[240:241], v[154:155], s[68:69] op_sel_hi:[1,0]
	v_lshlrev_b32_e32 v242, 16, v229
	v_and_b32_e32 v243, 0xffff0000, v229
	v_pk_fma_f32 v[234:235], v[240:241], v[242:243], v[234:235]
	v_pk_mul_f32 v[240:241], v[156:157], s[68:69] op_sel_hi:[1,0]
	v_lshlrev_b32_e32 v242, 16, v230
	v_and_b32_e32 v243, 0xffff0000, v230
	v_pk_fma_f32 v[236:237], v[240:241], v[242:243], v[236:237]
	v_pk_mul_f32 v[240:241], v[158:159], s[68:69] op_sel_hi:[1,0]
	v_lshlrev_b32_e32 v242, 16, v231
	v_and_b32_e32 v243, 0xffff0000, v231
	v_pk_fma_f32 v[238:239], v[240:241], v[242:243], v[238:239]
	v_cvt_pk_bf16_f32 v248, v232, v233
	v_cvt_pk_bf16_f32 v249, v234, v235
	v_cvt_pk_bf16_f32 v250, v236, v237
	v_cvt_pk_bf16_f32 v251, v238, v239
	s_lshl_b32 s58, s54, 11
	s_add_u32 s60, s52, s58
	s_addc_u32 s61, s53, 0
	global_store_dwordx4 v126, v[248:251], s[60:61]
	s_add_i32 s54, s41, 0x5000
	s_cmp_lt_u32 s54, 0x8000
	s_cselect_b32 s55, s70, s71
	s_and_b32 s56, s54, s55
	s_add_i32 s57, s55, 1
	s_add_i32 s58, s56, -2
	s_cmp_lt_u32 s58, s57
	s_cselect_b32 s58, -2, 0
	s_add_i32 s58, s54, s58
	s_mul_i32 s58, s58, 0x5a00
	s_add_u32 s60, s50, s58
	s_addc_u32 s61, s51, 0
	global_load_dwordx4 v[200:203], v126, s[60:61]
	s_add_i32 s58, s56, -1
	s_cmp_lt_u32 s58, s57
	s_cselect_b32 s58, -1, 0
	s_add_i32 s58, s54, s58
	s_mul_i32 s58, s58, 0x5a00
	s_add_u32 s60, s50, s58
	s_addc_u32 s61, s51, 0
	global_load_dwordx4 v[204:207], v126, s[60:61]
	s_mul_i32 s58, s54, 0x5a00
	s_add_u32 s60, s50, s58
	s_addc_u32 s61, s51, 0
	global_load_dwordx4 v[208:211], v126, s[60:61]
	s_add_i32 s58, s56, 1
	s_cmp_lt_u32 s58, s57
	s_cselect_b32 s58, 1, 0
	s_add_i32 s58, s54, s58
	s_mul_i32 s58, s58, 0x5a00
	s_add_u32 s60, s50, s58
	s_addc_u32 s61, s51, 0
	global_load_dwordx4 v[212:215], v126, s[60:61]
	s_add_i32 s54, s41, 0x5400
	s_cmp_lt_u32 s54, 0x8000
	s_cselect_b32 s55, s70, s71
	s_and_b32 s56, s54, s55
	s_add_i32 s57, s55, 1
	s_add_i32 s58, s56, -2
	s_cmp_lt_u32 s58, s57
	s_cselect_b32 s58, -2, 0
	s_add_i32 s58, s54, s58
	s_mul_i32 s58, s58, 0x5a00
	s_add_u32 s60, s50, s58
	s_addc_u32 s61, s51, 0
	global_load_dwordx4 v[216:219], v126, s[60:61]
	s_add_i32 s58, s56, -1
	s_cmp_lt_u32 s58, s57
	s_cselect_b32 s58, -1, 0
	s_add_i32 s58, s54, s58
	s_mul_i32 s58, s58, 0x5a00
	s_add_u32 s60, s50, s58
	s_addc_u32 s61, s51, 0
	global_load_dwordx4 v[220:223], v126, s[60:61]
	s_mul_i32 s58, s54, 0x5a00
	s_add_u32 s60, s50, s58
	s_addc_u32 s61, s51, 0
	global_load_dwordx4 v[224:227], v126, s[60:61]
	s_add_i32 s58, s56, 1
	s_cmp_lt_u32 s58, s57
	s_cselect_b32 s58, 1, 0
	s_add_i32 s58, s54, s58
	s_mul_i32 s58, s58, 0x5a00
	s_add_u32 s60, s50, s58
	s_addc_u32 s61, s51, 0
	global_load_dwordx4 v[228:231], v126, s[60:61]
	s_waitcnt vmcnt(20)
	s_add_i32 s54, s41, 0x4000
	s_cmp_lt_u32 s54, 0x8000
	s_cselect_b32 s55, s70, s71
	s_and_b32 s56, s54, s55
	s_add_i32 s57, s55, 1
	s_add_i32 s58, s56, -2
	s_cmp_lt_u32 s58, s57
	s_cselect_b32 s62, 1.0, 0
	s_add_i32 s58, s56, -1
	s_cmp_lt_u32 s58, s57
	s_cselect_b32 s64, 1.0, 0
	s_mov_b32 s66, 1.0
	s_add_i32 s58, s56, 1
	s_cmp_lt_u32 s58, s57
	s_cselect_b32 s68, 1.0, 0
	v_pk_mul_f32 v[240:241], v[128:129], s[62:63] op_sel_hi:[1,0]
	v_lshlrev_b32_e32 v242, 16, v40
	v_and_b32_e32 v243, 0xffff0000, v40
	v_pk_fma_f32 v[232:233], v[240:241], v[242:243], v[160:161]
	v_pk_mul_f32 v[240:241], v[130:131], s[62:63] op_sel_hi:[1,0]
	v_lshlrev_b32_e32 v242, 16, v41
	v_and_b32_e32 v243, 0xffff0000, v41
	v_pk_fma_f32 v[234:235], v[240:241], v[242:243], v[162:163]
	v_pk_mul_f32 v[240:241], v[132:133], s[62:63] op_sel_hi:[1,0]
	v_lshlrev_b32_e32 v242, 16, v42
	v_and_b32_e32 v243, 0xffff0000, v42
	v_pk_fma_f32 v[236:237], v[240:241], v[242:243], v[164:165]
	v_pk_mul_f32 v[240:241], v[134:135], s[62:63] op_sel_hi:[1,0]
	v_lshlrev_b32_e32 v242, 16, v43
	v_and_b32_e32 v243, 0xffff0000, v43
	v_pk_fma_f32 v[238:239], v[240:241], v[242:243], v[166:167]
	v_pk_mul_f32 v[240:241], v[136:137], s[64:65] op_sel_hi:[1,0]
	v_lshlrev_b32_e32 v242, 16, v44
	v_and_b32_e32 v243, 0xffff0000, v44
	v_pk_fma_f32 v[232:233], v[240:241], v[242:243], v[232:233]
	v_pk_mul_f32 v[240:241], v[138:139], s[64:65] op_sel_hi:[1,0]
	v_lshlrev_b32_e32 v242, 16, v45
	v_and_b32_e32 v243, 0xffff0000, v45
	v_pk_fma_f32 v[234:235], v[240:241], v[242:243], v[234:235]
	v_pk_mul_f32 v[240:241], v[140:141], s[64:65] op_sel_hi:[1,0]
	v_lshlrev_b32_e32 v242, 16, v46
	v_and_b32_e32 v243, 0xffff0000, v46
	v_pk_fma_f32 v[236:237], v[240:241], v[242:243], v[236:237]
	v_pk_mul_f32 v[240:241], v[142:143], s[64:65] op_sel_hi:[1,0]
	v_lshlrev_b32_e32 v242, 16, v47
	v_and_b32_e32 v243, 0xffff0000, v47
	v_pk_fma_f32 v[238:239], v[240:241], v[242:243], v[238:239]
	v_pk_mul_f32 v[240:241], v[144:145], s[66:67] op_sel_hi:[1,0]
	v_lshlrev_b32_e32 v242, 16, v48
	v_and_b32_e32 v243, 0xffff0000, v48
	v_pk_fma_f32 v[232:233], v[240:241], v[242:243], v[232:233]
	v_pk_mul_f32 v[240:241], v[146:147], s[66:67] op_sel_hi:[1,0]
	v_lshlrev_b32_e32 v242, 16, v49
	v_and_b32_e32 v243, 0xffff0000, v49
	v_pk_fma_f32 v[234:235], v[240:241], v[242:243], v[234:235]
	v_pk_mul_f32 v[240:241], v[148:149], s[66:67] op_sel_hi:[1,0]
	v_lshlrev_b32_e32 v242, 16, v50
	v_and_b32_e32 v243, 0xffff0000, v50
	v_pk_fma_f32 v[236:237], v[240:241], v[242:243], v[236:237]
	v_pk_mul_f32 v[240:241], v[150:151], s[66:67] op_sel_hi:[1,0]
	v_lshlrev_b32_e32 v242, 16, v51
	v_and_b32_e32 v243, 0xffff0000, v51
	v_pk_fma_f32 v[238:239], v[240:241], v[242:243], v[238:239]
	v_pk_mul_f32 v[240:241], v[152:153], s[68:69] op_sel_hi:[1,0]
	v_lshlrev_b32_e32 v242, 16, v52
	v_and_b32_e32 v243, 0xffff0000, v52
	v_pk_fma_f32 v[232:233], v[240:241], v[242:243], v[232:233]
	v_pk_mul_f32 v[240:241], v[154:155], s[68:69] op_sel_hi:[1,0]
	v_lshlrev_b32_e32 v242, 16, v53
	v_and_b32_e32 v243, 0xffff0000, v53
	v_pk_fma_f32 v[234:235], v[240:241], v[242:243], v[234:235]
	v_pk_mul_f32 v[240:241], v[156:157], s[68:69] op_sel_hi:[1,0]
	v_lshlrev_b32_e32 v242, 16, v54
	v_and_b32_e32 v243, 0xffff0000, v54
	v_pk_fma_f32 v[236:237], v[240:241], v[242:243], v[236:237]
	v_pk_mul_f32 v[240:241], v[158:159], s[68:69] op_sel_hi:[1,0]
	v_lshlrev_b32_e32 v242, 16, v55
	v_and_b32_e32 v243, 0xffff0000, v55
	v_pk_fma_f32 v[238:239], v[240:241], v[242:243], v[238:239]
	v_cvt_pk_bf16_f32 v248, v232, v233
	v_cvt_pk_bf16_f32 v249, v234, v235
	v_cvt_pk_bf16_f32 v250, v236, v237
	v_cvt_pk_bf16_f32 v251, v238, v239
	s_lshl_b32 s58, s54, 11
	s_add_u32 s60, s52, s58
	s_addc_u32 s61, s53, 0
	global_store_dwordx4 v126, v[248:251], s[60:61]
	s_add_i32 s54, s41, 0x4400
	s_cmp_lt_u32 s54, 0x8000
	s_cselect_b32 s55, s70, s71
	s_and_b32 s56, s54, s55
	s_add_i32 s57, s55, 1
	s_add_i32 s58, s56, -2
	s_cmp_lt_u32 s58, s57
	s_cselect_b32 s62, 1.0, 0
	s_add_i32 s58, s56, -1
	s_cmp_lt_u32 s58, s57
	s_cselect_b32 s64, 1.0, 0
	s_mov_b32 s66, 1.0
	s_add_i32 s58, s56, 1
	s_cmp_lt_u32 s58, s57
	s_cselect_b32 s68, 1.0, 0
	v_pk_mul_f32 v[240:241], v[128:129], s[62:63] op_sel_hi:[1,0]
	v_lshlrev_b32_e32 v242, 16, v56
	v_and_b32_e32 v243, 0xffff0000, v56
	v_pk_fma_f32 v[232:233], v[240:241], v[242:243], v[160:161]
	v_pk_mul_f32 v[240:241], v[130:131], s[62:63] op_sel_hi:[1,0]
	v_lshlrev_b32_e32 v242, 16, v57
	v_and_b32_e32 v243, 0xffff0000, v57
	v_pk_fma_f32 v[234:235], v[240:241], v[242:243], v[162:163]
	v_pk_mul_f32 v[240:241], v[132:133], s[62:63] op_sel_hi:[1,0]
	v_lshlrev_b32_e32 v242, 16, v58
	v_and_b32_e32 v243, 0xffff0000, v58
	v_pk_fma_f32 v[236:237], v[240:241], v[242:243], v[164:165]
	v_pk_mul_f32 v[240:241], v[134:135], s[62:63] op_sel_hi:[1,0]
	v_lshlrev_b32_e32 v242, 16, v59
	v_and_b32_e32 v243, 0xffff0000, v59
	v_pk_fma_f32 v[238:239], v[240:241], v[242:243], v[166:167]
	v_pk_mul_f32 v[240:241], v[136:137], s[64:65] op_sel_hi:[1,0]
	v_lshlrev_b32_e32 v242, 16, v60
	v_and_b32_e32 v243, 0xffff0000, v60
	v_pk_fma_f32 v[232:233], v[240:241], v[242:243], v[232:233]
	v_pk_mul_f32 v[240:241], v[138:139], s[64:65] op_sel_hi:[1,0]
	v_lshlrev_b32_e32 v242, 16, v61
	v_and_b32_e32 v243, 0xffff0000, v61
	v_pk_fma_f32 v[234:235], v[240:241], v[242:243], v[234:235]
	v_pk_mul_f32 v[240:241], v[140:141], s[64:65] op_sel_hi:[1,0]
	v_lshlrev_b32_e32 v242, 16, v62
	v_and_b32_e32 v243, 0xffff0000, v62
	v_pk_fma_f32 v[236:237], v[240:241], v[242:243], v[236:237]
	v_pk_mul_f32 v[240:241], v[142:143], s[64:65] op_sel_hi:[1,0]
	v_lshlrev_b32_e32 v242, 16, v63
	v_and_b32_e32 v243, 0xffff0000, v63
	v_pk_fma_f32 v[238:239], v[240:241], v[242:243], v[238:239]
	v_pk_mul_f32 v[240:241], v[144:145], s[66:67] op_sel_hi:[1,0]
	v_lshlrev_b32_e32 v242, 16, v64
	v_and_b32_e32 v243, 0xffff0000, v64
	v_pk_fma_f32 v[232:233], v[240:241], v[242:243], v[232:233]
	v_pk_mul_f32 v[240:241], v[146:147], s[66:67] op_sel_hi:[1,0]
	v_lshlrev_b32_e32 v242, 16, v65
	v_and_b32_e32 v243, 0xffff0000, v65
	v_pk_fma_f32 v[234:235], v[240:241], v[242:243], v[234:235]
	v_pk_mul_f32 v[240:241], v[148:149], s[66:67] op_sel_hi:[1,0]
	v_lshlrev_b32_e32 v242, 16, v66
	v_and_b32_e32 v243, 0xffff0000, v66
	v_pk_fma_f32 v[236:237], v[240:241], v[242:243], v[236:237]
	v_pk_mul_f32 v[240:241], v[150:151], s[66:67] op_sel_hi:[1,0]
	v_lshlrev_b32_e32 v242, 16, v67
	v_and_b32_e32 v243, 0xffff0000, v67
	v_pk_fma_f32 v[238:239], v[240:241], v[242:243], v[238:239]
	v_pk_mul_f32 v[240:241], v[152:153], s[68:69] op_sel_hi:[1,0]
	v_lshlrev_b32_e32 v242, 16, v68
	v_and_b32_e32 v243, 0xffff0000, v68
	v_pk_fma_f32 v[232:233], v[240:241], v[242:243], v[232:233]
	v_pk_mul_f32 v[240:241], v[154:155], s[68:69] op_sel_hi:[1,0]
	v_lshlrev_b32_e32 v242, 16, v69
	v_and_b32_e32 v243, 0xffff0000, v69
	v_pk_fma_f32 v[234:235], v[240:241], v[242:243], v[234:235]
	v_pk_mul_f32 v[240:241], v[156:157], s[68:69] op_sel_hi:[1,0]
	v_lshlrev_b32_e32 v242, 16, v70
	v_and_b32_e32 v243, 0xffff0000, v70
	v_pk_fma_f32 v[236:237], v[240:241], v[242:243], v[236:237]
	v_pk_mul_f32 v[240:241], v[158:159], s[68:69] op_sel_hi:[1,0]
	v_lshlrev_b32_e32 v242, 16, v71
	v_and_b32_e32 v243, 0xffff0000, v71
	v_pk_fma_f32 v[238:239], v[240:241], v[242:243], v[238:239]
	v_cvt_pk_bf16_f32 v248, v232, v233
	v_cvt_pk_bf16_f32 v249, v234, v235
	v_cvt_pk_bf16_f32 v250, v236, v237
	v_cvt_pk_bf16_f32 v251, v238, v239
	s_lshl_b32 s58, s54, 11
	s_add_u32 s60, s52, s58
	s_addc_u32 s61, s53, 0
	global_store_dwordx4 v126, v[248:251], s[60:61]
	s_add_i32 s54, s41, 0x5800
	s_cmp_lt_u32 s54, 0x8000
	s_cselect_b32 s55, s70, s71
	s_and_b32 s56, s54, s55
	s_add_i32 s57, s55, 1
	s_add_i32 s58, s56, -2
	s_cmp_lt_u32 s58, s57
	s_cselect_b32 s58, -2, 0
	s_add_i32 s58, s54, s58
	s_mul_i32 s58, s58, 0x5a00
	s_add_u32 s60, s50, s58
	s_addc_u32 s61, s51, 0
	global_load_dwordx4 v[40:43], v126, s[60:61]
	s_add_i32 s58, s56, -1
	s_cmp_lt_u32 s58, s57
	s_cselect_b32 s58, -1, 0
	s_add_i32 s58, s54, s58
	s_mul_i32 s58, s58, 0x5a00
	s_add_u32 s60, s50, s58
	s_addc_u32 s61, s51, 0
	global_load_dwordx4 v[44:47], v126, s[60:61]
	s_mul_i32 s58, s54, 0x5a00
	s_add_u32 s60, s50, s58
	s_addc_u32 s61, s51, 0
	global_load_dwordx4 v[48:51], v126, s[60:61]
	s_add_i32 s58, s56, 1
	s_cmp_lt_u32 s58, s57
	s_cselect_b32 s58, 1, 0
	s_add_i32 s58, s54, s58
	s_mul_i32 s58, s58, 0x5a00
	s_add_u32 s60, s50, s58
	s_addc_u32 s61, s51, 0
	global_load_dwordx4 v[52:55], v126, s[60:61]
	s_add_i32 s54, s41, 0x5c00
	s_cmp_lt_u32 s54, 0x8000
	s_cselect_b32 s55, s70, s71
	s_and_b32 s56, s54, s55
	s_add_i32 s57, s55, 1
	s_add_i32 s58, s56, -2
	s_cmp_lt_u32 s58, s57
	s_cselect_b32 s58, -2, 0
	s_add_i32 s58, s54, s58
	s_mul_i32 s58, s58, 0x5a00
	s_add_u32 s60, s50, s58
	s_addc_u32 s61, s51, 0
	global_load_dwordx4 v[56:59], v126, s[60:61]
	s_add_i32 s58, s56, -1
	s_cmp_lt_u32 s58, s57
	s_cselect_b32 s58, -1, 0
	s_add_i32 s58, s54, s58
	s_mul_i32 s58, s58, 0x5a00
	s_add_u32 s60, s50, s58
	s_addc_u32 s61, s51, 0
	global_load_dwordx4 v[60:63], v126, s[60:61]
	s_mul_i32 s58, s54, 0x5a00
	s_add_u32 s60, s50, s58
	s_addc_u32 s61, s51, 0
	global_load_dwordx4 v[64:67], v126, s[60:61]
	s_add_i32 s58, s56, 1
	s_cmp_lt_u32 s58, s57
	s_cselect_b32 s58, 1, 0
	s_add_i32 s58, s54, s58
	s_mul_i32 s58, s58, 0x5a00
	s_add_u32 s60, s50, s58
	s_addc_u32 s61, s51, 0
	global_load_dwordx4 v[68:71], v126, s[60:61]
	s_waitcnt vmcnt(20)
	s_add_i32 s54, s41, 0x4800
	s_cmp_lt_u32 s54, 0x8000
	s_cselect_b32 s55, s70, s71
	s_and_b32 s56, s54, s55
	s_add_i32 s57, s55, 1
	s_add_i32 s58, s56, -2
	s_cmp_lt_u32 s58, s57
	s_cselect_b32 s62, 1.0, 0
	s_add_i32 s58, s56, -1
	s_cmp_lt_u32 s58, s57
	s_cselect_b32 s64, 1.0, 0
	s_mov_b32 s66, 1.0
	s_add_i32 s58, s56, 1
	s_cmp_lt_u32 s58, s57
	s_cselect_b32 s68, 1.0, 0
	v_pk_mul_f32 v[240:241], v[128:129], s[62:63] op_sel_hi:[1,0]
	v_lshlrev_b32_e32 v242, 16, v168
	v_and_b32_e32 v243, 0xffff0000, v168
	v_pk_fma_f32 v[232:233], v[240:241], v[242:243], v[160:161]
	v_pk_mul_f32 v[240:241], v[130:131], s[62:63] op_sel_hi:[1,0]
	v_lshlrev_b32_e32 v242, 16, v169
	v_and_b32_e32 v243, 0xffff0000, v169
	v_pk_fma_f32 v[234:235], v[240:241], v[242:243], v[162:163]
	v_pk_mul_f32 v[240:241], v[132:133], s[62:63] op_sel_hi:[1,0]
	v_lshlrev_b32_e32 v242, 16, v170
	v_and_b32_e32 v243, 0xffff0000, v170
	v_pk_fma_f32 v[236:237], v[240:241], v[242:243], v[164:165]
	v_pk_mul_f32 v[240:241], v[134:135], s[62:63] op_sel_hi:[1,0]
	v_lshlrev_b32_e32 v242, 16, v171
	v_and_b32_e32 v243, 0xffff0000, v171
	v_pk_fma_f32 v[238:239], v[240:241], v[242:243], v[166:167]
	v_pk_mul_f32 v[240:241], v[136:137], s[64:65] op_sel_hi:[1,0]
	v_lshlrev_b32_e32 v242, 16, v172
	v_and_b32_e32 v243, 0xffff0000, v172
	v_pk_fma_f32 v[232:233], v[240:241], v[242:243], v[232:233]
	v_pk_mul_f32 v[240:241], v[138:139], s[64:65] op_sel_hi:[1,0]
	v_lshlrev_b32_e32 v242, 16, v173
	v_and_b32_e32 v243, 0xffff0000, v173
	v_pk_fma_f32 v[234:235], v[240:241], v[242:243], v[234:235]
	v_pk_mul_f32 v[240:241], v[140:141], s[64:65] op_sel_hi:[1,0]
	v_lshlrev_b32_e32 v242, 16, v174
	v_and_b32_e32 v243, 0xffff0000, v174
	v_pk_fma_f32 v[236:237], v[240:241], v[242:243], v[236:237]
	v_pk_mul_f32 v[240:241], v[142:143], s[64:65] op_sel_hi:[1,0]
	v_lshlrev_b32_e32 v242, 16, v175
	v_and_b32_e32 v243, 0xffff0000, v175
	v_pk_fma_f32 v[238:239], v[240:241], v[242:243], v[238:239]
	v_pk_mul_f32 v[240:241], v[144:145], s[66:67] op_sel_hi:[1,0]
	v_lshlrev_b32_e32 v242, 16, v176
	v_and_b32_e32 v243, 0xffff0000, v176
	v_pk_fma_f32 v[232:233], v[240:241], v[242:243], v[232:233]
	v_pk_mul_f32 v[240:241], v[146:147], s[66:67] op_sel_hi:[1,0]
	v_lshlrev_b32_e32 v242, 16, v177
	v_and_b32_e32 v243, 0xffff0000, v177
	v_pk_fma_f32 v[234:235], v[240:241], v[242:243], v[234:235]
	v_pk_mul_f32 v[240:241], v[148:149], s[66:67] op_sel_hi:[1,0]
	v_lshlrev_b32_e32 v242, 16, v178
	v_and_b32_e32 v243, 0xffff0000, v178
	v_pk_fma_f32 v[236:237], v[240:241], v[242:243], v[236:237]
	v_pk_mul_f32 v[240:241], v[150:151], s[66:67] op_sel_hi:[1,0]
	v_lshlrev_b32_e32 v242, 16, v179
	v_and_b32_e32 v243, 0xffff0000, v179
	v_pk_fma_f32 v[238:239], v[240:241], v[242:243], v[238:239]
	v_pk_mul_f32 v[240:241], v[152:153], s[68:69] op_sel_hi:[1,0]
	v_lshlrev_b32_e32 v242, 16, v180
	v_and_b32_e32 v243, 0xffff0000, v180
	v_pk_fma_f32 v[232:233], v[240:241], v[242:243], v[232:233]
	v_pk_mul_f32 v[240:241], v[154:155], s[68:69] op_sel_hi:[1,0]
	v_lshlrev_b32_e32 v242, 16, v181
	v_and_b32_e32 v243, 0xffff0000, v181
	v_pk_fma_f32 v[234:235], v[240:241], v[242:243], v[234:235]
	v_pk_mul_f32 v[240:241], v[156:157], s[68:69] op_sel_hi:[1,0]
	v_lshlrev_b32_e32 v242, 16, v182
	v_and_b32_e32 v243, 0xffff0000, v182
	v_pk_fma_f32 v[236:237], v[240:241], v[242:243], v[236:237]
	v_pk_mul_f32 v[240:241], v[158:159], s[68:69] op_sel_hi:[1,0]
	v_lshlrev_b32_e32 v242, 16, v183
	v_and_b32_e32 v243, 0xffff0000, v183
	v_pk_fma_f32 v[238:239], v[240:241], v[242:243], v[238:239]
	v_cvt_pk_bf16_f32 v248, v232, v233
	v_cvt_pk_bf16_f32 v249, v234, v235
	v_cvt_pk_bf16_f32 v250, v236, v237
	v_cvt_pk_bf16_f32 v251, v238, v239
	s_lshl_b32 s58, s54, 11
	s_add_u32 s60, s52, s58
	s_addc_u32 s61, s53, 0
	global_store_dwordx4 v126, v[248:251], s[60:61]
	s_add_i32 s54, s41, 0x4c00
	s_cmp_lt_u32 s54, 0x8000
	s_cselect_b32 s55, s70, s71
	s_and_b32 s56, s54, s55
	s_add_i32 s57, s55, 1
	s_add_i32 s58, s56, -2
	s_cmp_lt_u32 s58, s57
	s_cselect_b32 s62, 1.0, 0
	s_add_i32 s58, s56, -1
	s_cmp_lt_u32 s58, s57
	s_cselect_b32 s64, 1.0, 0
	s_mov_b32 s66, 1.0
	s_add_i32 s58, s56, 1
	s_cmp_lt_u32 s58, s57
	s_cselect_b32 s68, 1.0, 0
	v_pk_mul_f32 v[240:241], v[128:129], s[62:63] op_sel_hi:[1,0]
	v_lshlrev_b32_e32 v242, 16, v184
	v_and_b32_e32 v243, 0xffff0000, v184
	v_pk_fma_f32 v[232:233], v[240:241], v[242:243], v[160:161]
	v_pk_mul_f32 v[240:241], v[130:131], s[62:63] op_sel_hi:[1,0]
	v_lshlrev_b32_e32 v242, 16, v185
	v_and_b32_e32 v243, 0xffff0000, v185
	v_pk_fma_f32 v[234:235], v[240:241], v[242:243], v[162:163]
	v_pk_mul_f32 v[240:241], v[132:133], s[62:63] op_sel_hi:[1,0]
	v_lshlrev_b32_e32 v242, 16, v186
	v_and_b32_e32 v243, 0xffff0000, v186
	v_pk_fma_f32 v[236:237], v[240:241], v[242:243], v[164:165]
	v_pk_mul_f32 v[240:241], v[134:135], s[62:63] op_sel_hi:[1,0]
	v_lshlrev_b32_e32 v242, 16, v187
	v_and_b32_e32 v243, 0xffff0000, v187
	v_pk_fma_f32 v[238:239], v[240:241], v[242:243], v[166:167]
	v_pk_mul_f32 v[240:241], v[136:137], s[64:65] op_sel_hi:[1,0]
	v_lshlrev_b32_e32 v242, 16, v188
	v_and_b32_e32 v243, 0xffff0000, v188
	v_pk_fma_f32 v[232:233], v[240:241], v[242:243], v[232:233]
	v_pk_mul_f32 v[240:241], v[138:139], s[64:65] op_sel_hi:[1,0]
	v_lshlrev_b32_e32 v242, 16, v189
	v_and_b32_e32 v243, 0xffff0000, v189
	v_pk_fma_f32 v[234:235], v[240:241], v[242:243], v[234:235]
	v_pk_mul_f32 v[240:241], v[140:141], s[64:65] op_sel_hi:[1,0]
	v_lshlrev_b32_e32 v242, 16, v190
	v_and_b32_e32 v243, 0xffff0000, v190
	v_pk_fma_f32 v[236:237], v[240:241], v[242:243], v[236:237]
	v_pk_mul_f32 v[240:241], v[142:143], s[64:65] op_sel_hi:[1,0]
	v_lshlrev_b32_e32 v242, 16, v191
	v_and_b32_e32 v243, 0xffff0000, v191
	v_pk_fma_f32 v[238:239], v[240:241], v[242:243], v[238:239]
	v_pk_mul_f32 v[240:241], v[144:145], s[66:67] op_sel_hi:[1,0]
	v_lshlrev_b32_e32 v242, 16, v192
	v_and_b32_e32 v243, 0xffff0000, v192
	v_pk_fma_f32 v[232:233], v[240:241], v[242:243], v[232:233]
	v_pk_mul_f32 v[240:241], v[146:147], s[66:67] op_sel_hi:[1,0]
	v_lshlrev_b32_e32 v242, 16, v193
	v_and_b32_e32 v243, 0xffff0000, v193
	v_pk_fma_f32 v[234:235], v[240:241], v[242:243], v[234:235]
	v_pk_mul_f32 v[240:241], v[148:149], s[66:67] op_sel_hi:[1,0]
	v_lshlrev_b32_e32 v242, 16, v194
	v_and_b32_e32 v243, 0xffff0000, v194
	v_pk_fma_f32 v[236:237], v[240:241], v[242:243], v[236:237]
	v_pk_mul_f32 v[240:241], v[150:151], s[66:67] op_sel_hi:[1,0]
	v_lshlrev_b32_e32 v242, 16, v195
	v_and_b32_e32 v243, 0xffff0000, v195
	v_pk_fma_f32 v[238:239], v[240:241], v[242:243], v[238:239]
	v_pk_mul_f32 v[240:241], v[152:153], s[68:69] op_sel_hi:[1,0]
	v_lshlrev_b32_e32 v242, 16, v196
	v_and_b32_e32 v243, 0xffff0000, v196
	v_pk_fma_f32 v[232:233], v[240:241], v[242:243], v[232:233]
	v_pk_mul_f32 v[240:241], v[154:155], s[68:69] op_sel_hi:[1,0]
	v_lshlrev_b32_e32 v242, 16, v197
	v_and_b32_e32 v243, 0xffff0000, v197
	v_pk_fma_f32 v[234:235], v[240:241], v[242:243], v[234:235]
	v_pk_mul_f32 v[240:241], v[156:157], s[68:69] op_sel_hi:[1,0]
	v_lshlrev_b32_e32 v242, 16, v198
	v_and_b32_e32 v243, 0xffff0000, v198
	v_pk_fma_f32 v[236:237], v[240:241], v[242:243], v[236:237]
	v_pk_mul_f32 v[240:241], v[158:159], s[68:69] op_sel_hi:[1,0]
	v_lshlrev_b32_e32 v242, 16, v199
	v_and_b32_e32 v243, 0xffff0000, v199
	v_pk_fma_f32 v[238:239], v[240:241], v[242:243], v[238:239]
	v_cvt_pk_bf16_f32 v248, v232, v233
	v_cvt_pk_bf16_f32 v249, v234, v235
	v_cvt_pk_bf16_f32 v250, v236, v237
	v_cvt_pk_bf16_f32 v251, v238, v239
	s_lshl_b32 s58, s54, 11
	s_add_u32 s60, s52, s58
	s_addc_u32 s61, s53, 0
	global_store_dwordx4 v126, v[248:251], s[60:61]
	s_add_i32 s54, s41, 0x6000
	s_cmp_lt_u32 s54, 0x8000
	s_cselect_b32 s55, s70, s71
	s_and_b32 s56, s54, s55
	s_add_i32 s57, s55, 1
	s_add_i32 s58, s56, -2
	s_cmp_lt_u32 s58, s57
	s_cselect_b32 s58, -2, 0
	s_add_i32 s58, s54, s58
	s_mul_i32 s58, s58, 0x5a00
	s_add_u32 s60, s50, s58
	s_addc_u32 s61, s51, 0
	global_load_dwordx4 v[168:171], v126, s[60:61]
	s_add_i32 s58, s56, -1
	s_cmp_lt_u32 s58, s57
	s_cselect_b32 s58, -1, 0
	s_add_i32 s58, s54, s58
	s_mul_i32 s58, s58, 0x5a00
	s_add_u32 s60, s50, s58
	s_addc_u32 s61, s51, 0
	global_load_dwordx4 v[172:175], v126, s[60:61]
	s_mul_i32 s58, s54, 0x5a00
	s_add_u32 s60, s50, s58
	s_addc_u32 s61, s51, 0
	global_load_dwordx4 v[176:179], v126, s[60:61]
	s_add_i32 s58, s56, 1
	s_cmp_lt_u32 s58, s57
	s_cselect_b32 s58, 1, 0
	s_add_i32 s58, s54, s58
	s_mul_i32 s58, s58, 0x5a00
	s_add_u32 s60, s50, s58
	s_addc_u32 s61, s51, 0
	global_load_dwordx4 v[180:183], v126, s[60:61]
	s_add_i32 s54, s41, 0x6400
	s_cmp_lt_u32 s54, 0x8000
	s_cselect_b32 s55, s70, s71
	s_and_b32 s56, s54, s55
	s_add_i32 s57, s55, 1
	s_add_i32 s58, s56, -2
	s_cmp_lt_u32 s58, s57
	s_cselect_b32 s58, -2, 0
	s_add_i32 s58, s54, s58
	s_mul_i32 s58, s58, 0x5a00
	s_add_u32 s60, s50, s58
	s_addc_u32 s61, s51, 0
	global_load_dwordx4 v[184:187], v126, s[60:61]
	s_add_i32 s58, s56, -1
	s_cmp_lt_u32 s58, s57
	s_cselect_b32 s58, -1, 0
	s_add_i32 s58, s54, s58
	s_mul_i32 s58, s58, 0x5a00
	s_add_u32 s60, s50, s58
	s_addc_u32 s61, s51, 0
	global_load_dwordx4 v[188:191], v126, s[60:61]
	s_mul_i32 s58, s54, 0x5a00
	s_add_u32 s60, s50, s58
	s_addc_u32 s61, s51, 0
	global_load_dwordx4 v[192:195], v126, s[60:61]
	s_add_i32 s58, s56, 1
	s_cmp_lt_u32 s58, s57
	s_cselect_b32 s58, 1, 0
	s_add_i32 s58, s54, s58
	s_mul_i32 s58, s58, 0x5a00
	s_add_u32 s60, s50, s58
	s_addc_u32 s61, s51, 0
	global_load_dwordx4 v[196:199], v126, s[60:61]
	s_waitcnt vmcnt(20)
	s_add_i32 s54, s41, 0x5000
	s_cmp_lt_u32 s54, 0x8000
	s_cselect_b32 s55, s70, s71
	s_and_b32 s56, s54, s55
	s_add_i32 s57, s55, 1
	s_add_i32 s58, s56, -2
	s_cmp_lt_u32 s58, s57
	s_cselect_b32 s62, 1.0, 0
	s_add_i32 s58, s56, -1
	s_cmp_lt_u32 s58, s57
	s_cselect_b32 s64, 1.0, 0
	s_mov_b32 s66, 1.0
	s_add_i32 s58, s56, 1
	s_cmp_lt_u32 s58, s57
	s_cselect_b32 s68, 1.0, 0
	v_pk_mul_f32 v[240:241], v[128:129], s[62:63] op_sel_hi:[1,0]
	v_lshlrev_b32_e32 v242, 16, v200
	v_and_b32_e32 v243, 0xffff0000, v200
	v_pk_fma_f32 v[232:233], v[240:241], v[242:243], v[160:161]
	v_pk_mul_f32 v[240:241], v[130:131], s[62:63] op_sel_hi:[1,0]
	v_lshlrev_b32_e32 v242, 16, v201
	v_and_b32_e32 v243, 0xffff0000, v201
	v_pk_fma_f32 v[234:235], v[240:241], v[242:243], v[162:163]
	v_pk_mul_f32 v[240:241], v[132:133], s[62:63] op_sel_hi:[1,0]
	v_lshlrev_b32_e32 v242, 16, v202
	v_and_b32_e32 v243, 0xffff0000, v202
	v_pk_fma_f32 v[236:237], v[240:241], v[242:243], v[164:165]
	v_pk_mul_f32 v[240:241], v[134:135], s[62:63] op_sel_hi:[1,0]
	v_lshlrev_b32_e32 v242, 16, v203
	v_and_b32_e32 v243, 0xffff0000, v203
	v_pk_fma_f32 v[238:239], v[240:241], v[242:243], v[166:167]
	v_pk_mul_f32 v[240:241], v[136:137], s[64:65] op_sel_hi:[1,0]
	v_lshlrev_b32_e32 v242, 16, v204
	v_and_b32_e32 v243, 0xffff0000, v204
	v_pk_fma_f32 v[232:233], v[240:241], v[242:243], v[232:233]
	v_pk_mul_f32 v[240:241], v[138:139], s[64:65] op_sel_hi:[1,0]
	v_lshlrev_b32_e32 v242, 16, v205
	v_and_b32_e32 v243, 0xffff0000, v205
	v_pk_fma_f32 v[234:235], v[240:241], v[242:243], v[234:235]
	v_pk_mul_f32 v[240:241], v[140:141], s[64:65] op_sel_hi:[1,0]
	v_lshlrev_b32_e32 v242, 16, v206
	v_and_b32_e32 v243, 0xffff0000, v206
	v_pk_fma_f32 v[236:237], v[240:241], v[242:243], v[236:237]
	v_pk_mul_f32 v[240:241], v[142:143], s[64:65] op_sel_hi:[1,0]
	v_lshlrev_b32_e32 v242, 16, v207
	v_and_b32_e32 v243, 0xffff0000, v207
	v_pk_fma_f32 v[238:239], v[240:241], v[242:243], v[238:239]
	v_pk_mul_f32 v[240:241], v[144:145], s[66:67] op_sel_hi:[1,0]
	v_lshlrev_b32_e32 v242, 16, v208
	v_and_b32_e32 v243, 0xffff0000, v208
	v_pk_fma_f32 v[232:233], v[240:241], v[242:243], v[232:233]
	v_pk_mul_f32 v[240:241], v[146:147], s[66:67] op_sel_hi:[1,0]
	v_lshlrev_b32_e32 v242, 16, v209
	v_and_b32_e32 v243, 0xffff0000, v209
	v_pk_fma_f32 v[234:235], v[240:241], v[242:243], v[234:235]
	v_pk_mul_f32 v[240:241], v[148:149], s[66:67] op_sel_hi:[1,0]
	v_lshlrev_b32_e32 v242, 16, v210
	v_and_b32_e32 v243, 0xffff0000, v210
	v_pk_fma_f32 v[236:237], v[240:241], v[242:243], v[236:237]
	v_pk_mul_f32 v[240:241], v[150:151], s[66:67] op_sel_hi:[1,0]
	v_lshlrev_b32_e32 v242, 16, v211
	v_and_b32_e32 v243, 0xffff0000, v211
	v_pk_fma_f32 v[238:239], v[240:241], v[242:243], v[238:239]
	v_pk_mul_f32 v[240:241], v[152:153], s[68:69] op_sel_hi:[1,0]
	v_lshlrev_b32_e32 v242, 16, v212
	v_and_b32_e32 v243, 0xffff0000, v212
	v_pk_fma_f32 v[232:233], v[240:241], v[242:243], v[232:233]
	v_pk_mul_f32 v[240:241], v[154:155], s[68:69] op_sel_hi:[1,0]
	v_lshlrev_b32_e32 v242, 16, v213
	v_and_b32_e32 v243, 0xffff0000, v213
	v_pk_fma_f32 v[234:235], v[240:241], v[242:243], v[234:235]
	v_pk_mul_f32 v[240:241], v[156:157], s[68:69] op_sel_hi:[1,0]
	v_lshlrev_b32_e32 v242, 16, v214
	v_and_b32_e32 v243, 0xffff0000, v214
	v_pk_fma_f32 v[236:237], v[240:241], v[242:243], v[236:237]
	v_pk_mul_f32 v[240:241], v[158:159], s[68:69] op_sel_hi:[1,0]
	v_lshlrev_b32_e32 v242, 16, v215
	v_and_b32_e32 v243, 0xffff0000, v215
	v_pk_fma_f32 v[238:239], v[240:241], v[242:243], v[238:239]
	v_cvt_pk_bf16_f32 v248, v232, v233
	v_cvt_pk_bf16_f32 v249, v234, v235
	v_cvt_pk_bf16_f32 v250, v236, v237
	v_cvt_pk_bf16_f32 v251, v238, v239
	s_lshl_b32 s58, s54, 11
	s_add_u32 s60, s52, s58
	s_addc_u32 s61, s53, 0
	global_store_dwordx4 v126, v[248:251], s[60:61]
	s_add_i32 s54, s41, 0x5400
	s_cmp_lt_u32 s54, 0x8000
	s_cselect_b32 s55, s70, s71
	s_and_b32 s56, s54, s55
	s_add_i32 s57, s55, 1
	s_add_i32 s58, s56, -2
	s_cmp_lt_u32 s58, s57
	s_cselect_b32 s62, 1.0, 0
	s_add_i32 s58, s56, -1
	s_cmp_lt_u32 s58, s57
	s_cselect_b32 s64, 1.0, 0
	s_mov_b32 s66, 1.0
	s_add_i32 s58, s56, 1
	s_cmp_lt_u32 s58, s57
	s_cselect_b32 s68, 1.0, 0
	v_pk_mul_f32 v[240:241], v[128:129], s[62:63] op_sel_hi:[1,0]
	v_lshlrev_b32_e32 v242, 16, v216
	v_and_b32_e32 v243, 0xffff0000, v216
	v_pk_fma_f32 v[232:233], v[240:241], v[242:243], v[160:161]
	v_pk_mul_f32 v[240:241], v[130:131], s[62:63] op_sel_hi:[1,0]
	v_lshlrev_b32_e32 v242, 16, v217
	v_and_b32_e32 v243, 0xffff0000, v217
	v_pk_fma_f32 v[234:235], v[240:241], v[242:243], v[162:163]
	v_pk_mul_f32 v[240:241], v[132:133], s[62:63] op_sel_hi:[1,0]
	v_lshlrev_b32_e32 v242, 16, v218
	v_and_b32_e32 v243, 0xffff0000, v218
	v_pk_fma_f32 v[236:237], v[240:241], v[242:243], v[164:165]
	v_pk_mul_f32 v[240:241], v[134:135], s[62:63] op_sel_hi:[1,0]
	v_lshlrev_b32_e32 v242, 16, v219
	v_and_b32_e32 v243, 0xffff0000, v219
	v_pk_fma_f32 v[238:239], v[240:241], v[242:243], v[166:167]
	v_pk_mul_f32 v[240:241], v[136:137], s[64:65] op_sel_hi:[1,0]
	v_lshlrev_b32_e32 v242, 16, v220
	v_and_b32_e32 v243, 0xffff0000, v220
	v_pk_fma_f32 v[232:233], v[240:241], v[242:243], v[232:233]
	v_pk_mul_f32 v[240:241], v[138:139], s[64:65] op_sel_hi:[1,0]
	v_lshlrev_b32_e32 v242, 16, v221
	v_and_b32_e32 v243, 0xffff0000, v221
	v_pk_fma_f32 v[234:235], v[240:241], v[242:243], v[234:235]
	v_pk_mul_f32 v[240:241], v[140:141], s[64:65] op_sel_hi:[1,0]
	v_lshlrev_b32_e32 v242, 16, v222
	v_and_b32_e32 v243, 0xffff0000, v222
	v_pk_fma_f32 v[236:237], v[240:241], v[242:243], v[236:237]
	v_pk_mul_f32 v[240:241], v[142:143], s[64:65] op_sel_hi:[1,0]
	v_lshlrev_b32_e32 v242, 16, v223
	v_and_b32_e32 v243, 0xffff0000, v223
	v_pk_fma_f32 v[238:239], v[240:241], v[242:243], v[238:239]
	v_pk_mul_f32 v[240:241], v[144:145], s[66:67] op_sel_hi:[1,0]
	v_lshlrev_b32_e32 v242, 16, v224
	v_and_b32_e32 v243, 0xffff0000, v224
	v_pk_fma_f32 v[232:233], v[240:241], v[242:243], v[232:233]
	v_pk_mul_f32 v[240:241], v[146:147], s[66:67] op_sel_hi:[1,0]
	v_lshlrev_b32_e32 v242, 16, v225
	v_and_b32_e32 v243, 0xffff0000, v225
	v_pk_fma_f32 v[234:235], v[240:241], v[242:243], v[234:235]
	v_pk_mul_f32 v[240:241], v[148:149], s[66:67] op_sel_hi:[1,0]
	v_lshlrev_b32_e32 v242, 16, v226
	v_and_b32_e32 v243, 0xffff0000, v226
	v_pk_fma_f32 v[236:237], v[240:241], v[242:243], v[236:237]
	v_pk_mul_f32 v[240:241], v[150:151], s[66:67] op_sel_hi:[1,0]
	v_lshlrev_b32_e32 v242, 16, v227
	v_and_b32_e32 v243, 0xffff0000, v227
	v_pk_fma_f32 v[238:239], v[240:241], v[242:243], v[238:239]
	v_pk_mul_f32 v[240:241], v[152:153], s[68:69] op_sel_hi:[1,0]
	v_lshlrev_b32_e32 v242, 16, v228
	v_and_b32_e32 v243, 0xffff0000, v228
	v_pk_fma_f32 v[232:233], v[240:241], v[242:243], v[232:233]
	v_pk_mul_f32 v[240:241], v[154:155], s[68:69] op_sel_hi:[1,0]
	v_lshlrev_b32_e32 v242, 16, v229
	v_and_b32_e32 v243, 0xffff0000, v229
	v_pk_fma_f32 v[234:235], v[240:241], v[242:243], v[234:235]
	v_pk_mul_f32 v[240:241], v[156:157], s[68:69] op_sel_hi:[1,0]
	v_lshlrev_b32_e32 v242, 16, v230
	v_and_b32_e32 v243, 0xffff0000, v230
	v_pk_fma_f32 v[236:237], v[240:241], v[242:243], v[236:237]
	v_pk_mul_f32 v[240:241], v[158:159], s[68:69] op_sel_hi:[1,0]
	v_lshlrev_b32_e32 v242, 16, v231
	v_and_b32_e32 v243, 0xffff0000, v231
	v_pk_fma_f32 v[238:239], v[240:241], v[242:243], v[238:239]
	v_cvt_pk_bf16_f32 v248, v232, v233
	v_cvt_pk_bf16_f32 v249, v234, v235
	v_cvt_pk_bf16_f32 v250, v236, v237
	v_cvt_pk_bf16_f32 v251, v238, v239
	s_lshl_b32 s58, s54, 11
	s_add_u32 s60, s52, s58
	s_addc_u32 s61, s53, 0
	global_store_dwordx4 v126, v[248:251], s[60:61]
	s_add_i32 s54, s41, 0x6800
	s_cmp_lt_u32 s54, 0x8000
	s_cselect_b32 s55, s70, s71
	s_and_b32 s56, s54, s55
	s_add_i32 s57, s55, 1
	s_add_i32 s58, s56, -2
	s_cmp_lt_u32 s58, s57
	s_cselect_b32 s58, -2, 0
	s_add_i32 s58, s54, s58
	s_mul_i32 s58, s58, 0x5a00
	s_add_u32 s60, s50, s58
	s_addc_u32 s61, s51, 0
	global_load_dwordx4 v[200:203], v126, s[60:61]
	s_add_i32 s58, s56, -1
	s_cmp_lt_u32 s58, s57
	s_cselect_b32 s58, -1, 0
	s_add_i32 s58, s54, s58
	s_mul_i32 s58, s58, 0x5a00
	s_add_u32 s60, s50, s58
	s_addc_u32 s61, s51, 0
	global_load_dwordx4 v[204:207], v126, s[60:61]
	s_mul_i32 s58, s54, 0x5a00
	s_add_u32 s60, s50, s58
	s_addc_u32 s61, s51, 0
	global_load_dwordx4 v[208:211], v126, s[60:61]
	s_add_i32 s58, s56, 1
	s_cmp_lt_u32 s58, s57
	s_cselect_b32 s58, 1, 0
	s_add_i32 s58, s54, s58
	s_mul_i32 s58, s58, 0x5a00
	s_add_u32 s60, s50, s58
	s_addc_u32 s61, s51, 0
	global_load_dwordx4 v[212:215], v126, s[60:61]
	s_add_i32 s54, s41, 0x6c00
	s_cmp_lt_u32 s54, 0x8000
	s_cselect_b32 s55, s70, s71
	s_and_b32 s56, s54, s55
	s_add_i32 s57, s55, 1
	s_add_i32 s58, s56, -2
	s_cmp_lt_u32 s58, s57
	s_cselect_b32 s58, -2, 0
	s_add_i32 s58, s54, s58
	s_mul_i32 s58, s58, 0x5a00
	s_add_u32 s60, s50, s58
	s_addc_u32 s61, s51, 0
	global_load_dwordx4 v[216:219], v126, s[60:61]
	s_add_i32 s58, s56, -1
	s_cmp_lt_u32 s58, s57
	s_cselect_b32 s58, -1, 0
	s_add_i32 s58, s54, s58
	s_mul_i32 s58, s58, 0x5a00
	s_add_u32 s60, s50, s58
	s_addc_u32 s61, s51, 0
	global_load_dwordx4 v[220:223], v126, s[60:61]
	s_mul_i32 s58, s54, 0x5a00
	s_add_u32 s60, s50, s58
	s_addc_u32 s61, s51, 0
	global_load_dwordx4 v[224:227], v126, s[60:61]
	s_add_i32 s58, s56, 1
	s_cmp_lt_u32 s58, s57
	s_cselect_b32 s58, 1, 0
	s_add_i32 s58, s54, s58
	s_mul_i32 s58, s58, 0x5a00
	s_add_u32 s60, s50, s58
	s_addc_u32 s61, s51, 0
	global_load_dwordx4 v[228:231], v126, s[60:61]
	s_waitcnt vmcnt(20)
	s_add_i32 s54, s41, 0x5800
	s_cmp_lt_u32 s54, 0x8000
	s_cselect_b32 s55, s70, s71
	s_and_b32 s56, s54, s55
	s_add_i32 s57, s55, 1
	s_add_i32 s58, s56, -2
	s_cmp_lt_u32 s58, s57
	s_cselect_b32 s62, 1.0, 0
	s_add_i32 s58, s56, -1
	s_cmp_lt_u32 s58, s57
	s_cselect_b32 s64, 1.0, 0
	s_mov_b32 s66, 1.0
	s_add_i32 s58, s56, 1
	s_cmp_lt_u32 s58, s57
	s_cselect_b32 s68, 1.0, 0
	v_pk_mul_f32 v[240:241], v[128:129], s[62:63] op_sel_hi:[1,0]
	v_lshlrev_b32_e32 v242, 16, v40
	v_and_b32_e32 v243, 0xffff0000, v40
	v_pk_fma_f32 v[232:233], v[240:241], v[242:243], v[160:161]
	v_pk_mul_f32 v[240:241], v[130:131], s[62:63] op_sel_hi:[1,0]
	v_lshlrev_b32_e32 v242, 16, v41
	v_and_b32_e32 v243, 0xffff0000, v41
	v_pk_fma_f32 v[234:235], v[240:241], v[242:243], v[162:163]
	v_pk_mul_f32 v[240:241], v[132:133], s[62:63] op_sel_hi:[1,0]
	v_lshlrev_b32_e32 v242, 16, v42
	v_and_b32_e32 v243, 0xffff0000, v42
	v_pk_fma_f32 v[236:237], v[240:241], v[242:243], v[164:165]
	v_pk_mul_f32 v[240:241], v[134:135], s[62:63] op_sel_hi:[1,0]
	v_lshlrev_b32_e32 v242, 16, v43
	v_and_b32_e32 v243, 0xffff0000, v43
	v_pk_fma_f32 v[238:239], v[240:241], v[242:243], v[166:167]
	v_pk_mul_f32 v[240:241], v[136:137], s[64:65] op_sel_hi:[1,0]
	v_lshlrev_b32_e32 v242, 16, v44
	v_and_b32_e32 v243, 0xffff0000, v44
	v_pk_fma_f32 v[232:233], v[240:241], v[242:243], v[232:233]
	v_pk_mul_f32 v[240:241], v[138:139], s[64:65] op_sel_hi:[1,0]
	v_lshlrev_b32_e32 v242, 16, v45
	v_and_b32_e32 v243, 0xffff0000, v45
	v_pk_fma_f32 v[234:235], v[240:241], v[242:243], v[234:235]
	v_pk_mul_f32 v[240:241], v[140:141], s[64:65] op_sel_hi:[1,0]
	v_lshlrev_b32_e32 v242, 16, v46
	v_and_b32_e32 v243, 0xffff0000, v46
	v_pk_fma_f32 v[236:237], v[240:241], v[242:243], v[236:237]
	v_pk_mul_f32 v[240:241], v[142:143], s[64:65] op_sel_hi:[1,0]
	v_lshlrev_b32_e32 v242, 16, v47
	v_and_b32_e32 v243, 0xffff0000, v47
	v_pk_fma_f32 v[238:239], v[240:241], v[242:243], v[238:239]
	v_pk_mul_f32 v[240:241], v[144:145], s[66:67] op_sel_hi:[1,0]
	v_lshlrev_b32_e32 v242, 16, v48
	v_and_b32_e32 v243, 0xffff0000, v48
	v_pk_fma_f32 v[232:233], v[240:241], v[242:243], v[232:233]
	v_pk_mul_f32 v[240:241], v[146:147], s[66:67] op_sel_hi:[1,0]
	v_lshlrev_b32_e32 v242, 16, v49
	v_and_b32_e32 v243, 0xffff0000, v49
	v_pk_fma_f32 v[234:235], v[240:241], v[242:243], v[234:235]
	v_pk_mul_f32 v[240:241], v[148:149], s[66:67] op_sel_hi:[1,0]
	v_lshlrev_b32_e32 v242, 16, v50
	v_and_b32_e32 v243, 0xffff0000, v50
	v_pk_fma_f32 v[236:237], v[240:241], v[242:243], v[236:237]
	v_pk_mul_f32 v[240:241], v[150:151], s[66:67] op_sel_hi:[1,0]
	v_lshlrev_b32_e32 v242, 16, v51
	v_and_b32_e32 v243, 0xffff0000, v51
	v_pk_fma_f32 v[238:239], v[240:241], v[242:243], v[238:239]
	v_pk_mul_f32 v[240:241], v[152:153], s[68:69] op_sel_hi:[1,0]
	v_lshlrev_b32_e32 v242, 16, v52
	v_and_b32_e32 v243, 0xffff0000, v52
	v_pk_fma_f32 v[232:233], v[240:241], v[242:243], v[232:233]
	v_pk_mul_f32 v[240:241], v[154:155], s[68:69] op_sel_hi:[1,0]
	v_lshlrev_b32_e32 v242, 16, v53
	v_and_b32_e32 v243, 0xffff0000, v53
	v_pk_fma_f32 v[234:235], v[240:241], v[242:243], v[234:235]
	v_pk_mul_f32 v[240:241], v[156:157], s[68:69] op_sel_hi:[1,0]
	v_lshlrev_b32_e32 v242, 16, v54
	v_and_b32_e32 v243, 0xffff0000, v54
	v_pk_fma_f32 v[236:237], v[240:241], v[242:243], v[236:237]
	v_pk_mul_f32 v[240:241], v[158:159], s[68:69] op_sel_hi:[1,0]
	v_lshlrev_b32_e32 v242, 16, v55
	v_and_b32_e32 v243, 0xffff0000, v55
	v_pk_fma_f32 v[238:239], v[240:241], v[242:243], v[238:239]
	v_cvt_pk_bf16_f32 v248, v232, v233
	v_cvt_pk_bf16_f32 v249, v234, v235
	v_cvt_pk_bf16_f32 v250, v236, v237
	v_cvt_pk_bf16_f32 v251, v238, v239
	s_lshl_b32 s58, s54, 11
	s_add_u32 s60, s52, s58
	s_addc_u32 s61, s53, 0
	global_store_dwordx4 v126, v[248:251], s[60:61]
	s_add_i32 s54, s41, 0x5c00
	s_cmp_lt_u32 s54, 0x8000
	s_cselect_b32 s55, s70, s71
	s_and_b32 s56, s54, s55
	s_add_i32 s57, s55, 1
	s_add_i32 s58, s56, -2
	s_cmp_lt_u32 s58, s57
	s_cselect_b32 s62, 1.0, 0
	s_add_i32 s58, s56, -1
	s_cmp_lt_u32 s58, s57
	s_cselect_b32 s64, 1.0, 0
	s_mov_b32 s66, 1.0
	s_add_i32 s58, s56, 1
	s_cmp_lt_u32 s58, s57
	s_cselect_b32 s68, 1.0, 0
	v_pk_mul_f32 v[240:241], v[128:129], s[62:63] op_sel_hi:[1,0]
	v_lshlrev_b32_e32 v242, 16, v56
	v_and_b32_e32 v243, 0xffff0000, v56
	v_pk_fma_f32 v[232:233], v[240:241], v[242:243], v[160:161]
	v_pk_mul_f32 v[240:241], v[130:131], s[62:63] op_sel_hi:[1,0]
	v_lshlrev_b32_e32 v242, 16, v57
	v_and_b32_e32 v243, 0xffff0000, v57
	v_pk_fma_f32 v[234:235], v[240:241], v[242:243], v[162:163]
	v_pk_mul_f32 v[240:241], v[132:133], s[62:63] op_sel_hi:[1,0]
	v_lshlrev_b32_e32 v242, 16, v58
	v_and_b32_e32 v243, 0xffff0000, v58
	v_pk_fma_f32 v[236:237], v[240:241], v[242:243], v[164:165]
	v_pk_mul_f32 v[240:241], v[134:135], s[62:63] op_sel_hi:[1,0]
	v_lshlrev_b32_e32 v242, 16, v59
	v_and_b32_e32 v243, 0xffff0000, v59
	v_pk_fma_f32 v[238:239], v[240:241], v[242:243], v[166:167]
	v_pk_mul_f32 v[240:241], v[136:137], s[64:65] op_sel_hi:[1,0]
	v_lshlrev_b32_e32 v242, 16, v60
	v_and_b32_e32 v243, 0xffff0000, v60
	v_pk_fma_f32 v[232:233], v[240:241], v[242:243], v[232:233]
	v_pk_mul_f32 v[240:241], v[138:139], s[64:65] op_sel_hi:[1,0]
	v_lshlrev_b32_e32 v242, 16, v61
	v_and_b32_e32 v243, 0xffff0000, v61
	v_pk_fma_f32 v[234:235], v[240:241], v[242:243], v[234:235]
	v_pk_mul_f32 v[240:241], v[140:141], s[64:65] op_sel_hi:[1,0]
	v_lshlrev_b32_e32 v242, 16, v62
	v_and_b32_e32 v243, 0xffff0000, v62
	v_pk_fma_f32 v[236:237], v[240:241], v[242:243], v[236:237]
	v_pk_mul_f32 v[240:241], v[142:143], s[64:65] op_sel_hi:[1,0]
	v_lshlrev_b32_e32 v242, 16, v63
	v_and_b32_e32 v243, 0xffff0000, v63
	v_pk_fma_f32 v[238:239], v[240:241], v[242:243], v[238:239]
	v_pk_mul_f32 v[240:241], v[144:145], s[66:67] op_sel_hi:[1,0]
	v_lshlrev_b32_e32 v242, 16, v64
	v_and_b32_e32 v243, 0xffff0000, v64
	v_pk_fma_f32 v[232:233], v[240:241], v[242:243], v[232:233]
	v_pk_mul_f32 v[240:241], v[146:147], s[66:67] op_sel_hi:[1,0]
	v_lshlrev_b32_e32 v242, 16, v65
	v_and_b32_e32 v243, 0xffff0000, v65
	v_pk_fma_f32 v[234:235], v[240:241], v[242:243], v[234:235]
	v_pk_mul_f32 v[240:241], v[148:149], s[66:67] op_sel_hi:[1,0]
	v_lshlrev_b32_e32 v242, 16, v66
	v_and_b32_e32 v243, 0xffff0000, v66
	v_pk_fma_f32 v[236:237], v[240:241], v[242:243], v[236:237]
	v_pk_mul_f32 v[240:241], v[150:151], s[66:67] op_sel_hi:[1,0]
	v_lshlrev_b32_e32 v242, 16, v67
	v_and_b32_e32 v243, 0xffff0000, v67
	v_pk_fma_f32 v[238:239], v[240:241], v[242:243], v[238:239]
	v_pk_mul_f32 v[240:241], v[152:153], s[68:69] op_sel_hi:[1,0]
	v_lshlrev_b32_e32 v242, 16, v68
	v_and_b32_e32 v243, 0xffff0000, v68
	v_pk_fma_f32 v[232:233], v[240:241], v[242:243], v[232:233]
	v_pk_mul_f32 v[240:241], v[154:155], s[68:69] op_sel_hi:[1,0]
	v_lshlrev_b32_e32 v242, 16, v69
	v_and_b32_e32 v243, 0xffff0000, v69
	v_pk_fma_f32 v[234:235], v[240:241], v[242:243], v[234:235]
	v_pk_mul_f32 v[240:241], v[156:157], s[68:69] op_sel_hi:[1,0]
	v_lshlrev_b32_e32 v242, 16, v70
	v_and_b32_e32 v243, 0xffff0000, v70
	v_pk_fma_f32 v[236:237], v[240:241], v[242:243], v[236:237]
	v_pk_mul_f32 v[240:241], v[158:159], s[68:69] op_sel_hi:[1,0]
	v_lshlrev_b32_e32 v242, 16, v71
	v_and_b32_e32 v243, 0xffff0000, v71
	v_pk_fma_f32 v[238:239], v[240:241], v[242:243], v[238:239]
	v_cvt_pk_bf16_f32 v248, v232, v233
	v_cvt_pk_bf16_f32 v249, v234, v235
	v_cvt_pk_bf16_f32 v250, v236, v237
	v_cvt_pk_bf16_f32 v251, v238, v239
	s_lshl_b32 s58, s54, 11
	s_add_u32 s60, s52, s58
	s_addc_u32 s61, s53, 0
	global_store_dwordx4 v126, v[248:251], s[60:61]
	s_add_i32 s54, s41, 0x7000
	s_cmp_lt_u32 s54, 0x8000
	s_cselect_b32 s55, s70, s71
	s_and_b32 s56, s54, s55
	s_add_i32 s57, s55, 1
	s_add_i32 s58, s56, -2
	s_cmp_lt_u32 s58, s57
	s_cselect_b32 s58, -2, 0
	s_add_i32 s58, s54, s58
	s_mul_i32 s58, s58, 0x5a00
	s_add_u32 s60, s50, s58
	s_addc_u32 s61, s51, 0
	global_load_dwordx4 v[40:43], v126, s[60:61]
	s_add_i32 s58, s56, -1
	s_cmp_lt_u32 s58, s57
	s_cselect_b32 s58, -1, 0
	s_add_i32 s58, s54, s58
	s_mul_i32 s58, s58, 0x5a00
	s_add_u32 s60, s50, s58
	s_addc_u32 s61, s51, 0
	global_load_dwordx4 v[44:47], v126, s[60:61]
	s_mul_i32 s58, s54, 0x5a00
	s_add_u32 s60, s50, s58
	s_addc_u32 s61, s51, 0
	global_load_dwordx4 v[48:51], v126, s[60:61]
	s_add_i32 s58, s56, 1
	s_cmp_lt_u32 s58, s57
	s_cselect_b32 s58, 1, 0
	s_add_i32 s58, s54, s58
	s_mul_i32 s58, s58, 0x5a00
	s_add_u32 s60, s50, s58
	s_addc_u32 s61, s51, 0
	global_load_dwordx4 v[52:55], v126, s[60:61]
	s_add_i32 s54, s41, 0x7400
	s_cmp_lt_u32 s54, 0x8000
	s_cselect_b32 s55, s70, s71
	s_and_b32 s56, s54, s55
	s_add_i32 s57, s55, 1
	s_add_i32 s58, s56, -2
	s_cmp_lt_u32 s58, s57
	s_cselect_b32 s58, -2, 0
	s_add_i32 s58, s54, s58
	s_mul_i32 s58, s58, 0x5a00
	s_add_u32 s60, s50, s58
	s_addc_u32 s61, s51, 0
	global_load_dwordx4 v[56:59], v126, s[60:61]
	s_add_i32 s58, s56, -1
	s_cmp_lt_u32 s58, s57
	s_cselect_b32 s58, -1, 0
	s_add_i32 s58, s54, s58
	s_mul_i32 s58, s58, 0x5a00
	s_add_u32 s60, s50, s58
	s_addc_u32 s61, s51, 0
	global_load_dwordx4 v[60:63], v126, s[60:61]
	s_mul_i32 s58, s54, 0x5a00
	s_add_u32 s60, s50, s58
	s_addc_u32 s61, s51, 0
	global_load_dwordx4 v[64:67], v126, s[60:61]
	s_add_i32 s58, s56, 1
	s_cmp_lt_u32 s58, s57
	s_cselect_b32 s58, 1, 0
	s_add_i32 s58, s54, s58
	s_mul_i32 s58, s58, 0x5a00
	s_add_u32 s60, s50, s58
	s_addc_u32 s61, s51, 0
	global_load_dwordx4 v[68:71], v126, s[60:61]
	s_waitcnt vmcnt(20)
	s_add_i32 s54, s41, 0x6000
	s_cmp_lt_u32 s54, 0x8000
	s_cselect_b32 s55, s70, s71
	s_and_b32 s56, s54, s55
	s_add_i32 s57, s55, 1
	s_add_i32 s58, s56, -2
	s_cmp_lt_u32 s58, s57
	s_cselect_b32 s62, 1.0, 0
	s_add_i32 s58, s56, -1
	s_cmp_lt_u32 s58, s57
	s_cselect_b32 s64, 1.0, 0
	s_mov_b32 s66, 1.0
	s_add_i32 s58, s56, 1
	s_cmp_lt_u32 s58, s57
	s_cselect_b32 s68, 1.0, 0
	v_pk_mul_f32 v[240:241], v[128:129], s[62:63] op_sel_hi:[1,0]
	v_lshlrev_b32_e32 v242, 16, v168
	v_and_b32_e32 v243, 0xffff0000, v168
	v_pk_fma_f32 v[232:233], v[240:241], v[242:243], v[160:161]
	v_pk_mul_f32 v[240:241], v[130:131], s[62:63] op_sel_hi:[1,0]
	v_lshlrev_b32_e32 v242, 16, v169
	v_and_b32_e32 v243, 0xffff0000, v169
	v_pk_fma_f32 v[234:235], v[240:241], v[242:243], v[162:163]
	v_pk_mul_f32 v[240:241], v[132:133], s[62:63] op_sel_hi:[1,0]
	v_lshlrev_b32_e32 v242, 16, v170
	v_and_b32_e32 v243, 0xffff0000, v170
	v_pk_fma_f32 v[236:237], v[240:241], v[242:243], v[164:165]
	v_pk_mul_f32 v[240:241], v[134:135], s[62:63] op_sel_hi:[1,0]
	v_lshlrev_b32_e32 v242, 16, v171
	v_and_b32_e32 v243, 0xffff0000, v171
	v_pk_fma_f32 v[238:239], v[240:241], v[242:243], v[166:167]
	v_pk_mul_f32 v[240:241], v[136:137], s[64:65] op_sel_hi:[1,0]
	v_lshlrev_b32_e32 v242, 16, v172
	v_and_b32_e32 v243, 0xffff0000, v172
	v_pk_fma_f32 v[232:233], v[240:241], v[242:243], v[232:233]
	v_pk_mul_f32 v[240:241], v[138:139], s[64:65] op_sel_hi:[1,0]
	v_lshlrev_b32_e32 v242, 16, v173
	v_and_b32_e32 v243, 0xffff0000, v173
	v_pk_fma_f32 v[234:235], v[240:241], v[242:243], v[234:235]
	v_pk_mul_f32 v[240:241], v[140:141], s[64:65] op_sel_hi:[1,0]
	v_lshlrev_b32_e32 v242, 16, v174
	v_and_b32_e32 v243, 0xffff0000, v174
	v_pk_fma_f32 v[236:237], v[240:241], v[242:243], v[236:237]
	v_pk_mul_f32 v[240:241], v[142:143], s[64:65] op_sel_hi:[1,0]
	v_lshlrev_b32_e32 v242, 16, v175
	v_and_b32_e32 v243, 0xffff0000, v175
	v_pk_fma_f32 v[238:239], v[240:241], v[242:243], v[238:239]
	v_pk_mul_f32 v[240:241], v[144:145], s[66:67] op_sel_hi:[1,0]
	v_lshlrev_b32_e32 v242, 16, v176
	v_and_b32_e32 v243, 0xffff0000, v176
	v_pk_fma_f32 v[232:233], v[240:241], v[242:243], v[232:233]
	v_pk_mul_f32 v[240:241], v[146:147], s[66:67] op_sel_hi:[1,0]
	v_lshlrev_b32_e32 v242, 16, v177
	v_and_b32_e32 v243, 0xffff0000, v177
	v_pk_fma_f32 v[234:235], v[240:241], v[242:243], v[234:235]
	v_pk_mul_f32 v[240:241], v[148:149], s[66:67] op_sel_hi:[1,0]
	v_lshlrev_b32_e32 v242, 16, v178
	v_and_b32_e32 v243, 0xffff0000, v178
	v_pk_fma_f32 v[236:237], v[240:241], v[242:243], v[236:237]
	v_pk_mul_f32 v[240:241], v[150:151], s[66:67] op_sel_hi:[1,0]
	v_lshlrev_b32_e32 v242, 16, v179
	v_and_b32_e32 v243, 0xffff0000, v179
	v_pk_fma_f32 v[238:239], v[240:241], v[242:243], v[238:239]
	v_pk_mul_f32 v[240:241], v[152:153], s[68:69] op_sel_hi:[1,0]
	v_lshlrev_b32_e32 v242, 16, v180
	v_and_b32_e32 v243, 0xffff0000, v180
	v_pk_fma_f32 v[232:233], v[240:241], v[242:243], v[232:233]
	v_pk_mul_f32 v[240:241], v[154:155], s[68:69] op_sel_hi:[1,0]
	v_lshlrev_b32_e32 v242, 16, v181
	v_and_b32_e32 v243, 0xffff0000, v181
	v_pk_fma_f32 v[234:235], v[240:241], v[242:243], v[234:235]
	v_pk_mul_f32 v[240:241], v[156:157], s[68:69] op_sel_hi:[1,0]
	v_lshlrev_b32_e32 v242, 16, v182
	v_and_b32_e32 v243, 0xffff0000, v182
	v_pk_fma_f32 v[236:237], v[240:241], v[242:243], v[236:237]
	v_pk_mul_f32 v[240:241], v[158:159], s[68:69] op_sel_hi:[1,0]
	v_lshlrev_b32_e32 v242, 16, v183
	v_and_b32_e32 v243, 0xffff0000, v183
	v_pk_fma_f32 v[238:239], v[240:241], v[242:243], v[238:239]
	v_cvt_pk_bf16_f32 v248, v232, v233
	v_cvt_pk_bf16_f32 v249, v234, v235
	v_cvt_pk_bf16_f32 v250, v236, v237
	v_cvt_pk_bf16_f32 v251, v238, v239
	s_lshl_b32 s58, s54, 11
	s_add_u32 s60, s52, s58
	s_addc_u32 s61, s53, 0
	global_store_dwordx4 v126, v[248:251], s[60:61]
	s_add_i32 s54, s41, 0x6400
	s_cmp_lt_u32 s54, 0x8000
	s_cselect_b32 s55, s70, s71
	s_and_b32 s56, s54, s55
	s_add_i32 s57, s55, 1
	s_add_i32 s58, s56, -2
	s_cmp_lt_u32 s58, s57
	s_cselect_b32 s62, 1.0, 0
	s_add_i32 s58, s56, -1
	s_cmp_lt_u32 s58, s57
	s_cselect_b32 s64, 1.0, 0
	s_mov_b32 s66, 1.0
	s_add_i32 s58, s56, 1
	s_cmp_lt_u32 s58, s57
	s_cselect_b32 s68, 1.0, 0
	v_pk_mul_f32 v[240:241], v[128:129], s[62:63] op_sel_hi:[1,0]
	v_lshlrev_b32_e32 v242, 16, v184
	v_and_b32_e32 v243, 0xffff0000, v184
	v_pk_fma_f32 v[232:233], v[240:241], v[242:243], v[160:161]
	v_pk_mul_f32 v[240:241], v[130:131], s[62:63] op_sel_hi:[1,0]
	v_lshlrev_b32_e32 v242, 16, v185
	v_and_b32_e32 v243, 0xffff0000, v185
	v_pk_fma_f32 v[234:235], v[240:241], v[242:243], v[162:163]
	v_pk_mul_f32 v[240:241], v[132:133], s[62:63] op_sel_hi:[1,0]
	v_lshlrev_b32_e32 v242, 16, v186
	v_and_b32_e32 v243, 0xffff0000, v186
	v_pk_fma_f32 v[236:237], v[240:241], v[242:243], v[164:165]
	v_pk_mul_f32 v[240:241], v[134:135], s[62:63] op_sel_hi:[1,0]
	v_lshlrev_b32_e32 v242, 16, v187
	v_and_b32_e32 v243, 0xffff0000, v187
	v_pk_fma_f32 v[238:239], v[240:241], v[242:243], v[166:167]
	v_pk_mul_f32 v[240:241], v[136:137], s[64:65] op_sel_hi:[1,0]
	v_lshlrev_b32_e32 v242, 16, v188
	v_and_b32_e32 v243, 0xffff0000, v188
	v_pk_fma_f32 v[232:233], v[240:241], v[242:243], v[232:233]
	v_pk_mul_f32 v[240:241], v[138:139], s[64:65] op_sel_hi:[1,0]
	v_lshlrev_b32_e32 v242, 16, v189
	v_and_b32_e32 v243, 0xffff0000, v189
	v_pk_fma_f32 v[234:235], v[240:241], v[242:243], v[234:235]
	v_pk_mul_f32 v[240:241], v[140:141], s[64:65] op_sel_hi:[1,0]
	v_lshlrev_b32_e32 v242, 16, v190
	v_and_b32_e32 v243, 0xffff0000, v190
	v_pk_fma_f32 v[236:237], v[240:241], v[242:243], v[236:237]
	v_pk_mul_f32 v[240:241], v[142:143], s[64:65] op_sel_hi:[1,0]
	v_lshlrev_b32_e32 v242, 16, v191
	v_and_b32_e32 v243, 0xffff0000, v191
	v_pk_fma_f32 v[238:239], v[240:241], v[242:243], v[238:239]
	v_pk_mul_f32 v[240:241], v[144:145], s[66:67] op_sel_hi:[1,0]
	v_lshlrev_b32_e32 v242, 16, v192
	v_and_b32_e32 v243, 0xffff0000, v192
	v_pk_fma_f32 v[232:233], v[240:241], v[242:243], v[232:233]
	v_pk_mul_f32 v[240:241], v[146:147], s[66:67] op_sel_hi:[1,0]
	v_lshlrev_b32_e32 v242, 16, v193
	v_and_b32_e32 v243, 0xffff0000, v193
	v_pk_fma_f32 v[234:235], v[240:241], v[242:243], v[234:235]
	v_pk_mul_f32 v[240:241], v[148:149], s[66:67] op_sel_hi:[1,0]
	v_lshlrev_b32_e32 v242, 16, v194
	v_and_b32_e32 v243, 0xffff0000, v194
	v_pk_fma_f32 v[236:237], v[240:241], v[242:243], v[236:237]
	v_pk_mul_f32 v[240:241], v[150:151], s[66:67] op_sel_hi:[1,0]
	v_lshlrev_b32_e32 v242, 16, v195
	v_and_b32_e32 v243, 0xffff0000, v195
	v_pk_fma_f32 v[238:239], v[240:241], v[242:243], v[238:239]
	v_pk_mul_f32 v[240:241], v[152:153], s[68:69] op_sel_hi:[1,0]
	v_lshlrev_b32_e32 v242, 16, v196
	v_and_b32_e32 v243, 0xffff0000, v196
	v_pk_fma_f32 v[232:233], v[240:241], v[242:243], v[232:233]
	v_pk_mul_f32 v[240:241], v[154:155], s[68:69] op_sel_hi:[1,0]
	v_lshlrev_b32_e32 v242, 16, v197
	v_and_b32_e32 v243, 0xffff0000, v197
	v_pk_fma_f32 v[234:235], v[240:241], v[242:243], v[234:235]
	v_pk_mul_f32 v[240:241], v[156:157], s[68:69] op_sel_hi:[1,0]
	v_lshlrev_b32_e32 v242, 16, v198
	v_and_b32_e32 v243, 0xffff0000, v198
	v_pk_fma_f32 v[236:237], v[240:241], v[242:243], v[236:237]
	v_pk_mul_f32 v[240:241], v[158:159], s[68:69] op_sel_hi:[1,0]
	v_lshlrev_b32_e32 v242, 16, v199
	v_and_b32_e32 v243, 0xffff0000, v199
	v_pk_fma_f32 v[238:239], v[240:241], v[242:243], v[238:239]
	v_cvt_pk_bf16_f32 v248, v232, v233
	v_cvt_pk_bf16_f32 v249, v234, v235
	v_cvt_pk_bf16_f32 v250, v236, v237
	v_cvt_pk_bf16_f32 v251, v238, v239
	s_lshl_b32 s58, s54, 11
	s_add_u32 s60, s52, s58
	s_addc_u32 s61, s53, 0
	global_store_dwordx4 v126, v[248:251], s[60:61]
	s_add_i32 s54, s41, 0x7800
	s_cmp_lt_u32 s54, 0x8000
	s_cselect_b32 s55, s70, s71
	s_and_b32 s56, s54, s55
	s_add_i32 s57, s55, 1
	s_add_i32 s58, s56, -2
	s_cmp_lt_u32 s58, s57
	s_cselect_b32 s58, -2, 0
	s_add_i32 s58, s54, s58
	s_mul_i32 s58, s58, 0x5a00
	s_add_u32 s60, s50, s58
	s_addc_u32 s61, s51, 0
	global_load_dwordx4 v[168:171], v126, s[60:61]
	s_add_i32 s58, s56, -1
	s_cmp_lt_u32 s58, s57
	s_cselect_b32 s58, -1, 0
	s_add_i32 s58, s54, s58
	s_mul_i32 s58, s58, 0x5a00
	s_add_u32 s60, s50, s58
	s_addc_u32 s61, s51, 0
	global_load_dwordx4 v[172:175], v126, s[60:61]
	s_mul_i32 s58, s54, 0x5a00
	s_add_u32 s60, s50, s58
	s_addc_u32 s61, s51, 0
	global_load_dwordx4 v[176:179], v126, s[60:61]
	s_add_i32 s58, s56, 1
	s_cmp_lt_u32 s58, s57
	s_cselect_b32 s58, 1, 0
	s_add_i32 s58, s54, s58
	s_mul_i32 s58, s58, 0x5a00
	s_add_u32 s60, s50, s58
	s_addc_u32 s61, s51, 0
	global_load_dwordx4 v[180:183], v126, s[60:61]
	s_add_i32 s54, s41, 0x7c00
	s_cmp_lt_u32 s54, 0x8000
	s_cselect_b32 s55, s70, s71
	s_and_b32 s56, s54, s55
	s_add_i32 s57, s55, 1
	s_add_i32 s58, s56, -2
	s_cmp_lt_u32 s58, s57
	s_cselect_b32 s58, -2, 0
	s_add_i32 s58, s54, s58
	s_mul_i32 s58, s58, 0x5a00
	s_add_u32 s60, s50, s58
	s_addc_u32 s61, s51, 0
	global_load_dwordx4 v[184:187], v126, s[60:61]
	s_add_i32 s58, s56, -1
	s_cmp_lt_u32 s58, s57
	s_cselect_b32 s58, -1, 0
	s_add_i32 s58, s54, s58
	s_mul_i32 s58, s58, 0x5a00
	s_add_u32 s60, s50, s58
	s_addc_u32 s61, s51, 0
	global_load_dwordx4 v[188:191], v126, s[60:61]
	s_mul_i32 s58, s54, 0x5a00
	s_add_u32 s60, s50, s58
	s_addc_u32 s61, s51, 0
	global_load_dwordx4 v[192:195], v126, s[60:61]
	s_add_i32 s58, s56, 1
	s_cmp_lt_u32 s58, s57
	s_cselect_b32 s58, 1, 0
	s_add_i32 s58, s54, s58
	s_mul_i32 s58, s58, 0x5a00
	s_add_u32 s60, s50, s58
	s_addc_u32 s61, s51, 0
	global_load_dwordx4 v[196:199], v126, s[60:61]
	s_waitcnt vmcnt(20)
	s_add_i32 s54, s41, 0x6800
	s_cmp_lt_u32 s54, 0x8000
	s_cselect_b32 s55, s70, s71
	s_and_b32 s56, s54, s55
	s_add_i32 s57, s55, 1
	s_add_i32 s58, s56, -2
	s_cmp_lt_u32 s58, s57
	s_cselect_b32 s62, 1.0, 0
	s_add_i32 s58, s56, -1
	s_cmp_lt_u32 s58, s57
	s_cselect_b32 s64, 1.0, 0
	s_mov_b32 s66, 1.0
	s_add_i32 s58, s56, 1
	s_cmp_lt_u32 s58, s57
	s_cselect_b32 s68, 1.0, 0
	v_pk_mul_f32 v[240:241], v[128:129], s[62:63] op_sel_hi:[1,0]
	v_lshlrev_b32_e32 v242, 16, v200
	v_and_b32_e32 v243, 0xffff0000, v200
	v_pk_fma_f32 v[232:233], v[240:241], v[242:243], v[160:161]
	v_pk_mul_f32 v[240:241], v[130:131], s[62:63] op_sel_hi:[1,0]
	v_lshlrev_b32_e32 v242, 16, v201
	v_and_b32_e32 v243, 0xffff0000, v201
	v_pk_fma_f32 v[234:235], v[240:241], v[242:243], v[162:163]
	v_pk_mul_f32 v[240:241], v[132:133], s[62:63] op_sel_hi:[1,0]
	v_lshlrev_b32_e32 v242, 16, v202
	v_and_b32_e32 v243, 0xffff0000, v202
	v_pk_fma_f32 v[236:237], v[240:241], v[242:243], v[164:165]
	v_pk_mul_f32 v[240:241], v[134:135], s[62:63] op_sel_hi:[1,0]
	v_lshlrev_b32_e32 v242, 16, v203
	v_and_b32_e32 v243, 0xffff0000, v203
	v_pk_fma_f32 v[238:239], v[240:241], v[242:243], v[166:167]
	v_pk_mul_f32 v[240:241], v[136:137], s[64:65] op_sel_hi:[1,0]
	v_lshlrev_b32_e32 v242, 16, v204
	v_and_b32_e32 v243, 0xffff0000, v204
	v_pk_fma_f32 v[232:233], v[240:241], v[242:243], v[232:233]
	v_pk_mul_f32 v[240:241], v[138:139], s[64:65] op_sel_hi:[1,0]
	v_lshlrev_b32_e32 v242, 16, v205
	v_and_b32_e32 v243, 0xffff0000, v205
	v_pk_fma_f32 v[234:235], v[240:241], v[242:243], v[234:235]
	v_pk_mul_f32 v[240:241], v[140:141], s[64:65] op_sel_hi:[1,0]
	v_lshlrev_b32_e32 v242, 16, v206
	v_and_b32_e32 v243, 0xffff0000, v206
	v_pk_fma_f32 v[236:237], v[240:241], v[242:243], v[236:237]
	v_pk_mul_f32 v[240:241], v[142:143], s[64:65] op_sel_hi:[1,0]
	v_lshlrev_b32_e32 v242, 16, v207
	v_and_b32_e32 v243, 0xffff0000, v207
	v_pk_fma_f32 v[238:239], v[240:241], v[242:243], v[238:239]
	v_pk_mul_f32 v[240:241], v[144:145], s[66:67] op_sel_hi:[1,0]
	v_lshlrev_b32_e32 v242, 16, v208
	v_and_b32_e32 v243, 0xffff0000, v208
	v_pk_fma_f32 v[232:233], v[240:241], v[242:243], v[232:233]
	v_pk_mul_f32 v[240:241], v[146:147], s[66:67] op_sel_hi:[1,0]
	v_lshlrev_b32_e32 v242, 16, v209
	v_and_b32_e32 v243, 0xffff0000, v209
	v_pk_fma_f32 v[234:235], v[240:241], v[242:243], v[234:235]
	v_pk_mul_f32 v[240:241], v[148:149], s[66:67] op_sel_hi:[1,0]
	v_lshlrev_b32_e32 v242, 16, v210
	v_and_b32_e32 v243, 0xffff0000, v210
	v_pk_fma_f32 v[236:237], v[240:241], v[242:243], v[236:237]
	v_pk_mul_f32 v[240:241], v[150:151], s[66:67] op_sel_hi:[1,0]
	v_lshlrev_b32_e32 v242, 16, v211
	v_and_b32_e32 v243, 0xffff0000, v211
	v_pk_fma_f32 v[238:239], v[240:241], v[242:243], v[238:239]
	v_pk_mul_f32 v[240:241], v[152:153], s[68:69] op_sel_hi:[1,0]
	v_lshlrev_b32_e32 v242, 16, v212
	v_and_b32_e32 v243, 0xffff0000, v212
	v_pk_fma_f32 v[232:233], v[240:241], v[242:243], v[232:233]
	v_pk_mul_f32 v[240:241], v[154:155], s[68:69] op_sel_hi:[1,0]
	v_lshlrev_b32_e32 v242, 16, v213
	v_and_b32_e32 v243, 0xffff0000, v213
	v_pk_fma_f32 v[234:235], v[240:241], v[242:243], v[234:235]
	v_pk_mul_f32 v[240:241], v[156:157], s[68:69] op_sel_hi:[1,0]
	v_lshlrev_b32_e32 v242, 16, v214
	v_and_b32_e32 v243, 0xffff0000, v214
	v_pk_fma_f32 v[236:237], v[240:241], v[242:243], v[236:237]
	v_pk_mul_f32 v[240:241], v[158:159], s[68:69] op_sel_hi:[1,0]
	v_lshlrev_b32_e32 v242, 16, v215
	v_and_b32_e32 v243, 0xffff0000, v215
	v_pk_fma_f32 v[238:239], v[240:241], v[242:243], v[238:239]
	v_cvt_pk_bf16_f32 v248, v232, v233
	v_cvt_pk_bf16_f32 v249, v234, v235
	v_cvt_pk_bf16_f32 v250, v236, v237
	v_cvt_pk_bf16_f32 v251, v238, v239
	s_lshl_b32 s58, s54, 11
	s_add_u32 s60, s52, s58
	s_addc_u32 s61, s53, 0
	global_store_dwordx4 v126, v[248:251], s[60:61]
	s_add_i32 s54, s41, 0x6c00
	s_cmp_lt_u32 s54, 0x8000
	s_cselect_b32 s55, s70, s71
	s_and_b32 s56, s54, s55
	s_add_i32 s57, s55, 1
	s_add_i32 s58, s56, -2
	s_cmp_lt_u32 s58, s57
	s_cselect_b32 s62, 1.0, 0
	s_add_i32 s58, s56, -1
	s_cmp_lt_u32 s58, s57
	s_cselect_b32 s64, 1.0, 0
	s_mov_b32 s66, 1.0
	s_add_i32 s58, s56, 1
	s_cmp_lt_u32 s58, s57
	s_cselect_b32 s68, 1.0, 0
	v_pk_mul_f32 v[240:241], v[128:129], s[62:63] op_sel_hi:[1,0]
	v_lshlrev_b32_e32 v242, 16, v216
	v_and_b32_e32 v243, 0xffff0000, v216
	v_pk_fma_f32 v[232:233], v[240:241], v[242:243], v[160:161]
	v_pk_mul_f32 v[240:241], v[130:131], s[62:63] op_sel_hi:[1,0]
	v_lshlrev_b32_e32 v242, 16, v217
	v_and_b32_e32 v243, 0xffff0000, v217
	v_pk_fma_f32 v[234:235], v[240:241], v[242:243], v[162:163]
	v_pk_mul_f32 v[240:241], v[132:133], s[62:63] op_sel_hi:[1,0]
	v_lshlrev_b32_e32 v242, 16, v218
	v_and_b32_e32 v243, 0xffff0000, v218
	v_pk_fma_f32 v[236:237], v[240:241], v[242:243], v[164:165]
	v_pk_mul_f32 v[240:241], v[134:135], s[62:63] op_sel_hi:[1,0]
	v_lshlrev_b32_e32 v242, 16, v219
	v_and_b32_e32 v243, 0xffff0000, v219
	v_pk_fma_f32 v[238:239], v[240:241], v[242:243], v[166:167]
	v_pk_mul_f32 v[240:241], v[136:137], s[64:65] op_sel_hi:[1,0]
	v_lshlrev_b32_e32 v242, 16, v220
	v_and_b32_e32 v243, 0xffff0000, v220
	v_pk_fma_f32 v[232:233], v[240:241], v[242:243], v[232:233]
	v_pk_mul_f32 v[240:241], v[138:139], s[64:65] op_sel_hi:[1,0]
	v_lshlrev_b32_e32 v242, 16, v221
	v_and_b32_e32 v243, 0xffff0000, v221
	v_pk_fma_f32 v[234:235], v[240:241], v[242:243], v[234:235]
	v_pk_mul_f32 v[240:241], v[140:141], s[64:65] op_sel_hi:[1,0]
	v_lshlrev_b32_e32 v242, 16, v222
	v_and_b32_e32 v243, 0xffff0000, v222
	v_pk_fma_f32 v[236:237], v[240:241], v[242:243], v[236:237]
	v_pk_mul_f32 v[240:241], v[142:143], s[64:65] op_sel_hi:[1,0]
	v_lshlrev_b32_e32 v242, 16, v223
	v_and_b32_e32 v243, 0xffff0000, v223
	v_pk_fma_f32 v[238:239], v[240:241], v[242:243], v[238:239]
	v_pk_mul_f32 v[240:241], v[144:145], s[66:67] op_sel_hi:[1,0]
	v_lshlrev_b32_e32 v242, 16, v224
	v_and_b32_e32 v243, 0xffff0000, v224
	v_pk_fma_f32 v[232:233], v[240:241], v[242:243], v[232:233]
	v_pk_mul_f32 v[240:241], v[146:147], s[66:67] op_sel_hi:[1,0]
	v_lshlrev_b32_e32 v242, 16, v225
	v_and_b32_e32 v243, 0xffff0000, v225
	v_pk_fma_f32 v[234:235], v[240:241], v[242:243], v[234:235]
	v_pk_mul_f32 v[240:241], v[148:149], s[66:67] op_sel_hi:[1,0]
	v_lshlrev_b32_e32 v242, 16, v226
	v_and_b32_e32 v243, 0xffff0000, v226
	v_pk_fma_f32 v[236:237], v[240:241], v[242:243], v[236:237]
	v_pk_mul_f32 v[240:241], v[150:151], s[66:67] op_sel_hi:[1,0]
	v_lshlrev_b32_e32 v242, 16, v227
	v_and_b32_e32 v243, 0xffff0000, v227
	v_pk_fma_f32 v[238:239], v[240:241], v[242:243], v[238:239]
	v_pk_mul_f32 v[240:241], v[152:153], s[68:69] op_sel_hi:[1,0]
	v_lshlrev_b32_e32 v242, 16, v228
	v_and_b32_e32 v243, 0xffff0000, v228
	v_pk_fma_f32 v[232:233], v[240:241], v[242:243], v[232:233]
	v_pk_mul_f32 v[240:241], v[154:155], s[68:69] op_sel_hi:[1,0]
	v_lshlrev_b32_e32 v242, 16, v229
	v_and_b32_e32 v243, 0xffff0000, v229
	v_pk_fma_f32 v[234:235], v[240:241], v[242:243], v[234:235]
	v_pk_mul_f32 v[240:241], v[156:157], s[68:69] op_sel_hi:[1,0]
	v_lshlrev_b32_e32 v242, 16, v230
	v_and_b32_e32 v243, 0xffff0000, v230
	v_pk_fma_f32 v[236:237], v[240:241], v[242:243], v[236:237]
	v_pk_mul_f32 v[240:241], v[158:159], s[68:69] op_sel_hi:[1,0]
	v_lshlrev_b32_e32 v242, 16, v231
	v_and_b32_e32 v243, 0xffff0000, v231
	v_pk_fma_f32 v[238:239], v[240:241], v[242:243], v[238:239]
	v_cvt_pk_bf16_f32 v248, v232, v233
	v_cvt_pk_bf16_f32 v249, v234, v235
	v_cvt_pk_bf16_f32 v250, v236, v237
	v_cvt_pk_bf16_f32 v251, v238, v239
	s_lshl_b32 s58, s54, 11
	s_add_u32 s60, s52, s58
	s_addc_u32 s61, s53, 0
	global_store_dwordx4 v126, v[248:251], s[60:61]
	s_add_i32 s54, s41, 0x8000
	s_cmp_lt_u32 s54, 0x8000
	s_cselect_b32 s55, s70, s71
	s_and_b32 s56, s54, s55
	s_add_i32 s57, s55, 1
	s_add_i32 s58, s56, -2
	s_cmp_lt_u32 s58, s57
	s_cselect_b32 s58, -2, 0
	s_add_i32 s58, s54, s58
	s_mul_i32 s58, s58, 0x5a00
	s_add_u32 s60, s50, s58
	s_addc_u32 s61, s51, 0
	global_load_dwordx4 v[200:203], v126, s[60:61]
	s_add_i32 s58, s56, -1
	s_cmp_lt_u32 s58, s57
	s_cselect_b32 s58, -1, 0
	s_add_i32 s58, s54, s58
	s_mul_i32 s58, s58, 0x5a00
	s_add_u32 s60, s50, s58
	s_addc_u32 s61, s51, 0
	global_load_dwordx4 v[204:207], v126, s[60:61]
	s_mul_i32 s58, s54, 0x5a00
	s_add_u32 s60, s50, s58
	s_addc_u32 s61, s51, 0
	global_load_dwordx4 v[208:211], v126, s[60:61]
	s_add_i32 s58, s56, 1
	s_cmp_lt_u32 s58, s57
	s_cselect_b32 s58, 1, 0
	s_add_i32 s58, s54, s58
	s_mul_i32 s58, s58, 0x5a00
	s_add_u32 s60, s50, s58
	s_addc_u32 s61, s51, 0
	global_load_dwordx4 v[212:215], v126, s[60:61]
	s_add_i32 s54, s41, 0x8400
	s_cmp_lt_u32 s54, 0x8000
	s_cselect_b32 s55, s70, s71
	s_and_b32 s56, s54, s55
	s_add_i32 s57, s55, 1
	s_add_i32 s58, s56, -2
	s_cmp_lt_u32 s58, s57
	s_cselect_b32 s58, -2, 0
	s_add_i32 s58, s54, s58
	s_mul_i32 s58, s58, 0x5a00
	s_add_u32 s60, s50, s58
	s_addc_u32 s61, s51, 0
	global_load_dwordx4 v[216:219], v126, s[60:61]
	s_add_i32 s58, s56, -1
	s_cmp_lt_u32 s58, s57
	s_cselect_b32 s58, -1, 0
	s_add_i32 s58, s54, s58
	s_mul_i32 s58, s58, 0x5a00
	s_add_u32 s60, s50, s58
	s_addc_u32 s61, s51, 0
	global_load_dwordx4 v[220:223], v126, s[60:61]
	s_mul_i32 s58, s54, 0x5a00
	s_add_u32 s60, s50, s58
	s_addc_u32 s61, s51, 0
	global_load_dwordx4 v[224:227], v126, s[60:61]
	s_add_i32 s58, s56, 1
	s_cmp_lt_u32 s58, s57
	s_cselect_b32 s58, 1, 0
	s_add_i32 s58, s54, s58
	s_mul_i32 s58, s58, 0x5a00
	s_add_u32 s60, s50, s58
	s_addc_u32 s61, s51, 0
	global_load_dwordx4 v[228:231], v126, s[60:61]
	s_waitcnt vmcnt(20)
	s_add_i32 s54, s41, 0x7000
	s_cmp_lt_u32 s54, 0x8000
	s_cselect_b32 s55, s70, s71
	s_and_b32 s56, s54, s55
	s_add_i32 s57, s55, 1
	s_add_i32 s58, s56, -2
	s_cmp_lt_u32 s58, s57
	s_cselect_b32 s62, 1.0, 0
	s_add_i32 s58, s56, -1
	s_cmp_lt_u32 s58, s57
	s_cselect_b32 s64, 1.0, 0
	s_mov_b32 s66, 1.0
	s_add_i32 s58, s56, 1
	s_cmp_lt_u32 s58, s57
	s_cselect_b32 s68, 1.0, 0
	v_pk_mul_f32 v[240:241], v[128:129], s[62:63] op_sel_hi:[1,0]
	v_lshlrev_b32_e32 v242, 16, v40
	v_and_b32_e32 v243, 0xffff0000, v40
	v_pk_fma_f32 v[232:233], v[240:241], v[242:243], v[160:161]
	v_pk_mul_f32 v[240:241], v[130:131], s[62:63] op_sel_hi:[1,0]
	v_lshlrev_b32_e32 v242, 16, v41
	v_and_b32_e32 v243, 0xffff0000, v41
	v_pk_fma_f32 v[234:235], v[240:241], v[242:243], v[162:163]
	v_pk_mul_f32 v[240:241], v[132:133], s[62:63] op_sel_hi:[1,0]
	v_lshlrev_b32_e32 v242, 16, v42
	v_and_b32_e32 v243, 0xffff0000, v42
	v_pk_fma_f32 v[236:237], v[240:241], v[242:243], v[164:165]
	v_pk_mul_f32 v[240:241], v[134:135], s[62:63] op_sel_hi:[1,0]
	v_lshlrev_b32_e32 v242, 16, v43
	v_and_b32_e32 v243, 0xffff0000, v43
	v_pk_fma_f32 v[238:239], v[240:241], v[242:243], v[166:167]
	v_pk_mul_f32 v[240:241], v[136:137], s[64:65] op_sel_hi:[1,0]
	v_lshlrev_b32_e32 v242, 16, v44
	v_and_b32_e32 v243, 0xffff0000, v44
	v_pk_fma_f32 v[232:233], v[240:241], v[242:243], v[232:233]
	v_pk_mul_f32 v[240:241], v[138:139], s[64:65] op_sel_hi:[1,0]
	v_lshlrev_b32_e32 v242, 16, v45
	v_and_b32_e32 v243, 0xffff0000, v45
	v_pk_fma_f32 v[234:235], v[240:241], v[242:243], v[234:235]
	v_pk_mul_f32 v[240:241], v[140:141], s[64:65] op_sel_hi:[1,0]
	v_lshlrev_b32_e32 v242, 16, v46
	v_and_b32_e32 v243, 0xffff0000, v46
	v_pk_fma_f32 v[236:237], v[240:241], v[242:243], v[236:237]
	v_pk_mul_f32 v[240:241], v[142:143], s[64:65] op_sel_hi:[1,0]
	v_lshlrev_b32_e32 v242, 16, v47
	v_and_b32_e32 v243, 0xffff0000, v47
	v_pk_fma_f32 v[238:239], v[240:241], v[242:243], v[238:239]
	v_pk_mul_f32 v[240:241], v[144:145], s[66:67] op_sel_hi:[1,0]
	v_lshlrev_b32_e32 v242, 16, v48
	v_and_b32_e32 v243, 0xffff0000, v48
	v_pk_fma_f32 v[232:233], v[240:241], v[242:243], v[232:233]
	v_pk_mul_f32 v[240:241], v[146:147], s[66:67] op_sel_hi:[1,0]
	v_lshlrev_b32_e32 v242, 16, v49
	v_and_b32_e32 v243, 0xffff0000, v49
	v_pk_fma_f32 v[234:235], v[240:241], v[242:243], v[234:235]
	v_pk_mul_f32 v[240:241], v[148:149], s[66:67] op_sel_hi:[1,0]
	v_lshlrev_b32_e32 v242, 16, v50
	v_and_b32_e32 v243, 0xffff0000, v50
	v_pk_fma_f32 v[236:237], v[240:241], v[242:243], v[236:237]
	v_pk_mul_f32 v[240:241], v[150:151], s[66:67] op_sel_hi:[1,0]
	v_lshlrev_b32_e32 v242, 16, v51
	v_and_b32_e32 v243, 0xffff0000, v51
	v_pk_fma_f32 v[238:239], v[240:241], v[242:243], v[238:239]
	v_pk_mul_f32 v[240:241], v[152:153], s[68:69] op_sel_hi:[1,0]
	v_lshlrev_b32_e32 v242, 16, v52
	v_and_b32_e32 v243, 0xffff0000, v52
	v_pk_fma_f32 v[232:233], v[240:241], v[242:243], v[232:233]
	v_pk_mul_f32 v[240:241], v[154:155], s[68:69] op_sel_hi:[1,0]
	v_lshlrev_b32_e32 v242, 16, v53
	v_and_b32_e32 v243, 0xffff0000, v53
	v_pk_fma_f32 v[234:235], v[240:241], v[242:243], v[234:235]
	v_pk_mul_f32 v[240:241], v[156:157], s[68:69] op_sel_hi:[1,0]
	v_lshlrev_b32_e32 v242, 16, v54
	v_and_b32_e32 v243, 0xffff0000, v54
	v_pk_fma_f32 v[236:237], v[240:241], v[242:243], v[236:237]
	v_pk_mul_f32 v[240:241], v[158:159], s[68:69] op_sel_hi:[1,0]
	v_lshlrev_b32_e32 v242, 16, v55
	v_and_b32_e32 v243, 0xffff0000, v55
	v_pk_fma_f32 v[238:239], v[240:241], v[242:243], v[238:239]
	v_cvt_pk_bf16_f32 v248, v232, v233
	v_cvt_pk_bf16_f32 v249, v234, v235
	v_cvt_pk_bf16_f32 v250, v236, v237
	v_cvt_pk_bf16_f32 v251, v238, v239
	s_lshl_b32 s58, s54, 11
	s_add_u32 s60, s52, s58
	s_addc_u32 s61, s53, 0
	global_store_dwordx4 v126, v[248:251], s[60:61]
	s_add_i32 s54, s41, 0x7400
	s_cmp_lt_u32 s54, 0x8000
	s_cselect_b32 s55, s70, s71
	s_and_b32 s56, s54, s55
	s_add_i32 s57, s55, 1
	s_add_i32 s58, s56, -2
	s_cmp_lt_u32 s58, s57
	s_cselect_b32 s62, 1.0, 0
	s_add_i32 s58, s56, -1
	s_cmp_lt_u32 s58, s57
	s_cselect_b32 s64, 1.0, 0
	s_mov_b32 s66, 1.0
	s_add_i32 s58, s56, 1
	s_cmp_lt_u32 s58, s57
	s_cselect_b32 s68, 1.0, 0
	v_pk_mul_f32 v[240:241], v[128:129], s[62:63] op_sel_hi:[1,0]
	v_lshlrev_b32_e32 v242, 16, v56
	v_and_b32_e32 v243, 0xffff0000, v56
	v_pk_fma_f32 v[232:233], v[240:241], v[242:243], v[160:161]
	v_pk_mul_f32 v[240:241], v[130:131], s[62:63] op_sel_hi:[1,0]
	v_lshlrev_b32_e32 v242, 16, v57
	v_and_b32_e32 v243, 0xffff0000, v57
	v_pk_fma_f32 v[234:235], v[240:241], v[242:243], v[162:163]
	v_pk_mul_f32 v[240:241], v[132:133], s[62:63] op_sel_hi:[1,0]
	v_lshlrev_b32_e32 v242, 16, v58
	v_and_b32_e32 v243, 0xffff0000, v58
	v_pk_fma_f32 v[236:237], v[240:241], v[242:243], v[164:165]
	v_pk_mul_f32 v[240:241], v[134:135], s[62:63] op_sel_hi:[1,0]
	v_lshlrev_b32_e32 v242, 16, v59
	v_and_b32_e32 v243, 0xffff0000, v59
	v_pk_fma_f32 v[238:239], v[240:241], v[242:243], v[166:167]
	v_pk_mul_f32 v[240:241], v[136:137], s[64:65] op_sel_hi:[1,0]
	v_lshlrev_b32_e32 v242, 16, v60
	v_and_b32_e32 v243, 0xffff0000, v60
	v_pk_fma_f32 v[232:233], v[240:241], v[242:243], v[232:233]
	v_pk_mul_f32 v[240:241], v[138:139], s[64:65] op_sel_hi:[1,0]
	v_lshlrev_b32_e32 v242, 16, v61
	v_and_b32_e32 v243, 0xffff0000, v61
	v_pk_fma_f32 v[234:235], v[240:241], v[242:243], v[234:235]
	v_pk_mul_f32 v[240:241], v[140:141], s[64:65] op_sel_hi:[1,0]
	v_lshlrev_b32_e32 v242, 16, v62
	v_and_b32_e32 v243, 0xffff0000, v62
	v_pk_fma_f32 v[236:237], v[240:241], v[242:243], v[236:237]
	v_pk_mul_f32 v[240:241], v[142:143], s[64:65] op_sel_hi:[1,0]
	v_lshlrev_b32_e32 v242, 16, v63
	v_and_b32_e32 v243, 0xffff0000, v63
	v_pk_fma_f32 v[238:239], v[240:241], v[242:243], v[238:239]
	v_pk_mul_f32 v[240:241], v[144:145], s[66:67] op_sel_hi:[1,0]
	v_lshlrev_b32_e32 v242, 16, v64
	v_and_b32_e32 v243, 0xffff0000, v64
	v_pk_fma_f32 v[232:233], v[240:241], v[242:243], v[232:233]
	v_pk_mul_f32 v[240:241], v[146:147], s[66:67] op_sel_hi:[1,0]
	v_lshlrev_b32_e32 v242, 16, v65
	v_and_b32_e32 v243, 0xffff0000, v65
	v_pk_fma_f32 v[234:235], v[240:241], v[242:243], v[234:235]
	v_pk_mul_f32 v[240:241], v[148:149], s[66:67] op_sel_hi:[1,0]
	v_lshlrev_b32_e32 v242, 16, v66
	v_and_b32_e32 v243, 0xffff0000, v66
	v_pk_fma_f32 v[236:237], v[240:241], v[242:243], v[236:237]
	v_pk_mul_f32 v[240:241], v[150:151], s[66:67] op_sel_hi:[1,0]
	v_lshlrev_b32_e32 v242, 16, v67
	v_and_b32_e32 v243, 0xffff0000, v67
	v_pk_fma_f32 v[238:239], v[240:241], v[242:243], v[238:239]
	v_pk_mul_f32 v[240:241], v[152:153], s[68:69] op_sel_hi:[1,0]
	v_lshlrev_b32_e32 v242, 16, v68
	v_and_b32_e32 v243, 0xffff0000, v68
	v_pk_fma_f32 v[232:233], v[240:241], v[242:243], v[232:233]
	v_pk_mul_f32 v[240:241], v[154:155], s[68:69] op_sel_hi:[1,0]
	v_lshlrev_b32_e32 v242, 16, v69
	v_and_b32_e32 v243, 0xffff0000, v69
	v_pk_fma_f32 v[234:235], v[240:241], v[242:243], v[234:235]
	v_pk_mul_f32 v[240:241], v[156:157], s[68:69] op_sel_hi:[1,0]
	v_lshlrev_b32_e32 v242, 16, v70
	v_and_b32_e32 v243, 0xffff0000, v70
	v_pk_fma_f32 v[236:237], v[240:241], v[242:243], v[236:237]
	v_pk_mul_f32 v[240:241], v[158:159], s[68:69] op_sel_hi:[1,0]
	v_lshlrev_b32_e32 v242, 16, v71
	v_and_b32_e32 v243, 0xffff0000, v71
	v_pk_fma_f32 v[238:239], v[240:241], v[242:243], v[238:239]
	v_cvt_pk_bf16_f32 v248, v232, v233
	v_cvt_pk_bf16_f32 v249, v234, v235
	v_cvt_pk_bf16_f32 v250, v236, v237
	v_cvt_pk_bf16_f32 v251, v238, v239
	s_lshl_b32 s58, s54, 11
	s_add_u32 s60, s52, s58
	s_addc_u32 s61, s53, 0
	global_store_dwordx4 v126, v[248:251], s[60:61]
	s_waitcnt vmcnt(12)
	s_add_i32 s54, s41, 0x7800
	s_cmp_lt_u32 s54, 0x8000
	s_cselect_b32 s55, s70, s71
	s_and_b32 s56, s54, s55
	s_add_i32 s57, s55, 1
	s_add_i32 s58, s56, -2
	s_cmp_lt_u32 s58, s57
	s_cselect_b32 s62, 1.0, 0
	s_add_i32 s58, s56, -1
	s_cmp_lt_u32 s58, s57
	s_cselect_b32 s64, 1.0, 0
	s_mov_b32 s66, 1.0
	s_add_i32 s58, s56, 1
	s_cmp_lt_u32 s58, s57
	s_cselect_b32 s68, 1.0, 0
	v_pk_mul_f32 v[240:241], v[128:129], s[62:63] op_sel_hi:[1,0]
	v_lshlrev_b32_e32 v242, 16, v168
	v_and_b32_e32 v243, 0xffff0000, v168
	v_pk_fma_f32 v[232:233], v[240:241], v[242:243], v[160:161]
	v_pk_mul_f32 v[240:241], v[130:131], s[62:63] op_sel_hi:[1,0]
	v_lshlrev_b32_e32 v242, 16, v169
	v_and_b32_e32 v243, 0xffff0000, v169
	v_pk_fma_f32 v[234:235], v[240:241], v[242:243], v[162:163]
	v_pk_mul_f32 v[240:241], v[132:133], s[62:63] op_sel_hi:[1,0]
	v_lshlrev_b32_e32 v242, 16, v170
	v_and_b32_e32 v243, 0xffff0000, v170
	v_pk_fma_f32 v[236:237], v[240:241], v[242:243], v[164:165]
	v_pk_mul_f32 v[240:241], v[134:135], s[62:63] op_sel_hi:[1,0]
	v_lshlrev_b32_e32 v242, 16, v171
	v_and_b32_e32 v243, 0xffff0000, v171
	v_pk_fma_f32 v[238:239], v[240:241], v[242:243], v[166:167]
	v_pk_mul_f32 v[240:241], v[136:137], s[64:65] op_sel_hi:[1,0]
	v_lshlrev_b32_e32 v242, 16, v172
	v_and_b32_e32 v243, 0xffff0000, v172
	v_pk_fma_f32 v[232:233], v[240:241], v[242:243], v[232:233]
	v_pk_mul_f32 v[240:241], v[138:139], s[64:65] op_sel_hi:[1,0]
	v_lshlrev_b32_e32 v242, 16, v173
	v_and_b32_e32 v243, 0xffff0000, v173
	v_pk_fma_f32 v[234:235], v[240:241], v[242:243], v[234:235]
	v_pk_mul_f32 v[240:241], v[140:141], s[64:65] op_sel_hi:[1,0]
	v_lshlrev_b32_e32 v242, 16, v174
	v_and_b32_e32 v243, 0xffff0000, v174
	v_pk_fma_f32 v[236:237], v[240:241], v[242:243], v[236:237]
	v_pk_mul_f32 v[240:241], v[142:143], s[64:65] op_sel_hi:[1,0]
	v_lshlrev_b32_e32 v242, 16, v175
	v_and_b32_e32 v243, 0xffff0000, v175
	v_pk_fma_f32 v[238:239], v[240:241], v[242:243], v[238:239]
	v_pk_mul_f32 v[240:241], v[144:145], s[66:67] op_sel_hi:[1,0]
	v_lshlrev_b32_e32 v242, 16, v176
	v_and_b32_e32 v243, 0xffff0000, v176
	v_pk_fma_f32 v[232:233], v[240:241], v[242:243], v[232:233]
	v_pk_mul_f32 v[240:241], v[146:147], s[66:67] op_sel_hi:[1,0]
	v_lshlrev_b32_e32 v242, 16, v177
	v_and_b32_e32 v243, 0xffff0000, v177
	v_pk_fma_f32 v[234:235], v[240:241], v[242:243], v[234:235]
	v_pk_mul_f32 v[240:241], v[148:149], s[66:67] op_sel_hi:[1,0]
	v_lshlrev_b32_e32 v242, 16, v178
	v_and_b32_e32 v243, 0xffff0000, v178
	v_pk_fma_f32 v[236:237], v[240:241], v[242:243], v[236:237]
	v_pk_mul_f32 v[240:241], v[150:151], s[66:67] op_sel_hi:[1,0]
	v_lshlrev_b32_e32 v242, 16, v179
	v_and_b32_e32 v243, 0xffff0000, v179
	v_pk_fma_f32 v[238:239], v[240:241], v[242:243], v[238:239]
	v_pk_mul_f32 v[240:241], v[152:153], s[68:69] op_sel_hi:[1,0]
	v_lshlrev_b32_e32 v242, 16, v180
	v_and_b32_e32 v243, 0xffff0000, v180
	v_pk_fma_f32 v[232:233], v[240:241], v[242:243], v[232:233]
	v_pk_mul_f32 v[240:241], v[154:155], s[68:69] op_sel_hi:[1,0]
	v_lshlrev_b32_e32 v242, 16, v181
	v_and_b32_e32 v243, 0xffff0000, v181
	v_pk_fma_f32 v[234:235], v[240:241], v[242:243], v[234:235]
	v_pk_mul_f32 v[240:241], v[156:157], s[68:69] op_sel_hi:[1,0]
	v_lshlrev_b32_e32 v242, 16, v182
	v_and_b32_e32 v243, 0xffff0000, v182
	v_pk_fma_f32 v[236:237], v[240:241], v[242:243], v[236:237]
	v_pk_mul_f32 v[240:241], v[158:159], s[68:69] op_sel_hi:[1,0]
	v_lshlrev_b32_e32 v242, 16, v183
	v_and_b32_e32 v243, 0xffff0000, v183
	v_pk_fma_f32 v[238:239], v[240:241], v[242:243], v[238:239]
	v_cvt_pk_bf16_f32 v248, v232, v233
	v_cvt_pk_bf16_f32 v249, v234, v235
	v_cvt_pk_bf16_f32 v250, v236, v237
	v_cvt_pk_bf16_f32 v251, v238, v239
	s_lshl_b32 s58, s54, 11
	s_add_u32 s60, s52, s58
	s_addc_u32 s61, s53, 0
	global_store_dwordx4 v126, v[248:251], s[60:61]
	s_add_i32 s54, s41, 0x7c00
	s_cmp_lt_u32 s54, 0x8000
	s_cselect_b32 s55, s70, s71
	s_and_b32 s56, s54, s55
	s_add_i32 s57, s55, 1
	s_add_i32 s58, s56, -2
	s_cmp_lt_u32 s58, s57
	s_cselect_b32 s62, 1.0, 0
	s_add_i32 s58, s56, -1
	s_cmp_lt_u32 s58, s57
	s_cselect_b32 s64, 1.0, 0
	s_mov_b32 s66, 1.0
	s_add_i32 s58, s56, 1
	s_cmp_lt_u32 s58, s57
	s_cselect_b32 s68, 1.0, 0
	v_pk_mul_f32 v[240:241], v[128:129], s[62:63] op_sel_hi:[1,0]
	v_lshlrev_b32_e32 v242, 16, v184
	v_and_b32_e32 v243, 0xffff0000, v184
	v_pk_fma_f32 v[232:233], v[240:241], v[242:243], v[160:161]
	v_pk_mul_f32 v[240:241], v[130:131], s[62:63] op_sel_hi:[1,0]
	v_lshlrev_b32_e32 v242, 16, v185
	v_and_b32_e32 v243, 0xffff0000, v185
	v_pk_fma_f32 v[234:235], v[240:241], v[242:243], v[162:163]
	v_pk_mul_f32 v[240:241], v[132:133], s[62:63] op_sel_hi:[1,0]
	v_lshlrev_b32_e32 v242, 16, v186
	v_and_b32_e32 v243, 0xffff0000, v186
	v_pk_fma_f32 v[236:237], v[240:241], v[242:243], v[164:165]
	v_pk_mul_f32 v[240:241], v[134:135], s[62:63] op_sel_hi:[1,0]
	v_lshlrev_b32_e32 v242, 16, v187
	v_and_b32_e32 v243, 0xffff0000, v187
	v_pk_fma_f32 v[238:239], v[240:241], v[242:243], v[166:167]
	v_pk_mul_f32 v[240:241], v[136:137], s[64:65] op_sel_hi:[1,0]
	v_lshlrev_b32_e32 v242, 16, v188
	v_and_b32_e32 v243, 0xffff0000, v188
	v_pk_fma_f32 v[232:233], v[240:241], v[242:243], v[232:233]
	v_pk_mul_f32 v[240:241], v[138:139], s[64:65] op_sel_hi:[1,0]
	v_lshlrev_b32_e32 v242, 16, v189
	v_and_b32_e32 v243, 0xffff0000, v189
	v_pk_fma_f32 v[234:235], v[240:241], v[242:243], v[234:235]
	v_pk_mul_f32 v[240:241], v[140:141], s[64:65] op_sel_hi:[1,0]
	v_lshlrev_b32_e32 v242, 16, v190
	v_and_b32_e32 v243, 0xffff0000, v190
	v_pk_fma_f32 v[236:237], v[240:241], v[242:243], v[236:237]
	v_pk_mul_f32 v[240:241], v[142:143], s[64:65] op_sel_hi:[1,0]
	v_lshlrev_b32_e32 v242, 16, v191
	v_and_b32_e32 v243, 0xffff0000, v191
	v_pk_fma_f32 v[238:239], v[240:241], v[242:243], v[238:239]
	v_pk_mul_f32 v[240:241], v[144:145], s[66:67] op_sel_hi:[1,0]
	v_lshlrev_b32_e32 v242, 16, v192
	v_and_b32_e32 v243, 0xffff0000, v192
	v_pk_fma_f32 v[232:233], v[240:241], v[242:243], v[232:233]
	v_pk_mul_f32 v[240:241], v[146:147], s[66:67] op_sel_hi:[1,0]
	v_lshlrev_b32_e32 v242, 16, v193
	v_and_b32_e32 v243, 0xffff0000, v193
	v_pk_fma_f32 v[234:235], v[240:241], v[242:243], v[234:235]
	v_pk_mul_f32 v[240:241], v[148:149], s[66:67] op_sel_hi:[1,0]
	v_lshlrev_b32_e32 v242, 16, v194
	v_and_b32_e32 v243, 0xffff0000, v194
	v_pk_fma_f32 v[236:237], v[240:241], v[242:243], v[236:237]
	v_pk_mul_f32 v[240:241], v[150:151], s[66:67] op_sel_hi:[1,0]
	v_lshlrev_b32_e32 v242, 16, v195
	v_and_b32_e32 v243, 0xffff0000, v195
	v_pk_fma_f32 v[238:239], v[240:241], v[242:243], v[238:239]
	v_pk_mul_f32 v[240:241], v[152:153], s[68:69] op_sel_hi:[1,0]
	v_lshlrev_b32_e32 v242, 16, v196
	v_and_b32_e32 v243, 0xffff0000, v196
	v_pk_fma_f32 v[232:233], v[240:241], v[242:243], v[232:233]
	v_pk_mul_f32 v[240:241], v[154:155], s[68:69] op_sel_hi:[1,0]
	v_lshlrev_b32_e32 v242, 16, v197
	v_and_b32_e32 v243, 0xffff0000, v197
	v_pk_fma_f32 v[234:235], v[240:241], v[242:243], v[234:235]
	v_pk_mul_f32 v[240:241], v[156:157], s[68:69] op_sel_hi:[1,0]
	v_lshlrev_b32_e32 v242, 16, v198
	v_and_b32_e32 v243, 0xffff0000, v198
	v_pk_fma_f32 v[236:237], v[240:241], v[242:243], v[236:237]
	v_pk_mul_f32 v[240:241], v[158:159], s[68:69] op_sel_hi:[1,0]
	v_lshlrev_b32_e32 v242, 16, v199
	v_and_b32_e32 v243, 0xffff0000, v199
	v_pk_fma_f32 v[238:239], v[240:241], v[242:243], v[238:239]
	v_cvt_pk_bf16_f32 v248, v232, v233
	v_cvt_pk_bf16_f32 v249, v234, v235
	v_cvt_pk_bf16_f32 v250, v236, v237
	v_cvt_pk_bf16_f32 v251, v238, v239
	s_lshl_b32 s58, s54, 11
	s_add_u32 s60, s52, s58
	s_addc_u32 s61, s53, 0
	global_store_dwordx4 v126, v[248:251], s[60:61]
	s_waitcnt vmcnt(4)
	s_add_i32 s54, s41, 0x8000
	s_cmp_lt_u32 s54, 0x8000
	s_cselect_b32 s55, s70, s71
	s_and_b32 s56, s54, s55
	s_add_i32 s57, s55, 1
	s_add_i32 s58, s56, -2
	s_cmp_lt_u32 s58, s57
	s_cselect_b32 s62, 1.0, 0
	s_add_i32 s58, s56, -1
	s_cmp_lt_u32 s58, s57
	s_cselect_b32 s64, 1.0, 0
	s_mov_b32 s66, 1.0
	s_add_i32 s58, s56, 1
	s_cmp_lt_u32 s58, s57
	s_cselect_b32 s68, 1.0, 0
	v_pk_mul_f32 v[240:241], v[128:129], s[62:63] op_sel_hi:[1,0]
	v_lshlrev_b32_e32 v242, 16, v200
	v_and_b32_e32 v243, 0xffff0000, v200
	v_pk_fma_f32 v[232:233], v[240:241], v[242:243], v[160:161]
	v_pk_mul_f32 v[240:241], v[130:131], s[62:63] op_sel_hi:[1,0]
	v_lshlrev_b32_e32 v242, 16, v201
	v_and_b32_e32 v243, 0xffff0000, v201
	v_pk_fma_f32 v[234:235], v[240:241], v[242:243], v[162:163]
	v_pk_mul_f32 v[240:241], v[132:133], s[62:63] op_sel_hi:[1,0]
	v_lshlrev_b32_e32 v242, 16, v202
	v_and_b32_e32 v243, 0xffff0000, v202
	v_pk_fma_f32 v[236:237], v[240:241], v[242:243], v[164:165]
	v_pk_mul_f32 v[240:241], v[134:135], s[62:63] op_sel_hi:[1,0]
	v_lshlrev_b32_e32 v242, 16, v203
	v_and_b32_e32 v243, 0xffff0000, v203
	v_pk_fma_f32 v[238:239], v[240:241], v[242:243], v[166:167]
	v_pk_mul_f32 v[240:241], v[136:137], s[64:65] op_sel_hi:[1,0]
	v_lshlrev_b32_e32 v242, 16, v204
	v_and_b32_e32 v243, 0xffff0000, v204
	v_pk_fma_f32 v[232:233], v[240:241], v[242:243], v[232:233]
	v_pk_mul_f32 v[240:241], v[138:139], s[64:65] op_sel_hi:[1,0]
	v_lshlrev_b32_e32 v242, 16, v205
	v_and_b32_e32 v243, 0xffff0000, v205
	v_pk_fma_f32 v[234:235], v[240:241], v[242:243], v[234:235]
	v_pk_mul_f32 v[240:241], v[140:141], s[64:65] op_sel_hi:[1,0]
	v_lshlrev_b32_e32 v242, 16, v206
	v_and_b32_e32 v243, 0xffff0000, v206
	v_pk_fma_f32 v[236:237], v[240:241], v[242:243], v[236:237]
	v_pk_mul_f32 v[240:241], v[142:143], s[64:65] op_sel_hi:[1,0]
	v_lshlrev_b32_e32 v242, 16, v207
	v_and_b32_e32 v243, 0xffff0000, v207
	v_pk_fma_f32 v[238:239], v[240:241], v[242:243], v[238:239]
	v_pk_mul_f32 v[240:241], v[144:145], s[66:67] op_sel_hi:[1,0]
	v_lshlrev_b32_e32 v242, 16, v208
	v_and_b32_e32 v243, 0xffff0000, v208
	v_pk_fma_f32 v[232:233], v[240:241], v[242:243], v[232:233]
	v_pk_mul_f32 v[240:241], v[146:147], s[66:67] op_sel_hi:[1,0]
	v_lshlrev_b32_e32 v242, 16, v209
	v_and_b32_e32 v243, 0xffff0000, v209
	v_pk_fma_f32 v[234:235], v[240:241], v[242:243], v[234:235]
	v_pk_mul_f32 v[240:241], v[148:149], s[66:67] op_sel_hi:[1,0]
	v_lshlrev_b32_e32 v242, 16, v210
	v_and_b32_e32 v243, 0xffff0000, v210
	v_pk_fma_f32 v[236:237], v[240:241], v[242:243], v[236:237]
	v_pk_mul_f32 v[240:241], v[150:151], s[66:67] op_sel_hi:[1,0]
	v_lshlrev_b32_e32 v242, 16, v211
	v_and_b32_e32 v243, 0xffff0000, v211
	v_pk_fma_f32 v[238:239], v[240:241], v[242:243], v[238:239]
	v_pk_mul_f32 v[240:241], v[152:153], s[68:69] op_sel_hi:[1,0]
	v_lshlrev_b32_e32 v242, 16, v212
	v_and_b32_e32 v243, 0xffff0000, v212
	v_pk_fma_f32 v[232:233], v[240:241], v[242:243], v[232:233]
	v_pk_mul_f32 v[240:241], v[154:155], s[68:69] op_sel_hi:[1,0]
	v_lshlrev_b32_e32 v242, 16, v213
	v_and_b32_e32 v243, 0xffff0000, v213
	v_pk_fma_f32 v[234:235], v[240:241], v[242:243], v[234:235]
	v_pk_mul_f32 v[240:241], v[156:157], s[68:69] op_sel_hi:[1,0]
	v_lshlrev_b32_e32 v242, 16, v214
	v_and_b32_e32 v243, 0xffff0000, v214
	v_pk_fma_f32 v[236:237], v[240:241], v[242:243], v[236:237]
	v_pk_mul_f32 v[240:241], v[158:159], s[68:69] op_sel_hi:[1,0]
	v_lshlrev_b32_e32 v242, 16, v215
	v_and_b32_e32 v243, 0xffff0000, v215
	v_pk_fma_f32 v[238:239], v[240:241], v[242:243], v[238:239]
	v_cvt_pk_bf16_f32 v248, v232, v233
	v_cvt_pk_bf16_f32 v249, v234, v235
	v_cvt_pk_bf16_f32 v250, v236, v237
	v_cvt_pk_bf16_f32 v251, v238, v239
	s_lshl_b32 s58, s54, 11
	s_add_u32 s60, s52, s58
	s_addc_u32 s61, s53, 0
	global_store_dwordx4 v126, v[248:251], s[60:61]
	s_add_i32 s54, s41, 0x8400
	s_cmp_lt_u32 s54, 0x8000
	s_cselect_b32 s55, s70, s71
	s_and_b32 s56, s54, s55
	s_add_i32 s57, s55, 1
	s_add_i32 s58, s56, -2
	s_cmp_lt_u32 s58, s57
	s_cselect_b32 s62, 1.0, 0
	s_add_i32 s58, s56, -1
	s_cmp_lt_u32 s58, s57
	s_cselect_b32 s64, 1.0, 0
	s_mov_b32 s66, 1.0
	s_add_i32 s58, s56, 1
	s_cmp_lt_u32 s58, s57
	s_cselect_b32 s68, 1.0, 0
	v_pk_mul_f32 v[240:241], v[128:129], s[62:63] op_sel_hi:[1,0]
	v_lshlrev_b32_e32 v242, 16, v216
	v_and_b32_e32 v243, 0xffff0000, v216
	v_pk_fma_f32 v[232:233], v[240:241], v[242:243], v[160:161]
	v_pk_mul_f32 v[240:241], v[130:131], s[62:63] op_sel_hi:[1,0]
	v_lshlrev_b32_e32 v242, 16, v217
	v_and_b32_e32 v243, 0xffff0000, v217
	v_pk_fma_f32 v[234:235], v[240:241], v[242:243], v[162:163]
	v_pk_mul_f32 v[240:241], v[132:133], s[62:63] op_sel_hi:[1,0]
	v_lshlrev_b32_e32 v242, 16, v218
	v_and_b32_e32 v243, 0xffff0000, v218
	v_pk_fma_f32 v[236:237], v[240:241], v[242:243], v[164:165]
	v_pk_mul_f32 v[240:241], v[134:135], s[62:63] op_sel_hi:[1,0]
	v_lshlrev_b32_e32 v242, 16, v219
	v_and_b32_e32 v243, 0xffff0000, v219
	v_pk_fma_f32 v[238:239], v[240:241], v[242:243], v[166:167]
	v_pk_mul_f32 v[240:241], v[136:137], s[64:65] op_sel_hi:[1,0]
	v_lshlrev_b32_e32 v242, 16, v220
	v_and_b32_e32 v243, 0xffff0000, v220
	v_pk_fma_f32 v[232:233], v[240:241], v[242:243], v[232:233]
	v_pk_mul_f32 v[240:241], v[138:139], s[64:65] op_sel_hi:[1,0]
	v_lshlrev_b32_e32 v242, 16, v221
	v_and_b32_e32 v243, 0xffff0000, v221
	v_pk_fma_f32 v[234:235], v[240:241], v[242:243], v[234:235]
	v_pk_mul_f32 v[240:241], v[140:141], s[64:65] op_sel_hi:[1,0]
	v_lshlrev_b32_e32 v242, 16, v222
	v_and_b32_e32 v243, 0xffff0000, v222
	v_pk_fma_f32 v[236:237], v[240:241], v[242:243], v[236:237]
	v_pk_mul_f32 v[240:241], v[142:143], s[64:65] op_sel_hi:[1,0]
	v_lshlrev_b32_e32 v242, 16, v223
	v_and_b32_e32 v243, 0xffff0000, v223
	v_pk_fma_f32 v[238:239], v[240:241], v[242:243], v[238:239]
	v_pk_mul_f32 v[240:241], v[144:145], s[66:67] op_sel_hi:[1,0]
	v_lshlrev_b32_e32 v242, 16, v224
	v_and_b32_e32 v243, 0xffff0000, v224
	v_pk_fma_f32 v[232:233], v[240:241], v[242:243], v[232:233]
	v_pk_mul_f32 v[240:241], v[146:147], s[66:67] op_sel_hi:[1,0]
	v_lshlrev_b32_e32 v242, 16, v225
	v_and_b32_e32 v243, 0xffff0000, v225
	v_pk_fma_f32 v[234:235], v[240:241], v[242:243], v[234:235]
	v_pk_mul_f32 v[240:241], v[148:149], s[66:67] op_sel_hi:[1,0]
	v_lshlrev_b32_e32 v242, 16, v226
	v_and_b32_e32 v243, 0xffff0000, v226
	v_pk_fma_f32 v[236:237], v[240:241], v[242:243], v[236:237]
	v_pk_mul_f32 v[240:241], v[150:151], s[66:67] op_sel_hi:[1,0]
	v_lshlrev_b32_e32 v242, 16, v227
	v_and_b32_e32 v243, 0xffff0000, v227
	v_pk_fma_f32 v[238:239], v[240:241], v[242:243], v[238:239]
	v_pk_mul_f32 v[240:241], v[152:153], s[68:69] op_sel_hi:[1,0]
	v_lshlrev_b32_e32 v242, 16, v228
	v_and_b32_e32 v243, 0xffff0000, v228
	v_pk_fma_f32 v[232:233], v[240:241], v[242:243], v[232:233]
	v_pk_mul_f32 v[240:241], v[154:155], s[68:69] op_sel_hi:[1,0]
	v_lshlrev_b32_e32 v242, 16, v229
	v_and_b32_e32 v243, 0xffff0000, v229
	v_pk_fma_f32 v[234:235], v[240:241], v[242:243], v[234:235]
	v_pk_mul_f32 v[240:241], v[156:157], s[68:69] op_sel_hi:[1,0]
	v_lshlrev_b32_e32 v242, 16, v230
	v_and_b32_e32 v243, 0xffff0000, v230
	v_pk_fma_f32 v[236:237], v[240:241], v[242:243], v[236:237]
	v_pk_mul_f32 v[240:241], v[158:159], s[68:69] op_sel_hi:[1,0]
	v_lshlrev_b32_e32 v242, 16, v231
	v_and_b32_e32 v243, 0xffff0000, v231
	v_pk_fma_f32 v[238:239], v[240:241], v[242:243], v[238:239]
	v_cvt_pk_bf16_f32 v248, v232, v233
	v_cvt_pk_bf16_f32 v249, v234, v235
	v_cvt_pk_bf16_f32 v250, v236, v237
	v_cvt_pk_bf16_f32 v251, v238, v239
	s_lshl_b32 s58, s54, 11
	s_add_u32 s60, s52, s58
	s_addc_u32 s61, s53, 0
	global_store_dwordx4 v126, v[248:251], s[60:61]
	s_branch .LBB0_340

.LBB0_2158:
	s_cmp_lt_i32 s88, 20
	s_cselect_b64 s[14:15], -1, 0
	s_and_b64 s[2:3], s[14:15], s[2:3]
	s_andn2_b64 vcc, exec, s[2:3]
	s_cbranch_vccnz .LBB0_2181
	v_mbcnt_lo_u32_b32 v0, -1, 0
	v_mbcnt_hi_u32_b32 v0, -1, v0
	v_readlane_b32 s2, v254, 0
	s_mov_b64 s[16:17], s[86:87]
	v_lshl_or_b32 v80, s96, 6, v0
	s_mov_b32 s18, s2
	s_load_dword s21, s[0:1], 0x108
	v_lshl_add_u32 v0, s18, 9, v80
	v_ashrrev_i32_e32 v74, 7, v0
	s_mov_b32 s19, 0x8800
	v_lshlrev_b32_e32 v78, 3, v80
	v_cmp_gt_i32_e32 vcc, s19, v74
	s_load_dwordx2 s[2:3], s[0:1], 0x60
	s_waitcnt lgkmcnt(0)
	s_load_dwordx2 s[8:9], s[0:1], 0x68
	s_waitcnt lgkmcnt(0)
	s_and_saveexec_b64 s[4:5], vcc
	s_cbranch_execz .LBB0_2164
	s_waitcnt vmcnt(0)
	v_and_b32_e32 v56, 0x3f8, v78
	v_mov_b32_e32 v73, 0
	v_lshlrev_b32_e32 v72, 2, v56
	v_lshl_add_u64 v[0:1], s[8:9], 0, v[72:73]
	v_add_co_u32_e32 v10, vcc, 0x1000, v0
	v_lshl_add_u64 v[24:25], s[2:3], 0, v[72:73]
	s_nop 0
	v_addc_co_u32_e32 v11, vcc, 0, v1, vcc
	v_add_co_u32_e32 v16, vcc, 0x7000, v24
	s_mov_b64 s[2:3], 0x4000
	s_nop 0
	v_addc_co_u32_e32 v17, vcc, 0, v25, vcc
	v_add_co_u32_e32 v26, vcc, 0x6000, v24
	v_lshl_add_u64 v[58:59], v[24:25], 0, s[2:3]
	s_nop 0
	v_addc_co_u32_e32 v27, vcc, 0, v25, vcc
	v_add_co_u32_e32 v32, vcc, 0x5000, v24
	s_mov_b64 s[2:3], 0x7000
	s_nop 0
	v_addc_co_u32_e32 v33, vcc, 0, v25, vcc
	v_lshl_add_u64 v[60:61], v[24:25], 0, s[2:3]
	s_mov_b64 s[2:3], 0x6000
	v_add_co_u32_e32 v34, vcc, 0x4000, v24
	s_mov_b64 s[8:9], 0x1000
	v_lshl_add_u64 v[18:19], v[24:25], 0, s[2:3]
	s_mov_b64 s[2:3], 0x5000
	v_addc_co_u32_e32 v35, vcc, 0, v25, vcc
	s_mov_b32 s22, 0x8000
	v_lshl_add_u64 v[8:9], v[0:1], 0, s[8:9]
	v_lshl_add_u64 v[28:29], v[24:25], 0, s[2:3]
	v_cmp_gt_i32_e32 vcc, s22, v74
	v_mov_b32_e32 v82, 0xff
	v_mov_b32_e32 v83, 0xfff
	global_load_dwordx4 v[0:3], v[10:11], off
	global_load_dwordx4 v[4:7], v[8:9], off offset:16
	s_nop 0
	global_load_dwordx4 v[8:11], v[16:17], off
	global_load_dwordx4 v[12:15], v[18:19], off offset:16
	s_nop 0
	global_load_dwordx4 v[16:19], v[26:27], off
	global_load_dwordx4 v[20:23], v[28:29], off offset:16
	s_nop 0
	global_load_dwordx4 v[24:27], v[32:33], off
	global_load_dwordx4 v[28:31], v[34:35], off
	v_cndmask_b32_e32 v32, v82, v83, vcc
	v_mov_b32_e32 v79, 0x100
	v_mov_b32_e32 v81, 0x1000
	v_and_b32_e32 v37, v32, v74
	s_add_u32 s6, s16, 0x17900000
	v_cndmask_b32_e32 v36, v79, v81, vcc
	v_add_u32_e32 v32, -2, v37
	s_addc_u32 s7, s17, 0
	v_add_u32_e32 v33, -2, v74
	v_cmp_lt_u32_e32 vcc, v32, v36
	s_movk_i32 s23, 0x5a00
	v_lshlrev_b32_e32 v72, 1, v56
	v_cndmask_b32_e32 v34, v74, v33, vcc
	v_mov_b64_e32 v[32:33], s[6:7]
	v_mad_i64_i32 v[34:35], s[2:3], v34, s23, v[32:33]
	s_movk_i32 s20, 0x1000
	v_lshl_add_u64 v[34:35], v[34:35], 0, v[72:73]
	v_add_co_u32_e32 v62, vcc, s20, v34
	v_add_u32_e32 v34, -1, v37
	s_nop 0
	v_addc_co_u32_e32 v63, vcc, 0, v35, vcc
	v_cmp_lt_u32_e32 vcc, v34, v36
	v_ashrrev_i32_e32 v75, 31, v74
	v_and_b32_e32 v57, 0x7f, v80
	v_subbrev_co_u32_e32 v34, vcc, 0, v74, vcc
	v_mad_i64_i32 v[34:35], s[2:3], v34, s23, v[32:33]
	v_lshl_add_u64 v[34:35], v[34:35], 0, v[72:73]
	v_add_co_u32_e32 v64, vcc, s20, v34
	s_waitcnt lgkmcnt(0)
	s_lshl_b32 s8, s21, 2
	v_addc_co_u32_e32 v65, vcc, 0, v35, vcc
	v_mad_i64_i32 v[34:35], s[2:3], v74, s23, v[32:33]
	v_lshl_add_u64 v[34:35], v[34:35], 0, v[72:73]
	v_add_co_u32_e32 v66, vcc, s20, v34
	v_add_u32_e32 v34, 1, v37
	s_nop 0
	v_addc_co_u32_e32 v67, vcc, 0, v35, vcc
	v_cmp_lt_u32_e32 vcc, v34, v36
	s_ashr_i32 s9, s8, 31
	s_lshl_b64 s[10:11], s[8:9], 11
	v_addc_co_u32_e32 v34, vcc, 0, v74, vcc
	v_mad_i64_i32 v[32:33], s[2:3], v34, s23, v[32:33]
	v_lshl_add_u64 v[32:33], v[32:33], 0, v[72:73]
	v_add_co_u32_e32 v68, vcc, s20, v32
	s_mov_b64 s[2:3], 0x6a600000
	s_nop 0
	v_addc_co_u32_e32 v69, vcc, 0, v33, vcc
	global_load_dwordx4 v[44:47], v[66:67], off offset:2048
	global_load_dwordx4 v[40:43], v[68:69], off offset:2048
	global_load_dwordx4 v[52:55], v[62:63], off offset:2048
	global_load_dwordx4 v[48:51], v[64:65], off offset:2048
	global_load_dwordx4 v[32:35], v[60:61], off offset:16
	global_load_dwordx4 v[36:39], v[58:59], off offset:16
	v_lshlrev_b64 v[58:59], 11, v[74:75]
	v_lshl_or_b32 v58, v57, 4, v58
	v_lshl_add_u64 v[58:59], s[16:17], 0, v[58:59]
	v_lshl_add_u64 v[76:77], v[58:59], 0, s[2:3]
	v_lshlrev_b32_e32 v72, 1, v56
	s_mov_b64 s[12:13], 0
	s_mov_b32 s9, 0x87ff
	s_waitcnt vmcnt(5)
	v_mov_b64_e32 v[66:67], v[46:47]
	s_waitcnt vmcnt(4)
	v_mov_b64_e32 v[70:71], v[42:43]
	s_waitcnt vmcnt(3)
	v_mov_b64_e32 v[58:59], v[54:55]
	s_waitcnt vmcnt(2)
	v_mov_b64_e32 v[62:63], v[50:51]
	v_mov_b64_e32 v[68:69], v[40:41]
	v_mov_b64_e32 v[64:65], v[44:45]
	v_mov_b64_e32 v[60:61], v[48:49]
	v_mov_b64_e32 v[56:57], v[52:53]
	s_waitcnt vmcnt(0)
	s_cmp_eq_u32 s21, 0x100
	s_cbranch_scc1 .Lconv_fast_L1
	s_branch .LBB0_2162
.Lconv_fast_L1:
	v_mbcnt_lo_u32_b32 v126, -1, 0
	v_mbcnt_hi_u32_b32 v126, -1, v126
	s_and_b32 s40, s96, 1
	s_lshl_b32 s40, s40, 6
	v_or_b32_e32 v126, s40, v126
	v_lshlrev_b32_e32 v127, 5, v126
	v_lshlrev_b32_e32 v126, 4, v126
	v_readlane_b32 s41, v254, 0
	s_lshr_b32 s42, s96, 1
	s_lshl_b32 s41, s41, 2
	s_add_i32 s41, s41, s42
	s_load_dwordx2 s[44:45], s[0:1], 0x60
	s_load_dwordx2 s[46:47], s[0:1], 0x68
	s_waitcnt lgkmcnt(0)
	s_add_u32 s48, s44, 0x4000
	s_addc_u32 s49, s45, 0
	global_load_dwordx4 v[128:131], v127, s[48:49]
	global_load_dwordx4 v[132:135], v127, s[48:49] offset:16
	s_add_u32 s48, s44, 0x5000
	s_addc_u32 s49, s45, 0
	global_load_dwordx4 v[136:139], v127, s[48:49]
	global_load_dwordx4 v[140:143], v127, s[48:49] offset:16
	s_add_u32 s48, s44, 0x6000
	s_addc_u32 s49, s45, 0
	global_load_dwordx4 v[144:147], v127, s[48:49]
	global_load_dwordx4 v[148:151], v127, s[48:49] offset:16
	s_add_u32 s48, s44, 0x7000
	s_addc_u32 s49, s45, 0
	global_load_dwordx4 v[152:155], v127, s[48:49]
	global_load_dwordx4 v[156:159], v127, s[48:49] offset:16
	s_add_u32 s48, s46, 0x1000
	s_addc_u32 s49, s47, 0
	global_load_dwordx4 v[160:163], v127, s[48:49]
	global_load_dwordx4 v[164:167], v127, s[48:49] offset:16
	s_add_u32 s50, s86, 0x17901800
	s_addc_u32 s51, s87, 0
	s_add_u32 s52, s86, 0x6a600000
	s_addc_u32 s53, s87, 0
	s_movk_i32 s70, 0xfff
	s_movk_i32 s71, 0xff
	s_waitcnt vmcnt(0)
	s_add_i32 s54, s41, 0x0
	s_cmp_lt_u32 s54, 0x8000
	s_cselect_b32 s55, s70, s71
	s_and_b32 s56, s54, s55
	s_add_i32 s57, s55, 1
	s_add_i32 s58, s56, -2
	s_cmp_lt_u32 s58, s57
	s_cselect_b32 s58, -2, 0
	s_add_i32 s58, s54, s58
	s_mul_i32 s58, s58, 0x5a00
	s_add_u32 s60, s50, s58
	s_addc_u32 s61, s51, 0
	global_load_dwordx4 v[168:171], v126, s[60:61]
	s_add_i32 s58, s56, -1
	s_cmp_lt_u32 s58, s57
	s_cselect_b32 s58, -1, 0
	s_add_i32 s58, s54, s58
	s_mul_i32 s58, s58, 0x5a00
	s_add_u32 s60, s50, s58
	s_addc_u32 s61, s51, 0
	global_load_dwordx4 v[172:175], v126, s[60:61]
	s_mul_i32 s58, s54, 0x5a00
	s_add_u32 s60, s50, s58
	s_addc_u32 s61, s51, 0
	global_load_dwordx4 v[176:179], v126, s[60:61]
	s_add_i32 s58, s56, 1
	s_cmp_lt_u32 s58, s57
	s_cselect_b32 s58, 1, 0
	s_add_i32 s58, s54, s58
	s_mul_i32 s58, s58, 0x5a00
	s_add_u32 s60, s50, s58
	s_addc_u32 s61, s51, 0
	global_load_dwordx4 v[180:183], v126, s[60:61]
	s_add_i32 s54, s41, 0x400
	s_cmp_lt_u32 s54, 0x8000
	s_cselect_b32 s55, s70, s71
	s_and_b32 s56, s54, s55
	s_add_i32 s57, s55, 1
	s_add_i32 s58, s56, -2
	s_cmp_lt_u32 s58, s57
	s_cselect_b32 s58, -2, 0
	s_add_i32 s58, s54, s58
	s_mul_i32 s58, s58, 0x5a00
	s_add_u32 s60, s50, s58
	s_addc_u32 s61, s51, 0
	global_load_dwordx4 v[184:187], v126, s[60:61]
	s_add_i32 s58, s56, -1
	s_cmp_lt_u32 s58, s57
	s_cselect_b32 s58, -1, 0
	s_add_i32 s58, s54, s58
	s_mul_i32 s58, s58, 0x5a00
	s_add_u32 s60, s50, s58
	s_addc_u32 s61, s51, 0
	global_load_dwordx4 v[188:191], v126, s[60:61]
	s_mul_i32 s58, s54, 0x5a00
	s_add_u32 s60, s50, s58
	s_addc_u32 s61, s51, 0
	global_load_dwordx4 v[192:195], v126, s[60:61]
	s_add_i32 s58, s56, 1
	s_cmp_lt_u32 s58, s57
	s_cselect_b32 s58, 1, 0
	s_add_i32 s58, s54, s58
	s_mul_i32 s58, s58, 0x5a00
	s_add_u32 s60, s50, s58
	s_addc_u32 s61, s51, 0
	global_load_dwordx4 v[196:199], v126, s[60:61]
	s_add_i32 s54, s41, 0x800
	s_cmp_lt_u32 s54, 0x8000
	s_cselect_b32 s55, s70, s71
	s_and_b32 s56, s54, s55
	s_add_i32 s57, s55, 1
	s_add_i32 s58, s56, -2
	s_cmp_lt_u32 s58, s57
	s_cselect_b32 s58, -2, 0
	s_add_i32 s58, s54, s58
	s_mul_i32 s58, s58, 0x5a00
	s_add_u32 s60, s50, s58
	s_addc_u32 s61, s51, 0
	global_load_dwordx4 v[200:203], v126, s[60:61]
	s_add_i32 s58, s56, -1
	s_cmp_lt_u32 s58, s57
	s_cselect_b32 s58, -1, 0
	s_add_i32 s58, s54, s58
	s_mul_i32 s58, s58, 0x5a00
	s_add_u32 s60, s50, s58
	s_addc_u32 s61, s51, 0
	global_load_dwordx4 v[204:207], v126, s[60:61]
	s_mul_i32 s58, s54, 0x5a00
	s_add_u32 s60, s50, s58
	s_addc_u32 s61, s51, 0
	global_load_dwordx4 v[208:211], v126, s[60:61]
	s_add_i32 s58, s56, 1
	s_cmp_lt_u32 s58, s57
	s_cselect_b32 s58, 1, 0
	s_add_i32 s58, s54, s58
	s_mul_i32 s58, s58, 0x5a00
	s_add_u32 s60, s50, s58
	s_addc_u32 s61, s51, 0
	global_load_dwordx4 v[212:215], v126, s[60:61]
	s_add_i32 s54, s41, 0xc00
	s_cmp_lt_u32 s54, 0x8000
	s_cselect_b32 s55, s70, s71
	s_and_b32 s56, s54, s55
	s_add_i32 s57, s55, 1
	s_add_i32 s58, s56, -2
	s_cmp_lt_u32 s58, s57
	s_cselect_b32 s58, -2, 0
	s_add_i32 s58, s54, s58
	s_mul_i32 s58, s58, 0x5a00
	s_add_u32 s60, s50, s58
	s_addc_u32 s61, s51, 0
	global_load_dwordx4 v[216:219], v126, s[60:61]
	s_add_i32 s58, s56, -1
	s_cmp_lt_u32 s58, s57
	s_cselect_b32 s58, -1, 0
	s_add_i32 s58, s54, s58
	s_mul_i32 s58, s58, 0x5a00
	s_add_u32 s60, s50, s58
	s_addc_u32 s61, s51, 0
	global_load_dwordx4 v[220:223], v126, s[60:61]
	s_mul_i32 s58, s54, 0x5a00
	s_add_u32 s60, s50, s58
	s_addc_u32 s61, s51, 0
	global_load_dwordx4 v[224:227], v126, s[60:61]
	s_add_i32 s58, s56, 1
	s_cmp_lt_u32 s58, s57
	s_cselect_b32 s58, 1, 0
	s_add_i32 s58, s54, s58
	s_mul_i32 s58, s58, 0x5a00
	s_add_u32 s60, s50, s58
	s_addc_u32 s61, s51, 0
	global_load_dwordx4 v[228:231], v126, s[60:61]
	s_add_i32 s54, s41, 0x1000
	s_cmp_lt_u32 s54, 0x8000
	s_cselect_b32 s55, s70, s71
	s_and_b32 s56, s54, s55
	s_add_i32 s57, s55, 1
	s_add_i32 s58, s56, -2
	s_cmp_lt_u32 s58, s57
	s_cselect_b32 s58, -2, 0
	s_add_i32 s58, s54, s58
	s_mul_i32 s58, s58, 0x5a00
	s_add_u32 s60, s50, s58
	s_addc_u32 s61, s51, 0
	global_load_dwordx4 v[40:43], v126, s[60:61]
	s_add_i32 s58, s56, -1
	s_cmp_lt_u32 s58, s57
	s_cselect_b32 s58, -1, 0
	s_add_i32 s58, s54, s58
	s_mul_i32 s58, s58, 0x5a00
	s_add_u32 s60, s50, s58
	s_addc_u32 s61, s51, 0
	global_load_dwordx4 v[44:47], v126, s[60:61]
	s_mul_i32 s58, s54, 0x5a00
	s_add_u32 s60, s50, s58
	s_addc_u32 s61, s51, 0
	global_load_dwordx4 v[48:51], v126, s[60:61]
	s_add_i32 s58, s56, 1
	s_cmp_lt_u32 s58, s57
	s_cselect_b32 s58, 1, 0
	s_add_i32 s58, s54, s58
	s_mul_i32 s58, s58, 0x5a00
	s_add_u32 s60, s50, s58
	s_addc_u32 s61, s51, 0
	global_load_dwordx4 v[52:55], v126, s[60:61]
	s_add_i32 s54, s41, 0x1400
	s_cmp_lt_u32 s54, 0x8000
	s_cselect_b32 s55, s70, s71
	s_and_b32 s56, s54, s55
	s_add_i32 s57, s55, 1
	s_add_i32 s58, s56, -2
	s_cmp_lt_u32 s58, s57
	s_cselect_b32 s58, -2, 0
	s_add_i32 s58, s54, s58
	s_mul_i32 s58, s58, 0x5a00
	s_add_u32 s60, s50, s58
	s_addc_u32 s61, s51, 0
	global_load_dwordx4 v[56:59], v126, s[60:61]
	s_add_i32 s58, s56, -1
	s_cmp_lt_u32 s58, s57
	s_cselect_b32 s58, -1, 0
	s_add_i32 s58, s54, s58
	s_mul_i32 s58, s58, 0x5a00
	s_add_u32 s60, s50, s58
	s_addc_u32 s61, s51, 0
	global_load_dwordx4 v[60:63], v126, s[60:61]
	s_mul_i32 s58, s54, 0x5a00
	s_add_u32 s60, s50, s58
	s_addc_u32 s61, s51, 0
	global_load_dwordx4 v[64:67], v126, s[60:61]
	s_add_i32 s58, s56, 1
	s_cmp_lt_u32 s58, s57
	s_cselect_b32 s58, 1, 0
	s_add_i32 s58, s54, s58
	s_mul_i32 s58, s58, 0x5a00
	s_add_u32 s60, s50, s58
	s_addc_u32 s61, s51, 0
	global_load_dwordx4 v[68:71], v126, s[60:61]
	s_waitcnt vmcnt(16)
	s_add_i32 s54, s41, 0x0
	s_cmp_lt_u32 s54, 0x8000
	s_cselect_b32 s55, s70, s71
	s_and_b32 s56, s54, s55
	s_add_i32 s57, s55, 1
	s_add_i32 s58, s56, -2
	s_cmp_lt_u32 s58, s57
	s_cselect_b32 s62, 1.0, 0
	s_add_i32 s58, s56, -1
	s_cmp_lt_u32 s58, s57
	s_cselect_b32 s64, 1.0, 0
	s_mov_b32 s66, 1.0
	s_add_i32 s58, s56, 1
	s_cmp_lt_u32 s58, s57
	s_cselect_b32 s68, 1.0, 0
	v_pk_mul_f32 v[240:241], v[128:129], s[62:63] op_sel_hi:[1,0]
	v_lshlrev_b32_e32 v242, 16, v168
	v_and_b32_e32 v243, 0xffff0000, v168
	v_pk_fma_f32 v[232:233], v[240:241], v[242:243], v[160:161]
	v_pk_mul_f32 v[240:241], v[130:131], s[62:63] op_sel_hi:[1,0]
	v_lshlrev_b32_e32 v242, 16, v169
	v_and_b32_e32 v243, 0xffff0000, v169
	v_pk_fma_f32 v[234:235], v[240:241], v[242:243], v[162:163]
	v_pk_mul_f32 v[240:241], v[132:133], s[62:63] op_sel_hi:[1,0]
	v_lshlrev_b32_e32 v242, 16, v170
	v_and_b32_e32 v243, 0xffff0000, v170
	v_pk_fma_f32 v[236:237], v[240:241], v[242:243], v[164:165]
	v_pk_mul_f32 v[240:241], v[134:135], s[62:63] op_sel_hi:[1,0]
	v_lshlrev_b32_e32 v242, 16, v171
	v_and_b32_e32 v243, 0xffff0000, v171
	v_pk_fma_f32 v[238:239], v[240:241], v[242:243], v[166:167]
	v_pk_mul_f32 v[240:241], v[136:137], s[64:65] op_sel_hi:[1,0]
	v_lshlrev_b32_e32 v242, 16, v172
	v_and_b32_e32 v243, 0xffff0000, v172
	v_pk_fma_f32 v[232:233], v[240:241], v[242:243], v[232:233]
	v_pk_mul_f32 v[240:241], v[138:139], s[64:65] op_sel_hi:[1,0]
	v_lshlrev_b32_e32 v242, 16, v173
	v_and_b32_e32 v243, 0xffff0000, v173
	v_pk_fma_f32 v[234:235], v[240:241], v[242:243], v[234:235]
	v_pk_mul_f32 v[240:241], v[140:141], s[64:65] op_sel_hi:[1,0]
	v_lshlrev_b32_e32 v242, 16, v174
	v_and_b32_e32 v243, 0xffff0000, v174
	v_pk_fma_f32 v[236:237], v[240:241], v[242:243], v[236:237]
	v_pk_mul_f32 v[240:241], v[142:143], s[64:65] op_sel_hi:[1,0]
	v_lshlrev_b32_e32 v242, 16, v175
	v_and_b32_e32 v243, 0xffff0000, v175
	v_pk_fma_f32 v[238:239], v[240:241], v[242:243], v[238:239]
	v_pk_mul_f32 v[240:241], v[144:145], s[66:67] op_sel_hi:[1,0]
	v_lshlrev_b32_e32 v242, 16, v176
	v_and_b32_e32 v243, 0xffff0000, v176
	v_pk_fma_f32 v[232:233], v[240:241], v[242:243], v[232:233]
	v_pk_mul_f32 v[240:241], v[146:147], s[66:67] op_sel_hi:[1,0]
	v_lshlrev_b32_e32 v242, 16, v177
	v_and_b32_e32 v243, 0xffff0000, v177
	v_pk_fma_f32 v[234:235], v[240:241], v[242:243], v[234:235]
	v_pk_mul_f32 v[240:241], v[148:149], s[66:67] op_sel_hi:[1,0]
	v_lshlrev_b32_e32 v242, 16, v178
	v_and_b32_e32 v243, 0xffff0000, v178
	v_pk_fma_f32 v[236:237], v[240:241], v[242:243], v[236:237]
	v_pk_mul_f32 v[240:241], v[150:151], s[66:67] op_sel_hi:[1,0]
	v_lshlrev_b32_e32 v242, 16, v179
	v_and_b32_e32 v243, 0xffff0000, v179
	v_pk_fma_f32 v[238:239], v[240:241], v[242:243], v[238:239]
	v_pk_mul_f32 v[240:241], v[152:153], s[68:69] op_sel_hi:[1,0]
	v_lshlrev_b32_e32 v242, 16, v180
	v_and_b32_e32 v243, 0xffff0000, v180
	v_pk_fma_f32 v[232:233], v[240:241], v[242:243], v[232:233]
	v_pk_mul_f32 v[240:241], v[154:155], s[68:69] op_sel_hi:[1,0]
	v_lshlrev_b32_e32 v242, 16, v181
	v_and_b32_e32 v243, 0xffff0000, v181
	v_pk_fma_f32 v[234:235], v[240:241], v[242:243], v[234:235]
	v_pk_mul_f32 v[240:241], v[156:157], s[68:69] op_sel_hi:[1,0]
	v_lshlrev_b32_e32 v242, 16, v182
	v_and_b32_e32 v243, 0xffff0000, v182
	v_pk_fma_f32 v[236:237], v[240:241], v[242:243], v[236:237]
	v_pk_mul_f32 v[240:241], v[158:159], s[68:69] op_sel_hi:[1,0]
	v_lshlrev_b32_e32 v242, 16, v183
	v_and_b32_e32 v243, 0xffff0000, v183
	v_pk_fma_f32 v[238:239], v[240:241], v[242:243], v[238:239]
	v_cvt_pk_bf16_f32 v248, v232, v233
	v_cvt_pk_bf16_f32 v249, v234, v235
	v_cvt_pk_bf16_f32 v250, v236, v237
	v_cvt_pk_bf16_f32 v251, v238, v239
	s_lshl_b32 s58, s54, 11
	s_add_u32 s60, s52, s58
	s_addc_u32 s61, s53, 0
	global_store_dwordx4 v126, v[248:251], s[60:61]
	s_add_i32 s54, s41, 0x400
	s_cmp_lt_u32 s54, 0x8000
	s_cselect_b32 s55, s70, s71
	s_and_b32 s56, s54, s55
	s_add_i32 s57, s55, 1
	s_add_i32 s58, s56, -2
	s_cmp_lt_u32 s58, s57
	s_cselect_b32 s62, 1.0, 0
	s_add_i32 s58, s56, -1
	s_cmp_lt_u32 s58, s57
	s_cselect_b32 s64, 1.0, 0
	s_mov_b32 s66, 1.0
	s_add_i32 s58, s56, 1
	s_cmp_lt_u32 s58, s57
	s_cselect_b32 s68, 1.0, 0
	v_pk_mul_f32 v[240:241], v[128:129], s[62:63] op_sel_hi:[1,0]
	v_lshlrev_b32_e32 v242, 16, v184
	v_and_b32_e32 v243, 0xffff0000, v184
	v_pk_fma_f32 v[232:233], v[240:241], v[242:243], v[160:161]
	v_pk_mul_f32 v[240:241], v[130:131], s[62:63] op_sel_hi:[1,0]
	v_lshlrev_b32_e32 v242, 16, v185
	v_and_b32_e32 v243, 0xffff0000, v185
	v_pk_fma_f32 v[234:235], v[240:241], v[242:243], v[162:163]
	v_pk_mul_f32 v[240:241], v[132:133], s[62:63] op_sel_hi:[1,0]
	v_lshlrev_b32_e32 v242, 16, v186
	v_and_b32_e32 v243, 0xffff0000, v186
	v_pk_fma_f32 v[236:237], v[240:241], v[242:243], v[164:165]
	v_pk_mul_f32 v[240:241], v[134:135], s[62:63] op_sel_hi:[1,0]
	v_lshlrev_b32_e32 v242, 16, v187
	v_and_b32_e32 v243, 0xffff0000, v187
	v_pk_fma_f32 v[238:239], v[240:241], v[242:243], v[166:167]
	v_pk_mul_f32 v[240:241], v[136:137], s[64:65] op_sel_hi:[1,0]
	v_lshlrev_b32_e32 v242, 16, v188
	v_and_b32_e32 v243, 0xffff0000, v188
	v_pk_fma_f32 v[232:233], v[240:241], v[242:243], v[232:233]
	v_pk_mul_f32 v[240:241], v[138:139], s[64:65] op_sel_hi:[1,0]
	v_lshlrev_b32_e32 v242, 16, v189
	v_and_b32_e32 v243, 0xffff0000, v189
	v_pk_fma_f32 v[234:235], v[240:241], v[242:243], v[234:235]
	v_pk_mul_f32 v[240:241], v[140:141], s[64:65] op_sel_hi:[1,0]
	v_lshlrev_b32_e32 v242, 16, v190
	v_and_b32_e32 v243, 0xffff0000, v190
	v_pk_fma_f32 v[236:237], v[240:241], v[242:243], v[236:237]
	v_pk_mul_f32 v[240:241], v[142:143], s[64:65] op_sel_hi:[1,0]
	v_lshlrev_b32_e32 v242, 16, v191
	v_and_b32_e32 v243, 0xffff0000, v191
	v_pk_fma_f32 v[238:239], v[240:241], v[242:243], v[238:239]
	v_pk_mul_f32 v[240:241], v[144:145], s[66:67] op_sel_hi:[1,0]
	v_lshlrev_b32_e32 v242, 16, v192
	v_and_b32_e32 v243, 0xffff0000, v192
	v_pk_fma_f32 v[232:233], v[240:241], v[242:243], v[232:233]
	v_pk_mul_f32 v[240:241], v[146:147], s[66:67] op_sel_hi:[1,0]
	v_lshlrev_b32_e32 v242, 16, v193
	v_and_b32_e32 v243, 0xffff0000, v193
	v_pk_fma_f32 v[234:235], v[240:241], v[242:243], v[234:235]
	v_pk_mul_f32 v[240:241], v[148:149], s[66:67] op_sel_hi:[1,0]
	v_lshlrev_b32_e32 v242, 16, v194
	v_and_b32_e32 v243, 0xffff0000, v194
	v_pk_fma_f32 v[236:237], v[240:241], v[242:243], v[236:237]
	v_pk_mul_f32 v[240:241], v[150:151], s[66:67] op_sel_hi:[1,0]
	v_lshlrev_b32_e32 v242, 16, v195
	v_and_b32_e32 v243, 0xffff0000, v195
	v_pk_fma_f32 v[238:239], v[240:241], v[242:243], v[238:239]
	v_pk_mul_f32 v[240:241], v[152:153], s[68:69] op_sel_hi:[1,0]
	v_lshlrev_b32_e32 v242, 16, v196
	v_and_b32_e32 v243, 0xffff0000, v196
	v_pk_fma_f32 v[232:233], v[240:241], v[242:243], v[232:233]
	v_pk_mul_f32 v[240:241], v[154:155], s[68:69] op_sel_hi:[1,0]
	v_lshlrev_b32_e32 v242, 16, v197
	v_and_b32_e32 v243, 0xffff0000, v197
	v_pk_fma_f32 v[234:235], v[240:241], v[242:243], v[234:235]
	v_pk_mul_f32 v[240:241], v[156:157], s[68:69] op_sel_hi:[1,0]
	v_lshlrev_b32_e32 v242, 16, v198
	v_and_b32_e32 v243, 0xffff0000, v198
	v_pk_fma_f32 v[236:237], v[240:241], v[242:243], v[236:237]
	v_pk_mul_f32 v[240:241], v[158:159], s[68:69] op_sel_hi:[1,0]
	v_lshlrev_b32_e32 v242, 16, v199
	v_and_b32_e32 v243, 0xffff0000, v199
	v_pk_fma_f32 v[238:239], v[240:241], v[242:243], v[238:239]
	v_cvt_pk_bf16_f32 v248, v232, v233
	v_cvt_pk_bf16_f32 v249, v234, v235
	v_cvt_pk_bf16_f32 v250, v236, v237
	v_cvt_pk_bf16_f32 v251, v238, v239
	s_lshl_b32 s58, s54, 11
	s_add_u32 s60, s52, s58
	s_addc_u32 s61, s53, 0
	global_store_dwordx4 v126, v[248:251], s[60:61]
	s_add_i32 s54, s41, 0x1800
	s_cmp_lt_u32 s54, 0x8000
	s_cselect_b32 s55, s70, s71
	s_and_b32 s56, s54, s55
	s_add_i32 s57, s55, 1
	s_add_i32 s58, s56, -2
	s_cmp_lt_u32 s58, s57
	s_cselect_b32 s58, -2, 0
	s_add_i32 s58, s54, s58
	s_mul_i32 s58, s58, 0x5a00
	s_add_u32 s60, s50, s58
	s_addc_u32 s61, s51, 0
	global_load_dwordx4 v[168:171], v126, s[60:61]
	s_add_i32 s58, s56, -1
	s_cmp_lt_u32 s58, s57
	s_cselect_b32 s58, -1, 0
	s_add_i32 s58, s54, s58
	s_mul_i32 s58, s58, 0x5a00
	s_add_u32 s60, s50, s58
	s_addc_u32 s61, s51, 0
	global_load_dwordx4 v[172:175], v126, s[60:61]
	s_mul_i32 s58, s54, 0x5a00
	s_add_u32 s60, s50, s58
	s_addc_u32 s61, s51, 0
	global_load_dwordx4 v[176:179], v126, s[60:61]
	s_add_i32 s58, s56, 1
	s_cmp_lt_u32 s58, s57
	s_cselect_b32 s58, 1, 0
	s_add_i32 s58, s54, s58
	s_mul_i32 s58, s58, 0x5a00
	s_add_u32 s60, s50, s58
	s_addc_u32 s61, s51, 0
	global_load_dwordx4 v[180:183], v126, s[60:61]
	s_add_i32 s54, s41, 0x1c00
	s_cmp_lt_u32 s54, 0x8000
	s_cselect_b32 s55, s70, s71
	s_and_b32 s56, s54, s55
	s_add_i32 s57, s55, 1
	s_add_i32 s58, s56, -2
	s_cmp_lt_u32 s58, s57
	s_cselect_b32 s58, -2, 0
	s_add_i32 s58, s54, s58
	s_mul_i32 s58, s58, 0x5a00
	s_add_u32 s60, s50, s58
	s_addc_u32 s61, s51, 0
	global_load_dwordx4 v[184:187], v126, s[60:61]
	s_add_i32 s58, s56, -1
	s_cmp_lt_u32 s58, s57
	s_cselect_b32 s58, -1, 0
	s_add_i32 s58, s54, s58
	s_mul_i32 s58, s58, 0x5a00
	s_add_u32 s60, s50, s58
	s_addc_u32 s61, s51, 0
	global_load_dwordx4 v[188:191], v126, s[60:61]
	s_mul_i32 s58, s54, 0x5a00
	s_add_u32 s60, s50, s58
	s_addc_u32 s61, s51, 0
	global_load_dwordx4 v[192:195], v126, s[60:61]
	s_add_i32 s58, s56, 1
	s_cmp_lt_u32 s58, s57
	s_cselect_b32 s58, 1, 0
	s_add_i32 s58, s54, s58
	s_mul_i32 s58, s58, 0x5a00
	s_add_u32 s60, s50, s58
	s_addc_u32 s61, s51, 0
	global_load_dwordx4 v[196:199], v126, s[60:61]
	s_waitcnt vmcnt(18)
	s_add_i32 s54, s41, 0x800
	s_cmp_lt_u32 s54, 0x8000
	s_cselect_b32 s55, s70, s71
	s_and_b32 s56, s54, s55
	s_add_i32 s57, s55, 1
	s_add_i32 s58, s56, -2
	s_cmp_lt_u32 s58, s57
	s_cselect_b32 s62, 1.0, 0
	s_add_i32 s58, s56, -1
	s_cmp_lt_u32 s58, s57
	s_cselect_b32 s64, 1.0, 0
	s_mov_b32 s66, 1.0
	s_add_i32 s58, s56, 1
	s_cmp_lt_u32 s58, s57
	s_cselect_b32 s68, 1.0, 0
	v_pk_mul_f32 v[240:241], v[128:129], s[62:63] op_sel_hi:[1,0]
	v_lshlrev_b32_e32 v242, 16, v200
	v_and_b32_e32 v243, 0xffff0000, v200
	v_pk_fma_f32 v[232:233], v[240:241], v[242:243], v[160:161]
	v_pk_mul_f32 v[240:241], v[130:131], s[62:63] op_sel_hi:[1,0]
	v_lshlrev_b32_e32 v242, 16, v201
	v_and_b32_e32 v243, 0xffff0000, v201
	v_pk_fma_f32 v[234:235], v[240:241], v[242:243], v[162:163]
	v_pk_mul_f32 v[240:241], v[132:133], s[62:63] op_sel_hi:[1,0]
	v_lshlrev_b32_e32 v242, 16, v202
	v_and_b32_e32 v243, 0xffff0000, v202
	v_pk_fma_f32 v[236:237], v[240:241], v[242:243], v[164:165]
	v_pk_mul_f32 v[240:241], v[134:135], s[62:63] op_sel_hi:[1,0]
	v_lshlrev_b32_e32 v242, 16, v203
	v_and_b32_e32 v243, 0xffff0000, v203
	v_pk_fma_f32 v[238:239], v[240:241], v[242:243], v[166:167]
	v_pk_mul_f32 v[240:241], v[136:137], s[64:65] op_sel_hi:[1,0]
	v_lshlrev_b32_e32 v242, 16, v204
	v_and_b32_e32 v243, 0xffff0000, v204
	v_pk_fma_f32 v[232:233], v[240:241], v[242:243], v[232:233]
	v_pk_mul_f32 v[240:241], v[138:139], s[64:65] op_sel_hi:[1,0]
	v_lshlrev_b32_e32 v242, 16, v205
	v_and_b32_e32 v243, 0xffff0000, v205
	v_pk_fma_f32 v[234:235], v[240:241], v[242:243], v[234:235]
	v_pk_mul_f32 v[240:241], v[140:141], s[64:65] op_sel_hi:[1,0]
	v_lshlrev_b32_e32 v242, 16, v206
	v_and_b32_e32 v243, 0xffff0000, v206
	v_pk_fma_f32 v[236:237], v[240:241], v[242:243], v[236:237]
	v_pk_mul_f32 v[240:241], v[142:143], s[64:65] op_sel_hi:[1,0]
	v_lshlrev_b32_e32 v242, 16, v207
	v_and_b32_e32 v243, 0xffff0000, v207
	v_pk_fma_f32 v[238:239], v[240:241], v[242:243], v[238:239]
	v_pk_mul_f32 v[240:241], v[144:145], s[66:67] op_sel_hi:[1,0]
	v_lshlrev_b32_e32 v242, 16, v208
	v_and_b32_e32 v243, 0xffff0000, v208
	v_pk_fma_f32 v[232:233], v[240:241], v[242:243], v[232:233]
	v_pk_mul_f32 v[240:241], v[146:147], s[66:67] op_sel_hi:[1,0]
	v_lshlrev_b32_e32 v242, 16, v209
	v_and_b32_e32 v243, 0xffff0000, v209
	v_pk_fma_f32 v[234:235], v[240:241], v[242:243], v[234:235]
	v_pk_mul_f32 v[240:241], v[148:149], s[66:67] op_sel_hi:[1,0]
	v_lshlrev_b32_e32 v242, 16, v210
	v_and_b32_e32 v243, 0xffff0000, v210
	v_pk_fma_f32 v[236:237], v[240:241], v[242:243], v[236:237]
	v_pk_mul_f32 v[240:241], v[150:151], s[66:67] op_sel_hi:[1,0]
	v_lshlrev_b32_e32 v242, 16, v211
	v_and_b32_e32 v243, 0xffff0000, v211
	v_pk_fma_f32 v[238:239], v[240:241], v[242:243], v[238:239]
	v_pk_mul_f32 v[240:241], v[152:153], s[68:69] op_sel_hi:[1,0]
	v_lshlrev_b32_e32 v242, 16, v212
	v_and_b32_e32 v243, 0xffff0000, v212
	v_pk_fma_f32 v[232:233], v[240:241], v[242:243], v[232:233]
	v_pk_mul_f32 v[240:241], v[154:155], s[68:69] op_sel_hi:[1,0]
	v_lshlrev_b32_e32 v242, 16, v213
	v_and_b32_e32 v243, 0xffff0000, v213
	v_pk_fma_f32 v[234:235], v[240:241], v[242:243], v[234:235]
	v_pk_mul_f32 v[240:241], v[156:157], s[68:69] op_sel_hi:[1,0]
	v_lshlrev_b32_e32 v242, 16, v214
	v_and_b32_e32 v243, 0xffff0000, v214
	v_pk_fma_f32 v[236:237], v[240:241], v[242:243], v[236:237]
	v_pk_mul_f32 v[240:241], v[158:159], s[68:69] op_sel_hi:[1,0]
	v_lshlrev_b32_e32 v242, 16, v215
	v_and_b32_e32 v243, 0xffff0000, v215
	v_pk_fma_f32 v[238:239], v[240:241], v[242:243], v[238:239]
	v_cvt_pk_bf16_f32 v248, v232, v233
	v_cvt_pk_bf16_f32 v249, v234, v235
	v_cvt_pk_bf16_f32 v250, v236, v237
	v_cvt_pk_bf16_f32 v251, v238, v239
	s_lshl_b32 s58, s54, 11
	s_add_u32 s60, s52, s58
	s_addc_u32 s61, s53, 0
	global_store_dwordx4 v126, v[248:251], s[60:61]
	s_add_i32 s54, s41, 0xc00
	s_cmp_lt_u32 s54, 0x8000
	s_cselect_b32 s55, s70, s71
	s_and_b32 s56, s54, s55
	s_add_i32 s57, s55, 1
	s_add_i32 s58, s56, -2
	s_cmp_lt_u32 s58, s57
	s_cselect_b32 s62, 1.0, 0
	s_add_i32 s58, s56, -1
	s_cmp_lt_u32 s58, s57
	s_cselect_b32 s64, 1.0, 0
	s_mov_b32 s66, 1.0
	s_add_i32 s58, s56, 1
	s_cmp_lt_u32 s58, s57
	s_cselect_b32 s68, 1.0, 0
	v_pk_mul_f32 v[240:241], v[128:129], s[62:63] op_sel_hi:[1,0]
	v_lshlrev_b32_e32 v242, 16, v216
	v_and_b32_e32 v243, 0xffff0000, v216
	v_pk_fma_f32 v[232:233], v[240:241], v[242:243], v[160:161]
	v_pk_mul_f32 v[240:241], v[130:131], s[62:63] op_sel_hi:[1,0]
	v_lshlrev_b32_e32 v242, 16, v217
	v_and_b32_e32 v243, 0xffff0000, v217
	v_pk_fma_f32 v[234:235], v[240:241], v[242:243], v[162:163]
	v_pk_mul_f32 v[240:241], v[132:133], s[62:63] op_sel_hi:[1,0]
	v_lshlrev_b32_e32 v242, 16, v218
	v_and_b32_e32 v243, 0xffff0000, v218
	v_pk_fma_f32 v[236:237], v[240:241], v[242:243], v[164:165]
	v_pk_mul_f32 v[240:241], v[134:135], s[62:63] op_sel_hi:[1,0]
	v_lshlrev_b32_e32 v242, 16, v219
	v_and_b32_e32 v243, 0xffff0000, v219
	v_pk_fma_f32 v[238:239], v[240:241], v[242:243], v[166:167]
	v_pk_mul_f32 v[240:241], v[136:137], s[64:65] op_sel_hi:[1,0]
	v_lshlrev_b32_e32 v242, 16, v220
	v_and_b32_e32 v243, 0xffff0000, v220
	v_pk_fma_f32 v[232:233], v[240:241], v[242:243], v[232:233]
	v_pk_mul_f32 v[240:241], v[138:139], s[64:65] op_sel_hi:[1,0]
	v_lshlrev_b32_e32 v242, 16, v221
	v_and_b32_e32 v243, 0xffff0000, v221
	v_pk_fma_f32 v[234:235], v[240:241], v[242:243], v[234:235]
	v_pk_mul_f32 v[240:241], v[140:141], s[64:65] op_sel_hi:[1,0]
	v_lshlrev_b32_e32 v242, 16, v222
	v_and_b32_e32 v243, 0xffff0000, v222
	v_pk_fma_f32 v[236:237], v[240:241], v[242:243], v[236:237]
	v_pk_mul_f32 v[240:241], v[142:143], s[64:65] op_sel_hi:[1,0]
	v_lshlrev_b32_e32 v242, 16, v223
	v_and_b32_e32 v243, 0xffff0000, v223
	v_pk_fma_f32 v[238:239], v[240:241], v[242:243], v[238:239]
	v_pk_mul_f32 v[240:241], v[144:145], s[66:67] op_sel_hi:[1,0]
	v_lshlrev_b32_e32 v242, 16, v224
	v_and_b32_e32 v243, 0xffff0000, v224
	v_pk_fma_f32 v[232:233], v[240:241], v[242:243], v[232:233]
	v_pk_mul_f32 v[240:241], v[146:147], s[66:67] op_sel_hi:[1,0]
	v_lshlrev_b32_e32 v242, 16, v225
	v_and_b32_e32 v243, 0xffff0000, v225
	v_pk_fma_f32 v[234:235], v[240:241], v[242:243], v[234:235]
	v_pk_mul_f32 v[240:241], v[148:149], s[66:67] op_sel_hi:[1,0]
	v_lshlrev_b32_e32 v242, 16, v226
	v_and_b32_e32 v243, 0xffff0000, v226
	v_pk_fma_f32 v[236:237], v[240:241], v[242:243], v[236:237]
	v_pk_mul_f32 v[240:241], v[150:151], s[66:67] op_sel_hi:[1,0]
	v_lshlrev_b32_e32 v242, 16, v227
	v_and_b32_e32 v243, 0xffff0000, v227
	v_pk_fma_f32 v[238:239], v[240:241], v[242:243], v[238:239]
	v_pk_mul_f32 v[240:241], v[152:153], s[68:69] op_sel_hi:[1,0]
	v_lshlrev_b32_e32 v242, 16, v228
	v_and_b32_e32 v243, 0xffff0000, v228
	v_pk_fma_f32 v[232:233], v[240:241], v[242:243], v[232:233]
	v_pk_mul_f32 v[240:241], v[154:155], s[68:69] op_sel_hi:[1,0]
	v_lshlrev_b32_e32 v242, 16, v229
	v_and_b32_e32 v243, 0xffff0000, v229
	v_pk_fma_f32 v[234:235], v[240:241], v[242:243], v[234:235]
	v_pk_mul_f32 v[240:241], v[156:157], s[68:69] op_sel_hi:[1,0]
	v_lshlrev_b32_e32 v242, 16, v230
	v_and_b32_e32 v243, 0xffff0000, v230
	v_pk_fma_f32 v[236:237], v[240:241], v[242:243], v[236:237]
	v_pk_mul_f32 v[240:241], v[158:159], s[68:69] op_sel_hi:[1,0]
	v_lshlrev_b32_e32 v242, 16, v231
	v_and_b32_e32 v243, 0xffff0000, v231
	v_pk_fma_f32 v[238:239], v[240:241], v[242:243], v[238:239]
	v_cvt_pk_bf16_f32 v248, v232, v233
	v_cvt_pk_bf16_f32 v249, v234, v235
	v_cvt_pk_bf16_f32 v250, v236, v237
	v_cvt_pk_bf16_f32 v251, v238, v239
	s_lshl_b32 s58, s54, 11
	s_add_u32 s60, s52, s58
	s_addc_u32 s61, s53, 0
	global_store_dwordx4 v126, v[248:251], s[60:61]
	s_add_i32 s54, s41, 0x2000
	s_cmp_lt_u32 s54, 0x8000
	s_cselect_b32 s55, s70, s71
	s_and_b32 s56, s54, s55
	s_add_i32 s57, s55, 1
	s_add_i32 s58, s56, -2
	s_cmp_lt_u32 s58, s57
	s_cselect_b32 s58, -2, 0
	s_add_i32 s58, s54, s58
	s_mul_i32 s58, s58, 0x5a00
	s_add_u32 s60, s50, s58
	s_addc_u32 s61, s51, 0
	global_load_dwordx4 v[200:203], v126, s[60:61]
	s_add_i32 s58, s56, -1
	s_cmp_lt_u32 s58, s57
	s_cselect_b32 s58, -1, 0
	s_add_i32 s58, s54, s58
	s_mul_i32 s58, s58, 0x5a00
	s_add_u32 s60, s50, s58
	s_addc_u32 s61, s51, 0
	global_load_dwordx4 v[204:207], v126, s[60:61]
	s_mul_i32 s58, s54, 0x5a00
	s_add_u32 s60, s50, s58
	s_addc_u32 s61, s51, 0
	global_load_dwordx4 v[208:211], v126, s[60:61]
	s_add_i32 s58, s56, 1
	s_cmp_lt_u32 s58, s57
	s_cselect_b32 s58, 1, 0
	s_add_i32 s58, s54, s58
	s_mul_i32 s58, s58, 0x5a00
	s_add_u32 s60, s50, s58
	s_addc_u32 s61, s51, 0
	global_load_dwordx4 v[212:215], v126, s[60:61]
	s_add_i32 s54, s41, 0x2400
	s_cmp_lt_u32 s54, 0x8000
	s_cselect_b32 s55, s70, s71
	s_and_b32 s56, s54, s55
	s_add_i32 s57, s55, 1
	s_add_i32 s58, s56, -2
	s_cmp_lt_u32 s58, s57
	s_cselect_b32 s58, -2, 0
	s_add_i32 s58, s54, s58
	s_mul_i32 s58, s58, 0x5a00
	s_add_u32 s60, s50, s58
	s_addc_u32 s61, s51, 0
	global_load_dwordx4 v[216:219], v126, s[60:61]
	s_add_i32 s58, s56, -1
	s_cmp_lt_u32 s58, s57
	s_cselect_b32 s58, -1, 0
	s_add_i32 s58, s54, s58
	s_mul_i32 s58, s58, 0x5a00
	s_add_u32 s60, s50, s58
	s_addc_u32 s61, s51, 0
	global_load_dwordx4 v[220:223], v126, s[60:61]
	s_mul_i32 s58, s54, 0x5a00
	s_add_u32 s60, s50, s58
	s_addc_u32 s61, s51, 0
	global_load_dwordx4 v[224:227], v126, s[60:61]
	s_add_i32 s58, s56, 1
	s_cmp_lt_u32 s58, s57
	s_cselect_b32 s58, 1, 0
	s_add_i32 s58, s54, s58
	s_mul_i32 s58, s58, 0x5a00
	s_add_u32 s60, s50, s58
	s_addc_u32 s61, s51, 0
	global_load_dwordx4 v[228:231], v126, s[60:61]
	s_waitcnt vmcnt(20)
	s_add_i32 s54, s41, 0x1000
	s_cmp_lt_u32 s54, 0x8000
	s_cselect_b32 s55, s70, s71
	s_and_b32 s56, s54, s55
	s_add_i32 s57, s55, 1
	s_add_i32 s58, s56, -2
	s_cmp_lt_u32 s58, s57
	s_cselect_b32 s62, 1.0, 0
	s_add_i32 s58, s56, -1
	s_cmp_lt_u32 s58, s57
	s_cselect_b32 s64, 1.0, 0
	s_mov_b32 s66, 1.0
	s_add_i32 s58, s56, 1
	s_cmp_lt_u32 s58, s57
	s_cselect_b32 s68, 1.0, 0
	v_pk_mul_f32 v[240:241], v[128:129], s[62:63] op_sel_hi:[1,0]
	v_lshlrev_b32_e32 v242, 16, v40
	v_and_b32_e32 v243, 0xffff0000, v40
	v_pk_fma_f32 v[232:233], v[240:241], v[242:243], v[160:161]
	v_pk_mul_f32 v[240:241], v[130:131], s[62:63] op_sel_hi:[1,0]
	v_lshlrev_b32_e32 v242, 16, v41
	v_and_b32_e32 v243, 0xffff0000, v41
	v_pk_fma_f32 v[234:235], v[240:241], v[242:243], v[162:163]
	v_pk_mul_f32 v[240:241], v[132:133], s[62:63] op_sel_hi:[1,0]
	v_lshlrev_b32_e32 v242, 16, v42
	v_and_b32_e32 v243, 0xffff0000, v42
	v_pk_fma_f32 v[236:237], v[240:241], v[242:243], v[164:165]
	v_pk_mul_f32 v[240:241], v[134:135], s[62:63] op_sel_hi:[1,0]
	v_lshlrev_b32_e32 v242, 16, v43
	v_and_b32_e32 v243, 0xffff0000, v43
	v_pk_fma_f32 v[238:239], v[240:241], v[242:243], v[166:167]
	v_pk_mul_f32 v[240:241], v[136:137], s[64:65] op_sel_hi:[1,0]
	v_lshlrev_b32_e32 v242, 16, v44
	v_and_b32_e32 v243, 0xffff0000, v44
	v_pk_fma_f32 v[232:233], v[240:241], v[242:243], v[232:233]
	v_pk_mul_f32 v[240:241], v[138:139], s[64:65] op_sel_hi:[1,0]
	v_lshlrev_b32_e32 v242, 16, v45
	v_and_b32_e32 v243, 0xffff0000, v45
	v_pk_fma_f32 v[234:235], v[240:241], v[242:243], v[234:235]
	v_pk_mul_f32 v[240:241], v[140:141], s[64:65] op_sel_hi:[1,0]
	v_lshlrev_b32_e32 v242, 16, v46
	v_and_b32_e32 v243, 0xffff0000, v46
	v_pk_fma_f32 v[236:237], v[240:241], v[242:243], v[236:237]
	v_pk_mul_f32 v[240:241], v[142:143], s[64:65] op_sel_hi:[1,0]
	v_lshlrev_b32_e32 v242, 16, v47
	v_and_b32_e32 v243, 0xffff0000, v47
	v_pk_fma_f32 v[238:239], v[240:241], v[242:243], v[238:239]
	v_pk_mul_f32 v[240:241], v[144:145], s[66:67] op_sel_hi:[1,0]
	v_lshlrev_b32_e32 v242, 16, v48
	v_and_b32_e32 v243, 0xffff0000, v48
	v_pk_fma_f32 v[232:233], v[240:241], v[242:243], v[232:233]
	v_pk_mul_f32 v[240:241], v[146:147], s[66:67] op_sel_hi:[1,0]
	v_lshlrev_b32_e32 v242, 16, v49
	v_and_b32_e32 v243, 0xffff0000, v49
	v_pk_fma_f32 v[234:235], v[240:241], v[242:243], v[234:235]
	v_pk_mul_f32 v[240:241], v[148:149], s[66:67] op_sel_hi:[1,0]
	v_lshlrev_b32_e32 v242, 16, v50
	v_and_b32_e32 v243, 0xffff0000, v50
	v_pk_fma_f32 v[236:237], v[240:241], v[242:243], v[236:237]
	v_pk_mul_f32 v[240:241], v[150:151], s[66:67] op_sel_hi:[1,0]
	v_lshlrev_b32_e32 v242, 16, v51
	v_and_b32_e32 v243, 0xffff0000, v51
	v_pk_fma_f32 v[238:239], v[240:241], v[242:243], v[238:239]
	v_pk_mul_f32 v[240:241], v[152:153], s[68:69] op_sel_hi:[1,0]
	v_lshlrev_b32_e32 v242, 16, v52
	v_and_b32_e32 v243, 0xffff0000, v52
	v_pk_fma_f32 v[232:233], v[240:241], v[242:243], v[232:233]
	v_pk_mul_f32 v[240:241], v[154:155], s[68:69] op_sel_hi:[1,0]
	v_lshlrev_b32_e32 v242, 16, v53
	v_and_b32_e32 v243, 0xffff0000, v53
	v_pk_fma_f32 v[234:235], v[240:241], v[242:243], v[234:235]
	v_pk_mul_f32 v[240:241], v[156:157], s[68:69] op_sel_hi:[1,0]
	v_lshlrev_b32_e32 v242, 16, v54
	v_and_b32_e32 v243, 0xffff0000, v54
	v_pk_fma_f32 v[236:237], v[240:241], v[242:243], v[236:237]
	v_pk_mul_f32 v[240:241], v[158:159], s[68:69] op_sel_hi:[1,0]
	v_lshlrev_b32_e32 v242, 16, v55
	v_and_b32_e32 v243, 0xffff0000, v55
	v_pk_fma_f32 v[238:239], v[240:241], v[242:243], v[238:239]
	v_cvt_pk_bf16_f32 v248, v232, v233
	v_cvt_pk_bf16_f32 v249, v234, v235
	v_cvt_pk_bf16_f32 v250, v236, v237
	v_cvt_pk_bf16_f32 v251, v238, v239
	s_lshl_b32 s58, s54, 11
	s_add_u32 s60, s52, s58
	s_addc_u32 s61, s53, 0
	global_store_dwordx4 v126, v[248:251], s[60:61]
	s_add_i32 s54, s41, 0x1400
	s_cmp_lt_u32 s54, 0x8000
	s_cselect_b32 s55, s70, s71
	s_and_b32 s56, s54, s55
	s_add_i32 s57, s55, 1
	s_add_i32 s58, s56, -2
	s_cmp_lt_u32 s58, s57
	s_cselect_b32 s62, 1.0, 0
	s_add_i32 s58, s56, -1
	s_cmp_lt_u32 s58, s57
	s_cselect_b32 s64, 1.0, 0
	s_mov_b32 s66, 1.0
	s_add_i32 s58, s56, 1
	s_cmp_lt_u32 s58, s57
	s_cselect_b32 s68, 1.0, 0
	v_pk_mul_f32 v[240:241], v[128:129], s[62:63] op_sel_hi:[1,0]
	v_lshlrev_b32_e32 v242, 16, v56
	v_and_b32_e32 v243, 0xffff0000, v56
	v_pk_fma_f32 v[232:233], v[240:241], v[242:243], v[160:161]
	v_pk_mul_f32 v[240:241], v[130:131], s[62:63] op_sel_hi:[1,0]
	v_lshlrev_b32_e32 v242, 16, v57
	v_and_b32_e32 v243, 0xffff0000, v57
	v_pk_fma_f32 v[234:235], v[240:241], v[242:243], v[162:163]
	v_pk_mul_f32 v[240:241], v[132:133], s[62:63] op_sel_hi:[1,0]
	v_lshlrev_b32_e32 v242, 16, v58
	v_and_b32_e32 v243, 0xffff0000, v58
	v_pk_fma_f32 v[236:237], v[240:241], v[242:243], v[164:165]
	v_pk_mul_f32 v[240:241], v[134:135], s[62:63] op_sel_hi:[1,0]
	v_lshlrev_b32_e32 v242, 16, v59
	v_and_b32_e32 v243, 0xffff0000, v59
	v_pk_fma_f32 v[238:239], v[240:241], v[242:243], v[166:167]
	v_pk_mul_f32 v[240:241], v[136:137], s[64:65] op_sel_hi:[1,0]
	v_lshlrev_b32_e32 v242, 16, v60
	v_and_b32_e32 v243, 0xffff0000, v60
	v_pk_fma_f32 v[232:233], v[240:241], v[242:243], v[232:233]
	v_pk_mul_f32 v[240:241], v[138:139], s[64:65] op_sel_hi:[1,0]
	v_lshlrev_b32_e32 v242, 16, v61
	v_and_b32_e32 v243, 0xffff0000, v61
	v_pk_fma_f32 v[234:235], v[240:241], v[242:243], v[234:235]
	v_pk_mul_f32 v[240:241], v[140:141], s[64:65] op_sel_hi:[1,0]
	v_lshlrev_b32_e32 v242, 16, v62
	v_and_b32_e32 v243, 0xffff0000, v62
	v_pk_fma_f32 v[236:237], v[240:241], v[242:243], v[236:237]
	v_pk_mul_f32 v[240:241], v[142:143], s[64:65] op_sel_hi:[1,0]
	v_lshlrev_b32_e32 v242, 16, v63
	v_and_b32_e32 v243, 0xffff0000, v63
	v_pk_fma_f32 v[238:239], v[240:241], v[242:243], v[238:239]
	v_pk_mul_f32 v[240:241], v[144:145], s[66:67] op_sel_hi:[1,0]
	v_lshlrev_b32_e32 v242, 16, v64
	v_and_b32_e32 v243, 0xffff0000, v64
	v_pk_fma_f32 v[232:233], v[240:241], v[242:243], v[232:233]
	v_pk_mul_f32 v[240:241], v[146:147], s[66:67] op_sel_hi:[1,0]
	v_lshlrev_b32_e32 v242, 16, v65
	v_and_b32_e32 v243, 0xffff0000, v65
	v_pk_fma_f32 v[234:235], v[240:241], v[242:243], v[234:235]
	v_pk_mul_f32 v[240:241], v[148:149], s[66:67] op_sel_hi:[1,0]
	v_lshlrev_b32_e32 v242, 16, v66
	v_and_b32_e32 v243, 0xffff0000, v66
	v_pk_fma_f32 v[236:237], v[240:241], v[242:243], v[236:237]
	v_pk_mul_f32 v[240:241], v[150:151], s[66:67] op_sel_hi:[1,0]
	v_lshlrev_b32_e32 v242, 16, v67
	v_and_b32_e32 v243, 0xffff0000, v67
	v_pk_fma_f32 v[238:239], v[240:241], v[242:243], v[238:239]
	v_pk_mul_f32 v[240:241], v[152:153], s[68:69] op_sel_hi:[1,0]
	v_lshlrev_b32_e32 v242, 16, v68
	v_and_b32_e32 v243, 0xffff0000, v68
	v_pk_fma_f32 v[232:233], v[240:241], v[242:243], v[232:233]
	v_pk_mul_f32 v[240:241], v[154:155], s[68:69] op_sel_hi:[1,0]
	v_lshlrev_b32_e32 v242, 16, v69
	v_and_b32_e32 v243, 0xffff0000, v69
	v_pk_fma_f32 v[234:235], v[240:241], v[242:243], v[234:235]
	v_pk_mul_f32 v[240:241], v[156:157], s[68:69] op_sel_hi:[1,0]
	v_lshlrev_b32_e32 v242, 16, v70
	v_and_b32_e32 v243, 0xffff0000, v70
	v_pk_fma_f32 v[236:237], v[240:241], v[242:243], v[236:237]
	v_pk_mul_f32 v[240:241], v[158:159], s[68:69] op_sel_hi:[1,0]
	v_lshlrev_b32_e32 v242, 16, v71
	v_and_b32_e32 v243, 0xffff0000, v71
	v_pk_fma_f32 v[238:239], v[240:241], v[242:243], v[238:239]
	v_cvt_pk_bf16_f32 v248, v232, v233
	v_cvt_pk_bf16_f32 v249, v234, v235
	v_cvt_pk_bf16_f32 v250, v236, v237
	v_cvt_pk_bf16_f32 v251, v238, v239
	s_lshl_b32 s58, s54, 11
	s_add_u32 s60, s52, s58
	s_addc_u32 s61, s53, 0
	global_store_dwordx4 v126, v[248:251], s[60:61]
	s_add_i32 s54, s41, 0x2800
	s_cmp_lt_u32 s54, 0x8000
	s_cselect_b32 s55, s70, s71
	s_and_b32 s56, s54, s55
	s_add_i32 s57, s55, 1
	s_add_i32 s58, s56, -2
	s_cmp_lt_u32 s58, s57
	s_cselect_b32 s58, -2, 0
	s_add_i32 s58, s54, s58
	s_mul_i32 s58, s58, 0x5a00
	s_add_u32 s60, s50, s58
	s_addc_u32 s61, s51, 0
	global_load_dwordx4 v[40:43], v126, s[60:61]
	s_add_i32 s58, s56, -1
	s_cmp_lt_u32 s58, s57
	s_cselect_b32 s58, -1, 0
	s_add_i32 s58, s54, s58
	s_mul_i32 s58, s58, 0x5a00
	s_add_u32 s60, s50, s58
	s_addc_u32 s61, s51, 0
	global_load_dwordx4 v[44:47], v126, s[60:61]
	s_mul_i32 s58, s54, 0x5a00
	s_add_u32 s60, s50, s58
	s_addc_u32 s61, s51, 0
	global_load_dwordx4 v[48:51], v126, s[60:61]
	s_add_i32 s58, s56, 1
	s_cmp_lt_u32 s58, s57
	s_cselect_b32 s58, 1, 0
	s_add_i32 s58, s54, s58
	s_mul_i32 s58, s58, 0x5a00
	s_add_u32 s60, s50, s58
	s_addc_u32 s61, s51, 0
	global_load_dwordx4 v[52:55], v126, s[60:61]
	s_add_i32 s54, s41, 0x2c00
	s_cmp_lt_u32 s54, 0x8000
	s_cselect_b32 s55, s70, s71
	s_and_b32 s56, s54, s55
	s_add_i32 s57, s55, 1
	s_add_i32 s58, s56, -2
	s_cmp_lt_u32 s58, s57
	s_cselect_b32 s58, -2, 0
	s_add_i32 s58, s54, s58
	s_mul_i32 s58, s58, 0x5a00
	s_add_u32 s60, s50, s58
	s_addc_u32 s61, s51, 0
	global_load_dwordx4 v[56:59], v126, s[60:61]
	s_add_i32 s58, s56, -1
	s_cmp_lt_u32 s58, s57
	s_cselect_b32 s58, -1, 0
	s_add_i32 s58, s54, s58
	s_mul_i32 s58, s58, 0x5a00
	s_add_u32 s60, s50, s58
	s_addc_u32 s61, s51, 0
	global_load_dwordx4 v[60:63], v126, s[60:61]
	s_mul_i32 s58, s54, 0x5a00
	s_add_u32 s60, s50, s58
	s_addc_u32 s61, s51, 0
	global_load_dwordx4 v[64:67], v126, s[60:61]
	s_add_i32 s58, s56, 1
	s_cmp_lt_u32 s58, s57
	s_cselect_b32 s58, 1, 0
	s_add_i32 s58, s54, s58
	s_mul_i32 s58, s58, 0x5a00
	s_add_u32 s60, s50, s58
	s_addc_u32 s61, s51, 0
	global_load_dwordx4 v[68:71], v126, s[60:61]
	s_waitcnt vmcnt(20)
	s_add_i32 s54, s41, 0x1800
	s_cmp_lt_u32 s54, 0x8000
	s_cselect_b32 s55, s70, s71
	s_and_b32 s56, s54, s55
	s_add_i32 s57, s55, 1
	s_add_i32 s58, s56, -2
	s_cmp_lt_u32 s58, s57
	s_cselect_b32 s62, 1.0, 0
	s_add_i32 s58, s56, -1
	s_cmp_lt_u32 s58, s57
	s_cselect_b32 s64, 1.0, 0
	s_mov_b32 s66, 1.0
	s_add_i32 s58, s56, 1
	s_cmp_lt_u32 s58, s57
	s_cselect_b32 s68, 1.0, 0
	v_pk_mul_f32 v[240:241], v[128:129], s[62:63] op_sel_hi:[1,0]
	v_lshlrev_b32_e32 v242, 16, v168
	v_and_b32_e32 v243, 0xffff0000, v168
	v_pk_fma_f32 v[232:233], v[240:241], v[242:243], v[160:161]
	v_pk_mul_f32 v[240:241], v[130:131], s[62:63] op_sel_hi:[1,0]
	v_lshlrev_b32_e32 v242, 16, v169
	v_and_b32_e32 v243, 0xffff0000, v169
	v_pk_fma_f32 v[234:235], v[240:241], v[242:243], v[162:163]
	v_pk_mul_f32 v[240:241], v[132:133], s[62:63] op_sel_hi:[1,0]
	v_lshlrev_b32_e32 v242, 16, v170
	v_and_b32_e32 v243, 0xffff0000, v170
	v_pk_fma_f32 v[236:237], v[240:241], v[242:243], v[164:165]
	v_pk_mul_f32 v[240:241], v[134:135], s[62:63] op_sel_hi:[1,0]
	v_lshlrev_b32_e32 v242, 16, v171
	v_and_b32_e32 v243, 0xffff0000, v171
	v_pk_fma_f32 v[238:239], v[240:241], v[242:243], v[166:167]
	v_pk_mul_f32 v[240:241], v[136:137], s[64:65] op_sel_hi:[1,0]
	v_lshlrev_b32_e32 v242, 16, v172
	v_and_b32_e32 v243, 0xffff0000, v172
	v_pk_fma_f32 v[232:233], v[240:241], v[242:243], v[232:233]
	v_pk_mul_f32 v[240:241], v[138:139], s[64:65] op_sel_hi:[1,0]
	v_lshlrev_b32_e32 v242, 16, v173
	v_and_b32_e32 v243, 0xffff0000, v173
	v_pk_fma_f32 v[234:235], v[240:241], v[242:243], v[234:235]
	v_pk_mul_f32 v[240:241], v[140:141], s[64:65] op_sel_hi:[1,0]
	v_lshlrev_b32_e32 v242, 16, v174
	v_and_b32_e32 v243, 0xffff0000, v174
	v_pk_fma_f32 v[236:237], v[240:241], v[242:243], v[236:237]
	v_pk_mul_f32 v[240:241], v[142:143], s[64:65] op_sel_hi:[1,0]
	v_lshlrev_b32_e32 v242, 16, v175
	v_and_b32_e32 v243, 0xffff0000, v175
	v_pk_fma_f32 v[238:239], v[240:241], v[242:243], v[238:239]
	v_pk_mul_f32 v[240:241], v[144:145], s[66:67] op_sel_hi:[1,0]
	v_lshlrev_b32_e32 v242, 16, v176
	v_and_b32_e32 v243, 0xffff0000, v176
	v_pk_fma_f32 v[232:233], v[240:241], v[242:243], v[232:233]
	v_pk_mul_f32 v[240:241], v[146:147], s[66:67] op_sel_hi:[1,0]
	v_lshlrev_b32_e32 v242, 16, v177
	v_and_b32_e32 v243, 0xffff0000, v177
	v_pk_fma_f32 v[234:235], v[240:241], v[242:243], v[234:235]
	v_pk_mul_f32 v[240:241], v[148:149], s[66:67] op_sel_hi:[1,0]
	v_lshlrev_b32_e32 v242, 16, v178
	v_and_b32_e32 v243, 0xffff0000, v178
	v_pk_fma_f32 v[236:237], v[240:241], v[242:243], v[236:237]
	v_pk_mul_f32 v[240:241], v[150:151], s[66:67] op_sel_hi:[1,0]
	v_lshlrev_b32_e32 v242, 16, v179
	v_and_b32_e32 v243, 0xffff0000, v179
	v_pk_fma_f32 v[238:239], v[240:241], v[242:243], v[238:239]
	v_pk_mul_f32 v[240:241], v[152:153], s[68:69] op_sel_hi:[1,0]
	v_lshlrev_b32_e32 v242, 16, v180
	v_and_b32_e32 v243, 0xffff0000, v180
	v_pk_fma_f32 v[232:233], v[240:241], v[242:243], v[232:233]
	v_pk_mul_f32 v[240:241], v[154:155], s[68:69] op_sel_hi:[1,0]
	v_lshlrev_b32_e32 v242, 16, v181
	v_and_b32_e32 v243, 0xffff0000, v181
	v_pk_fma_f32 v[234:235], v[240:241], v[242:243], v[234:235]
	v_pk_mul_f32 v[240:241], v[156:157], s[68:69] op_sel_hi:[1,0]
	v_lshlrev_b32_e32 v242, 16, v182
	v_and_b32_e32 v243, 0xffff0000, v182
	v_pk_fma_f32 v[236:237], v[240:241], v[242:243], v[236:237]
	v_pk_mul_f32 v[240:241], v[158:159], s[68:69] op_sel_hi:[1,0]
	v_lshlrev_b32_e32 v242, 16, v183
	v_and_b32_e32 v243, 0xffff0000, v183
	v_pk_fma_f32 v[238:239], v[240:241], v[242:243], v[238:239]
	v_cvt_pk_bf16_f32 v248, v232, v233
	v_cvt_pk_bf16_f32 v249, v234, v235
	v_cvt_pk_bf16_f32 v250, v236, v237
	v_cvt_pk_bf16_f32 v251, v238, v239
	s_lshl_b32 s58, s54, 11
	s_add_u32 s60, s52, s58
	s_addc_u32 s61, s53, 0
	global_store_dwordx4 v126, v[248:251], s[60:61]
	s_add_i32 s54, s41, 0x1c00
	s_cmp_lt_u32 s54, 0x8000
	s_cselect_b32 s55, s70, s71
	s_and_b32 s56, s54, s55
	s_add_i32 s57, s55, 1
	s_add_i32 s58, s56, -2
	s_cmp_lt_u32 s58, s57
	s_cselect_b32 s62, 1.0, 0
	s_add_i32 s58, s56, -1
	s_cmp_lt_u32 s58, s57
	s_cselect_b32 s64, 1.0, 0
	s_mov_b32 s66, 1.0
	s_add_i32 s58, s56, 1
	s_cmp_lt_u32 s58, s57
	s_cselect_b32 s68, 1.0, 0
	v_pk_mul_f32 v[240:241], v[128:129], s[62:63] op_sel_hi:[1,0]
	v_lshlrev_b32_e32 v242, 16, v184
	v_and_b32_e32 v243, 0xffff0000, v184
	v_pk_fma_f32 v[232:233], v[240:241], v[242:243], v[160:161]
	v_pk_mul_f32 v[240:241], v[130:131], s[62:63] op_sel_hi:[1,0]
	v_lshlrev_b32_e32 v242, 16, v185
	v_and_b32_e32 v243, 0xffff0000, v185
	v_pk_fma_f32 v[234:235], v[240:241], v[242:243], v[162:163]
	v_pk_mul_f32 v[240:241], v[132:133], s[62:63] op_sel_hi:[1,0]
	v_lshlrev_b32_e32 v242, 16, v186
	v_and_b32_e32 v243, 0xffff0000, v186
	v_pk_fma_f32 v[236:237], v[240:241], v[242:243], v[164:165]
	v_pk_mul_f32 v[240:241], v[134:135], s[62:63] op_sel_hi:[1,0]
	v_lshlrev_b32_e32 v242, 16, v187
	v_and_b32_e32 v243, 0xffff0000, v187
	v_pk_fma_f32 v[238:239], v[240:241], v[242:243], v[166:167]
	v_pk_mul_f32 v[240:241], v[136:137], s[64:65] op_sel_hi:[1,0]
	v_lshlrev_b32_e32 v242, 16, v188
	v_and_b32_e32 v243, 0xffff0000, v188
	v_pk_fma_f32 v[232:233], v[240:241], v[242:243], v[232:233]
	v_pk_mul_f32 v[240:241], v[138:139], s[64:65] op_sel_hi:[1,0]
	v_lshlrev_b32_e32 v242, 16, v189
	v_and_b32_e32 v243, 0xffff0000, v189
	v_pk_fma_f32 v[234:235], v[240:241], v[242:243], v[234:235]
	v_pk_mul_f32 v[240:241], v[140:141], s[64:65] op_sel_hi:[1,0]
	v_lshlrev_b32_e32 v242, 16, v190
	v_and_b32_e32 v243, 0xffff0000, v190
	v_pk_fma_f32 v[236:237], v[240:241], v[242:243], v[236:237]
	v_pk_mul_f32 v[240:241], v[142:143], s[64:65] op_sel_hi:[1,0]
	v_lshlrev_b32_e32 v242, 16, v191
	v_and_b32_e32 v243, 0xffff0000, v191
	v_pk_fma_f32 v[238:239], v[240:241], v[242:243], v[238:239]
	v_pk_mul_f32 v[240:241], v[144:145], s[66:67] op_sel_hi:[1,0]
	v_lshlrev_b32_e32 v242, 16, v192
	v_and_b32_e32 v243, 0xffff0000, v192
	v_pk_fma_f32 v[232:233], v[240:241], v[242:243], v[232:233]
	v_pk_mul_f32 v[240:241], v[146:147], s[66:67] op_sel_hi:[1,0]
	v_lshlrev_b32_e32 v242, 16, v193
	v_and_b32_e32 v243, 0xffff0000, v193
	v_pk_fma_f32 v[234:235], v[240:241], v[242:243], v[234:235]
	v_pk_mul_f32 v[240:241], v[148:149], s[66:67] op_sel_hi:[1,0]
	v_lshlrev_b32_e32 v242, 16, v194
	v_and_b32_e32 v243, 0xffff0000, v194
	v_pk_fma_f32 v[236:237], v[240:241], v[242:243], v[236:237]
	v_pk_mul_f32 v[240:241], v[150:151], s[66:67] op_sel_hi:[1,0]
	v_lshlrev_b32_e32 v242, 16, v195
	v_and_b32_e32 v243, 0xffff0000, v195
	v_pk_fma_f32 v[238:239], v[240:241], v[242:243], v[238:239]
	v_pk_mul_f32 v[240:241], v[152:153], s[68:69] op_sel_hi:[1,0]
	v_lshlrev_b32_e32 v242, 16, v196
	v_and_b32_e32 v243, 0xffff0000, v196
	v_pk_fma_f32 v[232:233], v[240:241], v[242:243], v[232:233]
	v_pk_mul_f32 v[240:241], v[154:155], s[68:69] op_sel_hi:[1,0]
	v_lshlrev_b32_e32 v242, 16, v197
	v_and_b32_e32 v243, 0xffff0000, v197
	v_pk_fma_f32 v[234:235], v[240:241], v[242:243], v[234:235]
	v_pk_mul_f32 v[240:241], v[156:157], s[68:69] op_sel_hi:[1,0]
	v_lshlrev_b32_e32 v242, 16, v198
	v_and_b32_e32 v243, 0xffff0000, v198
	v_pk_fma_f32 v[236:237], v[240:241], v[242:243], v[236:237]
	v_pk_mul_f32 v[240:241], v[158:159], s[68:69] op_sel_hi:[1,0]
	v_lshlrev_b32_e32 v242, 16, v199
	v_and_b32_e32 v243, 0xffff0000, v199
	v_pk_fma_f32 v[238:239], v[240:241], v[242:243], v[238:239]
	v_cvt_pk_bf16_f32 v248, v232, v233
	v_cvt_pk_bf16_f32 v249, v234, v235
	v_cvt_pk_bf16_f32 v250, v236, v237
	v_cvt_pk_bf16_f32 v251, v238, v239
	s_lshl_b32 s58, s54, 11
	s_add_u32 s60, s52, s58
	s_addc_u32 s61, s53, 0
	global_store_dwordx4 v126, v[248:251], s[60:61]
	s_add_i32 s54, s41, 0x3000
	s_cmp_lt_u32 s54, 0x8000
	s_cselect_b32 s55, s70, s71
	s_and_b32 s56, s54, s55
	s_add_i32 s57, s55, 1
	s_add_i32 s58, s56, -2
	s_cmp_lt_u32 s58, s57
	s_cselect_b32 s58, -2, 0
	s_add_i32 s58, s54, s58
	s_mul_i32 s58, s58, 0x5a00
	s_add_u32 s60, s50, s58
	s_addc_u32 s61, s51, 0
	global_load_dwordx4 v[168:171], v126, s[60:61]
	s_add_i32 s58, s56, -1
	s_cmp_lt_u32 s58, s57
	s_cselect_b32 s58, -1, 0
	s_add_i32 s58, s54, s58
	s_mul_i32 s58, s58, 0x5a00
	s_add_u32 s60, s50, s58
	s_addc_u32 s61, s51, 0
	global_load_dwordx4 v[172:175], v126, s[60:61]
	s_mul_i32 s58, s54, 0x5a00
	s_add_u32 s60, s50, s58
	s_addc_u32 s61, s51, 0
	global_load_dwordx4 v[176:179], v126, s[60:61]
	s_add_i32 s58, s56, 1
	s_cmp_lt_u32 s58, s57
	s_cselect_b32 s58, 1, 0
	s_add_i32 s58, s54, s58
	s_mul_i32 s58, s58, 0x5a00
	s_add_u32 s60, s50, s58
	s_addc_u32 s61, s51, 0
	global_load_dwordx4 v[180:183], v126, s[60:61]
	s_add_i32 s54, s41, 0x3400
	s_cmp_lt_u32 s54, 0x8000
	s_cselect_b32 s55, s70, s71
	s_and_b32 s56, s54, s55
	s_add_i32 s57, s55, 1
	s_add_i32 s58, s56, -2
	s_cmp_lt_u32 s58, s57
	s_cselect_b32 s58, -2, 0
	s_add_i32 s58, s54, s58
	s_mul_i32 s58, s58, 0x5a00
	s_add_u32 s60, s50, s58
	s_addc_u32 s61, s51, 0
	global_load_dwordx4 v[184:187], v126, s[60:61]
	s_add_i32 s58, s56, -1
	s_cmp_lt_u32 s58, s57
	s_cselect_b32 s58, -1, 0
	s_add_i32 s58, s54, s58
	s_mul_i32 s58, s58, 0x5a00
	s_add_u32 s60, s50, s58
	s_addc_u32 s61, s51, 0
	global_load_dwordx4 v[188:191], v126, s[60:61]
	s_mul_i32 s58, s54, 0x5a00
	s_add_u32 s60, s50, s58
	s_addc_u32 s61, s51, 0
	global_load_dwordx4 v[192:195], v126, s[60:61]
	s_add_i32 s58, s56, 1
	s_cmp_lt_u32 s58, s57
	s_cselect_b32 s58, 1, 0
	s_add_i32 s58, s54, s58
	s_mul_i32 s58, s58, 0x5a00
	s_add_u32 s60, s50, s58
	s_addc_u32 s61, s51, 0
	global_load_dwordx4 v[196:199], v126, s[60:61]
	s_waitcnt vmcnt(20)
	s_add_i32 s54, s41, 0x2000
	s_cmp_lt_u32 s54, 0x8000
	s_cselect_b32 s55, s70, s71
	s_and_b32 s56, s54, s55
	s_add_i32 s57, s55, 1
	s_add_i32 s58, s56, -2
	s_cmp_lt_u32 s58, s57
	s_cselect_b32 s62, 1.0, 0
	s_add_i32 s58, s56, -1
	s_cmp_lt_u32 s58, s57
	s_cselect_b32 s64, 1.0, 0
	s_mov_b32 s66, 1.0
	s_add_i32 s58, s56, 1
	s_cmp_lt_u32 s58, s57
	s_cselect_b32 s68, 1.0, 0
	v_pk_mul_f32 v[240:241], v[128:129], s[62:63] op_sel_hi:[1,0]
	v_lshlrev_b32_e32 v242, 16, v200
	v_and_b32_e32 v243, 0xffff0000, v200
	v_pk_fma_f32 v[232:233], v[240:241], v[242:243], v[160:161]
	v_pk_mul_f32 v[240:241], v[130:131], s[62:63] op_sel_hi:[1,0]
	v_lshlrev_b32_e32 v242, 16, v201
	v_and_b32_e32 v243, 0xffff0000, v201
	v_pk_fma_f32 v[234:235], v[240:241], v[242:243], v[162:163]
	v_pk_mul_f32 v[240:241], v[132:133], s[62:63] op_sel_hi:[1,0]
	v_lshlrev_b32_e32 v242, 16, v202
	v_and_b32_e32 v243, 0xffff0000, v202
	v_pk_fma_f32 v[236:237], v[240:241], v[242:243], v[164:165]
	v_pk_mul_f32 v[240:241], v[134:135], s[62:63] op_sel_hi:[1,0]
	v_lshlrev_b32_e32 v242, 16, v203
	v_and_b32_e32 v243, 0xffff0000, v203
	v_pk_fma_f32 v[238:239], v[240:241], v[242:243], v[166:167]
	v_pk_mul_f32 v[240:241], v[136:137], s[64:65] op_sel_hi:[1,0]
	v_lshlrev_b32_e32 v242, 16, v204
	v_and_b32_e32 v243, 0xffff0000, v204
	v_pk_fma_f32 v[232:233], v[240:241], v[242:243], v[232:233]
	v_pk_mul_f32 v[240:241], v[138:139], s[64:65] op_sel_hi:[1,0]
	v_lshlrev_b32_e32 v242, 16, v205
	v_and_b32_e32 v243, 0xffff0000, v205
	v_pk_fma_f32 v[234:235], v[240:241], v[242:243], v[234:235]
	v_pk_mul_f32 v[240:241], v[140:141], s[64:65] op_sel_hi:[1,0]
	v_lshlrev_b32_e32 v242, 16, v206
	v_and_b32_e32 v243, 0xffff0000, v206
	v_pk_fma_f32 v[236:237], v[240:241], v[242:243], v[236:237]
	v_pk_mul_f32 v[240:241], v[142:143], s[64:65] op_sel_hi:[1,0]
	v_lshlrev_b32_e32 v242, 16, v207
	v_and_b32_e32 v243, 0xffff0000, v207
	v_pk_fma_f32 v[238:239], v[240:241], v[242:243], v[238:239]
	v_pk_mul_f32 v[240:241], v[144:145], s[66:67] op_sel_hi:[1,0]
	v_lshlrev_b32_e32 v242, 16, v208
	v_and_b32_e32 v243, 0xffff0000, v208
	v_pk_fma_f32 v[232:233], v[240:241], v[242:243], v[232:233]
	v_pk_mul_f32 v[240:241], v[146:147], s[66:67] op_sel_hi:[1,0]
	v_lshlrev_b32_e32 v242, 16, v209
	v_and_b32_e32 v243, 0xffff0000, v209
	v_pk_fma_f32 v[234:235], v[240:241], v[242:243], v[234:235]
	v_pk_mul_f32 v[240:241], v[148:149], s[66:67] op_sel_hi:[1,0]
	v_lshlrev_b32_e32 v242, 16, v210
	v_and_b32_e32 v243, 0xffff0000, v210
	v_pk_fma_f32 v[236:237], v[240:241], v[242:243], v[236:237]
	v_pk_mul_f32 v[240:241], v[150:151], s[66:67] op_sel_hi:[1,0]
	v_lshlrev_b32_e32 v242, 16, v211
	v_and_b32_e32 v243, 0xffff0000, v211
	v_pk_fma_f32 v[238:239], v[240:241], v[242:243], v[238:239]
	v_pk_mul_f32 v[240:241], v[152:153], s[68:69] op_sel_hi:[1,0]
	v_lshlrev_b32_e32 v242, 16, v212
	v_and_b32_e32 v243, 0xffff0000, v212
	v_pk_fma_f32 v[232:233], v[240:241], v[242:243], v[232:233]
	v_pk_mul_f32 v[240:241], v[154:155], s[68:69] op_sel_hi:[1,0]
	v_lshlrev_b32_e32 v242, 16, v213
	v_and_b32_e32 v243, 0xffff0000, v213
	v_pk_fma_f32 v[234:235], v[240:241], v[242:243], v[234:235]
	v_pk_mul_f32 v[240:241], v[156:157], s[68:69] op_sel_hi:[1,0]
	v_lshlrev_b32_e32 v242, 16, v214
	v_and_b32_e32 v243, 0xffff0000, v214
	v_pk_fma_f32 v[236:237], v[240:241], v[242:243], v[236:237]
	v_pk_mul_f32 v[240:241], v[158:159], s[68:69] op_sel_hi:[1,0]
	v_lshlrev_b32_e32 v242, 16, v215
	v_and_b32_e32 v243, 0xffff0000, v215
	v_pk_fma_f32 v[238:239], v[240:241], v[242:243], v[238:239]
	v_cvt_pk_bf16_f32 v248, v232, v233
	v_cvt_pk_bf16_f32 v249, v234, v235
	v_cvt_pk_bf16_f32 v250, v236, v237
	v_cvt_pk_bf16_f32 v251, v238, v239
	s_lshl_b32 s58, s54, 11
	s_add_u32 s60, s52, s58
	s_addc_u32 s61, s53, 0
	global_store_dwordx4 v126, v[248:251], s[60:61]
	s_add_i32 s54, s41, 0x2400
	s_cmp_lt_u32 s54, 0x8000
	s_cselect_b32 s55, s70, s71
	s_and_b32 s56, s54, s55
	s_add_i32 s57, s55, 1
	s_add_i32 s58, s56, -2
	s_cmp_lt_u32 s58, s57
	s_cselect_b32 s62, 1.0, 0
	s_add_i32 s58, s56, -1
	s_cmp_lt_u32 s58, s57
	s_cselect_b32 s64, 1.0, 0
	s_mov_b32 s66, 1.0
	s_add_i32 s58, s56, 1
	s_cmp_lt_u32 s58, s57
	s_cselect_b32 s68, 1.0, 0
	v_pk_mul_f32 v[240:241], v[128:129], s[62:63] op_sel_hi:[1,0]
	v_lshlrev_b32_e32 v242, 16, v216
	v_and_b32_e32 v243, 0xffff0000, v216
	v_pk_fma_f32 v[232:233], v[240:241], v[242:243], v[160:161]
	v_pk_mul_f32 v[240:241], v[130:131], s[62:63] op_sel_hi:[1,0]
	v_lshlrev_b32_e32 v242, 16, v217
	v_and_b32_e32 v243, 0xffff0000, v217
	v_pk_fma_f32 v[234:235], v[240:241], v[242:243], v[162:163]
	v_pk_mul_f32 v[240:241], v[132:133], s[62:63] op_sel_hi:[1,0]
	v_lshlrev_b32_e32 v242, 16, v218
	v_and_b32_e32 v243, 0xffff0000, v218
	v_pk_fma_f32 v[236:237], v[240:241], v[242:243], v[164:165]
	v_pk_mul_f32 v[240:241], v[134:135], s[62:63] op_sel_hi:[1,0]
	v_lshlrev_b32_e32 v242, 16, v219
	v_and_b32_e32 v243, 0xffff0000, v219
	v_pk_fma_f32 v[238:239], v[240:241], v[242:243], v[166:167]
	v_pk_mul_f32 v[240:241], v[136:137], s[64:65] op_sel_hi:[1,0]
	v_lshlrev_b32_e32 v242, 16, v220
	v_and_b32_e32 v243, 0xffff0000, v220
	v_pk_fma_f32 v[232:233], v[240:241], v[242:243], v[232:233]
	v_pk_mul_f32 v[240:241], v[138:139], s[64:65] op_sel_hi:[1,0]
	v_lshlrev_b32_e32 v242, 16, v221
	v_and_b32_e32 v243, 0xffff0000, v221
	v_pk_fma_f32 v[234:235], v[240:241], v[242:243], v[234:235]
	v_pk_mul_f32 v[240:241], v[140:141], s[64:65] op_sel_hi:[1,0]
	v_lshlrev_b32_e32 v242, 16, v222
	v_and_b32_e32 v243, 0xffff0000, v222
	v_pk_fma_f32 v[236:237], v[240:241], v[242:243], v[236:237]
	v_pk_mul_f32 v[240:241], v[142:143], s[64:65] op_sel_hi:[1,0]
	v_lshlrev_b32_e32 v242, 16, v223
	v_and_b32_e32 v243, 0xffff0000, v223
	v_pk_fma_f32 v[238:239], v[240:241], v[242:243], v[238:239]
	v_pk_mul_f32 v[240:241], v[144:145], s[66:67] op_sel_hi:[1,0]
	v_lshlrev_b32_e32 v242, 16, v224
	v_and_b32_e32 v243, 0xffff0000, v224
	v_pk_fma_f32 v[232:233], v[240:241], v[242:243], v[232:233]
	v_pk_mul_f32 v[240:241], v[146:147], s[66:67] op_sel_hi:[1,0]
	v_lshlrev_b32_e32 v242, 16, v225
	v_and_b32_e32 v243, 0xffff0000, v225
	v_pk_fma_f32 v[234:235], v[240:241], v[242:243], v[234:235]
	v_pk_mul_f32 v[240:241], v[148:149], s[66:67] op_sel_hi:[1,0]
	v_lshlrev_b32_e32 v242, 16, v226
	v_and_b32_e32 v243, 0xffff0000, v226
	v_pk_fma_f32 v[236:237], v[240:241], v[242:243], v[236:237]
	v_pk_mul_f32 v[240:241], v[150:151], s[66:67] op_sel_hi:[1,0]
	v_lshlrev_b32_e32 v242, 16, v227
	v_and_b32_e32 v243, 0xffff0000, v227
	v_pk_fma_f32 v[238:239], v[240:241], v[242:243], v[238:239]
	v_pk_mul_f32 v[240:241], v[152:153], s[68:69] op_sel_hi:[1,0]
	v_lshlrev_b32_e32 v242, 16, v228
	v_and_b32_e32 v243, 0xffff0000, v228
	v_pk_fma_f32 v[232:233], v[240:241], v[242:243], v[232:233]
	v_pk_mul_f32 v[240:241], v[154:155], s[68:69] op_sel_hi:[1,0]
	v_lshlrev_b32_e32 v242, 16, v229
	v_and_b32_e32 v243, 0xffff0000, v229
	v_pk_fma_f32 v[234:235], v[240:241], v[242:243], v[234:235]
	v_pk_mul_f32 v[240:241], v[156:157], s[68:69] op_sel_hi:[1,0]
	v_lshlrev_b32_e32 v242, 16, v230
	v_and_b32_e32 v243, 0xffff0000, v230
	v_pk_fma_f32 v[236:237], v[240:241], v[242:243], v[236:237]
	v_pk_mul_f32 v[240:241], v[158:159], s[68:69] op_sel_hi:[1,0]
	v_lshlrev_b32_e32 v242, 16, v231
	v_and_b32_e32 v243, 0xffff0000, v231
	v_pk_fma_f32 v[238:239], v[240:241], v[242:243], v[238:239]
	v_cvt_pk_bf16_f32 v248, v232, v233
	v_cvt_pk_bf16_f32 v249, v234, v235
	v_cvt_pk_bf16_f32 v250, v236, v237
	v_cvt_pk_bf16_f32 v251, v238, v239
	s_lshl_b32 s58, s54, 11
	s_add_u32 s60, s52, s58
	s_addc_u32 s61, s53, 0
	global_store_dwordx4 v126, v[248:251], s[60:61]
	s_add_i32 s54, s41, 0x3800
	s_cmp_lt_u32 s54, 0x8000
	s_cselect_b32 s55, s70, s71
	s_and_b32 s56, s54, s55
	s_add_i32 s57, s55, 1
	s_add_i32 s58, s56, -2
	s_cmp_lt_u32 s58, s57
	s_cselect_b32 s58, -2, 0
	s_add_i32 s58, s54, s58
	s_mul_i32 s58, s58, 0x5a00
	s_add_u32 s60, s50, s58
	s_addc_u32 s61, s51, 0
	global_load_dwordx4 v[200:203], v126, s[60:61]
	s_add_i32 s58, s56, -1
	s_cmp_lt_u32 s58, s57
	s_cselect_b32 s58, -1, 0
	s_add_i32 s58, s54, s58
	s_mul_i32 s58, s58, 0x5a00
	s_add_u32 s60, s50, s58
	s_addc_u32 s61, s51, 0
	global_load_dwordx4 v[204:207], v126, s[60:61]
	s_mul_i32 s58, s54, 0x5a00
	s_add_u32 s60, s50, s58
	s_addc_u32 s61, s51, 0
	global_load_dwordx4 v[208:211], v126, s[60:61]
	s_add_i32 s58, s56, 1
	s_cmp_lt_u32 s58, s57
	s_cselect_b32 s58, 1, 0
	s_add_i32 s58, s54, s58
	s_mul_i32 s58, s58, 0x5a00
	s_add_u32 s60, s50, s58
	s_addc_u32 s61, s51, 0
	global_load_dwordx4 v[212:215], v126, s[60:61]
	s_add_i32 s54, s41, 0x3c00
	s_cmp_lt_u32 s54, 0x8000
	s_cselect_b32 s55, s70, s71
	s_and_b32 s56, s54, s55
	s_add_i32 s57, s55, 1
	s_add_i32 s58, s56, -2
	s_cmp_lt_u32 s58, s57
	s_cselect_b32 s58, -2, 0
	s_add_i32 s58, s54, s58
	s_mul_i32 s58, s58, 0x5a00
	s_add_u32 s60, s50, s58
	s_addc_u32 s61, s51, 0
	global_load_dwordx4 v[216:219], v126, s[60:61]
	s_add_i32 s58, s56, -1
	s_cmp_lt_u32 s58, s57
	s_cselect_b32 s58, -1, 0
	s_add_i32 s58, s54, s58
	s_mul_i32 s58, s58, 0x5a00
	s_add_u32 s60, s50, s58
	s_addc_u32 s61, s51, 0
	global_load_dwordx4 v[220:223], v126, s[60:61]
	s_mul_i32 s58, s54, 0x5a00
	s_add_u32 s60, s50, s58
	s_addc_u32 s61, s51, 0
	global_load_dwordx4 v[224:227], v126, s[60:61]
	s_add_i32 s58, s56, 1
	s_cmp_lt_u32 s58, s57
	s_cselect_b32 s58, 1, 0
	s_add_i32 s58, s54, s58
	s_mul_i32 s58, s58, 0x5a00
	s_add_u32 s60, s50, s58
	s_addc_u32 s61, s51, 0
	global_load_dwordx4 v[228:231], v126, s[60:61]
	s_waitcnt vmcnt(20)
	s_add_i32 s54, s41, 0x2800
	s_cmp_lt_u32 s54, 0x8000
	s_cselect_b32 s55, s70, s71
	s_and_b32 s56, s54, s55
	s_add_i32 s57, s55, 1
	s_add_i32 s58, s56, -2
	s_cmp_lt_u32 s58, s57
	s_cselect_b32 s62, 1.0, 0
	s_add_i32 s58, s56, -1
	s_cmp_lt_u32 s58, s57
	s_cselect_b32 s64, 1.0, 0
	s_mov_b32 s66, 1.0
	s_add_i32 s58, s56, 1
	s_cmp_lt_u32 s58, s57
	s_cselect_b32 s68, 1.0, 0
	v_pk_mul_f32 v[240:241], v[128:129], s[62:63] op_sel_hi:[1,0]
	v_lshlrev_b32_e32 v242, 16, v40
	v_and_b32_e32 v243, 0xffff0000, v40
	v_pk_fma_f32 v[232:233], v[240:241], v[242:243], v[160:161]
	v_pk_mul_f32 v[240:241], v[130:131], s[62:63] op_sel_hi:[1,0]
	v_lshlrev_b32_e32 v242, 16, v41
	v_and_b32_e32 v243, 0xffff0000, v41
	v_pk_fma_f32 v[234:235], v[240:241], v[242:243], v[162:163]
	v_pk_mul_f32 v[240:241], v[132:133], s[62:63] op_sel_hi:[1,0]
	v_lshlrev_b32_e32 v242, 16, v42
	v_and_b32_e32 v243, 0xffff0000, v42
	v_pk_fma_f32 v[236:237], v[240:241], v[242:243], v[164:165]
	v_pk_mul_f32 v[240:241], v[134:135], s[62:63] op_sel_hi:[1,0]
	v_lshlrev_b32_e32 v242, 16, v43
	v_and_b32_e32 v243, 0xffff0000, v43
	v_pk_fma_f32 v[238:239], v[240:241], v[242:243], v[166:167]
	v_pk_mul_f32 v[240:241], v[136:137], s[64:65] op_sel_hi:[1,0]
	v_lshlrev_b32_e32 v242, 16, v44
	v_and_b32_e32 v243, 0xffff0000, v44
	v_pk_fma_f32 v[232:233], v[240:241], v[242:243], v[232:233]
	v_pk_mul_f32 v[240:241], v[138:139], s[64:65] op_sel_hi:[1,0]
	v_lshlrev_b32_e32 v242, 16, v45
	v_and_b32_e32 v243, 0xffff0000, v45
	v_pk_fma_f32 v[234:235], v[240:241], v[242:243], v[234:235]
	v_pk_mul_f32 v[240:241], v[140:141], s[64:65] op_sel_hi:[1,0]
	v_lshlrev_b32_e32 v242, 16, v46
	v_and_b32_e32 v243, 0xffff0000, v46
	v_pk_fma_f32 v[236:237], v[240:241], v[242:243], v[236:237]
	v_pk_mul_f32 v[240:241], v[142:143], s[64:65] op_sel_hi:[1,0]
	v_lshlrev_b32_e32 v242, 16, v47
	v_and_b32_e32 v243, 0xffff0000, v47
	v_pk_fma_f32 v[238:239], v[240:241], v[242:243], v[238:239]
	v_pk_mul_f32 v[240:241], v[144:145], s[66:67] op_sel_hi:[1,0]
	v_lshlrev_b32_e32 v242, 16, v48
	v_and_b32_e32 v243, 0xffff0000, v48
	v_pk_fma_f32 v[232:233], v[240:241], v[242:243], v[232:233]
	v_pk_mul_f32 v[240:241], v[146:147], s[66:67] op_sel_hi:[1,0]
	v_lshlrev_b32_e32 v242, 16, v49
	v_and_b32_e32 v243, 0xffff0000, v49
	v_pk_fma_f32 v[234:235], v[240:241], v[242:243], v[234:235]
	v_pk_mul_f32 v[240:241], v[148:149], s[66:67] op_sel_hi:[1,0]
	v_lshlrev_b32_e32 v242, 16, v50
	v_and_b32_e32 v243, 0xffff0000, v50
	v_pk_fma_f32 v[236:237], v[240:241], v[242:243], v[236:237]
	v_pk_mul_f32 v[240:241], v[150:151], s[66:67] op_sel_hi:[1,0]
	v_lshlrev_b32_e32 v242, 16, v51
	v_and_b32_e32 v243, 0xffff0000, v51
	v_pk_fma_f32 v[238:239], v[240:241], v[242:243], v[238:239]
	v_pk_mul_f32 v[240:241], v[152:153], s[68:69] op_sel_hi:[1,0]
	v_lshlrev_b32_e32 v242, 16, v52
	v_and_b32_e32 v243, 0xffff0000, v52
	v_pk_fma_f32 v[232:233], v[240:241], v[242:243], v[232:233]
	v_pk_mul_f32 v[240:241], v[154:155], s[68:69] op_sel_hi:[1,0]
	v_lshlrev_b32_e32 v242, 16, v53
	v_and_b32_e32 v243, 0xffff0000, v53
	v_pk_fma_f32 v[234:235], v[240:241], v[242:243], v[234:235]
	v_pk_mul_f32 v[240:241], v[156:157], s[68:69] op_sel_hi:[1,0]
	v_lshlrev_b32_e32 v242, 16, v54
	v_and_b32_e32 v243, 0xffff0000, v54
	v_pk_fma_f32 v[236:237], v[240:241], v[242:243], v[236:237]
	v_pk_mul_f32 v[240:241], v[158:159], s[68:69] op_sel_hi:[1,0]
	v_lshlrev_b32_e32 v242, 16, v55
	v_and_b32_e32 v243, 0xffff0000, v55
	v_pk_fma_f32 v[238:239], v[240:241], v[242:243], v[238:239]
	v_cvt_pk_bf16_f32 v248, v232, v233
	v_cvt_pk_bf16_f32 v249, v234, v235
	v_cvt_pk_bf16_f32 v250, v236, v237
	v_cvt_pk_bf16_f32 v251, v238, v239
	s_lshl_b32 s58, s54, 11
	s_add_u32 s60, s52, s58
	s_addc_u32 s61, s53, 0
	global_store_dwordx4 v126, v[248:251], s[60:61]
	s_add_i32 s54, s41, 0x2c00
	s_cmp_lt_u32 s54, 0x8000
	s_cselect_b32 s55, s70, s71
	s_and_b32 s56, s54, s55
	s_add_i32 s57, s55, 1
	s_add_i32 s58, s56, -2
	s_cmp_lt_u32 s58, s57
	s_cselect_b32 s62, 1.0, 0
	s_add_i32 s58, s56, -1
	s_cmp_lt_u32 s58, s57
	s_cselect_b32 s64, 1.0, 0
	s_mov_b32 s66, 1.0
	s_add_i32 s58, s56, 1
	s_cmp_lt_u32 s58, s57
	s_cselect_b32 s68, 1.0, 0
	v_pk_mul_f32 v[240:241], v[128:129], s[62:63] op_sel_hi:[1,0]
	v_lshlrev_b32_e32 v242, 16, v56
	v_and_b32_e32 v243, 0xffff0000, v56
	v_pk_fma_f32 v[232:233], v[240:241], v[242:243], v[160:161]
	v_pk_mul_f32 v[240:241], v[130:131], s[62:63] op_sel_hi:[1,0]
	v_lshlrev_b32_e32 v242, 16, v57
	v_and_b32_e32 v243, 0xffff0000, v57
	v_pk_fma_f32 v[234:235], v[240:241], v[242:243], v[162:163]
	v_pk_mul_f32 v[240:241], v[132:133], s[62:63] op_sel_hi:[1,0]
	v_lshlrev_b32_e32 v242, 16, v58
	v_and_b32_e32 v243, 0xffff0000, v58
	v_pk_fma_f32 v[236:237], v[240:241], v[242:243], v[164:165]
	v_pk_mul_f32 v[240:241], v[134:135], s[62:63] op_sel_hi:[1,0]
	v_lshlrev_b32_e32 v242, 16, v59
	v_and_b32_e32 v243, 0xffff0000, v59
	v_pk_fma_f32 v[238:239], v[240:241], v[242:243], v[166:167]
	v_pk_mul_f32 v[240:241], v[136:137], s[64:65] op_sel_hi:[1,0]
	v_lshlrev_b32_e32 v242, 16, v60
	v_and_b32_e32 v243, 0xffff0000, v60
	v_pk_fma_f32 v[232:233], v[240:241], v[242:243], v[232:233]
	v_pk_mul_f32 v[240:241], v[138:139], s[64:65] op_sel_hi:[1,0]
	v_lshlrev_b32_e32 v242, 16, v61
	v_and_b32_e32 v243, 0xffff0000, v61
	v_pk_fma_f32 v[234:235], v[240:241], v[242:243], v[234:235]
	v_pk_mul_f32 v[240:241], v[140:141], s[64:65] op_sel_hi:[1,0]
	v_lshlrev_b32_e32 v242, 16, v62
	v_and_b32_e32 v243, 0xffff0000, v62
	v_pk_fma_f32 v[236:237], v[240:241], v[242:243], v[236:237]
	v_pk_mul_f32 v[240:241], v[142:143], s[64:65] op_sel_hi:[1,0]
	v_lshlrev_b32_e32 v242, 16, v63
	v_and_b32_e32 v243, 0xffff0000, v63
	v_pk_fma_f32 v[238:239], v[240:241], v[242:243], v[238:239]
	v_pk_mul_f32 v[240:241], v[144:145], s[66:67] op_sel_hi:[1,0]
	v_lshlrev_b32_e32 v242, 16, v64
	v_and_b32_e32 v243, 0xffff0000, v64
	v_pk_fma_f32 v[232:233], v[240:241], v[242:243], v[232:233]
	v_pk_mul_f32 v[240:241], v[146:147], s[66:67] op_sel_hi:[1,0]
	v_lshlrev_b32_e32 v242, 16, v65
	v_and_b32_e32 v243, 0xffff0000, v65
	v_pk_fma_f32 v[234:235], v[240:241], v[242:243], v[234:235]
	v_pk_mul_f32 v[240:241], v[148:149], s[66:67] op_sel_hi:[1,0]
	v_lshlrev_b32_e32 v242, 16, v66
	v_and_b32_e32 v243, 0xffff0000, v66
	v_pk_fma_f32 v[236:237], v[240:241], v[242:243], v[236:237]
	v_pk_mul_f32 v[240:241], v[150:151], s[66:67] op_sel_hi:[1,0]
	v_lshlrev_b32_e32 v242, 16, v67
	v_and_b32_e32 v243, 0xffff0000, v67
	v_pk_fma_f32 v[238:239], v[240:241], v[242:243], v[238:239]
	v_pk_mul_f32 v[240:241], v[152:153], s[68:69] op_sel_hi:[1,0]
	v_lshlrev_b32_e32 v242, 16, v68
	v_and_b32_e32 v243, 0xffff0000, v68
	v_pk_fma_f32 v[232:233], v[240:241], v[242:243], v[232:233]
	v_pk_mul_f32 v[240:241], v[154:155], s[68:69] op_sel_hi:[1,0]
	v_lshlrev_b32_e32 v242, 16, v69
	v_and_b32_e32 v243, 0xffff0000, v69
	v_pk_fma_f32 v[234:235], v[240:241], v[242:243], v[234:235]
	v_pk_mul_f32 v[240:241], v[156:157], s[68:69] op_sel_hi:[1,0]
	v_lshlrev_b32_e32 v242, 16, v70
	v_and_b32_e32 v243, 0xffff0000, v70
	v_pk_fma_f32 v[236:237], v[240:241], v[242:243], v[236:237]
	v_pk_mul_f32 v[240:241], v[158:159], s[68:69] op_sel_hi:[1,0]
	v_lshlrev_b32_e32 v242, 16, v71
	v_and_b32_e32 v243, 0xffff0000, v71
	v_pk_fma_f32 v[238:239], v[240:241], v[242:243], v[238:239]
	v_cvt_pk_bf16_f32 v248, v232, v233
	v_cvt_pk_bf16_f32 v249, v234, v235
	v_cvt_pk_bf16_f32 v250, v236, v237
	v_cvt_pk_bf16_f32 v251, v238, v239
	s_lshl_b32 s58, s54, 11
	s_add_u32 s60, s52, s58
	s_addc_u32 s61, s53, 0
	global_store_dwordx4 v126, v[248:251], s[60:61]
	s_add_i32 s54, s41, 0x4000
	s_cmp_lt_u32 s54, 0x8000
	s_cselect_b32 s55, s70, s71
	s_and_b32 s56, s54, s55
	s_add_i32 s57, s55, 1
	s_add_i32 s58, s56, -2
	s_cmp_lt_u32 s58, s57
	s_cselect_b32 s58, -2, 0
	s_add_i32 s58, s54, s58
	s_mul_i32 s58, s58, 0x5a00
	s_add_u32 s60, s50, s58
	s_addc_u32 s61, s51, 0
	global_load_dwordx4 v[40:43], v126, s[60:61]
	s_add_i32 s58, s56, -1
	s_cmp_lt_u32 s58, s57
	s_cselect_b32 s58, -1, 0
	s_add_i32 s58, s54, s58
	s_mul_i32 s58, s58, 0x5a00
	s_add_u32 s60, s50, s58
	s_addc_u32 s61, s51, 0
	global_load_dwordx4 v[44:47], v126, s[60:61]
	s_mul_i32 s58, s54, 0x5a00
	s_add_u32 s60, s50, s58
	s_addc_u32 s61, s51, 0
	global_load_dwordx4 v[48:51], v126, s[60:61]
	s_add_i32 s58, s56, 1
	s_cmp_lt_u32 s58, s57
	s_cselect_b32 s58, 1, 0
	s_add_i32 s58, s54, s58
	s_mul_i32 s58, s58, 0x5a00
	s_add_u32 s60, s50, s58
	s_addc_u32 s61, s51, 0
	global_load_dwordx4 v[52:55], v126, s[60:61]
	s_add_i32 s54, s41, 0x4400
	s_cmp_lt_u32 s54, 0x8000
	s_cselect_b32 s55, s70, s71
	s_and_b32 s56, s54, s55
	s_add_i32 s57, s55, 1
	s_add_i32 s58, s56, -2
	s_cmp_lt_u32 s58, s57
	s_cselect_b32 s58, -2, 0
	s_add_i32 s58, s54, s58
	s_mul_i32 s58, s58, 0x5a00
	s_add_u32 s60, s50, s58
	s_addc_u32 s61, s51, 0
	global_load_dwordx4 v[56:59], v126, s[60:61]
	s_add_i32 s58, s56, -1
	s_cmp_lt_u32 s58, s57
	s_cselect_b32 s58, -1, 0
	s_add_i32 s58, s54, s58
	s_mul_i32 s58, s58, 0x5a00
	s_add_u32 s60, s50, s58
	s_addc_u32 s61, s51, 0
	global_load_dwordx4 v[60:63], v126, s[60:61]
	s_mul_i32 s58, s54, 0x5a00
	s_add_u32 s60, s50, s58
	s_addc_u32 s61, s51, 0
	global_load_dwordx4 v[64:67], v126, s[60:61]
	s_add_i32 s58, s56, 1
	s_cmp_lt_u32 s58, s57
	s_cselect_b32 s58, 1, 0
	s_add_i32 s58, s54, s58
	s_mul_i32 s58, s58, 0x5a00
	s_add_u32 s60, s50, s58
	s_addc_u32 s61, s51, 0
	global_load_dwordx4 v[68:71], v126, s[60:61]
	s_waitcnt vmcnt(20)
	s_add_i32 s54, s41, 0x3000
	s_cmp_lt_u32 s54, 0x8000
	s_cselect_b32 s55, s70, s71
	s_and_b32 s56, s54, s55
	s_add_i32 s57, s55, 1
	s_add_i32 s58, s56, -2
	s_cmp_lt_u32 s58, s57
	s_cselect_b32 s62, 1.0, 0
	s_add_i32 s58, s56, -1
	s_cmp_lt_u32 s58, s57
	s_cselect_b32 s64, 1.0, 0
	s_mov_b32 s66, 1.0
	s_add_i32 s58, s56, 1
	s_cmp_lt_u32 s58, s57
	s_cselect_b32 s68, 1.0, 0
	v_pk_mul_f32 v[240:241], v[128:129], s[62:63] op_sel_hi:[1,0]
	v_lshlrev_b32_e32 v242, 16, v168
	v_and_b32_e32 v243, 0xffff0000, v168
	v_pk_fma_f32 v[232:233], v[240:241], v[242:243], v[160:161]
	v_pk_mul_f32 v[240:241], v[130:131], s[62:63] op_sel_hi:[1,0]
	v_lshlrev_b32_e32 v242, 16, v169
	v_and_b32_e32 v243, 0xffff0000, v169
	v_pk_fma_f32 v[234:235], v[240:241], v[242:243], v[162:163]
	v_pk_mul_f32 v[240:241], v[132:133], s[62:63] op_sel_hi:[1,0]
	v_lshlrev_b32_e32 v242, 16, v170
	v_and_b32_e32 v243, 0xffff0000, v170
	v_pk_fma_f32 v[236:237], v[240:241], v[242:243], v[164:165]
	v_pk_mul_f32 v[240:241], v[134:135], s[62:63] op_sel_hi:[1,0]
	v_lshlrev_b32_e32 v242, 16, v171
	v_and_b32_e32 v243, 0xffff0000, v171
	v_pk_fma_f32 v[238:239], v[240:241], v[242:243], v[166:167]
	v_pk_mul_f32 v[240:241], v[136:137], s[64:65] op_sel_hi:[1,0]
	v_lshlrev_b32_e32 v242, 16, v172
	v_and_b32_e32 v243, 0xffff0000, v172
	v_pk_fma_f32 v[232:233], v[240:241], v[242:243], v[232:233]
	v_pk_mul_f32 v[240:241], v[138:139], s[64:65] op_sel_hi:[1,0]
	v_lshlrev_b32_e32 v242, 16, v173
	v_and_b32_e32 v243, 0xffff0000, v173
	v_pk_fma_f32 v[234:235], v[240:241], v[242:243], v[234:235]
	v_pk_mul_f32 v[240:241], v[140:141], s[64:65] op_sel_hi:[1,0]
	v_lshlrev_b32_e32 v242, 16, v174
	v_and_b32_e32 v243, 0xffff0000, v174
	v_pk_fma_f32 v[236:237], v[240:241], v[242:243], v[236:237]
	v_pk_mul_f32 v[240:241], v[142:143], s[64:65] op_sel_hi:[1,0]
	v_lshlrev_b32_e32 v242, 16, v175
	v_and_b32_e32 v243, 0xffff0000, v175
	v_pk_fma_f32 v[238:239], v[240:241], v[242:243], v[238:239]
	v_pk_mul_f32 v[240:241], v[144:145], s[66:67] op_sel_hi:[1,0]
	v_lshlrev_b32_e32 v242, 16, v176
	v_and_b32_e32 v243, 0xffff0000, v176
	v_pk_fma_f32 v[232:233], v[240:241], v[242:243], v[232:233]
	v_pk_mul_f32 v[240:241], v[146:147], s[66:67] op_sel_hi:[1,0]
	v_lshlrev_b32_e32 v242, 16, v177
	v_and_b32_e32 v243, 0xffff0000, v177
	v_pk_fma_f32 v[234:235], v[240:241], v[242:243], v[234:235]
	v_pk_mul_f32 v[240:241], v[148:149], s[66:67] op_sel_hi:[1,0]
	v_lshlrev_b32_e32 v242, 16, v178
	v_and_b32_e32 v243, 0xffff0000, v178
	v_pk_fma_f32 v[236:237], v[240:241], v[242:243], v[236:237]
	v_pk_mul_f32 v[240:241], v[150:151], s[66:67] op_sel_hi:[1,0]
	v_lshlrev_b32_e32 v242, 16, v179
	v_and_b32_e32 v243, 0xffff0000, v179
	v_pk_fma_f32 v[238:239], v[240:241], v[242:243], v[238:239]
	v_pk_mul_f32 v[240:241], v[152:153], s[68:69] op_sel_hi:[1,0]
	v_lshlrev_b32_e32 v242, 16, v180
	v_and_b32_e32 v243, 0xffff0000, v180
	v_pk_fma_f32 v[232:233], v[240:241], v[242:243], v[232:233]
	v_pk_mul_f32 v[240:241], v[154:155], s[68:69] op_sel_hi:[1,0]
	v_lshlrev_b32_e32 v242, 16, v181
	v_and_b32_e32 v243, 0xffff0000, v181
	v_pk_fma_f32 v[234:235], v[240:241], v[242:243], v[234:235]
	v_pk_mul_f32 v[240:241], v[156:157], s[68:69] op_sel_hi:[1,0]
	v_lshlrev_b32_e32 v242, 16, v182
	v_and_b32_e32 v243, 0xffff0000, v182
	v_pk_fma_f32 v[236:237], v[240:241], v[242:243], v[236:237]
	v_pk_mul_f32 v[240:241], v[158:159], s[68:69] op_sel_hi:[1,0]
	v_lshlrev_b32_e32 v242, 16, v183
	v_and_b32_e32 v243, 0xffff0000, v183
	v_pk_fma_f32 v[238:239], v[240:241], v[242:243], v[238:239]
	v_cvt_pk_bf16_f32 v248, v232, v233
	v_cvt_pk_bf16_f32 v249, v234, v235
	v_cvt_pk_bf16_f32 v250, v236, v237
	v_cvt_pk_bf16_f32 v251, v238, v239
	s_lshl_b32 s58, s54, 11
	s_add_u32 s60, s52, s58
	s_addc_u32 s61, s53, 0
	global_store_dwordx4 v126, v[248:251], s[60:61]
	s_add_i32 s54, s41, 0x3400
	s_cmp_lt_u32 s54, 0x8000
	s_cselect_b32 s55, s70, s71
	s_and_b32 s56, s54, s55
	s_add_i32 s57, s55, 1
	s_add_i32 s58, s56, -2
	s_cmp_lt_u32 s58, s57
	s_cselect_b32 s62, 1.0, 0
	s_add_i32 s58, s56, -1
	s_cmp_lt_u32 s58, s57
	s_cselect_b32 s64, 1.0, 0
	s_mov_b32 s66, 1.0
	s_add_i32 s58, s56, 1
	s_cmp_lt_u32 s58, s57
	s_cselect_b32 s68, 1.0, 0
	v_pk_mul_f32 v[240:241], v[128:129], s[62:63] op_sel_hi:[1,0]
	v_lshlrev_b32_e32 v242, 16, v184
	v_and_b32_e32 v243, 0xffff0000, v184
	v_pk_fma_f32 v[232:233], v[240:241], v[242:243], v[160:161]
	v_pk_mul_f32 v[240:241], v[130:131], s[62:63] op_sel_hi:[1,0]
	v_lshlrev_b32_e32 v242, 16, v185
	v_and_b32_e32 v243, 0xffff0000, v185
	v_pk_fma_f32 v[234:235], v[240:241], v[242:243], v[162:163]
	v_pk_mul_f32 v[240:241], v[132:133], s[62:63] op_sel_hi:[1,0]
	v_lshlrev_b32_e32 v242, 16, v186
	v_and_b32_e32 v243, 0xffff0000, v186
	v_pk_fma_f32 v[236:237], v[240:241], v[242:243], v[164:165]
	v_pk_mul_f32 v[240:241], v[134:135], s[62:63] op_sel_hi:[1,0]
	v_lshlrev_b32_e32 v242, 16, v187
	v_and_b32_e32 v243, 0xffff0000, v187
	v_pk_fma_f32 v[238:239], v[240:241], v[242:243], v[166:167]
	v_pk_mul_f32 v[240:241], v[136:137], s[64:65] op_sel_hi:[1,0]
	v_lshlrev_b32_e32 v242, 16, v188
	v_and_b32_e32 v243, 0xffff0000, v188
	v_pk_fma_f32 v[232:233], v[240:241], v[242:243], v[232:233]
	v_pk_mul_f32 v[240:241], v[138:139], s[64:65] op_sel_hi:[1,0]
	v_lshlrev_b32_e32 v242, 16, v189
	v_and_b32_e32 v243, 0xffff0000, v189
	v_pk_fma_f32 v[234:235], v[240:241], v[242:243], v[234:235]
	v_pk_mul_f32 v[240:241], v[140:141], s[64:65] op_sel_hi:[1,0]
	v_lshlrev_b32_e32 v242, 16, v190
	v_and_b32_e32 v243, 0xffff0000, v190
	v_pk_fma_f32 v[236:237], v[240:241], v[242:243], v[236:237]
	v_pk_mul_f32 v[240:241], v[142:143], s[64:65] op_sel_hi:[1,0]
	v_lshlrev_b32_e32 v242, 16, v191
	v_and_b32_e32 v243, 0xffff0000, v191
	v_pk_fma_f32 v[238:239], v[240:241], v[242:243], v[238:239]
	v_pk_mul_f32 v[240:241], v[144:145], s[66:67] op_sel_hi:[1,0]
	v_lshlrev_b32_e32 v242, 16, v192
	v_and_b32_e32 v243, 0xffff0000, v192
	v_pk_fma_f32 v[232:233], v[240:241], v[242:243], v[232:233]
	v_pk_mul_f32 v[240:241], v[146:147], s[66:67] op_sel_hi:[1,0]
	v_lshlrev_b32_e32 v242, 16, v193
	v_and_b32_e32 v243, 0xffff0000, v193
	v_pk_fma_f32 v[234:235], v[240:241], v[242:243], v[234:235]
	v_pk_mul_f32 v[240:241], v[148:149], s[66:67] op_sel_hi:[1,0]
	v_lshlrev_b32_e32 v242, 16, v194
	v_and_b32_e32 v243, 0xffff0000, v194
	v_pk_fma_f32 v[236:237], v[240:241], v[242:243], v[236:237]
	v_pk_mul_f32 v[240:241], v[150:151], s[66:67] op_sel_hi:[1,0]
	v_lshlrev_b32_e32 v242, 16, v195
	v_and_b32_e32 v243, 0xffff0000, v195
	v_pk_fma_f32 v[238:239], v[240:241], v[242:243], v[238:239]
	v_pk_mul_f32 v[240:241], v[152:153], s[68:69] op_sel_hi:[1,0]
	v_lshlrev_b32_e32 v242, 16, v196
	v_and_b32_e32 v243, 0xffff0000, v196
	v_pk_fma_f32 v[232:233], v[240:241], v[242:243], v[232:233]
	v_pk_mul_f32 v[240:241], v[154:155], s[68:69] op_sel_hi:[1,0]
	v_lshlrev_b32_e32 v242, 16, v197
	v_and_b32_e32 v243, 0xffff0000, v197
	v_pk_fma_f32 v[234:235], v[240:241], v[242:243], v[234:235]
	v_pk_mul_f32 v[240:241], v[156:157], s[68:69] op_sel_hi:[1,0]
	v_lshlrev_b32_e32 v242, 16, v198
	v_and_b32_e32 v243, 0xffff0000, v198
	v_pk_fma_f32 v[236:237], v[240:241], v[242:243], v[236:237]
	v_pk_mul_f32 v[240:241], v[158:159], s[68:69] op_sel_hi:[1,0]
	v_lshlrev_b32_e32 v242, 16, v199
	v_and_b32_e32 v243, 0xffff0000, v199
	v_pk_fma_f32 v[238:239], v[240:241], v[242:243], v[238:239]
	v_cvt_pk_bf16_f32 v248, v232, v233
	v_cvt_pk_bf16_f32 v249, v234, v235
	v_cvt_pk_bf16_f32 v250, v236, v237
	v_cvt_pk_bf16_f32 v251, v238, v239
	s_lshl_b32 s58, s54, 11
	s_add_u32 s60, s52, s58
	s_addc_u32 s61, s53, 0
	global_store_dwordx4 v126, v[248:251], s[60:61]
	s_add_i32 s54, s41, 0x4800
	s_cmp_lt_u32 s54, 0x8000
	s_cselect_b32 s55, s70, s71
	s_and_b32 s56, s54, s55
	s_add_i32 s57, s55, 1
	s_add_i32 s58, s56, -2
	s_cmp_lt_u32 s58, s57
	s_cselect_b32 s58, -2, 0
	s_add_i32 s58, s54, s58
	s_mul_i32 s58, s58, 0x5a00
	s_add_u32 s60, s50, s58
	s_addc_u32 s61, s51, 0
	global_load_dwordx4 v[168:171], v126, s[60:61]
	s_add_i32 s58, s56, -1
	s_cmp_lt_u32 s58, s57
	s_cselect_b32 s58, -1, 0
	s_add_i32 s58, s54, s58
	s_mul_i32 s58, s58, 0x5a00
	s_add_u32 s60, s50, s58
	s_addc_u32 s61, s51, 0
	global_load_dwordx4 v[172:175], v126, s[60:61]
	s_mul_i32 s58, s54, 0x5a00
	s_add_u32 s60, s50, s58
	s_addc_u32 s61, s51, 0
	global_load_dwordx4 v[176:179], v126, s[60:61]
	s_add_i32 s58, s56, 1
	s_cmp_lt_u32 s58, s57
	s_cselect_b32 s58, 1, 0
	s_add_i32 s58, s54, s58
	s_mul_i32 s58, s58, 0x5a00
	s_add_u32 s60, s50, s58
	s_addc_u32 s61, s51, 0
	global_load_dwordx4 v[180:183], v126, s[60:61]
	s_add_i32 s54, s41, 0x4c00
	s_cmp_lt_u32 s54, 0x8000
	s_cselect_b32 s55, s70, s71
	s_and_b32 s56, s54, s55
	s_add_i32 s57, s55, 1
	s_add_i32 s58, s56, -2
	s_cmp_lt_u32 s58, s57
	s_cselect_b32 s58, -2, 0
	s_add_i32 s58, s54, s58
	s_mul_i32 s58, s58, 0x5a00
	s_add_u32 s60, s50, s58
	s_addc_u32 s61, s51, 0
	global_load_dwordx4 v[184:187], v126, s[60:61]
	s_add_i32 s58, s56, -1
	s_cmp_lt_u32 s58, s57
	s_cselect_b32 s58, -1, 0
	s_add_i32 s58, s54, s58
	s_mul_i32 s58, s58, 0x5a00
	s_add_u32 s60, s50, s58
	s_addc_u32 s61, s51, 0
	global_load_dwordx4 v[188:191], v126, s[60:61]
	s_mul_i32 s58, s54, 0x5a00
	s_add_u32 s60, s50, s58
	s_addc_u32 s61, s51, 0
	global_load_dwordx4 v[192:195], v126, s[60:61]
	s_add_i32 s58, s56, 1
	s_cmp_lt_u32 s58, s57
	s_cselect_b32 s58, 1, 0
	s_add_i32 s58, s54, s58
	s_mul_i32 s58, s58, 0x5a00
	s_add_u32 s60, s50, s58
	s_addc_u32 s61, s51, 0
	global_load_dwordx4 v[196:199], v126, s[60:61]
	s_waitcnt vmcnt(20)
	s_add_i32 s54, s41, 0x3800
	s_cmp_lt_u32 s54, 0x8000
	s_cselect_b32 s55, s70, s71
	s_and_b32 s56, s54, s55
	s_add_i32 s57, s55, 1
	s_add_i32 s58, s56, -2
	s_cmp_lt_u32 s58, s57
	s_cselect_b32 s62, 1.0, 0
	s_add_i32 s58, s56, -1
	s_cmp_lt_u32 s58, s57
	s_cselect_b32 s64, 1.0, 0
	s_mov_b32 s66, 1.0
	s_add_i32 s58, s56, 1
	s_cmp_lt_u32 s58, s57
	s_cselect_b32 s68, 1.0, 0
	v_pk_mul_f32 v[240:241], v[128:129], s[62:63] op_sel_hi:[1,0]
	v_lshlrev_b32_e32 v242, 16, v200
	v_and_b32_e32 v243, 0xffff0000, v200
	v_pk_fma_f32 v[232:233], v[240:241], v[242:243], v[160:161]
	v_pk_mul_f32 v[240:241], v[130:131], s[62:63] op_sel_hi:[1,0]
	v_lshlrev_b32_e32 v242, 16, v201
	v_and_b32_e32 v243, 0xffff0000, v201
	v_pk_fma_f32 v[234:235], v[240:241], v[242:243], v[162:163]
	v_pk_mul_f32 v[240:241], v[132:133], s[62:63] op_sel_hi:[1,0]
	v_lshlrev_b32_e32 v242, 16, v202
	v_and_b32_e32 v243, 0xffff0000, v202
	v_pk_fma_f32 v[236:237], v[240:241], v[242:243], v[164:165]
	v_pk_mul_f32 v[240:241], v[134:135], s[62:63] op_sel_hi:[1,0]
	v_lshlrev_b32_e32 v242, 16, v203
	v_and_b32_e32 v243, 0xffff0000, v203
	v_pk_fma_f32 v[238:239], v[240:241], v[242:243], v[166:167]
	v_pk_mul_f32 v[240:241], v[136:137], s[64:65] op_sel_hi:[1,0]
	v_lshlrev_b32_e32 v242, 16, v204
	v_and_b32_e32 v243, 0xffff0000, v204
	v_pk_fma_f32 v[232:233], v[240:241], v[242:243], v[232:233]
	v_pk_mul_f32 v[240:241], v[138:139], s[64:65] op_sel_hi:[1,0]
	v_lshlrev_b32_e32 v242, 16, v205
	v_and_b32_e32 v243, 0xffff0000, v205
	v_pk_fma_f32 v[234:235], v[240:241], v[242:243], v[234:235]
	v_pk_mul_f32 v[240:241], v[140:141], s[64:65] op_sel_hi:[1,0]
	v_lshlrev_b32_e32 v242, 16, v206
	v_and_b32_e32 v243, 0xffff0000, v206
	v_pk_fma_f32 v[236:237], v[240:241], v[242:243], v[236:237]
	v_pk_mul_f32 v[240:241], v[142:143], s[64:65] op_sel_hi:[1,0]
	v_lshlrev_b32_e32 v242, 16, v207
	v_and_b32_e32 v243, 0xffff0000, v207
	v_pk_fma_f32 v[238:239], v[240:241], v[242:243], v[238:239]
	v_pk_mul_f32 v[240:241], v[144:145], s[66:67] op_sel_hi:[1,0]
	v_lshlrev_b32_e32 v242, 16, v208
	v_and_b32_e32 v243, 0xffff0000, v208
	v_pk_fma_f32 v[232:233], v[240:241], v[242:243], v[232:233]
	v_pk_mul_f32 v[240:241], v[146:147], s[66:67] op_sel_hi:[1,0]
	v_lshlrev_b32_e32 v242, 16, v209
	v_and_b32_e32 v243, 0xffff0000, v209
	v_pk_fma_f32 v[234:235], v[240:241], v[242:243], v[234:235]
	v_pk_mul_f32 v[240:241], v[148:149], s[66:67] op_sel_hi:[1,0]
	v_lshlrev_b32_e32 v242, 16, v210
	v_and_b32_e32 v243, 0xffff0000, v210
	v_pk_fma_f32 v[236:237], v[240:241], v[242:243], v[236:237]
	v_pk_mul_f32 v[240:241], v[150:151], s[66:67] op_sel_hi:[1,0]
	v_lshlrev_b32_e32 v242, 16, v211
	v_and_b32_e32 v243, 0xffff0000, v211
	v_pk_fma_f32 v[238:239], v[240:241], v[242:243], v[238:239]
	v_pk_mul_f32 v[240:241], v[152:153], s[68:69] op_sel_hi:[1,0]
	v_lshlrev_b32_e32 v242, 16, v212
	v_and_b32_e32 v243, 0xffff0000, v212
	v_pk_fma_f32 v[232:233], v[240:241], v[242:243], v[232:233]
	v_pk_mul_f32 v[240:241], v[154:155], s[68:69] op_sel_hi:[1,0]
	v_lshlrev_b32_e32 v242, 16, v213
	v_and_b32_e32 v243, 0xffff0000, v213
	v_pk_fma_f32 v[234:235], v[240:241], v[242:243], v[234:235]
	v_pk_mul_f32 v[240:241], v[156:157], s[68:69] op_sel_hi:[1,0]
	v_lshlrev_b32_e32 v242, 16, v214
	v_and_b32_e32 v243, 0xffff0000, v214
	v_pk_fma_f32 v[236:237], v[240:241], v[242:243], v[236:237]
	v_pk_mul_f32 v[240:241], v[158:159], s[68:69] op_sel_hi:[1,0]
	v_lshlrev_b32_e32 v242, 16, v215
	v_and_b32_e32 v243, 0xffff0000, v215
	v_pk_fma_f32 v[238:239], v[240:241], v[242:243], v[238:239]
	v_cvt_pk_bf16_f32 v248, v232, v233
	v_cvt_pk_bf16_f32 v249, v234, v235
	v_cvt_pk_bf16_f32 v250, v236, v237
	v_cvt_pk_bf16_f32 v251, v238, v239
	s_lshl_b32 s58, s54, 11
	s_add_u32 s60, s52, s58
	s_addc_u32 s61, s53, 0
	global_store_dwordx4 v126, v[248:251], s[60:61]
	s_add_i32 s54, s41, 0x3c00
	s_cmp_lt_u32 s54, 0x8000
	s_cselect_b32 s55, s70, s71
	s_and_b32 s56, s54, s55
	s_add_i32 s57, s55, 1
	s_add_i32 s58, s56, -2
	s_cmp_lt_u32 s58, s57
	s_cselect_b32 s62, 1.0, 0
	s_add_i32 s58, s56, -1
	s_cmp_lt_u32 s58, s57
	s_cselect_b32 s64, 1.0, 0
	s_mov_b32 s66, 1.0
	s_add_i32 s58, s56, 1
	s_cmp_lt_u32 s58, s57
	s_cselect_b32 s68, 1.0, 0
	v_pk_mul_f32 v[240:241], v[128:129], s[62:63] op_sel_hi:[1,0]
	v_lshlrev_b32_e32 v242, 16, v216
	v_and_b32_e32 v243, 0xffff0000, v216
	v_pk_fma_f32 v[232:233], v[240:241], v[242:243], v[160:161]
	v_pk_mul_f32 v[240:241], v[130:131], s[62:63] op_sel_hi:[1,0]
	v_lshlrev_b32_e32 v242, 16, v217
	v_and_b32_e32 v243, 0xffff0000, v217
	v_pk_fma_f32 v[234:235], v[240:241], v[242:243], v[162:163]
	v_pk_mul_f32 v[240:241], v[132:133], s[62:63] op_sel_hi:[1,0]
	v_lshlrev_b32_e32 v242, 16, v218
	v_and_b32_e32 v243, 0xffff0000, v218
	v_pk_fma_f32 v[236:237], v[240:241], v[242:243], v[164:165]
	v_pk_mul_f32 v[240:241], v[134:135], s[62:63] op_sel_hi:[1,0]
	v_lshlrev_b32_e32 v242, 16, v219
	v_and_b32_e32 v243, 0xffff0000, v219
	v_pk_fma_f32 v[238:239], v[240:241], v[242:243], v[166:167]
	v_pk_mul_f32 v[240:241], v[136:137], s[64:65] op_sel_hi:[1,0]
	v_lshlrev_b32_e32 v242, 16, v220
	v_and_b32_e32 v243, 0xffff0000, v220
	v_pk_fma_f32 v[232:233], v[240:241], v[242:243], v[232:233]
	v_pk_mul_f32 v[240:241], v[138:139], s[64:65] op_sel_hi:[1,0]
	v_lshlrev_b32_e32 v242, 16, v221
	v_and_b32_e32 v243, 0xffff0000, v221
	v_pk_fma_f32 v[234:235], v[240:241], v[242:243], v[234:235]
	v_pk_mul_f32 v[240:241], v[140:141], s[64:65] op_sel_hi:[1,0]
	v_lshlrev_b32_e32 v242, 16, v222
	v_and_b32_e32 v243, 0xffff0000, v222
	v_pk_fma_f32 v[236:237], v[240:241], v[242:243], v[236:237]
	v_pk_mul_f32 v[240:241], v[142:143], s[64:65] op_sel_hi:[1,0]
	v_lshlrev_b32_e32 v242, 16, v223
	v_and_b32_e32 v243, 0xffff0000, v223
	v_pk_fma_f32 v[238:239], v[240:241], v[242:243], v[238:239]
	v_pk_mul_f32 v[240:241], v[144:145], s[66:67] op_sel_hi:[1,0]
	v_lshlrev_b32_e32 v242, 16, v224
	v_and_b32_e32 v243, 0xffff0000, v224
	v_pk_fma_f32 v[232:233], v[240:241], v[242:243], v[232:233]
	v_pk_mul_f32 v[240:241], v[146:147], s[66:67] op_sel_hi:[1,0]
	v_lshlrev_b32_e32 v242, 16, v225
	v_and_b32_e32 v243, 0xffff0000, v225
	v_pk_fma_f32 v[234:235], v[240:241], v[242:243], v[234:235]
	v_pk_mul_f32 v[240:241], v[148:149], s[66:67] op_sel_hi:[1,0]
	v_lshlrev_b32_e32 v242, 16, v226
	v_and_b32_e32 v243, 0xffff0000, v226
	v_pk_fma_f32 v[236:237], v[240:241], v[242:243], v[236:237]
	v_pk_mul_f32 v[240:241], v[150:151], s[66:67] op_sel_hi:[1,0]
	v_lshlrev_b32_e32 v242, 16, v227
	v_and_b32_e32 v243, 0xffff0000, v227
	v_pk_fma_f32 v[238:239], v[240:241], v[242:243], v[238:239]
	v_pk_mul_f32 v[240:241], v[152:153], s[68:69] op_sel_hi:[1,0]
	v_lshlrev_b32_e32 v242, 16, v228
	v_and_b32_e32 v243, 0xffff0000, v228
	v_pk_fma_f32 v[232:233], v[240:241], v[242:243], v[232:233]
	v_pk_mul_f32 v[240:241], v[154:155], s[68:69] op_sel_hi:[1,0]
	v_lshlrev_b32_e32 v242, 16, v229
	v_and_b32_e32 v243, 0xffff0000, v229
	v_pk_fma_f32 v[234:235], v[240:241], v[242:243], v[234:235]
	v_pk_mul_f32 v[240:241], v[156:157], s[68:69] op_sel_hi:[1,0]
	v_lshlrev_b32_e32 v242, 16, v230
	v_and_b32_e32 v243, 0xffff0000, v230
	v_pk_fma_f32 v[236:237], v[240:241], v[242:243], v[236:237]
	v_pk_mul_f32 v[240:241], v[158:159], s[68:69] op_sel_hi:[1,0]
	v_lshlrev_b32_e32 v242, 16, v231
	v_and_b32_e32 v243, 0xffff0000, v231
	v_pk_fma_f32 v[238:239], v[240:241], v[242:243], v[238:239]
	v_cvt_pk_bf16_f32 v248, v232, v233
	v_cvt_pk_bf16_f32 v249, v234, v235
	v_cvt_pk_bf16_f32 v250, v236, v237
	v_cvt_pk_bf16_f32 v251, v238, v239
	s_lshl_b32 s58, s54, 11
	s_add_u32 s60, s52, s58
	s_addc_u32 s61, s53, 0
	global_store_dwordx4 v126, v[248:251], s[60:61]
	s_add_i32 s54, s41, 0x5000
	s_cmp_lt_u32 s54, 0x8000
	s_cselect_b32 s55, s70, s71
	s_and_b32 s56, s54, s55
	s_add_i32 s57, s55, 1
	s_add_i32 s58, s56, -2
	s_cmp_lt_u32 s58, s57
	s_cselect_b32 s58, -2, 0
	s_add_i32 s58, s54, s58
	s_mul_i32 s58, s58, 0x5a00
	s_add_u32 s60, s50, s58
	s_addc_u32 s61, s51, 0
	global_load_dwordx4 v[200:203], v126, s[60:61]
	s_add_i32 s58, s56, -1
	s_cmp_lt_u32 s58, s57
	s_cselect_b32 s58, -1, 0
	s_add_i32 s58, s54, s58
	s_mul_i32 s58, s58, 0x5a00
	s_add_u32 s60, s50, s58
	s_addc_u32 s61, s51, 0
	global_load_dwordx4 v[204:207], v126, s[60:61]
	s_mul_i32 s58, s54, 0x5a00
	s_add_u32 s60, s50, s58
	s_addc_u32 s61, s51, 0
	global_load_dwordx4 v[208:211], v126, s[60:61]
	s_add_i32 s58, s56, 1
	s_cmp_lt_u32 s58, s57
	s_cselect_b32 s58, 1, 0
	s_add_i32 s58, s54, s58
	s_mul_i32 s58, s58, 0x5a00
	s_add_u32 s60, s50, s58
	s_addc_u32 s61, s51, 0
	global_load_dwordx4 v[212:215], v126, s[60:61]
	s_add_i32 s54, s41, 0x5400
	s_cmp_lt_u32 s54, 0x8000
	s_cselect_b32 s55, s70, s71
	s_and_b32 s56, s54, s55
	s_add_i32 s57, s55, 1
	s_add_i32 s58, s56, -2
	s_cmp_lt_u32 s58, s57
	s_cselect_b32 s58, -2, 0
	s_add_i32 s58, s54, s58
	s_mul_i32 s58, s58, 0x5a00
	s_add_u32 s60, s50, s58
	s_addc_u32 s61, s51, 0
	global_load_dwordx4 v[216:219], v126, s[60:61]
	s_add_i32 s58, s56, -1
	s_cmp_lt_u32 s58, s57
	s_cselect_b32 s58, -1, 0
	s_add_i32 s58, s54, s58
	s_mul_i32 s58, s58, 0x5a00
	s_add_u32 s60, s50, s58
	s_addc_u32 s61, s51, 0
	global_load_dwordx4 v[220:223], v126, s[60:61]
	s_mul_i32 s58, s54, 0x5a00
	s_add_u32 s60, s50, s58
	s_addc_u32 s61, s51, 0
	global_load_dwordx4 v[224:227], v126, s[60:61]
	s_add_i32 s58, s56, 1
	s_cmp_lt_u32 s58, s57
	s_cselect_b32 s58, 1, 0
	s_add_i32 s58, s54, s58
	s_mul_i32 s58, s58, 0x5a00
	s_add_u32 s60, s50, s58
	s_addc_u32 s61, s51, 0
	global_load_dwordx4 v[228:231], v126, s[60:61]
	s_waitcnt vmcnt(20)
	s_add_i32 s54, s41, 0x4000
	s_cmp_lt_u32 s54, 0x8000
	s_cselect_b32 s55, s70, s71
	s_and_b32 s56, s54, s55
	s_add_i32 s57, s55, 1
	s_add_i32 s58, s56, -2
	s_cmp_lt_u32 s58, s57
	s_cselect_b32 s62, 1.0, 0
	s_add_i32 s58, s56, -1
	s_cmp_lt_u32 s58, s57
	s_cselect_b32 s64, 1.0, 0
	s_mov_b32 s66, 1.0
	s_add_i32 s58, s56, 1
	s_cmp_lt_u32 s58, s57
	s_cselect_b32 s68, 1.0, 0
	v_pk_mul_f32 v[240:241], v[128:129], s[62:63] op_sel_hi:[1,0]
	v_lshlrev_b32_e32 v242, 16, v40
	v_and_b32_e32 v243, 0xffff0000, v40
	v_pk_fma_f32 v[232:233], v[240:241], v[242:243], v[160:161]
	v_pk_mul_f32 v[240:241], v[130:131], s[62:63] op_sel_hi:[1,0]
	v_lshlrev_b32_e32 v242, 16, v41
	v_and_b32_e32 v243, 0xffff0000, v41
	v_pk_fma_f32 v[234:235], v[240:241], v[242:243], v[162:163]
	v_pk_mul_f32 v[240:241], v[132:133], s[62:63] op_sel_hi:[1,0]
	v_lshlrev_b32_e32 v242, 16, v42
	v_and_b32_e32 v243, 0xffff0000, v42
	v_pk_fma_f32 v[236:237], v[240:241], v[242:243], v[164:165]
	v_pk_mul_f32 v[240:241], v[134:135], s[62:63] op_sel_hi:[1,0]
	v_lshlrev_b32_e32 v242, 16, v43
	v_and_b32_e32 v243, 0xffff0000, v43
	v_pk_fma_f32 v[238:239], v[240:241], v[242:243], v[166:167]
	v_pk_mul_f32 v[240:241], v[136:137], s[64:65] op_sel_hi:[1,0]
	v_lshlrev_b32_e32 v242, 16, v44
	v_and_b32_e32 v243, 0xffff0000, v44
	v_pk_fma_f32 v[232:233], v[240:241], v[242:243], v[232:233]
	v_pk_mul_f32 v[240:241], v[138:139], s[64:65] op_sel_hi:[1,0]
	v_lshlrev_b32_e32 v242, 16, v45
	v_and_b32_e32 v243, 0xffff0000, v45
	v_pk_fma_f32 v[234:235], v[240:241], v[242:243], v[234:235]
	v_pk_mul_f32 v[240:241], v[140:141], s[64:65] op_sel_hi:[1,0]
	v_lshlrev_b32_e32 v242, 16, v46
	v_and_b32_e32 v243, 0xffff0000, v46
	v_pk_fma_f32 v[236:237], v[240:241], v[242:243], v[236:237]
	v_pk_mul_f32 v[240:241], v[142:143], s[64:65] op_sel_hi:[1,0]
	v_lshlrev_b32_e32 v242, 16, v47
	v_and_b32_e32 v243, 0xffff0000, v47
	v_pk_fma_f32 v[238:239], v[240:241], v[242:243], v[238:239]
	v_pk_mul_f32 v[240:241], v[144:145], s[66:67] op_sel_hi:[1,0]
	v_lshlrev_b32_e32 v242, 16, v48
	v_and_b32_e32 v243, 0xffff0000, v48
	v_pk_fma_f32 v[232:233], v[240:241], v[242:243], v[232:233]
	v_pk_mul_f32 v[240:241], v[146:147], s[66:67] op_sel_hi:[1,0]
	v_lshlrev_b32_e32 v242, 16, v49
	v_and_b32_e32 v243, 0xffff0000, v49
	v_pk_fma_f32 v[234:235], v[240:241], v[242:243], v[234:235]
	v_pk_mul_f32 v[240:241], v[148:149], s[66:67] op_sel_hi:[1,0]
	v_lshlrev_b32_e32 v242, 16, v50
	v_and_b32_e32 v243, 0xffff0000, v50
	v_pk_fma_f32 v[236:237], v[240:241], v[242:243], v[236:237]
	v_pk_mul_f32 v[240:241], v[150:151], s[66:67] op_sel_hi:[1,0]
	v_lshlrev_b32_e32 v242, 16, v51
	v_and_b32_e32 v243, 0xffff0000, v51
	v_pk_fma_f32 v[238:239], v[240:241], v[242:243], v[238:239]
	v_pk_mul_f32 v[240:241], v[152:153], s[68:69] op_sel_hi:[1,0]
	v_lshlrev_b32_e32 v242, 16, v52
	v_and_b32_e32 v243, 0xffff0000, v52
	v_pk_fma_f32 v[232:233], v[240:241], v[242:243], v[232:233]
	v_pk_mul_f32 v[240:241], v[154:155], s[68:69] op_sel_hi:[1,0]
	v_lshlrev_b32_e32 v242, 16, v53
	v_and_b32_e32 v243, 0xffff0000, v53
	v_pk_fma_f32 v[234:235], v[240:241], v[242:243], v[234:235]
	v_pk_mul_f32 v[240:241], v[156:157], s[68:69] op_sel_hi:[1,0]
	v_lshlrev_b32_e32 v242, 16, v54
	v_and_b32_e32 v243, 0xffff0000, v54
	v_pk_fma_f32 v[236:237], v[240:241], v[242:243], v[236:237]
	v_pk_mul_f32 v[240:241], v[158:159], s[68:69] op_sel_hi:[1,0]
	v_lshlrev_b32_e32 v242, 16, v55
	v_and_b32_e32 v243, 0xffff0000, v55
	v_pk_fma_f32 v[238:239], v[240:241], v[242:243], v[238:239]
	v_cvt_pk_bf16_f32 v248, v232, v233
	v_cvt_pk_bf16_f32 v249, v234, v235
	v_cvt_pk_bf16_f32 v250, v236, v237
	v_cvt_pk_bf16_f32 v251, v238, v239
	s_lshl_b32 s58, s54, 11
	s_add_u32 s60, s52, s58
	s_addc_u32 s61, s53, 0
	global_store_dwordx4 v126, v[248:251], s[60:61]
	s_add_i32 s54, s41, 0x4400
	s_cmp_lt_u32 s54, 0x8000
	s_cselect_b32 s55, s70, s71
	s_and_b32 s56, s54, s55
	s_add_i32 s57, s55, 1
	s_add_i32 s58, s56, -2
	s_cmp_lt_u32 s58, s57
	s_cselect_b32 s62, 1.0, 0
	s_add_i32 s58, s56, -1
	s_cmp_lt_u32 s58, s57
	s_cselect_b32 s64, 1.0, 0
	s_mov_b32 s66, 1.0
	s_add_i32 s58, s56, 1
	s_cmp_lt_u32 s58, s57
	s_cselect_b32 s68, 1.0, 0
	v_pk_mul_f32 v[240:241], v[128:129], s[62:63] op_sel_hi:[1,0]
	v_lshlrev_b32_e32 v242, 16, v56
	v_and_b32_e32 v243, 0xffff0000, v56
	v_pk_fma_f32 v[232:233], v[240:241], v[242:243], v[160:161]
	v_pk_mul_f32 v[240:241], v[130:131], s[62:63] op_sel_hi:[1,0]
	v_lshlrev_b32_e32 v242, 16, v57
	v_and_b32_e32 v243, 0xffff0000, v57
	v_pk_fma_f32 v[234:235], v[240:241], v[242:243], v[162:163]
	v_pk_mul_f32 v[240:241], v[132:133], s[62:63] op_sel_hi:[1,0]
	v_lshlrev_b32_e32 v242, 16, v58
	v_and_b32_e32 v243, 0xffff0000, v58
	v_pk_fma_f32 v[236:237], v[240:241], v[242:243], v[164:165]
	v_pk_mul_f32 v[240:241], v[134:135], s[62:63] op_sel_hi:[1,0]
	v_lshlrev_b32_e32 v242, 16, v59
	v_and_b32_e32 v243, 0xffff0000, v59
	v_pk_fma_f32 v[238:239], v[240:241], v[242:243], v[166:167]
	v_pk_mul_f32 v[240:241], v[136:137], s[64:65] op_sel_hi:[1,0]
	v_lshlrev_b32_e32 v242, 16, v60
	v_and_b32_e32 v243, 0xffff0000, v60
	v_pk_fma_f32 v[232:233], v[240:241], v[242:243], v[232:233]
	v_pk_mul_f32 v[240:241], v[138:139], s[64:65] op_sel_hi:[1,0]
	v_lshlrev_b32_e32 v242, 16, v61
	v_and_b32_e32 v243, 0xffff0000, v61
	v_pk_fma_f32 v[234:235], v[240:241], v[242:243], v[234:235]
	v_pk_mul_f32 v[240:241], v[140:141], s[64:65] op_sel_hi:[1,0]
	v_lshlrev_b32_e32 v242, 16, v62
	v_and_b32_e32 v243, 0xffff0000, v62
	v_pk_fma_f32 v[236:237], v[240:241], v[242:243], v[236:237]
	v_pk_mul_f32 v[240:241], v[142:143], s[64:65] op_sel_hi:[1,0]
	v_lshlrev_b32_e32 v242, 16, v63
	v_and_b32_e32 v243, 0xffff0000, v63
	v_pk_fma_f32 v[238:239], v[240:241], v[242:243], v[238:239]
	v_pk_mul_f32 v[240:241], v[144:145], s[66:67] op_sel_hi:[1,0]
	v_lshlrev_b32_e32 v242, 16, v64
	v_and_b32_e32 v243, 0xffff0000, v64
	v_pk_fma_f32 v[232:233], v[240:241], v[242:243], v[232:233]
	v_pk_mul_f32 v[240:241], v[146:147], s[66:67] op_sel_hi:[1,0]
	v_lshlrev_b32_e32 v242, 16, v65
	v_and_b32_e32 v243, 0xffff0000, v65
	v_pk_fma_f32 v[234:235], v[240:241], v[242:243], v[234:235]
	v_pk_mul_f32 v[240:241], v[148:149], s[66:67] op_sel_hi:[1,0]
	v_lshlrev_b32_e32 v242, 16, v66
	v_and_b32_e32 v243, 0xffff0000, v66
	v_pk_fma_f32 v[236:237], v[240:241], v[242:243], v[236:237]
	v_pk_mul_f32 v[240:241], v[150:151], s[66:67] op_sel_hi:[1,0]
	v_lshlrev_b32_e32 v242, 16, v67
	v_and_b32_e32 v243, 0xffff0000, v67
	v_pk_fma_f32 v[238:239], v[240:241], v[242:243], v[238:239]
	v_pk_mul_f32 v[240:241], v[152:153], s[68:69] op_sel_hi:[1,0]
	v_lshlrev_b32_e32 v242, 16, v68
	v_and_b32_e32 v243, 0xffff0000, v68
	v_pk_fma_f32 v[232:233], v[240:241], v[242:243], v[232:233]
	v_pk_mul_f32 v[240:241], v[154:155], s[68:69] op_sel_hi:[1,0]
	v_lshlrev_b32_e32 v242, 16, v69
	v_and_b32_e32 v243, 0xffff0000, v69
	v_pk_fma_f32 v[234:235], v[240:241], v[242:243], v[234:235]
	v_pk_mul_f32 v[240:241], v[156:157], s[68:69] op_sel_hi:[1,0]
	v_lshlrev_b32_e32 v242, 16, v70
	v_and_b32_e32 v243, 0xffff0000, v70
	v_pk_fma_f32 v[236:237], v[240:241], v[242:243], v[236:237]
	v_pk_mul_f32 v[240:241], v[158:159], s[68:69] op_sel_hi:[1,0]
	v_lshlrev_b32_e32 v242, 16, v71
	v_and_b32_e32 v243, 0xffff0000, v71
	v_pk_fma_f32 v[238:239], v[240:241], v[242:243], v[238:239]
	v_cvt_pk_bf16_f32 v248, v232, v233
	v_cvt_pk_bf16_f32 v249, v234, v235
	v_cvt_pk_bf16_f32 v250, v236, v237
	v_cvt_pk_bf16_f32 v251, v238, v239
	s_lshl_b32 s58, s54, 11
	s_add_u32 s60, s52, s58
	s_addc_u32 s61, s53, 0
	global_store_dwordx4 v126, v[248:251], s[60:61]
	s_add_i32 s54, s41, 0x5800
	s_cmp_lt_u32 s54, 0x8000
	s_cselect_b32 s55, s70, s71
	s_and_b32 s56, s54, s55
	s_add_i32 s57, s55, 1
	s_add_i32 s58, s56, -2
	s_cmp_lt_u32 s58, s57
	s_cselect_b32 s58, -2, 0
	s_add_i32 s58, s54, s58
	s_mul_i32 s58, s58, 0x5a00
	s_add_u32 s60, s50, s58
	s_addc_u32 s61, s51, 0
	global_load_dwordx4 v[40:43], v126, s[60:61]
	s_add_i32 s58, s56, -1
	s_cmp_lt_u32 s58, s57
	s_cselect_b32 s58, -1, 0
	s_add_i32 s58, s54, s58
	s_mul_i32 s58, s58, 0x5a00
	s_add_u32 s60, s50, s58
	s_addc_u32 s61, s51, 0
	global_load_dwordx4 v[44:47], v126, s[60:61]
	s_mul_i32 s58, s54, 0x5a00
	s_add_u32 s60, s50, s58
	s_addc_u32 s61, s51, 0
	global_load_dwordx4 v[48:51], v126, s[60:61]
	s_add_i32 s58, s56, 1
	s_cmp_lt_u32 s58, s57
	s_cselect_b32 s58, 1, 0
	s_add_i32 s58, s54, s58
	s_mul_i32 s58, s58, 0x5a00
	s_add_u32 s60, s50, s58
	s_addc_u32 s61, s51, 0
	global_load_dwordx4 v[52:55], v126, s[60:61]
	s_add_i32 s54, s41, 0x5c00
	s_cmp_lt_u32 s54, 0x8000
	s_cselect_b32 s55, s70, s71
	s_and_b32 s56, s54, s55
	s_add_i32 s57, s55, 1
	s_add_i32 s58, s56, -2
	s_cmp_lt_u32 s58, s57
	s_cselect_b32 s58, -2, 0
	s_add_i32 s58, s54, s58
	s_mul_i32 s58, s58, 0x5a00
	s_add_u32 s60, s50, s58
	s_addc_u32 s61, s51, 0
	global_load_dwordx4 v[56:59], v126, s[60:61]
	s_add_i32 s58, s56, -1
	s_cmp_lt_u32 s58, s57
	s_cselect_b32 s58, -1, 0
	s_add_i32 s58, s54, s58
	s_mul_i32 s58, s58, 0x5a00
	s_add_u32 s60, s50, s58
	s_addc_u32 s61, s51, 0
	global_load_dwordx4 v[60:63], v126, s[60:61]
	s_mul_i32 s58, s54, 0x5a00
	s_add_u32 s60, s50, s58
	s_addc_u32 s61, s51, 0
	global_load_dwordx4 v[64:67], v126, s[60:61]
	s_add_i32 s58, s56, 1
	s_cmp_lt_u32 s58, s57
	s_cselect_b32 s58, 1, 0
	s_add_i32 s58, s54, s58
	s_mul_i32 s58, s58, 0x5a00
	s_add_u32 s60, s50, s58
	s_addc_u32 s61, s51, 0
	global_load_dwordx4 v[68:71], v126, s[60:61]
	s_waitcnt vmcnt(20)
	s_add_i32 s54, s41, 0x4800
	s_cmp_lt_u32 s54, 0x8000
	s_cselect_b32 s55, s70, s71
	s_and_b32 s56, s54, s55
	s_add_i32 s57, s55, 1
	s_add_i32 s58, s56, -2
	s_cmp_lt_u32 s58, s57
	s_cselect_b32 s62, 1.0, 0
	s_add_i32 s58, s56, -1
	s_cmp_lt_u32 s58, s57
	s_cselect_b32 s64, 1.0, 0
	s_mov_b32 s66, 1.0
	s_add_i32 s58, s56, 1
	s_cmp_lt_u32 s58, s57
	s_cselect_b32 s68, 1.0, 0
	v_pk_mul_f32 v[240:241], v[128:129], s[62:63] op_sel_hi:[1,0]
	v_lshlrev_b32_e32 v242, 16, v168
	v_and_b32_e32 v243, 0xffff0000, v168
	v_pk_fma_f32 v[232:233], v[240:241], v[242:243], v[160:161]
	v_pk_mul_f32 v[240:241], v[130:131], s[62:63] op_sel_hi:[1,0]
	v_lshlrev_b32_e32 v242, 16, v169
	v_and_b32_e32 v243, 0xffff0000, v169
	v_pk_fma_f32 v[234:235], v[240:241], v[242:243], v[162:163]
	v_pk_mul_f32 v[240:241], v[132:133], s[62:63] op_sel_hi:[1,0]
	v_lshlrev_b32_e32 v242, 16, v170
	v_and_b32_e32 v243, 0xffff0000, v170
	v_pk_fma_f32 v[236:237], v[240:241], v[242:243], v[164:165]
	v_pk_mul_f32 v[240:241], v[134:135], s[62:63] op_sel_hi:[1,0]
	v_lshlrev_b32_e32 v242, 16, v171
	v_and_b32_e32 v243, 0xffff0000, v171
	v_pk_fma_f32 v[238:239], v[240:241], v[242:243], v[166:167]
	v_pk_mul_f32 v[240:241], v[136:137], s[64:65] op_sel_hi:[1,0]
	v_lshlrev_b32_e32 v242, 16, v172
	v_and_b32_e32 v243, 0xffff0000, v172
	v_pk_fma_f32 v[232:233], v[240:241], v[242:243], v[232:233]
	v_pk_mul_f32 v[240:241], v[138:139], s[64:65] op_sel_hi:[1,0]
	v_lshlrev_b32_e32 v242, 16, v173
	v_and_b32_e32 v243, 0xffff0000, v173
	v_pk_fma_f32 v[234:235], v[240:241], v[242:243], v[234:235]
	v_pk_mul_f32 v[240:241], v[140:141], s[64:65] op_sel_hi:[1,0]
	v_lshlrev_b32_e32 v242, 16, v174
	v_and_b32_e32 v243, 0xffff0000, v174
	v_pk_fma_f32 v[236:237], v[240:241], v[242:243], v[236:237]
	v_pk_mul_f32 v[240:241], v[142:143], s[64:65] op_sel_hi:[1,0]
	v_lshlrev_b32_e32 v242, 16, v175
	v_and_b32_e32 v243, 0xffff0000, v175
	v_pk_fma_f32 v[238:239], v[240:241], v[242:243], v[238:239]
	v_pk_mul_f32 v[240:241], v[144:145], s[66:67] op_sel_hi:[1,0]
	v_lshlrev_b32_e32 v242, 16, v176
	v_and_b32_e32 v243, 0xffff0000, v176
	v_pk_fma_f32 v[232:233], v[240:241], v[242:243], v[232:233]
	v_pk_mul_f32 v[240:241], v[146:147], s[66:67] op_sel_hi:[1,0]
	v_lshlrev_b32_e32 v242, 16, v177
	v_and_b32_e32 v243, 0xffff0000, v177
	v_pk_fma_f32 v[234:235], v[240:241], v[242:243], v[234:235]
	v_pk_mul_f32 v[240:241], v[148:149], s[66:67] op_sel_hi:[1,0]
	v_lshlrev_b32_e32 v242, 16, v178
	v_and_b32_e32 v243, 0xffff0000, v178
	v_pk_fma_f32 v[236:237], v[240:241], v[242:243], v[236:237]
	v_pk_mul_f32 v[240:241], v[150:151], s[66:67] op_sel_hi:[1,0]
	v_lshlrev_b32_e32 v242, 16, v179
	v_and_b32_e32 v243, 0xffff0000, v179
	v_pk_fma_f32 v[238:239], v[240:241], v[242:243], v[238:239]
	v_pk_mul_f32 v[240:241], v[152:153], s[68:69] op_sel_hi:[1,0]
	v_lshlrev_b32_e32 v242, 16, v180
	v_and_b32_e32 v243, 0xffff0000, v180
	v_pk_fma_f32 v[232:233], v[240:241], v[242:243], v[232:233]
	v_pk_mul_f32 v[240:241], v[154:155], s[68:69] op_sel_hi:[1,0]
	v_lshlrev_b32_e32 v242, 16, v181
	v_and_b32_e32 v243, 0xffff0000, v181
	v_pk_fma_f32 v[234:235], v[240:241], v[242:243], v[234:235]
	v_pk_mul_f32 v[240:241], v[156:157], s[68:69] op_sel_hi:[1,0]
	v_lshlrev_b32_e32 v242, 16, v182
	v_and_b32_e32 v243, 0xffff0000, v182
	v_pk_fma_f32 v[236:237], v[240:241], v[242:243], v[236:237]
	v_pk_mul_f32 v[240:241], v[158:159], s[68:69] op_sel_hi:[1,0]
	v_lshlrev_b32_e32 v242, 16, v183
	v_and_b32_e32 v243, 0xffff0000, v183
	v_pk_fma_f32 v[238:239], v[240:241], v[242:243], v[238:239]
	v_cvt_pk_bf16_f32 v248, v232, v233
	v_cvt_pk_bf16_f32 v249, v234, v235
	v_cvt_pk_bf16_f32 v250, v236, v237
	v_cvt_pk_bf16_f32 v251, v238, v239
	s_lshl_b32 s58, s54, 11
	s_add_u32 s60, s52, s58
	s_addc_u32 s61, s53, 0
	global_store_dwordx4 v126, v[248:251], s[60:61]
	s_add_i32 s54, s41, 0x4c00
	s_cmp_lt_u32 s54, 0x8000
	s_cselect_b32 s55, s70, s71
	s_and_b32 s56, s54, s55
	s_add_i32 s57, s55, 1
	s_add_i32 s58, s56, -2
	s_cmp_lt_u32 s58, s57
	s_cselect_b32 s62, 1.0, 0
	s_add_i32 s58, s56, -1
	s_cmp_lt_u32 s58, s57
	s_cselect_b32 s64, 1.0, 0
	s_mov_b32 s66, 1.0
	s_add_i32 s58, s56, 1
	s_cmp_lt_u32 s58, s57
	s_cselect_b32 s68, 1.0, 0
	v_pk_mul_f32 v[240:241], v[128:129], s[62:63] op_sel_hi:[1,0]
	v_lshlrev_b32_e32 v242, 16, v184
	v_and_b32_e32 v243, 0xffff0000, v184
	v_pk_fma_f32 v[232:233], v[240:241], v[242:243], v[160:161]
	v_pk_mul_f32 v[240:241], v[130:131], s[62:63] op_sel_hi:[1,0]
	v_lshlrev_b32_e32 v242, 16, v185
	v_and_b32_e32 v243, 0xffff0000, v185
	v_pk_fma_f32 v[234:235], v[240:241], v[242:243], v[162:163]
	v_pk_mul_f32 v[240:241], v[132:133], s[62:63] op_sel_hi:[1,0]
	v_lshlrev_b32_e32 v242, 16, v186
	v_and_b32_e32 v243, 0xffff0000, v186
	v_pk_fma_f32 v[236:237], v[240:241], v[242:243], v[164:165]
	v_pk_mul_f32 v[240:241], v[134:135], s[62:63] op_sel_hi:[1,0]
	v_lshlrev_b32_e32 v242, 16, v187
	v_and_b32_e32 v243, 0xffff0000, v187
	v_pk_fma_f32 v[238:239], v[240:241], v[242:243], v[166:167]
	v_pk_mul_f32 v[240:241], v[136:137], s[64:65] op_sel_hi:[1,0]
	v_lshlrev_b32_e32 v242, 16, v188
	v_and_b32_e32 v243, 0xffff0000, v188
	v_pk_fma_f32 v[232:233], v[240:241], v[242:243], v[232:233]
	v_pk_mul_f32 v[240:241], v[138:139], s[64:65] op_sel_hi:[1,0]
	v_lshlrev_b32_e32 v242, 16, v189
	v_and_b32_e32 v243, 0xffff0000, v189
	v_pk_fma_f32 v[234:235], v[240:241], v[242:243], v[234:235]
	v_pk_mul_f32 v[240:241], v[140:141], s[64:65] op_sel_hi:[1,0]
	v_lshlrev_b32_e32 v242, 16, v190
	v_and_b32_e32 v243, 0xffff0000, v190
	v_pk_fma_f32 v[236:237], v[240:241], v[242:243], v[236:237]
	v_pk_mul_f32 v[240:241], v[142:143], s[64:65] op_sel_hi:[1,0]
	v_lshlrev_b32_e32 v242, 16, v191
	v_and_b32_e32 v243, 0xffff0000, v191
	v_pk_fma_f32 v[238:239], v[240:241], v[242:243], v[238:239]
	v_pk_mul_f32 v[240:241], v[144:145], s[66:67] op_sel_hi:[1,0]
	v_lshlrev_b32_e32 v242, 16, v192
	v_and_b32_e32 v243, 0xffff0000, v192
	v_pk_fma_f32 v[232:233], v[240:241], v[242:243], v[232:233]
	v_pk_mul_f32 v[240:241], v[146:147], s[66:67] op_sel_hi:[1,0]
	v_lshlrev_b32_e32 v242, 16, v193
	v_and_b32_e32 v243, 0xffff0000, v193
	v_pk_fma_f32 v[234:235], v[240:241], v[242:243], v[234:235]
	v_pk_mul_f32 v[240:241], v[148:149], s[66:67] op_sel_hi:[1,0]
	v_lshlrev_b32_e32 v242, 16, v194
	v_and_b32_e32 v243, 0xffff0000, v194
	v_pk_fma_f32 v[236:237], v[240:241], v[242:243], v[236:237]
	v_pk_mul_f32 v[240:241], v[150:151], s[66:67] op_sel_hi:[1,0]
	v_lshlrev_b32_e32 v242, 16, v195
	v_and_b32_e32 v243, 0xffff0000, v195
	v_pk_fma_f32 v[238:239], v[240:241], v[242:243], v[238:239]
	v_pk_mul_f32 v[240:241], v[152:153], s[68:69] op_sel_hi:[1,0]
	v_lshlrev_b32_e32 v242, 16, v196
	v_and_b32_e32 v243, 0xffff0000, v196
	v_pk_fma_f32 v[232:233], v[240:241], v[242:243], v[232:233]
	v_pk_mul_f32 v[240:241], v[154:155], s[68:69] op_sel_hi:[1,0]
	v_lshlrev_b32_e32 v242, 16, v197
	v_and_b32_e32 v243, 0xffff0000, v197
	v_pk_fma_f32 v[234:235], v[240:241], v[242:243], v[234:235]
	v_pk_mul_f32 v[240:241], v[156:157], s[68:69] op_sel_hi:[1,0]
	v_lshlrev_b32_e32 v242, 16, v198
	v_and_b32_e32 v243, 0xffff0000, v198
	v_pk_fma_f32 v[236:237], v[240:241], v[242:243], v[236:237]
	v_pk_mul_f32 v[240:241], v[158:159], s[68:69] op_sel_hi:[1,0]
	v_lshlrev_b32_e32 v242, 16, v199
	v_and_b32_e32 v243, 0xffff0000, v199
	v_pk_fma_f32 v[238:239], v[240:241], v[242:243], v[238:239]
	v_cvt_pk_bf16_f32 v248, v232, v233
	v_cvt_pk_bf16_f32 v249, v234, v235
	v_cvt_pk_bf16_f32 v250, v236, v237
	v_cvt_pk_bf16_f32 v251, v238, v239
	s_lshl_b32 s58, s54, 11
	s_add_u32 s60, s52, s58
	s_addc_u32 s61, s53, 0
	global_store_dwordx4 v126, v[248:251], s[60:61]
	s_add_i32 s54, s41, 0x6000
	s_cmp_lt_u32 s54, 0x8000
	s_cselect_b32 s55, s70, s71
	s_and_b32 s56, s54, s55
	s_add_i32 s57, s55, 1
	s_add_i32 s58, s56, -2
	s_cmp_lt_u32 s58, s57
	s_cselect_b32 s58, -2, 0
	s_add_i32 s58, s54, s58
	s_mul_i32 s58, s58, 0x5a00
	s_add_u32 s60, s50, s58
	s_addc_u32 s61, s51, 0
	global_load_dwordx4 v[168:171], v126, s[60:61]
	s_add_i32 s58, s56, -1
	s_cmp_lt_u32 s58, s57
	s_cselect_b32 s58, -1, 0
	s_add_i32 s58, s54, s58
	s_mul_i32 s58, s58, 0x5a00
	s_add_u32 s60, s50, s58
	s_addc_u32 s61, s51, 0
	global_load_dwordx4 v[172:175], v126, s[60:61]
	s_mul_i32 s58, s54, 0x5a00
	s_add_u32 s60, s50, s58
	s_addc_u32 s61, s51, 0
	global_load_dwordx4 v[176:179], v126, s[60:61]
	s_add_i32 s58, s56, 1
	s_cmp_lt_u32 s58, s57
	s_cselect_b32 s58, 1, 0
	s_add_i32 s58, s54, s58
	s_mul_i32 s58, s58, 0x5a00
	s_add_u32 s60, s50, s58
	s_addc_u32 s61, s51, 0
	global_load_dwordx4 v[180:183], v126, s[60:61]
	s_add_i32 s54, s41, 0x6400
	s_cmp_lt_u32 s54, 0x8000
	s_cselect_b32 s55, s70, s71
	s_and_b32 s56, s54, s55
	s_add_i32 s57, s55, 1
	s_add_i32 s58, s56, -2
	s_cmp_lt_u32 s58, s57
	s_cselect_b32 s58, -2, 0
	s_add_i32 s58, s54, s58
	s_mul_i32 s58, s58, 0x5a00
	s_add_u32 s60, s50, s58
	s_addc_u32 s61, s51, 0
	global_load_dwordx4 v[184:187], v126, s[60:61]
	s_add_i32 s58, s56, -1
	s_cmp_lt_u32 s58, s57
	s_cselect_b32 s58, -1, 0
	s_add_i32 s58, s54, s58
	s_mul_i32 s58, s58, 0x5a00
	s_add_u32 s60, s50, s58
	s_addc_u32 s61, s51, 0
	global_load_dwordx4 v[188:191], v126, s[60:61]
	s_mul_i32 s58, s54, 0x5a00
	s_add_u32 s60, s50, s58
	s_addc_u32 s61, s51, 0
	global_load_dwordx4 v[192:195], v126, s[60:61]
	s_add_i32 s58, s56, 1
	s_cmp_lt_u32 s58, s57
	s_cselect_b32 s58, 1, 0
	s_add_i32 s58, s54, s58
	s_mul_i32 s58, s58, 0x5a00
	s_add_u32 s60, s50, s58
	s_addc_u32 s61, s51, 0
	global_load_dwordx4 v[196:199], v126, s[60:61]
	s_waitcnt vmcnt(20)
	s_add_i32 s54, s41, 0x5000
	s_cmp_lt_u32 s54, 0x8000
	s_cselect_b32 s55, s70, s71
	s_and_b32 s56, s54, s55
	s_add_i32 s57, s55, 1
	s_add_i32 s58, s56, -2
	s_cmp_lt_u32 s58, s57
	s_cselect_b32 s62, 1.0, 0
	s_add_i32 s58, s56, -1
	s_cmp_lt_u32 s58, s57
	s_cselect_b32 s64, 1.0, 0
	s_mov_b32 s66, 1.0
	s_add_i32 s58, s56, 1
	s_cmp_lt_u32 s58, s57
	s_cselect_b32 s68, 1.0, 0
	v_pk_mul_f32 v[240:241], v[128:129], s[62:63] op_sel_hi:[1,0]
	v_lshlrev_b32_e32 v242, 16, v200
	v_and_b32_e32 v243, 0xffff0000, v200
	v_pk_fma_f32 v[232:233], v[240:241], v[242:243], v[160:161]
	v_pk_mul_f32 v[240:241], v[130:131], s[62:63] op_sel_hi:[1,0]
	v_lshlrev_b32_e32 v242, 16, v201
	v_and_b32_e32 v243, 0xffff0000, v201
	v_pk_fma_f32 v[234:235], v[240:241], v[242:243], v[162:163]
	v_pk_mul_f32 v[240:241], v[132:133], s[62:63] op_sel_hi:[1,0]
	v_lshlrev_b32_e32 v242, 16, v202
	v_and_b32_e32 v243, 0xffff0000, v202
	v_pk_fma_f32 v[236:237], v[240:241], v[242:243], v[164:165]
	v_pk_mul_f32 v[240:241], v[134:135], s[62:63] op_sel_hi:[1,0]
	v_lshlrev_b32_e32 v242, 16, v203
	v_and_b32_e32 v243, 0xffff0000, v203
	v_pk_fma_f32 v[238:239], v[240:241], v[242:243], v[166:167]
	v_pk_mul_f32 v[240:241], v[136:137], s[64:65] op_sel_hi:[1,0]
	v_lshlrev_b32_e32 v242, 16, v204
	v_and_b32_e32 v243, 0xffff0000, v204
	v_pk_fma_f32 v[232:233], v[240:241], v[242:243], v[232:233]
	v_pk_mul_f32 v[240:241], v[138:139], s[64:65] op_sel_hi:[1,0]
	v_lshlrev_b32_e32 v242, 16, v205
	v_and_b32_e32 v243, 0xffff0000, v205
	v_pk_fma_f32 v[234:235], v[240:241], v[242:243], v[234:235]
	v_pk_mul_f32 v[240:241], v[140:141], s[64:65] op_sel_hi:[1,0]
	v_lshlrev_b32_e32 v242, 16, v206
	v_and_b32_e32 v243, 0xffff0000, v206
	v_pk_fma_f32 v[236:237], v[240:241], v[242:243], v[236:237]
	v_pk_mul_f32 v[240:241], v[142:143], s[64:65] op_sel_hi:[1,0]
	v_lshlrev_b32_e32 v242, 16, v207
	v_and_b32_e32 v243, 0xffff0000, v207
	v_pk_fma_f32 v[238:239], v[240:241], v[242:243], v[238:239]
	v_pk_mul_f32 v[240:241], v[144:145], s[66:67] op_sel_hi:[1,0]
	v_lshlrev_b32_e32 v242, 16, v208
	v_and_b32_e32 v243, 0xffff0000, v208
	v_pk_fma_f32 v[232:233], v[240:241], v[242:243], v[232:233]
	v_pk_mul_f32 v[240:241], v[146:147], s[66:67] op_sel_hi:[1,0]
	v_lshlrev_b32_e32 v242, 16, v209
	v_and_b32_e32 v243, 0xffff0000, v209
	v_pk_fma_f32 v[234:235], v[240:241], v[242:243], v[234:235]
	v_pk_mul_f32 v[240:241], v[148:149], s[66:67] op_sel_hi:[1,0]
	v_lshlrev_b32_e32 v242, 16, v210
	v_and_b32_e32 v243, 0xffff0000, v210
	v_pk_fma_f32 v[236:237], v[240:241], v[242:243], v[236:237]
	v_pk_mul_f32 v[240:241], v[150:151], s[66:67] op_sel_hi:[1,0]
	v_lshlrev_b32_e32 v242, 16, v211
	v_and_b32_e32 v243, 0xffff0000, v211
	v_pk_fma_f32 v[238:239], v[240:241], v[242:243], v[238:239]
	v_pk_mul_f32 v[240:241], v[152:153], s[68:69] op_sel_hi:[1,0]
	v_lshlrev_b32_e32 v242, 16, v212
	v_and_b32_e32 v243, 0xffff0000, v212
	v_pk_fma_f32 v[232:233], v[240:241], v[242:243], v[232:233]
	v_pk_mul_f32 v[240:241], v[154:155], s[68:69] op_sel_hi:[1,0]
	v_lshlrev_b32_e32 v242, 16, v213
	v_and_b32_e32 v243, 0xffff0000, v213
	v_pk_fma_f32 v[234:235], v[240:241], v[242:243], v[234:235]
	v_pk_mul_f32 v[240:241], v[156:157], s[68:69] op_sel_hi:[1,0]
	v_lshlrev_b32_e32 v242, 16, v214
	v_and_b32_e32 v243, 0xffff0000, v214
	v_pk_fma_f32 v[236:237], v[240:241], v[242:243], v[236:237]
	v_pk_mul_f32 v[240:241], v[158:159], s[68:69] op_sel_hi:[1,0]
	v_lshlrev_b32_e32 v242, 16, v215
	v_and_b32_e32 v243, 0xffff0000, v215
	v_pk_fma_f32 v[238:239], v[240:241], v[242:243], v[238:239]
	v_cvt_pk_bf16_f32 v248, v232, v233
	v_cvt_pk_bf16_f32 v249, v234, v235
	v_cvt_pk_bf16_f32 v250, v236, v237
	v_cvt_pk_bf16_f32 v251, v238, v239
	s_lshl_b32 s58, s54, 11
	s_add_u32 s60, s52, s58
	s_addc_u32 s61, s53, 0
	global_store_dwordx4 v126, v[248:251], s[60:61]
	s_add_i32 s54, s41, 0x5400
	s_cmp_lt_u32 s54, 0x8000
	s_cselect_b32 s55, s70, s71
	s_and_b32 s56, s54, s55
	s_add_i32 s57, s55, 1
	s_add_i32 s58, s56, -2
	s_cmp_lt_u32 s58, s57
	s_cselect_b32 s62, 1.0, 0
	s_add_i32 s58, s56, -1
	s_cmp_lt_u32 s58, s57
	s_cselect_b32 s64, 1.0, 0
	s_mov_b32 s66, 1.0
	s_add_i32 s58, s56, 1
	s_cmp_lt_u32 s58, s57
	s_cselect_b32 s68, 1.0, 0
	v_pk_mul_f32 v[240:241], v[128:129], s[62:63] op_sel_hi:[1,0]
	v_lshlrev_b32_e32 v242, 16, v216
	v_and_b32_e32 v243, 0xffff0000, v216
	v_pk_fma_f32 v[232:233], v[240:241], v[242:243], v[160:161]
	v_pk_mul_f32 v[240:241], v[130:131], s[62:63] op_sel_hi:[1,0]
	v_lshlrev_b32_e32 v242, 16, v217
	v_and_b32_e32 v243, 0xffff0000, v217
	v_pk_fma_f32 v[234:235], v[240:241], v[242:243], v[162:163]
	v_pk_mul_f32 v[240:241], v[132:133], s[62:63] op_sel_hi:[1,0]
	v_lshlrev_b32_e32 v242, 16, v218
	v_and_b32_e32 v243, 0xffff0000, v218
	v_pk_fma_f32 v[236:237], v[240:241], v[242:243], v[164:165]
	v_pk_mul_f32 v[240:241], v[134:135], s[62:63] op_sel_hi:[1,0]
	v_lshlrev_b32_e32 v242, 16, v219
	v_and_b32_e32 v243, 0xffff0000, v219
	v_pk_fma_f32 v[238:239], v[240:241], v[242:243], v[166:167]
	v_pk_mul_f32 v[240:241], v[136:137], s[64:65] op_sel_hi:[1,0]
	v_lshlrev_b32_e32 v242, 16, v220
	v_and_b32_e32 v243, 0xffff0000, v220
	v_pk_fma_f32 v[232:233], v[240:241], v[242:243], v[232:233]
	v_pk_mul_f32 v[240:241], v[138:139], s[64:65] op_sel_hi:[1,0]
	v_lshlrev_b32_e32 v242, 16, v221
	v_and_b32_e32 v243, 0xffff0000, v221
	v_pk_fma_f32 v[234:235], v[240:241], v[242:243], v[234:235]
	v_pk_mul_f32 v[240:241], v[140:141], s[64:65] op_sel_hi:[1,0]
	v_lshlrev_b32_e32 v242, 16, v222
	v_and_b32_e32 v243, 0xffff0000, v222
	v_pk_fma_f32 v[236:237], v[240:241], v[242:243], v[236:237]
	v_pk_mul_f32 v[240:241], v[142:143], s[64:65] op_sel_hi:[1,0]
	v_lshlrev_b32_e32 v242, 16, v223
	v_and_b32_e32 v243, 0xffff0000, v223
	v_pk_fma_f32 v[238:239], v[240:241], v[242:243], v[238:239]
	v_pk_mul_f32 v[240:241], v[144:145], s[66:67] op_sel_hi:[1,0]
	v_lshlrev_b32_e32 v242, 16, v224
	v_and_b32_e32 v243, 0xffff0000, v224
	v_pk_fma_f32 v[232:233], v[240:241], v[242:243], v[232:233]
	v_pk_mul_f32 v[240:241], v[146:147], s[66:67] op_sel_hi:[1,0]
	v_lshlrev_b32_e32 v242, 16, v225
	v_and_b32_e32 v243, 0xffff0000, v225
	v_pk_fma_f32 v[234:235], v[240:241], v[242:243], v[234:235]
	v_pk_mul_f32 v[240:241], v[148:149], s[66:67] op_sel_hi:[1,0]
	v_lshlrev_b32_e32 v242, 16, v226
	v_and_b32_e32 v243, 0xffff0000, v226
	v_pk_fma_f32 v[236:237], v[240:241], v[242:243], v[236:237]
	v_pk_mul_f32 v[240:241], v[150:151], s[66:67] op_sel_hi:[1,0]
	v_lshlrev_b32_e32 v242, 16, v227
	v_and_b32_e32 v243, 0xffff0000, v227
	v_pk_fma_f32 v[238:239], v[240:241], v[242:243], v[238:239]
	v_pk_mul_f32 v[240:241], v[152:153], s[68:69] op_sel_hi:[1,0]
	v_lshlrev_b32_e32 v242, 16, v228
	v_and_b32_e32 v243, 0xffff0000, v228
	v_pk_fma_f32 v[232:233], v[240:241], v[242:243], v[232:233]
	v_pk_mul_f32 v[240:241], v[154:155], s[68:69] op_sel_hi:[1,0]
	v_lshlrev_b32_e32 v242, 16, v229
	v_and_b32_e32 v243, 0xffff0000, v229
	v_pk_fma_f32 v[234:235], v[240:241], v[242:243], v[234:235]
	v_pk_mul_f32 v[240:241], v[156:157], s[68:69] op_sel_hi:[1,0]
	v_lshlrev_b32_e32 v242, 16, v230
	v_and_b32_e32 v243, 0xffff0000, v230
	v_pk_fma_f32 v[236:237], v[240:241], v[242:243], v[236:237]
	v_pk_mul_f32 v[240:241], v[158:159], s[68:69] op_sel_hi:[1,0]
	v_lshlrev_b32_e32 v242, 16, v231
	v_and_b32_e32 v243, 0xffff0000, v231
	v_pk_fma_f32 v[238:239], v[240:241], v[242:243], v[238:239]
	v_cvt_pk_bf16_f32 v248, v232, v233
	v_cvt_pk_bf16_f32 v249, v234, v235
	v_cvt_pk_bf16_f32 v250, v236, v237
	v_cvt_pk_bf16_f32 v251, v238, v239
	s_lshl_b32 s58, s54, 11
	s_add_u32 s60, s52, s58
	s_addc_u32 s61, s53, 0
	global_store_dwordx4 v126, v[248:251], s[60:61]
	s_add_i32 s54, s41, 0x6800
	s_cmp_lt_u32 s54, 0x8000
	s_cselect_b32 s55, s70, s71
	s_and_b32 s56, s54, s55
	s_add_i32 s57, s55, 1
	s_add_i32 s58, s56, -2
	s_cmp_lt_u32 s58, s57
	s_cselect_b32 s58, -2, 0
	s_add_i32 s58, s54, s58
	s_mul_i32 s58, s58, 0x5a00
	s_add_u32 s60, s50, s58
	s_addc_u32 s61, s51, 0
	global_load_dwordx4 v[200:203], v126, s[60:61]
	s_add_i32 s58, s56, -1
	s_cmp_lt_u32 s58, s57
	s_cselect_b32 s58, -1, 0
	s_add_i32 s58, s54, s58
	s_mul_i32 s58, s58, 0x5a00
	s_add_u32 s60, s50, s58
	s_addc_u32 s61, s51, 0
	global_load_dwordx4 v[204:207], v126, s[60:61]
	s_mul_i32 s58, s54, 0x5a00
	s_add_u32 s60, s50, s58
	s_addc_u32 s61, s51, 0
	global_load_dwordx4 v[208:211], v126, s[60:61]
	s_add_i32 s58, s56, 1
	s_cmp_lt_u32 s58, s57
	s_cselect_b32 s58, 1, 0
	s_add_i32 s58, s54, s58
	s_mul_i32 s58, s58, 0x5a00
	s_add_u32 s60, s50, s58
	s_addc_u32 s61, s51, 0
	global_load_dwordx4 v[212:215], v126, s[60:61]
	s_add_i32 s54, s41, 0x6c00
	s_cmp_lt_u32 s54, 0x8000
	s_cselect_b32 s55, s70, s71
	s_and_b32 s56, s54, s55
	s_add_i32 s57, s55, 1
	s_add_i32 s58, s56, -2
	s_cmp_lt_u32 s58, s57
	s_cselect_b32 s58, -2, 0
	s_add_i32 s58, s54, s58
	s_mul_i32 s58, s58, 0x5a00
	s_add_u32 s60, s50, s58
	s_addc_u32 s61, s51, 0
	global_load_dwordx4 v[216:219], v126, s[60:61]
	s_add_i32 s58, s56, -1
	s_cmp_lt_u32 s58, s57
	s_cselect_b32 s58, -1, 0
	s_add_i32 s58, s54, s58
	s_mul_i32 s58, s58, 0x5a00
	s_add_u32 s60, s50, s58
	s_addc_u32 s61, s51, 0
	global_load_dwordx4 v[220:223], v126, s[60:61]
	s_mul_i32 s58, s54, 0x5a00
	s_add_u32 s60, s50, s58
	s_addc_u32 s61, s51, 0
	global_load_dwordx4 v[224:227], v126, s[60:61]
	s_add_i32 s58, s56, 1
	s_cmp_lt_u32 s58, s57
	s_cselect_b32 s58, 1, 0
	s_add_i32 s58, s54, s58
	s_mul_i32 s58, s58, 0x5a00
	s_add_u32 s60, s50, s58
	s_addc_u32 s61, s51, 0
	global_load_dwordx4 v[228:231], v126, s[60:61]
	s_waitcnt vmcnt(20)
	s_add_i32 s54, s41, 0x5800
	s_cmp_lt_u32 s54, 0x8000
	s_cselect_b32 s55, s70, s71
	s_and_b32 s56, s54, s55
	s_add_i32 s57, s55, 1
	s_add_i32 s58, s56, -2
	s_cmp_lt_u32 s58, s57
	s_cselect_b32 s62, 1.0, 0
	s_add_i32 s58, s56, -1
	s_cmp_lt_u32 s58, s57
	s_cselect_b32 s64, 1.0, 0
	s_mov_b32 s66, 1.0
	s_add_i32 s58, s56, 1
	s_cmp_lt_u32 s58, s57
	s_cselect_b32 s68, 1.0, 0
	v_pk_mul_f32 v[240:241], v[128:129], s[62:63] op_sel_hi:[1,0]
	v_lshlrev_b32_e32 v242, 16, v40
	v_and_b32_e32 v243, 0xffff0000, v40
	v_pk_fma_f32 v[232:233], v[240:241], v[242:243], v[160:161]
	v_pk_mul_f32 v[240:241], v[130:131], s[62:63] op_sel_hi:[1,0]
	v_lshlrev_b32_e32 v242, 16, v41
	v_and_b32_e32 v243, 0xffff0000, v41
	v_pk_fma_f32 v[234:235], v[240:241], v[242:243], v[162:163]
	v_pk_mul_f32 v[240:241], v[132:133], s[62:63] op_sel_hi:[1,0]
	v_lshlrev_b32_e32 v242, 16, v42
	v_and_b32_e32 v243, 0xffff0000, v42
	v_pk_fma_f32 v[236:237], v[240:241], v[242:243], v[164:165]
	v_pk_mul_f32 v[240:241], v[134:135], s[62:63] op_sel_hi:[1,0]
	v_lshlrev_b32_e32 v242, 16, v43
	v_and_b32_e32 v243, 0xffff0000, v43
	v_pk_fma_f32 v[238:239], v[240:241], v[242:243], v[166:167]
	v_pk_mul_f32 v[240:241], v[136:137], s[64:65] op_sel_hi:[1,0]
	v_lshlrev_b32_e32 v242, 16, v44
	v_and_b32_e32 v243, 0xffff0000, v44
	v_pk_fma_f32 v[232:233], v[240:241], v[242:243], v[232:233]
	v_pk_mul_f32 v[240:241], v[138:139], s[64:65] op_sel_hi:[1,0]
	v_lshlrev_b32_e32 v242, 16, v45
	v_and_b32_e32 v243, 0xffff0000, v45
	v_pk_fma_f32 v[234:235], v[240:241], v[242:243], v[234:235]
	v_pk_mul_f32 v[240:241], v[140:141], s[64:65] op_sel_hi:[1,0]
	v_lshlrev_b32_e32 v242, 16, v46
	v_and_b32_e32 v243, 0xffff0000, v46
	v_pk_fma_f32 v[236:237], v[240:241], v[242:243], v[236:237]
	v_pk_mul_f32 v[240:241], v[142:143], s[64:65] op_sel_hi:[1,0]
	v_lshlrev_b32_e32 v242, 16, v47
	v_and_b32_e32 v243, 0xffff0000, v47
	v_pk_fma_f32 v[238:239], v[240:241], v[242:243], v[238:239]
	v_pk_mul_f32 v[240:241], v[144:145], s[66:67] op_sel_hi:[1,0]
	v_lshlrev_b32_e32 v242, 16, v48
	v_and_b32_e32 v243, 0xffff0000, v48
	v_pk_fma_f32 v[232:233], v[240:241], v[242:243], v[232:233]
	v_pk_mul_f32 v[240:241], v[146:147], s[66:67] op_sel_hi:[1,0]
	v_lshlrev_b32_e32 v242, 16, v49
	v_and_b32_e32 v243, 0xffff0000, v49
	v_pk_fma_f32 v[234:235], v[240:241], v[242:243], v[234:235]
	v_pk_mul_f32 v[240:241], v[148:149], s[66:67] op_sel_hi:[1,0]
	v_lshlrev_b32_e32 v242, 16, v50
	v_and_b32_e32 v243, 0xffff0000, v50
	v_pk_fma_f32 v[236:237], v[240:241], v[242:243], v[236:237]
	v_pk_mul_f32 v[240:241], v[150:151], s[66:67] op_sel_hi:[1,0]
	v_lshlrev_b32_e32 v242, 16, v51
	v_and_b32_e32 v243, 0xffff0000, v51
	v_pk_fma_f32 v[238:239], v[240:241], v[242:243], v[238:239]
	v_pk_mul_f32 v[240:241], v[152:153], s[68:69] op_sel_hi:[1,0]
	v_lshlrev_b32_e32 v242, 16, v52
	v_and_b32_e32 v243, 0xffff0000, v52
	v_pk_fma_f32 v[232:233], v[240:241], v[242:243], v[232:233]
	v_pk_mul_f32 v[240:241], v[154:155], s[68:69] op_sel_hi:[1,0]
	v_lshlrev_b32_e32 v242, 16, v53
	v_and_b32_e32 v243, 0xffff0000, v53
	v_pk_fma_f32 v[234:235], v[240:241], v[242:243], v[234:235]
	v_pk_mul_f32 v[240:241], v[156:157], s[68:69] op_sel_hi:[1,0]
	v_lshlrev_b32_e32 v242, 16, v54
	v_and_b32_e32 v243, 0xffff0000, v54
	v_pk_fma_f32 v[236:237], v[240:241], v[242:243], v[236:237]
	v_pk_mul_f32 v[240:241], v[158:159], s[68:69] op_sel_hi:[1,0]
	v_lshlrev_b32_e32 v242, 16, v55
	v_and_b32_e32 v243, 0xffff0000, v55
	v_pk_fma_f32 v[238:239], v[240:241], v[242:243], v[238:239]
	v_cvt_pk_bf16_f32 v248, v232, v233
	v_cvt_pk_bf16_f32 v249, v234, v235
	v_cvt_pk_bf16_f32 v250, v236, v237
	v_cvt_pk_bf16_f32 v251, v238, v239
	s_lshl_b32 s58, s54, 11
	s_add_u32 s60, s52, s58
	s_addc_u32 s61, s53, 0
	global_store_dwordx4 v126, v[248:251], s[60:61]
	s_add_i32 s54, s41, 0x5c00
	s_cmp_lt_u32 s54, 0x8000
	s_cselect_b32 s55, s70, s71
	s_and_b32 s56, s54, s55
	s_add_i32 s57, s55, 1
	s_add_i32 s58, s56, -2
	s_cmp_lt_u32 s58, s57
	s_cselect_b32 s62, 1.0, 0
	s_add_i32 s58, s56, -1
	s_cmp_lt_u32 s58, s57
	s_cselect_b32 s64, 1.0, 0
	s_mov_b32 s66, 1.0
	s_add_i32 s58, s56, 1
	s_cmp_lt_u32 s58, s57
	s_cselect_b32 s68, 1.0, 0
	v_pk_mul_f32 v[240:241], v[128:129], s[62:63] op_sel_hi:[1,0]
	v_lshlrev_b32_e32 v242, 16, v56
	v_and_b32_e32 v243, 0xffff0000, v56
	v_pk_fma_f32 v[232:233], v[240:241], v[242:243], v[160:161]
	v_pk_mul_f32 v[240:241], v[130:131], s[62:63] op_sel_hi:[1,0]
	v_lshlrev_b32_e32 v242, 16, v57
	v_and_b32_e32 v243, 0xffff0000, v57
	v_pk_fma_f32 v[234:235], v[240:241], v[242:243], v[162:163]
	v_pk_mul_f32 v[240:241], v[132:133], s[62:63] op_sel_hi:[1,0]
	v_lshlrev_b32_e32 v242, 16, v58
	v_and_b32_e32 v243, 0xffff0000, v58
	v_pk_fma_f32 v[236:237], v[240:241], v[242:243], v[164:165]
	v_pk_mul_f32 v[240:241], v[134:135], s[62:63] op_sel_hi:[1,0]
	v_lshlrev_b32_e32 v242, 16, v59
	v_and_b32_e32 v243, 0xffff0000, v59
	v_pk_fma_f32 v[238:239], v[240:241], v[242:243], v[166:167]
	v_pk_mul_f32 v[240:241], v[136:137], s[64:65] op_sel_hi:[1,0]
	v_lshlrev_b32_e32 v242, 16, v60
	v_and_b32_e32 v243, 0xffff0000, v60
	v_pk_fma_f32 v[232:233], v[240:241], v[242:243], v[232:233]
	v_pk_mul_f32 v[240:241], v[138:139], s[64:65] op_sel_hi:[1,0]
	v_lshlrev_b32_e32 v242, 16, v61
	v_and_b32_e32 v243, 0xffff0000, v61
	v_pk_fma_f32 v[234:235], v[240:241], v[242:243], v[234:235]
	v_pk_mul_f32 v[240:241], v[140:141], s[64:65] op_sel_hi:[1,0]
	v_lshlrev_b32_e32 v242, 16, v62
	v_and_b32_e32 v243, 0xffff0000, v62
	v_pk_fma_f32 v[236:237], v[240:241], v[242:243], v[236:237]
	v_pk_mul_f32 v[240:241], v[142:143], s[64:65] op_sel_hi:[1,0]
	v_lshlrev_b32_e32 v242, 16, v63
	v_and_b32_e32 v243, 0xffff0000, v63
	v_pk_fma_f32 v[238:239], v[240:241], v[242:243], v[238:239]
	v_pk_mul_f32 v[240:241], v[144:145], s[66:67] op_sel_hi:[1,0]
	v_lshlrev_b32_e32 v242, 16, v64
	v_and_b32_e32 v243, 0xffff0000, v64
	v_pk_fma_f32 v[232:233], v[240:241], v[242:243], v[232:233]
	v_pk_mul_f32 v[240:241], v[146:147], s[66:67] op_sel_hi:[1,0]
	v_lshlrev_b32_e32 v242, 16, v65
	v_and_b32_e32 v243, 0xffff0000, v65
	v_pk_fma_f32 v[234:235], v[240:241], v[242:243], v[234:235]
	v_pk_mul_f32 v[240:241], v[148:149], s[66:67] op_sel_hi:[1,0]
	v_lshlrev_b32_e32 v242, 16, v66
	v_and_b32_e32 v243, 0xffff0000, v66
	v_pk_fma_f32 v[236:237], v[240:241], v[242:243], v[236:237]
	v_pk_mul_f32 v[240:241], v[150:151], s[66:67] op_sel_hi:[1,0]
	v_lshlrev_b32_e32 v242, 16, v67
	v_and_b32_e32 v243, 0xffff0000, v67
	v_pk_fma_f32 v[238:239], v[240:241], v[242:243], v[238:239]
	v_pk_mul_f32 v[240:241], v[152:153], s[68:69] op_sel_hi:[1,0]
	v_lshlrev_b32_e32 v242, 16, v68
	v_and_b32_e32 v243, 0xffff0000, v68
	v_pk_fma_f32 v[232:233], v[240:241], v[242:243], v[232:233]
	v_pk_mul_f32 v[240:241], v[154:155], s[68:69] op_sel_hi:[1,0]
	v_lshlrev_b32_e32 v242, 16, v69
	v_and_b32_e32 v243, 0xffff0000, v69
	v_pk_fma_f32 v[234:235], v[240:241], v[242:243], v[234:235]
	v_pk_mul_f32 v[240:241], v[156:157], s[68:69] op_sel_hi:[1,0]
	v_lshlrev_b32_e32 v242, 16, v70
	v_and_b32_e32 v243, 0xffff0000, v70
	v_pk_fma_f32 v[236:237], v[240:241], v[242:243], v[236:237]
	v_pk_mul_f32 v[240:241], v[158:159], s[68:69] op_sel_hi:[1,0]
	v_lshlrev_b32_e32 v242, 16, v71
	v_and_b32_e32 v243, 0xffff0000, v71
	v_pk_fma_f32 v[238:239], v[240:241], v[242:243], v[238:239]
	v_cvt_pk_bf16_f32 v248, v232, v233
	v_cvt_pk_bf16_f32 v249, v234, v235
	v_cvt_pk_bf16_f32 v250, v236, v237
	v_cvt_pk_bf16_f32 v251, v238, v239
	s_lshl_b32 s58, s54, 11
	s_add_u32 s60, s52, s58
	s_addc_u32 s61, s53, 0
	global_store_dwordx4 v126, v[248:251], s[60:61]
	s_add_i32 s54, s41, 0x7000
	s_cmp_lt_u32 s54, 0x8000
	s_cselect_b32 s55, s70, s71
	s_and_b32 s56, s54, s55
	s_add_i32 s57, s55, 1
	s_add_i32 s58, s56, -2
	s_cmp_lt_u32 s58, s57
	s_cselect_b32 s58, -2, 0
	s_add_i32 s58, s54, s58
	s_mul_i32 s58, s58, 0x5a00
	s_add_u32 s60, s50, s58
	s_addc_u32 s61, s51, 0
	global_load_dwordx4 v[40:43], v126, s[60:61]
	s_add_i32 s58, s56, -1
	s_cmp_lt_u32 s58, s57
	s_cselect_b32 s58, -1, 0
	s_add_i32 s58, s54, s58
	s_mul_i32 s58, s58, 0x5a00
	s_add_u32 s60, s50, s58
	s_addc_u32 s61, s51, 0
	global_load_dwordx4 v[44:47], v126, s[60:61]
	s_mul_i32 s58, s54, 0x5a00
	s_add_u32 s60, s50, s58
	s_addc_u32 s61, s51, 0
	global_load_dwordx4 v[48:51], v126, s[60:61]
	s_add_i32 s58, s56, 1
	s_cmp_lt_u32 s58, s57
	s_cselect_b32 s58, 1, 0
	s_add_i32 s58, s54, s58
	s_mul_i32 s58, s58, 0x5a00
	s_add_u32 s60, s50, s58
	s_addc_u32 s61, s51, 0
	global_load_dwordx4 v[52:55], v126, s[60:61]
	s_add_i32 s54, s41, 0x7400
	s_cmp_lt_u32 s54, 0x8000
	s_cselect_b32 s55, s70, s71
	s_and_b32 s56, s54, s55
	s_add_i32 s57, s55, 1
	s_add_i32 s58, s56, -2
	s_cmp_lt_u32 s58, s57
	s_cselect_b32 s58, -2, 0
	s_add_i32 s58, s54, s58
	s_mul_i32 s58, s58, 0x5a00
	s_add_u32 s60, s50, s58
	s_addc_u32 s61, s51, 0
	global_load_dwordx4 v[56:59], v126, s[60:61]
	s_add_i32 s58, s56, -1
	s_cmp_lt_u32 s58, s57
	s_cselect_b32 s58, -1, 0
	s_add_i32 s58, s54, s58
	s_mul_i32 s58, s58, 0x5a00
	s_add_u32 s60, s50, s58
	s_addc_u32 s61, s51, 0
	global_load_dwordx4 v[60:63], v126, s[60:61]
	s_mul_i32 s58, s54, 0x5a00
	s_add_u32 s60, s50, s58
	s_addc_u32 s61, s51, 0
	global_load_dwordx4 v[64:67], v126, s[60:61]
	s_add_i32 s58, s56, 1
	s_cmp_lt_u32 s58, s57
	s_cselect_b32 s58, 1, 0
	s_add_i32 s58, s54, s58
	s_mul_i32 s58, s58, 0x5a00
	s_add_u32 s60, s50, s58
	s_addc_u32 s61, s51, 0
	global_load_dwordx4 v[68:71], v126, s[60:61]
	s_waitcnt vmcnt(20)
	s_add_i32 s54, s41, 0x6000
	s_cmp_lt_u32 s54, 0x8000
	s_cselect_b32 s55, s70, s71
	s_and_b32 s56, s54, s55
	s_add_i32 s57, s55, 1
	s_add_i32 s58, s56, -2
	s_cmp_lt_u32 s58, s57
	s_cselect_b32 s62, 1.0, 0
	s_add_i32 s58, s56, -1
	s_cmp_lt_u32 s58, s57
	s_cselect_b32 s64, 1.0, 0
	s_mov_b32 s66, 1.0
	s_add_i32 s58, s56, 1
	s_cmp_lt_u32 s58, s57
	s_cselect_b32 s68, 1.0, 0
	v_pk_mul_f32 v[240:241], v[128:129], s[62:63] op_sel_hi:[1,0]
	v_lshlrev_b32_e32 v242, 16, v168
	v_and_b32_e32 v243, 0xffff0000, v168
	v_pk_fma_f32 v[232:233], v[240:241], v[242:243], v[160:161]
	v_pk_mul_f32 v[240:241], v[130:131], s[62:63] op_sel_hi:[1,0]
	v_lshlrev_b32_e32 v242, 16, v169
	v_and_b32_e32 v243, 0xffff0000, v169
	v_pk_fma_f32 v[234:235], v[240:241], v[242:243], v[162:163]
	v_pk_mul_f32 v[240:241], v[132:133], s[62:63] op_sel_hi:[1,0]
	v_lshlrev_b32_e32 v242, 16, v170
	v_and_b32_e32 v243, 0xffff0000, v170
	v_pk_fma_f32 v[236:237], v[240:241], v[242:243], v[164:165]
	v_pk_mul_f32 v[240:241], v[134:135], s[62:63] op_sel_hi:[1,0]
	v_lshlrev_b32_e32 v242, 16, v171
	v_and_b32_e32 v243, 0xffff0000, v171
	v_pk_fma_f32 v[238:239], v[240:241], v[242:243], v[166:167]
	v_pk_mul_f32 v[240:241], v[136:137], s[64:65] op_sel_hi:[1,0]
	v_lshlrev_b32_e32 v242, 16, v172
	v_and_b32_e32 v243, 0xffff0000, v172
	v_pk_fma_f32 v[232:233], v[240:241], v[242:243], v[232:233]
	v_pk_mul_f32 v[240:241], v[138:139], s[64:65] op_sel_hi:[1,0]
	v_lshlrev_b32_e32 v242, 16, v173
	v_and_b32_e32 v243, 0xffff0000, v173
	v_pk_fma_f32 v[234:235], v[240:241], v[242:243], v[234:235]
	v_pk_mul_f32 v[240:241], v[140:141], s[64:65] op_sel_hi:[1,0]
	v_lshlrev_b32_e32 v242, 16, v174
	v_and_b32_e32 v243, 0xffff0000, v174
	v_pk_fma_f32 v[236:237], v[240:241], v[242:243], v[236:237]
	v_pk_mul_f32 v[240:241], v[142:143], s[64:65] op_sel_hi:[1,0]
	v_lshlrev_b32_e32 v242, 16, v175
	v_and_b32_e32 v243, 0xffff0000, v175
	v_pk_fma_f32 v[238:239], v[240:241], v[242:243], v[238:239]
	v_pk_mul_f32 v[240:241], v[144:145], s[66:67] op_sel_hi:[1,0]
	v_lshlrev_b32_e32 v242, 16, v176
	v_and_b32_e32 v243, 0xffff0000, v176
	v_pk_fma_f32 v[232:233], v[240:241], v[242:243], v[232:233]
	v_pk_mul_f32 v[240:241], v[146:147], s[66:67] op_sel_hi:[1,0]
	v_lshlrev_b32_e32 v242, 16, v177
	v_and_b32_e32 v243, 0xffff0000, v177
	v_pk_fma_f32 v[234:235], v[240:241], v[242:243], v[234:235]
	v_pk_mul_f32 v[240:241], v[148:149], s[66:67] op_sel_hi:[1,0]
	v_lshlrev_b32_e32 v242, 16, v178
	v_and_b32_e32 v243, 0xffff0000, v178
	v_pk_fma_f32 v[236:237], v[240:241], v[242:243], v[236:237]
	v_pk_mul_f32 v[240:241], v[150:151], s[66:67] op_sel_hi:[1,0]
	v_lshlrev_b32_e32 v242, 16, v179
	v_and_b32_e32 v243, 0xffff0000, v179
	v_pk_fma_f32 v[238:239], v[240:241], v[242:243], v[238:239]
	v_pk_mul_f32 v[240:241], v[152:153], s[68:69] op_sel_hi:[1,0]
	v_lshlrev_b32_e32 v242, 16, v180
	v_and_b32_e32 v243, 0xffff0000, v180
	v_pk_fma_f32 v[232:233], v[240:241], v[242:243], v[232:233]
	v_pk_mul_f32 v[240:241], v[154:155], s[68:69] op_sel_hi:[1,0]
	v_lshlrev_b32_e32 v242, 16, v181
	v_and_b32_e32 v243, 0xffff0000, v181
	v_pk_fma_f32 v[234:235], v[240:241], v[242:243], v[234:235]
	v_pk_mul_f32 v[240:241], v[156:157], s[68:69] op_sel_hi:[1,0]
	v_lshlrev_b32_e32 v242, 16, v182
	v_and_b32_e32 v243, 0xffff0000, v182
	v_pk_fma_f32 v[236:237], v[240:241], v[242:243], v[236:237]
	v_pk_mul_f32 v[240:241], v[158:159], s[68:69] op_sel_hi:[1,0]
	v_lshlrev_b32_e32 v242, 16, v183
	v_and_b32_e32 v243, 0xffff0000, v183
	v_pk_fma_f32 v[238:239], v[240:241], v[242:243], v[238:239]
	v_cvt_pk_bf16_f32 v248, v232, v233
	v_cvt_pk_bf16_f32 v249, v234, v235
	v_cvt_pk_bf16_f32 v250, v236, v237
	v_cvt_pk_bf16_f32 v251, v238, v239
	s_lshl_b32 s58, s54, 11
	s_add_u32 s60, s52, s58
	s_addc_u32 s61, s53, 0
	global_store_dwordx4 v126, v[248:251], s[60:61]
	s_add_i32 s54, s41, 0x6400
	s_cmp_lt_u32 s54, 0x8000
	s_cselect_b32 s55, s70, s71
	s_and_b32 s56, s54, s55
	s_add_i32 s57, s55, 1
	s_add_i32 s58, s56, -2
	s_cmp_lt_u32 s58, s57
	s_cselect_b32 s62, 1.0, 0
	s_add_i32 s58, s56, -1
	s_cmp_lt_u32 s58, s57
	s_cselect_b32 s64, 1.0, 0
	s_mov_b32 s66, 1.0
	s_add_i32 s58, s56, 1
	s_cmp_lt_u32 s58, s57
	s_cselect_b32 s68, 1.0, 0
	v_pk_mul_f32 v[240:241], v[128:129], s[62:63] op_sel_hi:[1,0]
	v_lshlrev_b32_e32 v242, 16, v184
	v_and_b32_e32 v243, 0xffff0000, v184
	v_pk_fma_f32 v[232:233], v[240:241], v[242:243], v[160:161]
	v_pk_mul_f32 v[240:241], v[130:131], s[62:63] op_sel_hi:[1,0]
	v_lshlrev_b32_e32 v242, 16, v185
	v_and_b32_e32 v243, 0xffff0000, v185
	v_pk_fma_f32 v[234:235], v[240:241], v[242:243], v[162:163]
	v_pk_mul_f32 v[240:241], v[132:133], s[62:63] op_sel_hi:[1,0]
	v_lshlrev_b32_e32 v242, 16, v186
	v_and_b32_e32 v243, 0xffff0000, v186
	v_pk_fma_f32 v[236:237], v[240:241], v[242:243], v[164:165]
	v_pk_mul_f32 v[240:241], v[134:135], s[62:63] op_sel_hi:[1,0]
	v_lshlrev_b32_e32 v242, 16, v187
	v_and_b32_e32 v243, 0xffff0000, v187
	v_pk_fma_f32 v[238:239], v[240:241], v[242:243], v[166:167]
	v_pk_mul_f32 v[240:241], v[136:137], s[64:65] op_sel_hi:[1,0]
	v_lshlrev_b32_e32 v242, 16, v188
	v_and_b32_e32 v243, 0xffff0000, v188
	v_pk_fma_f32 v[232:233], v[240:241], v[242:243], v[232:233]
	v_pk_mul_f32 v[240:241], v[138:139], s[64:65] op_sel_hi:[1,0]
	v_lshlrev_b32_e32 v242, 16, v189
	v_and_b32_e32 v243, 0xffff0000, v189
	v_pk_fma_f32 v[234:235], v[240:241], v[242:243], v[234:235]
	v_pk_mul_f32 v[240:241], v[140:141], s[64:65] op_sel_hi:[1,0]
	v_lshlrev_b32_e32 v242, 16, v190
	v_and_b32_e32 v243, 0xffff0000, v190
	v_pk_fma_f32 v[236:237], v[240:241], v[242:243], v[236:237]
	v_pk_mul_f32 v[240:241], v[142:143], s[64:65] op_sel_hi:[1,0]
	v_lshlrev_b32_e32 v242, 16, v191
	v_and_b32_e32 v243, 0xffff0000, v191
	v_pk_fma_f32 v[238:239], v[240:241], v[242:243], v[238:239]
	v_pk_mul_f32 v[240:241], v[144:145], s[66:67] op_sel_hi:[1,0]
	v_lshlrev_b32_e32 v242, 16, v192
	v_and_b32_e32 v243, 0xffff0000, v192
	v_pk_fma_f32 v[232:233], v[240:241], v[242:243], v[232:233]
	v_pk_mul_f32 v[240:241], v[146:147], s[66:67] op_sel_hi:[1,0]
	v_lshlrev_b32_e32 v242, 16, v193
	v_and_b32_e32 v243, 0xffff0000, v193
	v_pk_fma_f32 v[234:235], v[240:241], v[242:243], v[234:235]
	v_pk_mul_f32 v[240:241], v[148:149], s[66:67] op_sel_hi:[1,0]
	v_lshlrev_b32_e32 v242, 16, v194
	v_and_b32_e32 v243, 0xffff0000, v194
	v_pk_fma_f32 v[236:237], v[240:241], v[242:243], v[236:237]
	v_pk_mul_f32 v[240:241], v[150:151], s[66:67] op_sel_hi:[1,0]
	v_lshlrev_b32_e32 v242, 16, v195
	v_and_b32_e32 v243, 0xffff0000, v195
	v_pk_fma_f32 v[238:239], v[240:241], v[242:243], v[238:239]
	v_pk_mul_f32 v[240:241], v[152:153], s[68:69] op_sel_hi:[1,0]
	v_lshlrev_b32_e32 v242, 16, v196
	v_and_b32_e32 v243, 0xffff0000, v196
	v_pk_fma_f32 v[232:233], v[240:241], v[242:243], v[232:233]
	v_pk_mul_f32 v[240:241], v[154:155], s[68:69] op_sel_hi:[1,0]
	v_lshlrev_b32_e32 v242, 16, v197
	v_and_b32_e32 v243, 0xffff0000, v197
	v_pk_fma_f32 v[234:235], v[240:241], v[242:243], v[234:235]
	v_pk_mul_f32 v[240:241], v[156:157], s[68:69] op_sel_hi:[1,0]
	v_lshlrev_b32_e32 v242, 16, v198
	v_and_b32_e32 v243, 0xffff0000, v198
	v_pk_fma_f32 v[236:237], v[240:241], v[242:243], v[236:237]
	v_pk_mul_f32 v[240:241], v[158:159], s[68:69] op_sel_hi:[1,0]
	v_lshlrev_b32_e32 v242, 16, v199
	v_and_b32_e32 v243, 0xffff0000, v199
	v_pk_fma_f32 v[238:239], v[240:241], v[242:243], v[238:239]
	v_cvt_pk_bf16_f32 v248, v232, v233
	v_cvt_pk_bf16_f32 v249, v234, v235
	v_cvt_pk_bf16_f32 v250, v236, v237
	v_cvt_pk_bf16_f32 v251, v238, v239
	s_lshl_b32 s58, s54, 11
	s_add_u32 s60, s52, s58
	s_addc_u32 s61, s53, 0
	global_store_dwordx4 v126, v[248:251], s[60:61]
	s_add_i32 s54, s41, 0x7800
	s_cmp_lt_u32 s54, 0x8000
	s_cselect_b32 s55, s70, s71
	s_and_b32 s56, s54, s55
	s_add_i32 s57, s55, 1
	s_add_i32 s58, s56, -2
	s_cmp_lt_u32 s58, s57
	s_cselect_b32 s58, -2, 0
	s_add_i32 s58, s54, s58
	s_mul_i32 s58, s58, 0x5a00
	s_add_u32 s60, s50, s58
	s_addc_u32 s61, s51, 0
	global_load_dwordx4 v[168:171], v126, s[60:61]
	s_add_i32 s58, s56, -1
	s_cmp_lt_u32 s58, s57
	s_cselect_b32 s58, -1, 0
	s_add_i32 s58, s54, s58
	s_mul_i32 s58, s58, 0x5a00
	s_add_u32 s60, s50, s58
	s_addc_u32 s61, s51, 0
	global_load_dwordx4 v[172:175], v126, s[60:61]
	s_mul_i32 s58, s54, 0x5a00
	s_add_u32 s60, s50, s58
	s_addc_u32 s61, s51, 0
	global_load_dwordx4 v[176:179], v126, s[60:61]
	s_add_i32 s58, s56, 1
	s_cmp_lt_u32 s58, s57
	s_cselect_b32 s58, 1, 0
	s_add_i32 s58, s54, s58
	s_mul_i32 s58, s58, 0x5a00
	s_add_u32 s60, s50, s58
	s_addc_u32 s61, s51, 0
	global_load_dwordx4 v[180:183], v126, s[60:61]
	s_add_i32 s54, s41, 0x7c00
	s_cmp_lt_u32 s54, 0x8000
	s_cselect_b32 s55, s70, s71
	s_and_b32 s56, s54, s55
	s_add_i32 s57, s55, 1
	s_add_i32 s58, s56, -2
	s_cmp_lt_u32 s58, s57
	s_cselect_b32 s58, -2, 0
	s_add_i32 s58, s54, s58
	s_mul_i32 s58, s58, 0x5a00
	s_add_u32 s60, s50, s58
	s_addc_u32 s61, s51, 0
	global_load_dwordx4 v[184:187], v126, s[60:61]
	s_add_i32 s58, s56, -1
	s_cmp_lt_u32 s58, s57
	s_cselect_b32 s58, -1, 0
	s_add_i32 s58, s54, s58
	s_mul_i32 s58, s58, 0x5a00
	s_add_u32 s60, s50, s58
	s_addc_u32 s61, s51, 0
	global_load_dwordx4 v[188:191], v126, s[60:61]
	s_mul_i32 s58, s54, 0x5a00
	s_add_u32 s60, s50, s58
	s_addc_u32 s61, s51, 0
	global_load_dwordx4 v[192:195], v126, s[60:61]
	s_add_i32 s58, s56, 1
	s_cmp_lt_u32 s58, s57
	s_cselect_b32 s58, 1, 0
	s_add_i32 s58, s54, s58
	s_mul_i32 s58, s58, 0x5a00
	s_add_u32 s60, s50, s58
	s_addc_u32 s61, s51, 0
	global_load_dwordx4 v[196:199], v126, s[60:61]
	s_waitcnt vmcnt(20)
	s_add_i32 s54, s41, 0x6800
	s_cmp_lt_u32 s54, 0x8000
	s_cselect_b32 s55, s70, s71
	s_and_b32 s56, s54, s55
	s_add_i32 s57, s55, 1
	s_add_i32 s58, s56, -2
	s_cmp_lt_u32 s58, s57
	s_cselect_b32 s62, 1.0, 0
	s_add_i32 s58, s56, -1
	s_cmp_lt_u32 s58, s57
	s_cselect_b32 s64, 1.0, 0
	s_mov_b32 s66, 1.0
	s_add_i32 s58, s56, 1
	s_cmp_lt_u32 s58, s57
	s_cselect_b32 s68, 1.0, 0
	v_pk_mul_f32 v[240:241], v[128:129], s[62:63] op_sel_hi:[1,0]
	v_lshlrev_b32_e32 v242, 16, v200
	v_and_b32_e32 v243, 0xffff0000, v200
	v_pk_fma_f32 v[232:233], v[240:241], v[242:243], v[160:161]
	v_pk_mul_f32 v[240:241], v[130:131], s[62:63] op_sel_hi:[1,0]
	v_lshlrev_b32_e32 v242, 16, v201
	v_and_b32_e32 v243, 0xffff0000, v201
	v_pk_fma_f32 v[234:235], v[240:241], v[242:243], v[162:163]
	v_pk_mul_f32 v[240:241], v[132:133], s[62:63] op_sel_hi:[1,0]
	v_lshlrev_b32_e32 v242, 16, v202
	v_and_b32_e32 v243, 0xffff0000, v202
	v_pk_fma_f32 v[236:237], v[240:241], v[242:243], v[164:165]
	v_pk_mul_f32 v[240:241], v[134:135], s[62:63] op_sel_hi:[1,0]
	v_lshlrev_b32_e32 v242, 16, v203
	v_and_b32_e32 v243, 0xffff0000, v203
	v_pk_fma_f32 v[238:239], v[240:241], v[242:243], v[166:167]
	v_pk_mul_f32 v[240:241], v[136:137], s[64:65] op_sel_hi:[1,0]
	v_lshlrev_b32_e32 v242, 16, v204
	v_and_b32_e32 v243, 0xffff0000, v204
	v_pk_fma_f32 v[232:233], v[240:241], v[242:243], v[232:233]
	v_pk_mul_f32 v[240:241], v[138:139], s[64:65] op_sel_hi:[1,0]
	v_lshlrev_b32_e32 v242, 16, v205
	v_and_b32_e32 v243, 0xffff0000, v205
	v_pk_fma_f32 v[234:235], v[240:241], v[242:243], v[234:235]
	v_pk_mul_f32 v[240:241], v[140:141], s[64:65] op_sel_hi:[1,0]
	v_lshlrev_b32_e32 v242, 16, v206
	v_and_b32_e32 v243, 0xffff0000, v206
	v_pk_fma_f32 v[236:237], v[240:241], v[242:243], v[236:237]
	v_pk_mul_f32 v[240:241], v[142:143], s[64:65] op_sel_hi:[1,0]
	v_lshlrev_b32_e32 v242, 16, v207
	v_and_b32_e32 v243, 0xffff0000, v207
	v_pk_fma_f32 v[238:239], v[240:241], v[242:243], v[238:239]
	v_pk_mul_f32 v[240:241], v[144:145], s[66:67] op_sel_hi:[1,0]
	v_lshlrev_b32_e32 v242, 16, v208
	v_and_b32_e32 v243, 0xffff0000, v208
	v_pk_fma_f32 v[232:233], v[240:241], v[242:243], v[232:233]
	v_pk_mul_f32 v[240:241], v[146:147], s[66:67] op_sel_hi:[1,0]
	v_lshlrev_b32_e32 v242, 16, v209
	v_and_b32_e32 v243, 0xffff0000, v209
	v_pk_fma_f32 v[234:235], v[240:241], v[242:243], v[234:235]
	v_pk_mul_f32 v[240:241], v[148:149], s[66:67] op_sel_hi:[1,0]
	v_lshlrev_b32_e32 v242, 16, v210
	v_and_b32_e32 v243, 0xffff0000, v210
	v_pk_fma_f32 v[236:237], v[240:241], v[242:243], v[236:237]
	v_pk_mul_f32 v[240:241], v[150:151], s[66:67] op_sel_hi:[1,0]
	v_lshlrev_b32_e32 v242, 16, v211
	v_and_b32_e32 v243, 0xffff0000, v211
	v_pk_fma_f32 v[238:239], v[240:241], v[242:243], v[238:239]
	v_pk_mul_f32 v[240:241], v[152:153], s[68:69] op_sel_hi:[1,0]
	v_lshlrev_b32_e32 v242, 16, v212
	v_and_b32_e32 v243, 0xffff0000, v212
	v_pk_fma_f32 v[232:233], v[240:241], v[242:243], v[232:233]
	v_pk_mul_f32 v[240:241], v[154:155], s[68:69] op_sel_hi:[1,0]
	v_lshlrev_b32_e32 v242, 16, v213
	v_and_b32_e32 v243, 0xffff0000, v213
	v_pk_fma_f32 v[234:235], v[240:241], v[242:243], v[234:235]
	v_pk_mul_f32 v[240:241], v[156:157], s[68:69] op_sel_hi:[1,0]
	v_lshlrev_b32_e32 v242, 16, v214
	v_and_b32_e32 v243, 0xffff0000, v214
	v_pk_fma_f32 v[236:237], v[240:241], v[242:243], v[236:237]
	v_pk_mul_f32 v[240:241], v[158:159], s[68:69] op_sel_hi:[1,0]
	v_lshlrev_b32_e32 v242, 16, v215
	v_and_b32_e32 v243, 0xffff0000, v215
	v_pk_fma_f32 v[238:239], v[240:241], v[242:243], v[238:239]
	v_cvt_pk_bf16_f32 v248, v232, v233
	v_cvt_pk_bf16_f32 v249, v234, v235
	v_cvt_pk_bf16_f32 v250, v236, v237
	v_cvt_pk_bf16_f32 v251, v238, v239
	s_lshl_b32 s58, s54, 11
	s_add_u32 s60, s52, s58
	s_addc_u32 s61, s53, 0
	global_store_dwordx4 v126, v[248:251], s[60:61]
	s_add_i32 s54, s41, 0x6c00
	s_cmp_lt_u32 s54, 0x8000
	s_cselect_b32 s55, s70, s71
	s_and_b32 s56, s54, s55
	s_add_i32 s57, s55, 1
	s_add_i32 s58, s56, -2
	s_cmp_lt_u32 s58, s57
	s_cselect_b32 s62, 1.0, 0
	s_add_i32 s58, s56, -1
	s_cmp_lt_u32 s58, s57
	s_cselect_b32 s64, 1.0, 0
	s_mov_b32 s66, 1.0
	s_add_i32 s58, s56, 1
	s_cmp_lt_u32 s58, s57
	s_cselect_b32 s68, 1.0, 0
	v_pk_mul_f32 v[240:241], v[128:129], s[62:63] op_sel_hi:[1,0]
	v_lshlrev_b32_e32 v242, 16, v216
	v_and_b32_e32 v243, 0xffff0000, v216
	v_pk_fma_f32 v[232:233], v[240:241], v[242:243], v[160:161]
	v_pk_mul_f32 v[240:241], v[130:131], s[62:63] op_sel_hi:[1,0]
	v_lshlrev_b32_e32 v242, 16, v217
	v_and_b32_e32 v243, 0xffff0000, v217
	v_pk_fma_f32 v[234:235], v[240:241], v[242:243], v[162:163]
	v_pk_mul_f32 v[240:241], v[132:133], s[62:63] op_sel_hi:[1,0]
	v_lshlrev_b32_e32 v242, 16, v218
	v_and_b32_e32 v243, 0xffff0000, v218
	v_pk_fma_f32 v[236:237], v[240:241], v[242:243], v[164:165]
	v_pk_mul_f32 v[240:241], v[134:135], s[62:63] op_sel_hi:[1,0]
	v_lshlrev_b32_e32 v242, 16, v219
	v_and_b32_e32 v243, 0xffff0000, v219
	v_pk_fma_f32 v[238:239], v[240:241], v[242:243], v[166:167]
	v_pk_mul_f32 v[240:241], v[136:137], s[64:65] op_sel_hi:[1,0]
	v_lshlrev_b32_e32 v242, 16, v220
	v_and_b32_e32 v243, 0xffff0000, v220
	v_pk_fma_f32 v[232:233], v[240:241], v[242:243], v[232:233]
	v_pk_mul_f32 v[240:241], v[138:139], s[64:65] op_sel_hi:[1,0]
	v_lshlrev_b32_e32 v242, 16, v221
	v_and_b32_e32 v243, 0xffff0000, v221
	v_pk_fma_f32 v[234:235], v[240:241], v[242:243], v[234:235]
	v_pk_mul_f32 v[240:241], v[140:141], s[64:65] op_sel_hi:[1,0]
	v_lshlrev_b32_e32 v242, 16, v222
	v_and_b32_e32 v243, 0xffff0000, v222
	v_pk_fma_f32 v[236:237], v[240:241], v[242:243], v[236:237]
	v_pk_mul_f32 v[240:241], v[142:143], s[64:65] op_sel_hi:[1,0]
	v_lshlrev_b32_e32 v242, 16, v223
	v_and_b32_e32 v243, 0xffff0000, v223
	v_pk_fma_f32 v[238:239], v[240:241], v[242:243], v[238:239]
	v_pk_mul_f32 v[240:241], v[144:145], s[66:67] op_sel_hi:[1,0]
	v_lshlrev_b32_e32 v242, 16, v224
	v_and_b32_e32 v243, 0xffff0000, v224
	v_pk_fma_f32 v[232:233], v[240:241], v[242:243], v[232:233]
	v_pk_mul_f32 v[240:241], v[146:147], s[66:67] op_sel_hi:[1,0]
	v_lshlrev_b32_e32 v242, 16, v225
	v_and_b32_e32 v243, 0xffff0000, v225
	v_pk_fma_f32 v[234:235], v[240:241], v[242:243], v[234:235]
	v_pk_mul_f32 v[240:241], v[148:149], s[66:67] op_sel_hi:[1,0]
	v_lshlrev_b32_e32 v242, 16, v226
	v_and_b32_e32 v243, 0xffff0000, v226
	v_pk_fma_f32 v[236:237], v[240:241], v[242:243], v[236:237]
	v_pk_mul_f32 v[240:241], v[150:151], s[66:67] op_sel_hi:[1,0]
	v_lshlrev_b32_e32 v242, 16, v227
	v_and_b32_e32 v243, 0xffff0000, v227
	v_pk_fma_f32 v[238:239], v[240:241], v[242:243], v[238:239]
	v_pk_mul_f32 v[240:241], v[152:153], s[68:69] op_sel_hi:[1,0]
	v_lshlrev_b32_e32 v242, 16, v228
	v_and_b32_e32 v243, 0xffff0000, v228
	v_pk_fma_f32 v[232:233], v[240:241], v[242:243], v[232:233]
	v_pk_mul_f32 v[240:241], v[154:155], s[68:69] op_sel_hi:[1,0]
	v_lshlrev_b32_e32 v242, 16, v229
	v_and_b32_e32 v243, 0xffff0000, v229
	v_pk_fma_f32 v[234:235], v[240:241], v[242:243], v[234:235]
	v_pk_mul_f32 v[240:241], v[156:157], s[68:69] op_sel_hi:[1,0]
	v_lshlrev_b32_e32 v242, 16, v230
	v_and_b32_e32 v243, 0xffff0000, v230
	v_pk_fma_f32 v[236:237], v[240:241], v[242:243], v[236:237]
	v_pk_mul_f32 v[240:241], v[158:159], s[68:69] op_sel_hi:[1,0]
	v_lshlrev_b32_e32 v242, 16, v231
	v_and_b32_e32 v243, 0xffff0000, v231
	v_pk_fma_f32 v[238:239], v[240:241], v[242:243], v[238:239]
	v_cvt_pk_bf16_f32 v248, v232, v233
	v_cvt_pk_bf16_f32 v249, v234, v235
	v_cvt_pk_bf16_f32 v250, v236, v237
	v_cvt_pk_bf16_f32 v251, v238, v239
	s_lshl_b32 s58, s54, 11
	s_add_u32 s60, s52, s58
	s_addc_u32 s61, s53, 0
	global_store_dwordx4 v126, v[248:251], s[60:61]
	s_add_i32 s54, s41, 0x8000
	s_cmp_lt_u32 s54, 0x8000
	s_cselect_b32 s55, s70, s71
	s_and_b32 s56, s54, s55
	s_add_i32 s57, s55, 1
	s_add_i32 s58, s56, -2
	s_cmp_lt_u32 s58, s57
	s_cselect_b32 s58, -2, 0
	s_add_i32 s58, s54, s58
	s_mul_i32 s58, s58, 0x5a00
	s_add_u32 s60, s50, s58
	s_addc_u32 s61, s51, 0
	global_load_dwordx4 v[200:203], v126, s[60:61]
	s_add_i32 s58, s56, -1
	s_cmp_lt_u32 s58, s57
	s_cselect_b32 s58, -1, 0
	s_add_i32 s58, s54, s58
	s_mul_i32 s58, s58, 0x5a00
	s_add_u32 s60, s50, s58
	s_addc_u32 s61, s51, 0
	global_load_dwordx4 v[204:207], v126, s[60:61]
	s_mul_i32 s58, s54, 0x5a00
	s_add_u32 s60, s50, s58
	s_addc_u32 s61, s51, 0
	global_load_dwordx4 v[208:211], v126, s[60:61]
	s_add_i32 s58, s56, 1
	s_cmp_lt_u32 s58, s57
	s_cselect_b32 s58, 1, 0
	s_add_i32 s58, s54, s58
	s_mul_i32 s58, s58, 0x5a00
	s_add_u32 s60, s50, s58
	s_addc_u32 s61, s51, 0
	global_load_dwordx4 v[212:215], v126, s[60:61]
	s_add_i32 s54, s41, 0x8400
	s_cmp_lt_u32 s54, 0x8000
	s_cselect_b32 s55, s70, s71
	s_and_b32 s56, s54, s55
	s_add_i32 s57, s55, 1
	s_add_i32 s58, s56, -2
	s_cmp_lt_u32 s58, s57
	s_cselect_b32 s58, -2, 0
	s_add_i32 s58, s54, s58
	s_mul_i32 s58, s58, 0x5a00
	s_add_u32 s60, s50, s58
	s_addc_u32 s61, s51, 0
	global_load_dwordx4 v[216:219], v126, s[60:61]
	s_add_i32 s58, s56, -1
	s_cmp_lt_u32 s58, s57
	s_cselect_b32 s58, -1, 0
	s_add_i32 s58, s54, s58
	s_mul_i32 s58, s58, 0x5a00
	s_add_u32 s60, s50, s58
	s_addc_u32 s61, s51, 0
	global_load_dwordx4 v[220:223], v126, s[60:61]
	s_mul_i32 s58, s54, 0x5a00
	s_add_u32 s60, s50, s58
	s_addc_u32 s61, s51, 0
	global_load_dwordx4 v[224:227], v126, s[60:61]
	s_add_i32 s58, s56, 1
	s_cmp_lt_u32 s58, s57
	s_cselect_b32 s58, 1, 0
	s_add_i32 s58, s54, s58
	s_mul_i32 s58, s58, 0x5a00
	s_add_u32 s60, s50, s58
	s_addc_u32 s61, s51, 0
	global_load_dwordx4 v[228:231], v126, s[60:61]
	s_waitcnt vmcnt(20)
	s_add_i32 s54, s41, 0x7000
	s_cmp_lt_u32 s54, 0x8000
	s_cselect_b32 s55, s70, s71
	s_and_b32 s56, s54, s55
	s_add_i32 s57, s55, 1
	s_add_i32 s58, s56, -2
	s_cmp_lt_u32 s58, s57
	s_cselect_b32 s62, 1.0, 0
	s_add_i32 s58, s56, -1
	s_cmp_lt_u32 s58, s57
	s_cselect_b32 s64, 1.0, 0
	s_mov_b32 s66, 1.0
	s_add_i32 s58, s56, 1
	s_cmp_lt_u32 s58, s57
	s_cselect_b32 s68, 1.0, 0
	v_pk_mul_f32 v[240:241], v[128:129], s[62:63] op_sel_hi:[1,0]
	v_lshlrev_b32_e32 v242, 16, v40
	v_and_b32_e32 v243, 0xffff0000, v40
	v_pk_fma_f32 v[232:233], v[240:241], v[242:243], v[160:161]
	v_pk_mul_f32 v[240:241], v[130:131], s[62:63] op_sel_hi:[1,0]
	v_lshlrev_b32_e32 v242, 16, v41
	v_and_b32_e32 v243, 0xffff0000, v41
	v_pk_fma_f32 v[234:235], v[240:241], v[242:243], v[162:163]
	v_pk_mul_f32 v[240:241], v[132:133], s[62:63] op_sel_hi:[1,0]
	v_lshlrev_b32_e32 v242, 16, v42
	v_and_b32_e32 v243, 0xffff0000, v42
	v_pk_fma_f32 v[236:237], v[240:241], v[242:243], v[164:165]
	v_pk_mul_f32 v[240:241], v[134:135], s[62:63] op_sel_hi:[1,0]
	v_lshlrev_b32_e32 v242, 16, v43
	v_and_b32_e32 v243, 0xffff0000, v43
	v_pk_fma_f32 v[238:239], v[240:241], v[242:243], v[166:167]
	v_pk_mul_f32 v[240:241], v[136:137], s[64:65] op_sel_hi:[1,0]
	v_lshlrev_b32_e32 v242, 16, v44
	v_and_b32_e32 v243, 0xffff0000, v44
	v_pk_fma_f32 v[232:233], v[240:241], v[242:243], v[232:233]
	v_pk_mul_f32 v[240:241], v[138:139], s[64:65] op_sel_hi:[1,0]
	v_lshlrev_b32_e32 v242, 16, v45
	v_and_b32_e32 v243, 0xffff0000, v45
	v_pk_fma_f32 v[234:235], v[240:241], v[242:243], v[234:235]
	v_pk_mul_f32 v[240:241], v[140:141], s[64:65] op_sel_hi:[1,0]
	v_lshlrev_b32_e32 v242, 16, v46
	v_and_b32_e32 v243, 0xffff0000, v46
	v_pk_fma_f32 v[236:237], v[240:241], v[242:243], v[236:237]
	v_pk_mul_f32 v[240:241], v[142:143], s[64:65] op_sel_hi:[1,0]
	v_lshlrev_b32_e32 v242, 16, v47
	v_and_b32_e32 v243, 0xffff0000, v47
	v_pk_fma_f32 v[238:239], v[240:241], v[242:243], v[238:239]
	v_pk_mul_f32 v[240:241], v[144:145], s[66:67] op_sel_hi:[1,0]
	v_lshlrev_b32_e32 v242, 16, v48
	v_and_b32_e32 v243, 0xffff0000, v48
	v_pk_fma_f32 v[232:233], v[240:241], v[242:243], v[232:233]
	v_pk_mul_f32 v[240:241], v[146:147], s[66:67] op_sel_hi:[1,0]
	v_lshlrev_b32_e32 v242, 16, v49
	v_and_b32_e32 v243, 0xffff0000, v49
	v_pk_fma_f32 v[234:235], v[240:241], v[242:243], v[234:235]
	v_pk_mul_f32 v[240:241], v[148:149], s[66:67] op_sel_hi:[1,0]
	v_lshlrev_b32_e32 v242, 16, v50
	v_and_b32_e32 v243, 0xffff0000, v50
	v_pk_fma_f32 v[236:237], v[240:241], v[242:243], v[236:237]
	v_pk_mul_f32 v[240:241], v[150:151], s[66:67] op_sel_hi:[1,0]
	v_lshlrev_b32_e32 v242, 16, v51
	v_and_b32_e32 v243, 0xffff0000, v51
	v_pk_fma_f32 v[238:239], v[240:241], v[242:243], v[238:239]
	v_pk_mul_f32 v[240:241], v[152:153], s[68:69] op_sel_hi:[1,0]
	v_lshlrev_b32_e32 v242, 16, v52
	v_and_b32_e32 v243, 0xffff0000, v52
	v_pk_fma_f32 v[232:233], v[240:241], v[242:243], v[232:233]
	v_pk_mul_f32 v[240:241], v[154:155], s[68:69] op_sel_hi:[1,0]
	v_lshlrev_b32_e32 v242, 16, v53
	v_and_b32_e32 v243, 0xffff0000, v53
	v_pk_fma_f32 v[234:235], v[240:241], v[242:243], v[234:235]
	v_pk_mul_f32 v[240:241], v[156:157], s[68:69] op_sel_hi:[1,0]
	v_lshlrev_b32_e32 v242, 16, v54
	v_and_b32_e32 v243, 0xffff0000, v54
	v_pk_fma_f32 v[236:237], v[240:241], v[242:243], v[236:237]
	v_pk_mul_f32 v[240:241], v[158:159], s[68:69] op_sel_hi:[1,0]
	v_lshlrev_b32_e32 v242, 16, v55
	v_and_b32_e32 v243, 0xffff0000, v55
	v_pk_fma_f32 v[238:239], v[240:241], v[242:243], v[238:239]
	v_cvt_pk_bf16_f32 v248, v232, v233
	v_cvt_pk_bf16_f32 v249, v234, v235
	v_cvt_pk_bf16_f32 v250, v236, v237
	v_cvt_pk_bf16_f32 v251, v238, v239
	s_lshl_b32 s58, s54, 11
	s_add_u32 s60, s52, s58
	s_addc_u32 s61, s53, 0
	global_store_dwordx4 v126, v[248:251], s[60:61]
	s_add_i32 s54, s41, 0x7400
	s_cmp_lt_u32 s54, 0x8000
	s_cselect_b32 s55, s70, s71
	s_and_b32 s56, s54, s55
	s_add_i32 s57, s55, 1
	s_add_i32 s58, s56, -2
	s_cmp_lt_u32 s58, s57
	s_cselect_b32 s62, 1.0, 0
	s_add_i32 s58, s56, -1
	s_cmp_lt_u32 s58, s57
	s_cselect_b32 s64, 1.0, 0
	s_mov_b32 s66, 1.0
	s_add_i32 s58, s56, 1
	s_cmp_lt_u32 s58, s57
	s_cselect_b32 s68, 1.0, 0
	v_pk_mul_f32 v[240:241], v[128:129], s[62:63] op_sel_hi:[1,0]
	v_lshlrev_b32_e32 v242, 16, v56
	v_and_b32_e32 v243, 0xffff0000, v56
	v_pk_fma_f32 v[232:233], v[240:241], v[242:243], v[160:161]
	v_pk_mul_f32 v[240:241], v[130:131], s[62:63] op_sel_hi:[1,0]
	v_lshlrev_b32_e32 v242, 16, v57
	v_and_b32_e32 v243, 0xffff0000, v57
	v_pk_fma_f32 v[234:235], v[240:241], v[242:243], v[162:163]
	v_pk_mul_f32 v[240:241], v[132:133], s[62:63] op_sel_hi:[1,0]
	v_lshlrev_b32_e32 v242, 16, v58
	v_and_b32_e32 v243, 0xffff0000, v58
	v_pk_fma_f32 v[236:237], v[240:241], v[242:243], v[164:165]
	v_pk_mul_f32 v[240:241], v[134:135], s[62:63] op_sel_hi:[1,0]
	v_lshlrev_b32_e32 v242, 16, v59
	v_and_b32_e32 v243, 0xffff0000, v59
	v_pk_fma_f32 v[238:239], v[240:241], v[242:243], v[166:167]
	v_pk_mul_f32 v[240:241], v[136:137], s[64:65] op_sel_hi:[1,0]
	v_lshlrev_b32_e32 v242, 16, v60
	v_and_b32_e32 v243, 0xffff0000, v60
	v_pk_fma_f32 v[232:233], v[240:241], v[242:243], v[232:233]
	v_pk_mul_f32 v[240:241], v[138:139], s[64:65] op_sel_hi:[1,0]
	v_lshlrev_b32_e32 v242, 16, v61
	v_and_b32_e32 v243, 0xffff0000, v61
	v_pk_fma_f32 v[234:235], v[240:241], v[242:243], v[234:235]
	v_pk_mul_f32 v[240:241], v[140:141], s[64:65] op_sel_hi:[1,0]
	v_lshlrev_b32_e32 v242, 16, v62
	v_and_b32_e32 v243, 0xffff0000, v62
	v_pk_fma_f32 v[236:237], v[240:241], v[242:243], v[236:237]
	v_pk_mul_f32 v[240:241], v[142:143], s[64:65] op_sel_hi:[1,0]
	v_lshlrev_b32_e32 v242, 16, v63
	v_and_b32_e32 v243, 0xffff0000, v63
	v_pk_fma_f32 v[238:239], v[240:241], v[242:243], v[238:239]
	v_pk_mul_f32 v[240:241], v[144:145], s[66:67] op_sel_hi:[1,0]
	v_lshlrev_b32_e32 v242, 16, v64
	v_and_b32_e32 v243, 0xffff0000, v64
	v_pk_fma_f32 v[232:233], v[240:241], v[242:243], v[232:233]
	v_pk_mul_f32 v[240:241], v[146:147], s[66:67] op_sel_hi:[1,0]
	v_lshlrev_b32_e32 v242, 16, v65
	v_and_b32_e32 v243, 0xffff0000, v65
	v_pk_fma_f32 v[234:235], v[240:241], v[242:243], v[234:235]
	v_pk_mul_f32 v[240:241], v[148:149], s[66:67] op_sel_hi:[1,0]
	v_lshlrev_b32_e32 v242, 16, v66
	v_and_b32_e32 v243, 0xffff0000, v66
	v_pk_fma_f32 v[236:237], v[240:241], v[242:243], v[236:237]
	v_pk_mul_f32 v[240:241], v[150:151], s[66:67] op_sel_hi:[1,0]
	v_lshlrev_b32_e32 v242, 16, v67
	v_and_b32_e32 v243, 0xffff0000, v67
	v_pk_fma_f32 v[238:239], v[240:241], v[242:243], v[238:239]
	v_pk_mul_f32 v[240:241], v[152:153], s[68:69] op_sel_hi:[1,0]
	v_lshlrev_b32_e32 v242, 16, v68
	v_and_b32_e32 v243, 0xffff0000, v68
	v_pk_fma_f32 v[232:233], v[240:241], v[242:243], v[232:233]
	v_pk_mul_f32 v[240:241], v[154:155], s[68:69] op_sel_hi:[1,0]
	v_lshlrev_b32_e32 v242, 16, v69
	v_and_b32_e32 v243, 0xffff0000, v69
	v_pk_fma_f32 v[234:235], v[240:241], v[242:243], v[234:235]
	v_pk_mul_f32 v[240:241], v[156:157], s[68:69] op_sel_hi:[1,0]
	v_lshlrev_b32_e32 v242, 16, v70
	v_and_b32_e32 v243, 0xffff0000, v70
	v_pk_fma_f32 v[236:237], v[240:241], v[242:243], v[236:237]
	v_pk_mul_f32 v[240:241], v[158:159], s[68:69] op_sel_hi:[1,0]
	v_lshlrev_b32_e32 v242, 16, v71
	v_and_b32_e32 v243, 0xffff0000, v71
	v_pk_fma_f32 v[238:239], v[240:241], v[242:243], v[238:239]
	v_cvt_pk_bf16_f32 v248, v232, v233
	v_cvt_pk_bf16_f32 v249, v234, v235
	v_cvt_pk_bf16_f32 v250, v236, v237
	v_cvt_pk_bf16_f32 v251, v238, v239
	s_lshl_b32 s58, s54, 11
	s_add_u32 s60, s52, s58
	s_addc_u32 s61, s53, 0
	global_store_dwordx4 v126, v[248:251], s[60:61]
	s_waitcnt vmcnt(12)
	s_add_i32 s54, s41, 0x7800
	s_cmp_lt_u32 s54, 0x8000
	s_cselect_b32 s55, s70, s71
	s_and_b32 s56, s54, s55
	s_add_i32 s57, s55, 1
	s_add_i32 s58, s56, -2
	s_cmp_lt_u32 s58, s57
	s_cselect_b32 s62, 1.0, 0
	s_add_i32 s58, s56, -1
	s_cmp_lt_u32 s58, s57
	s_cselect_b32 s64, 1.0, 0
	s_mov_b32 s66, 1.0
	s_add_i32 s58, s56, 1
	s_cmp_lt_u32 s58, s57
	s_cselect_b32 s68, 1.0, 0
	v_pk_mul_f32 v[240:241], v[128:129], s[62:63] op_sel_hi:[1,0]
	v_lshlrev_b32_e32 v242, 16, v168
	v_and_b32_e32 v243, 0xffff0000, v168
	v_pk_fma_f32 v[232:233], v[240:241], v[242:243], v[160:161]
	v_pk_mul_f32 v[240:241], v[130:131], s[62:63] op_sel_hi:[1,0]
	v_lshlrev_b32_e32 v242, 16, v169
	v_and_b32_e32 v243, 0xffff0000, v169
	v_pk_fma_f32 v[234:235], v[240:241], v[242:243], v[162:163]
	v_pk_mul_f32 v[240:241], v[132:133], s[62:63] op_sel_hi:[1,0]
	v_lshlrev_b32_e32 v242, 16, v170
	v_and_b32_e32 v243, 0xffff0000, v170
	v_pk_fma_f32 v[236:237], v[240:241], v[242:243], v[164:165]
	v_pk_mul_f32 v[240:241], v[134:135], s[62:63] op_sel_hi:[1,0]
	v_lshlrev_b32_e32 v242, 16, v171
	v_and_b32_e32 v243, 0xffff0000, v171
	v_pk_fma_f32 v[238:239], v[240:241], v[242:243], v[166:167]
	v_pk_mul_f32 v[240:241], v[136:137], s[64:65] op_sel_hi:[1,0]
	v_lshlrev_b32_e32 v242, 16, v172
	v_and_b32_e32 v243, 0xffff0000, v172
	v_pk_fma_f32 v[232:233], v[240:241], v[242:243], v[232:233]
	v_pk_mul_f32 v[240:241], v[138:139], s[64:65] op_sel_hi:[1,0]
	v_lshlrev_b32_e32 v242, 16, v173
	v_and_b32_e32 v243, 0xffff0000, v173
	v_pk_fma_f32 v[234:235], v[240:241], v[242:243], v[234:235]
	v_pk_mul_f32 v[240:241], v[140:141], s[64:65] op_sel_hi:[1,0]
	v_lshlrev_b32_e32 v242, 16, v174
	v_and_b32_e32 v243, 0xffff0000, v174
	v_pk_fma_f32 v[236:237], v[240:241], v[242:243], v[236:237]
	v_pk_mul_f32 v[240:241], v[142:143], s[64:65] op_sel_hi:[1,0]
	v_lshlrev_b32_e32 v242, 16, v175
	v_and_b32_e32 v243, 0xffff0000, v175
	v_pk_fma_f32 v[238:239], v[240:241], v[242:243], v[238:239]
	v_pk_mul_f32 v[240:241], v[144:145], s[66:67] op_sel_hi:[1,0]
	v_lshlrev_b32_e32 v242, 16, v176
	v_and_b32_e32 v243, 0xffff0000, v176
	v_pk_fma_f32 v[232:233], v[240:241], v[242:243], v[232:233]
	v_pk_mul_f32 v[240:241], v[146:147], s[66:67] op_sel_hi:[1,0]
	v_lshlrev_b32_e32 v242, 16, v177
	v_and_b32_e32 v243, 0xffff0000, v177
	v_pk_fma_f32 v[234:235], v[240:241], v[242:243], v[234:235]
	v_pk_mul_f32 v[240:241], v[148:149], s[66:67] op_sel_hi:[1,0]
	v_lshlrev_b32_e32 v242, 16, v178
	v_and_b32_e32 v243, 0xffff0000, v178
	v_pk_fma_f32 v[236:237], v[240:241], v[242:243], v[236:237]
	v_pk_mul_f32 v[240:241], v[150:151], s[66:67] op_sel_hi:[1,0]
	v_lshlrev_b32_e32 v242, 16, v179
	v_and_b32_e32 v243, 0xffff0000, v179
	v_pk_fma_f32 v[238:239], v[240:241], v[242:243], v[238:239]
	v_pk_mul_f32 v[240:241], v[152:153], s[68:69] op_sel_hi:[1,0]
	v_lshlrev_b32_e32 v242, 16, v180
	v_and_b32_e32 v243, 0xffff0000, v180
	v_pk_fma_f32 v[232:233], v[240:241], v[242:243], v[232:233]
	v_pk_mul_f32 v[240:241], v[154:155], s[68:69] op_sel_hi:[1,0]
	v_lshlrev_b32_e32 v242, 16, v181
	v_and_b32_e32 v243, 0xffff0000, v181
	v_pk_fma_f32 v[234:235], v[240:241], v[242:243], v[234:235]
	v_pk_mul_f32 v[240:241], v[156:157], s[68:69] op_sel_hi:[1,0]
	v_lshlrev_b32_e32 v242, 16, v182
	v_and_b32_e32 v243, 0xffff0000, v182
	v_pk_fma_f32 v[236:237], v[240:241], v[242:243], v[236:237]
	v_pk_mul_f32 v[240:241], v[158:159], s[68:69] op_sel_hi:[1,0]
	v_lshlrev_b32_e32 v242, 16, v183
	v_and_b32_e32 v243, 0xffff0000, v183
	v_pk_fma_f32 v[238:239], v[240:241], v[242:243], v[238:239]
	v_cvt_pk_bf16_f32 v248, v232, v233
	v_cvt_pk_bf16_f32 v249, v234, v235
	v_cvt_pk_bf16_f32 v250, v236, v237
	v_cvt_pk_bf16_f32 v251, v238, v239
	s_lshl_b32 s58, s54, 11
	s_add_u32 s60, s52, s58
	s_addc_u32 s61, s53, 0
	global_store_dwordx4 v126, v[248:251], s[60:61]
	s_add_i32 s54, s41, 0x7c00
	s_cmp_lt_u32 s54, 0x8000
	s_cselect_b32 s55, s70, s71
	s_and_b32 s56, s54, s55
	s_add_i32 s57, s55, 1
	s_add_i32 s58, s56, -2
	s_cmp_lt_u32 s58, s57
	s_cselect_b32 s62, 1.0, 0
	s_add_i32 s58, s56, -1
	s_cmp_lt_u32 s58, s57
	s_cselect_b32 s64, 1.0, 0
	s_mov_b32 s66, 1.0
	s_add_i32 s58, s56, 1
	s_cmp_lt_u32 s58, s57
	s_cselect_b32 s68, 1.0, 0
	v_pk_mul_f32 v[240:241], v[128:129], s[62:63] op_sel_hi:[1,0]
	v_lshlrev_b32_e32 v242, 16, v184
	v_and_b32_e32 v243, 0xffff0000, v184
	v_pk_fma_f32 v[232:233], v[240:241], v[242:243], v[160:161]
	v_pk_mul_f32 v[240:241], v[130:131], s[62:63] op_sel_hi:[1,0]
	v_lshlrev_b32_e32 v242, 16, v185
	v_and_b32_e32 v243, 0xffff0000, v185
	v_pk_fma_f32 v[234:235], v[240:241], v[242:243], v[162:163]
	v_pk_mul_f32 v[240:241], v[132:133], s[62:63] op_sel_hi:[1,0]
	v_lshlrev_b32_e32 v242, 16, v186
	v_and_b32_e32 v243, 0xffff0000, v186
	v_pk_fma_f32 v[236:237], v[240:241], v[242:243], v[164:165]
	v_pk_mul_f32 v[240:241], v[134:135], s[62:63] op_sel_hi:[1,0]
	v_lshlrev_b32_e32 v242, 16, v187
	v_and_b32_e32 v243, 0xffff0000, v187
	v_pk_fma_f32 v[238:239], v[240:241], v[242:243], v[166:167]
	v_pk_mul_f32 v[240:241], v[136:137], s[64:65] op_sel_hi:[1,0]
	v_lshlrev_b32_e32 v242, 16, v188
	v_and_b32_e32 v243, 0xffff0000, v188
	v_pk_fma_f32 v[232:233], v[240:241], v[242:243], v[232:233]
	v_pk_mul_f32 v[240:241], v[138:139], s[64:65] op_sel_hi:[1,0]
	v_lshlrev_b32_e32 v242, 16, v189
	v_and_b32_e32 v243, 0xffff0000, v189
	v_pk_fma_f32 v[234:235], v[240:241], v[242:243], v[234:235]
	v_pk_mul_f32 v[240:241], v[140:141], s[64:65] op_sel_hi:[1,0]
	v_lshlrev_b32_e32 v242, 16, v190
	v_and_b32_e32 v243, 0xffff0000, v190
	v_pk_fma_f32 v[236:237], v[240:241], v[242:243], v[236:237]
	v_pk_mul_f32 v[240:241], v[142:143], s[64:65] op_sel_hi:[1,0]
	v_lshlrev_b32_e32 v242, 16, v191
	v_and_b32_e32 v243, 0xffff0000, v191
	v_pk_fma_f32 v[238:239], v[240:241], v[242:243], v[238:239]
	v_pk_mul_f32 v[240:241], v[144:145], s[66:67] op_sel_hi:[1,0]
	v_lshlrev_b32_e32 v242, 16, v192
	v_and_b32_e32 v243, 0xffff0000, v192
	v_pk_fma_f32 v[232:233], v[240:241], v[242:243], v[232:233]
	v_pk_mul_f32 v[240:241], v[146:147], s[66:67] op_sel_hi:[1,0]
	v_lshlrev_b32_e32 v242, 16, v193
	v_and_b32_e32 v243, 0xffff0000, v193
	v_pk_fma_f32 v[234:235], v[240:241], v[242:243], v[234:235]
	v_pk_mul_f32 v[240:241], v[148:149], s[66:67] op_sel_hi:[1,0]
	v_lshlrev_b32_e32 v242, 16, v194
	v_and_b32_e32 v243, 0xffff0000, v194
	v_pk_fma_f32 v[236:237], v[240:241], v[242:243], v[236:237]
	v_pk_mul_f32 v[240:241], v[150:151], s[66:67] op_sel_hi:[1,0]
	v_lshlrev_b32_e32 v242, 16, v195
	v_and_b32_e32 v243, 0xffff0000, v195
	v_pk_fma_f32 v[238:239], v[240:241], v[242:243], v[238:239]
	v_pk_mul_f32 v[240:241], v[152:153], s[68:69] op_sel_hi:[1,0]
	v_lshlrev_b32_e32 v242, 16, v196
	v_and_b32_e32 v243, 0xffff0000, v196
	v_pk_fma_f32 v[232:233], v[240:241], v[242:243], v[232:233]
	v_pk_mul_f32 v[240:241], v[154:155], s[68:69] op_sel_hi:[1,0]
	v_lshlrev_b32_e32 v242, 16, v197
	v_and_b32_e32 v243, 0xffff0000, v197
	v_pk_fma_f32 v[234:235], v[240:241], v[242:243], v[234:235]
	v_pk_mul_f32 v[240:241], v[156:157], s[68:69] op_sel_hi:[1,0]
	v_lshlrev_b32_e32 v242, 16, v198
	v_and_b32_e32 v243, 0xffff0000, v198
	v_pk_fma_f32 v[236:237], v[240:241], v[242:243], v[236:237]
	v_pk_mul_f32 v[240:241], v[158:159], s[68:69] op_sel_hi:[1,0]
	v_lshlrev_b32_e32 v242, 16, v199
	v_and_b32_e32 v243, 0xffff0000, v199
	v_pk_fma_f32 v[238:239], v[240:241], v[242:243], v[238:239]
	v_cvt_pk_bf16_f32 v248, v232, v233
	v_cvt_pk_bf16_f32 v249, v234, v235
	v_cvt_pk_bf16_f32 v250, v236, v237
	v_cvt_pk_bf16_f32 v251, v238, v239
	s_lshl_b32 s58, s54, 11
	s_add_u32 s60, s52, s58
	s_addc_u32 s61, s53, 0
	global_store_dwordx4 v126, v[248:251], s[60:61]
	s_waitcnt vmcnt(4)
	s_add_i32 s54, s41, 0x8000
	s_cmp_lt_u32 s54, 0x8000
	s_cselect_b32 s55, s70, s71
	s_and_b32 s56, s54, s55
	s_add_i32 s57, s55, 1
	s_add_i32 s58, s56, -2
	s_cmp_lt_u32 s58, s57
	s_cselect_b32 s62, 1.0, 0
	s_add_i32 s58, s56, -1
	s_cmp_lt_u32 s58, s57
	s_cselect_b32 s64, 1.0, 0
	s_mov_b32 s66, 1.0
	s_add_i32 s58, s56, 1
	s_cmp_lt_u32 s58, s57
	s_cselect_b32 s68, 1.0, 0
	v_pk_mul_f32 v[240:241], v[128:129], s[62:63] op_sel_hi:[1,0]
	v_lshlrev_b32_e32 v242, 16, v200
	v_and_b32_e32 v243, 0xffff0000, v200
	v_pk_fma_f32 v[232:233], v[240:241], v[242:243], v[160:161]
	v_pk_mul_f32 v[240:241], v[130:131], s[62:63] op_sel_hi:[1,0]
	v_lshlrev_b32_e32 v242, 16, v201
	v_and_b32_e32 v243, 0xffff0000, v201
	v_pk_fma_f32 v[234:235], v[240:241], v[242:243], v[162:163]
	v_pk_mul_f32 v[240:241], v[132:133], s[62:63] op_sel_hi:[1,0]
	v_lshlrev_b32_e32 v242, 16, v202
	v_and_b32_e32 v243, 0xffff0000, v202
	v_pk_fma_f32 v[236:237], v[240:241], v[242:243], v[164:165]
	v_pk_mul_f32 v[240:241], v[134:135], s[62:63] op_sel_hi:[1,0]
	v_lshlrev_b32_e32 v242, 16, v203
	v_and_b32_e32 v243, 0xffff0000, v203
	v_pk_fma_f32 v[238:239], v[240:241], v[242:243], v[166:167]
	v_pk_mul_f32 v[240:241], v[136:137], s[64:65] op_sel_hi:[1,0]
	v_lshlrev_b32_e32 v242, 16, v204
	v_and_b32_e32 v243, 0xffff0000, v204
	v_pk_fma_f32 v[232:233], v[240:241], v[242:243], v[232:233]
	v_pk_mul_f32 v[240:241], v[138:139], s[64:65] op_sel_hi:[1,0]
	v_lshlrev_b32_e32 v242, 16, v205
	v_and_b32_e32 v243, 0xffff0000, v205
	v_pk_fma_f32 v[234:235], v[240:241], v[242:243], v[234:235]
	v_pk_mul_f32 v[240:241], v[140:141], s[64:65] op_sel_hi:[1,0]
	v_lshlrev_b32_e32 v242, 16, v206
	v_and_b32_e32 v243, 0xffff0000, v206
	v_pk_fma_f32 v[236:237], v[240:241], v[242:243], v[236:237]
	v_pk_mul_f32 v[240:241], v[142:143], s[64:65] op_sel_hi:[1,0]
	v_lshlrev_b32_e32 v242, 16, v207
	v_and_b32_e32 v243, 0xffff0000, v207
	v_pk_fma_f32 v[238:239], v[240:241], v[242:243], v[238:239]
	v_pk_mul_f32 v[240:241], v[144:145], s[66:67] op_sel_hi:[1,0]
	v_lshlrev_b32_e32 v242, 16, v208
	v_and_b32_e32 v243, 0xffff0000, v208
	v_pk_fma_f32 v[232:233], v[240:241], v[242:243], v[232:233]
	v_pk_mul_f32 v[240:241], v[146:147], s[66:67] op_sel_hi:[1,0]
	v_lshlrev_b32_e32 v242, 16, v209
	v_and_b32_e32 v243, 0xffff0000, v209
	v_pk_fma_f32 v[234:235], v[240:241], v[242:243], v[234:235]
	v_pk_mul_f32 v[240:241], v[148:149], s[66:67] op_sel_hi:[1,0]
	v_lshlrev_b32_e32 v242, 16, v210
	v_and_b32_e32 v243, 0xffff0000, v210
	v_pk_fma_f32 v[236:237], v[240:241], v[242:243], v[236:237]
	v_pk_mul_f32 v[240:241], v[150:151], s[66:67] op_sel_hi:[1,0]
	v_lshlrev_b32_e32 v242, 16, v211
	v_and_b32_e32 v243, 0xffff0000, v211
	v_pk_fma_f32 v[238:239], v[240:241], v[242:243], v[238:239]
	v_pk_mul_f32 v[240:241], v[152:153], s[68:69] op_sel_hi:[1,0]
	v_lshlrev_b32_e32 v242, 16, v212
	v_and_b32_e32 v243, 0xffff0000, v212
	v_pk_fma_f32 v[232:233], v[240:241], v[242:243], v[232:233]
	v_pk_mul_f32 v[240:241], v[154:155], s[68:69] op_sel_hi:[1,0]
	v_lshlrev_b32_e32 v242, 16, v213
	v_and_b32_e32 v243, 0xffff0000, v213
	v_pk_fma_f32 v[234:235], v[240:241], v[242:243], v[234:235]
	v_pk_mul_f32 v[240:241], v[156:157], s[68:69] op_sel_hi:[1,0]
	v_lshlrev_b32_e32 v242, 16, v214
	v_and_b32_e32 v243, 0xffff0000, v214
	v_pk_fma_f32 v[236:237], v[240:241], v[242:243], v[236:237]
	v_pk_mul_f32 v[240:241], v[158:159], s[68:69] op_sel_hi:[1,0]
	v_lshlrev_b32_e32 v242, 16, v215
	v_and_b32_e32 v243, 0xffff0000, v215
	v_pk_fma_f32 v[238:239], v[240:241], v[242:243], v[238:239]
	v_cvt_pk_bf16_f32 v248, v232, v233
	v_cvt_pk_bf16_f32 v249, v234, v235
	v_cvt_pk_bf16_f32 v250, v236, v237
	v_cvt_pk_bf16_f32 v251, v238, v239
	s_lshl_b32 s58, s54, 11
	s_add_u32 s60, s52, s58
	s_addc_u32 s61, s53, 0
	global_store_dwordx4 v126, v[248:251], s[60:61]
	s_add_i32 s54, s41, 0x8400
	s_cmp_lt_u32 s54, 0x8000
	s_cselect_b32 s55, s70, s71
	s_and_b32 s56, s54, s55
	s_add_i32 s57, s55, 1
	s_add_i32 s58, s56, -2
	s_cmp_lt_u32 s58, s57
	s_cselect_b32 s62, 1.0, 0
	s_add_i32 s58, s56, -1
	s_cmp_lt_u32 s58, s57
	s_cselect_b32 s64, 1.0, 0
	s_mov_b32 s66, 1.0
	s_add_i32 s58, s56, 1
	s_cmp_lt_u32 s58, s57
	s_cselect_b32 s68, 1.0, 0
	v_pk_mul_f32 v[240:241], v[128:129], s[62:63] op_sel_hi:[1,0]
	v_lshlrev_b32_e32 v242, 16, v216
	v_and_b32_e32 v243, 0xffff0000, v216
	v_pk_fma_f32 v[232:233], v[240:241], v[242:243], v[160:161]
	v_pk_mul_f32 v[240:241], v[130:131], s[62:63] op_sel_hi:[1,0]
	v_lshlrev_b32_e32 v242, 16, v217
	v_and_b32_e32 v243, 0xffff0000, v217
	v_pk_fma_f32 v[234:235], v[240:241], v[242:243], v[162:163]
	v_pk_mul_f32 v[240:241], v[132:133], s[62:63] op_sel_hi:[1,0]
	v_lshlrev_b32_e32 v242, 16, v218
	v_and_b32_e32 v243, 0xffff0000, v218
	v_pk_fma_f32 v[236:237], v[240:241], v[242:243], v[164:165]
	v_pk_mul_f32 v[240:241], v[134:135], s[62:63] op_sel_hi:[1,0]
	v_lshlrev_b32_e32 v242, 16, v219
	v_and_b32_e32 v243, 0xffff0000, v219
	v_pk_fma_f32 v[238:239], v[240:241], v[242:243], v[166:167]
	v_pk_mul_f32 v[240:241], v[136:137], s[64:65] op_sel_hi:[1,0]
	v_lshlrev_b32_e32 v242, 16, v220
	v_and_b32_e32 v243, 0xffff0000, v220
	v_pk_fma_f32 v[232:233], v[240:241], v[242:243], v[232:233]
	v_pk_mul_f32 v[240:241], v[138:139], s[64:65] op_sel_hi:[1,0]
	v_lshlrev_b32_e32 v242, 16, v221
	v_and_b32_e32 v243, 0xffff0000, v221
	v_pk_fma_f32 v[234:235], v[240:241], v[242:243], v[234:235]
	v_pk_mul_f32 v[240:241], v[140:141], s[64:65] op_sel_hi:[1,0]
	v_lshlrev_b32_e32 v242, 16, v222
	v_and_b32_e32 v243, 0xffff0000, v222
	v_pk_fma_f32 v[236:237], v[240:241], v[242:243], v[236:237]
	v_pk_mul_f32 v[240:241], v[142:143], s[64:65] op_sel_hi:[1,0]
	v_lshlrev_b32_e32 v242, 16, v223
	v_and_b32_e32 v243, 0xffff0000, v223
	v_pk_fma_f32 v[238:239], v[240:241], v[242:243], v[238:239]
	v_pk_mul_f32 v[240:241], v[144:145], s[66:67] op_sel_hi:[1,0]
	v_lshlrev_b32_e32 v242, 16, v224
	v_and_b32_e32 v243, 0xffff0000, v224
	v_pk_fma_f32 v[232:233], v[240:241], v[242:243], v[232:233]
	v_pk_mul_f32 v[240:241], v[146:147], s[66:67] op_sel_hi:[1,0]
	v_lshlrev_b32_e32 v242, 16, v225
	v_and_b32_e32 v243, 0xffff0000, v225
	v_pk_fma_f32 v[234:235], v[240:241], v[242:243], v[234:235]
	v_pk_mul_f32 v[240:241], v[148:149], s[66:67] op_sel_hi:[1,0]
	v_lshlrev_b32_e32 v242, 16, v226
	v_and_b32_e32 v243, 0xffff0000, v226
	v_pk_fma_f32 v[236:237], v[240:241], v[242:243], v[236:237]
	v_pk_mul_f32 v[240:241], v[150:151], s[66:67] op_sel_hi:[1,0]
	v_lshlrev_b32_e32 v242, 16, v227
	v_and_b32_e32 v243, 0xffff0000, v227
	v_pk_fma_f32 v[238:239], v[240:241], v[242:243], v[238:239]
	v_pk_mul_f32 v[240:241], v[152:153], s[68:69] op_sel_hi:[1,0]
	v_lshlrev_b32_e32 v242, 16, v228
	v_and_b32_e32 v243, 0xffff0000, v228
	v_pk_fma_f32 v[232:233], v[240:241], v[242:243], v[232:233]
	v_pk_mul_f32 v[240:241], v[154:155], s[68:69] op_sel_hi:[1,0]
	v_lshlrev_b32_e32 v242, 16, v229
	v_and_b32_e32 v243, 0xffff0000, v229
	v_pk_fma_f32 v[234:235], v[240:241], v[242:243], v[234:235]
	v_pk_mul_f32 v[240:241], v[156:157], s[68:69] op_sel_hi:[1,0]
	v_lshlrev_b32_e32 v242, 16, v230
	v_and_b32_e32 v243, 0xffff0000, v230
	v_pk_fma_f32 v[236:237], v[240:241], v[242:243], v[236:237]
	v_pk_mul_f32 v[240:241], v[158:159], s[68:69] op_sel_hi:[1,0]
	v_lshlrev_b32_e32 v242, 16, v231
	v_and_b32_e32 v243, 0xffff0000, v231
	v_pk_fma_f32 v[238:239], v[240:241], v[242:243], v[238:239]
	v_cvt_pk_bf16_f32 v248, v232, v233
	v_cvt_pk_bf16_f32 v249, v234, v235
	v_cvt_pk_bf16_f32 v250, v236, v237
	v_cvt_pk_bf16_f32 v251, v238, v239
	s_lshl_b32 s58, s54, 11
	s_add_u32 s60, s52, s58
	s_addc_u32 s61, s53, 0
	global_store_dwordx4 v126, v[248:251], s[60:61]
	s_branch .LBB0_2164
